# K-loop MFMA blocks: lgkmcnt(0) replaced by counted lgkmcnt ladder at first consumer; independent MFMAs ordered by operand arrival (all 14 GEMM instances)
# baseline (speedup 1.0000x reference)
.LBB0_374:
	v_mov_b64_e32 v[2:3], 0x800
	s_ashr_i32 s45, s44, 31
	v_cmp_lt_i64_e32 vcc, s[10:11], v[2:3]
	s_lshl_b64 s[10:11], s[44:45], 18
	s_add_u32 s48, s27, s10
	s_addc_u32 s49, s60, s11
	s_and_b64 s[10:11], vcc, exec
	ds_read_b128 v[2:5], v165
	ds_read_b128 v[6:9], v166
	ds_read_b128 v[10:13], v167
	ds_read_b128 v[14:17], v168
	s_cselect_b32 s12, s49, s9
	s_cselect_b32 s13, s48, s8
	s_ashr_i32 s43, s42, 31
	s_lshl_b64 s[10:11], s[42:43], 18
	s_add_u32 s50, s62, s10
	s_addc_u32 s51, s63, s11
	s_and_b64 s[10:11], vcc, exec
	s_cselect_b32 s28, s51, s7
	s_cselect_b32 s43, s50, s6
	s_add_u32 s10, s8, 0x20080
	s_addc_u32 s11, s9, 0
	s_add_i32 s45, s64, 0xc000
	v_add_u32_e32 v181, s72, v164
	v_lshl_add_u64 v[50:51], s[10:11], 0, v[150:151]
	s_mov_b32 m0, s45
	s_add_i32 s47, s64, 0xe000
	ds_read_b128 v[18:21], v181
	ds_read_b128 v[22:25], v181 offset:1024
	ds_read_b128 v[26:29], v181 offset:2048
	ds_read_b128 v[30:33], v181 offset:3072
	ds_read_b128 v[34:37], v181 offset:4096
	ds_read_b128 v[38:41], v181 offset:5120
	ds_read_b128 v[42:45], v181 offset:6144
	ds_read_b128 v[46:49], v181 offset:7168
	global_load_lds_dwordx4 v[50:51], off
	v_lshl_add_u64 v[50:51], s[10:11], 0, v[148:149]
	s_mov_b32 m0, s47
	s_nop 0
	global_load_lds_dwordx4 v[50:51], off
	s_waitcnt lgkmcnt(8)
	s_barrier
	s_setprio 1
	s_waitcnt lgkmcnt(6)
	v_mfma_scale_f32_16x16x128_f8f6f4 v[142:145], v[2:9], v[18:25], 0, v222, v222 op_sel_hi:[0,0,0]
	v_mfma_scale_f32_16x16x128_f8f6f4 v[138:141], v[10:17], v[18:25], 0, v222, v222 op_sel_hi:[0,0,0]
	s_waitcnt lgkmcnt(4)
	v_mfma_scale_f32_16x16x128_f8f6f4 v[126:129], v[2:9], v[26:33], 0, v222, v222 op_sel_hi:[0,0,0]
	v_mfma_scale_f32_16x16x128_f8f6f4 v[122:125], v[10:17], v[26:33], 0, v222, v222 op_sel_hi:[0,0,0]
	s_waitcnt lgkmcnt(2)
	v_mfma_scale_f32_16x16x128_f8f6f4 v[110:113], v[2:9], v[34:41], 0, v222, v222 op_sel_hi:[0,0,0]
	v_mfma_scale_f32_16x16x128_f8f6f4 v[106:109], v[10:17], v[34:41], 0, v222, v222 op_sel_hi:[0,0,0]
	s_waitcnt lgkmcnt(0)
	v_mfma_scale_f32_16x16x128_f8f6f4 v[94:97], v[2:9], v[42:49], 0, v222, v222 op_sel_hi:[0,0,0]
	v_mfma_scale_f32_16x16x128_f8f6f4 v[90:93], v[10:17], v[42:49], 0, v222, v222 op_sel_hi:[0,0,0]
	s_setprio 0
	s_barrier
	v_lshl_add_u64 v[160:161], s[6:7], 0, v[0:1]
	s_mov_b64 s[10:11], 0x100
	s_mov_b32 m0, s65
	v_lshl_add_u64 v[50:51], v[160:161], 0, s[10:11]
	v_lshl_add_u64 v[162:163], s[6:7], 0, v[146:147]
	ds_read_b128 v[188:191], v169
	ds_read_b128 v[192:195], v170
	ds_read_b128 v[196:199], v171
	ds_read_b128 v[200:203], v172
	global_load_lds_dwordx4 v[50:51], off
	v_lshl_add_u64 v[50:51], v[162:163], 0, s[10:11]
	s_mov_b32 m0, s66
	s_nop 0
	global_load_lds_dwordx4 v[50:51], off
	s_barrier
	s_setprio 1
	s_waitcnt lgkmcnt(2)
	v_mfma_scale_f32_16x16x128_f8f6f4 v[134:137], v[188:195], v[18:25], 0, v222, v222 op_sel_hi:[0,0,0]
	v_mfma_scale_f32_16x16x128_f8f6f4 v[118:121], v[188:195], v[26:33], 0, v222, v222 op_sel_hi:[0,0,0]
	v_mfma_scale_f32_16x16x128_f8f6f4 v[102:105], v[188:195], v[34:41], 0, v222, v222 op_sel_hi:[0,0,0]
	v_mfma_scale_f32_16x16x128_f8f6f4 v[86:89], v[188:195], v[42:49], 0, v222, v222 op_sel_hi:[0,0,0]
	s_waitcnt lgkmcnt(0)
	v_mfma_scale_f32_16x16x128_f8f6f4 v[130:133], v[196:203], v[18:25], 0, v222, v222 op_sel_hi:[0,0,0]
	v_mfma_scale_f32_16x16x128_f8f6f4 v[114:117], v[196:203], v[26:33], 0, v222, v222 op_sel_hi:[0,0,0]
	v_mfma_scale_f32_16x16x128_f8f6f4 v[98:101], v[196:203], v[34:41], 0, v222, v222 op_sel_hi:[0,0,0]
	v_mfma_scale_f32_16x16x128_f8f6f4 v[82:85], v[196:203], v[42:49], 0, v222, v222 op_sel_hi:[0,0,0]
	s_setprio 0
	v_lshl_add_u64 v[156:157], s[8:9], 0, v[150:151]
	s_mov_b32 m0, s64
	v_lshl_add_u64 v[26:27], v[156:157], 0, s[10:11]
	v_lshl_add_u64 v[158:159], s[8:9], 0, v[148:149]
	s_barrier
	ds_read_b128 v[18:21], v181 offset:16384
	ds_read_b128 v[22:25], v181 offset:17408
	ds_read_b128 v[34:37], v181 offset:18432
	ds_read_b128 v[38:41], v181 offset:19456
	ds_read_b128 v[204:207], v181 offset:20480
	ds_read_b128 v[208:211], v181 offset:21504
	ds_read_b128 v[212:215], v181 offset:22528
	ds_read_b128 v[216:219], v181 offset:23552
	global_load_lds_dwordx4 v[26:27], off
	v_lshl_add_u64 v[26:27], v[158:159], 0, s[10:11]
	s_mov_b32 m0, s67
	s_nop 0
	global_load_lds_dwordx4 v[26:27], off
	s_barrier
	s_setprio 1
	s_waitcnt lgkmcnt(6)
	v_mfma_scale_f32_16x16x128_f8f6f4 v[78:81], v[2:9], v[18:25], 0, v222, v222 op_sel_hi:[0,0,0]
	v_mfma_scale_f32_16x16x128_f8f6f4 v[74:77], v[10:17], v[18:25], 0, v222, v222 op_sel_hi:[0,0,0]
	s_waitcnt lgkmcnt(4)
	v_mfma_scale_f32_16x16x128_f8f6f4 v[62:65], v[2:9], v[34:41], 0, v222, v222 op_sel_hi:[0,0,0]
	v_mfma_scale_f32_16x16x128_f8f6f4 v[58:61], v[10:17], v[34:41], 0, v222, v222 op_sel_hi:[0,0,0]
	s_waitcnt lgkmcnt(2)
	v_mfma_scale_f32_16x16x128_f8f6f4 v[46:49], v[2:9], v[204:211], 0, v222, v222 op_sel_hi:[0,0,0]
	v_mfma_scale_f32_16x16x128_f8f6f4 v[42:45], v[10:17], v[204:211], 0, v222, v222 op_sel_hi:[0,0,0]
	s_waitcnt lgkmcnt(0)
	v_mfma_scale_f32_16x16x128_f8f6f4 v[30:33], v[2:9], v[212:219], 0, v222, v222 op_sel_hi:[0,0,0]
	v_mfma_scale_f32_16x16x128_f8f6f4 v[26:29], v[10:17], v[212:219], 0, v222, v222 op_sel_hi:[0,0,0]
	s_setprio 0
	s_barrier
	s_add_u32 s10, s6, 0x20100
	s_addc_u32 s11, s7, 0
	s_mov_b32 m0, s68
	v_lshl_add_u64 v[2:3], s[10:11], 0, v[0:1]
	global_load_lds_dwordx4 v[2:3], off
	v_lshl_add_u64 v[2:3], s[10:11], 0, v[146:147]
	s_mov_b32 m0, s69
	s_nop 0
	global_load_lds_dwordx4 v[2:3], off
	s_waitcnt vmcnt(6)
	s_barrier
	s_setprio 1
	v_mfma_scale_f32_16x16x128_f8f6f4 v[70:73], v[188:195], v[18:25], 0, v222, v222 op_sel_hi:[0,0,0]
	v_mfma_scale_f32_16x16x128_f8f6f4 v[66:69], v[196:203], v[18:25], 0, v222, v222 op_sel_hi:[0,0,0]
	v_mfma_scale_f32_16x16x128_f8f6f4 v[54:57], v[188:195], v[34:41], 0, v222, v222 op_sel_hi:[0,0,0]
	v_mfma_scale_f32_16x16x128_f8f6f4 v[50:53], v[196:203], v[34:41], 0, v222, v222 op_sel_hi:[0,0,0]
	v_mfma_scale_f32_16x16x128_f8f6f4 v[38:41], v[188:195], v[204:211], 0, v222, v222 op_sel_hi:[0,0,0]
	v_mfma_scale_f32_16x16x128_f8f6f4 v[34:37], v[196:203], v[204:211], 0, v222, v222 op_sel_hi:[0,0,0]
	v_mfma_scale_f32_16x16x128_f8f6f4 v[22:25], v[188:195], v[212:219], 0, v222, v222 op_sel_hi:[0,0,0]
	v_mfma_scale_f32_16x16x128_f8f6f4 v[18:21], v[196:203], v[212:219], 0, v222, v222 op_sel_hi:[0,0,0]
	s_setprio 0
	s_barrier
	ds_read_b128 v[2:5], v173
	ds_read_b128 v[6:9], v174
	ds_read_b128 v[10:13], v175
	ds_read_b128 v[14:17], v176
	s_add_u32 s10, s8, 0x20100
	s_addc_u32 s11, s9, 0
	s_mov_b32 m0, s70
	v_lshl_add_u64 v[182:183], s[10:11], 0, v[150:151]
	ds_read_b128 v[188:191], v181 offset:32768
	ds_read_b128 v[192:195], v181 offset:33792
	ds_read_b128 v[196:199], v181 offset:34816
	ds_read_b128 v[200:203], v181 offset:35840
	ds_read_b128 v[204:207], v181 offset:36864
	ds_read_b128 v[208:211], v181 offset:37888
	ds_read_b128 v[212:215], v181 offset:38912
	ds_read_b128 v[216:219], v181 offset:39936
	global_load_lds_dwordx4 v[182:183], off
	v_lshl_add_u64 v[182:183], s[10:11], 0, v[148:149]
	s_mov_b32 m0, s71
	s_nop 0
	global_load_lds_dwordx4 v[182:183], off
	s_waitcnt lgkmcnt(8)
	s_barrier
	s_setprio 1
	s_waitcnt lgkmcnt(6)
	v_mfma_scale_f32_16x16x128_f8f6f4 v[142:145], v[2:9], v[188:195], v[142:145], v222, v222 op_sel_hi:[0,0,0]
	v_mfma_scale_f32_16x16x128_f8f6f4 v[138:141], v[10:17], v[188:195], v[138:141], v222, v222 op_sel_hi:[0,0,0]
	s_waitcnt lgkmcnt(4)
	v_mfma_scale_f32_16x16x128_f8f6f4 v[126:129], v[2:9], v[196:203], v[126:129], v222, v222 op_sel_hi:[0,0,0]
	v_mfma_scale_f32_16x16x128_f8f6f4 v[122:125], v[10:17], v[196:203], v[122:125], v222, v222 op_sel_hi:[0,0,0]
	s_waitcnt lgkmcnt(2)
	v_mfma_scale_f32_16x16x128_f8f6f4 v[110:113], v[2:9], v[204:211], v[110:113], v222, v222 op_sel_hi:[0,0,0]
	v_mfma_scale_f32_16x16x128_f8f6f4 v[106:109], v[10:17], v[204:211], v[106:109], v222, v222 op_sel_hi:[0,0,0]
	s_waitcnt lgkmcnt(0)
	v_mfma_scale_f32_16x16x128_f8f6f4 v[94:97], v[2:9], v[212:219], v[94:97], v222, v222 op_sel_hi:[0,0,0]
	v_mfma_scale_f32_16x16x128_f8f6f4 v[90:93], v[10:17], v[212:219], v[90:93], v222, v222 op_sel_hi:[0,0,0]
	s_setprio 0
	s_barrier
	s_mov_b64 s[10:11], 0x180
	s_mov_b32 m0, s73
	v_lshl_add_u64 v[160:161], v[160:161], 0, s[10:11]
	ds_read_b128 v[232:235], v177
	ds_read_b128 v[236:239], v178
	ds_read_b128 v[240:243], v179
	ds_read_b128 v[244:247], v180
	global_load_lds_dwordx4 v[160:161], off
	v_lshl_add_u64 v[160:161], v[162:163], 0, s[10:11]
	s_mov_b32 m0, s74
	s_nop 0
	global_load_lds_dwordx4 v[160:161], off
	s_barrier
	s_setprio 1
	s_waitcnt lgkmcnt(2)
	v_mfma_scale_f32_16x16x128_f8f6f4 v[134:137], v[232:239], v[188:195], v[134:137], v222, v222 op_sel_hi:[0,0,0]
	v_mfma_scale_f32_16x16x128_f8f6f4 v[118:121], v[232:239], v[196:203], v[118:121], v222, v222 op_sel_hi:[0,0,0]
	v_mfma_scale_f32_16x16x128_f8f6f4 v[102:105], v[232:239], v[204:211], v[102:105], v222, v222 op_sel_hi:[0,0,0]
	v_mfma_scale_f32_16x16x128_f8f6f4 v[86:89], v[232:239], v[212:219], v[86:89], v222, v222 op_sel_hi:[0,0,0]
	s_waitcnt lgkmcnt(0)
	v_mfma_scale_f32_16x16x128_f8f6f4 v[130:133], v[240:247], v[188:195], v[130:133], v222, v222 op_sel_hi:[0,0,0]
	v_mfma_scale_f32_16x16x128_f8f6f4 v[114:117], v[240:247], v[196:203], v[114:117], v222, v222 op_sel_hi:[0,0,0]
	v_mfma_scale_f32_16x16x128_f8f6f4 v[98:101], v[240:247], v[204:211], v[98:101], v222, v222 op_sel_hi:[0,0,0]
	v_mfma_scale_f32_16x16x128_f8f6f4 v[82:85], v[240:247], v[212:219], v[82:85], v222, v222 op_sel_hi:[0,0,0]
	s_setprio 0
	s_mov_b32 m0, s75
	v_lshl_add_u64 v[156:157], v[156:157], 0, s[10:11]
	s_barrier
	ds_read_b128 v[188:191], v181 offset:49152
	ds_read_b128 v[192:195], v181 offset:50176
	ds_read_b128 v[196:199], v181 offset:51200
	ds_read_b128 v[200:203], v181 offset:52224
	ds_read_b128 v[204:207], v181 offset:53248
	ds_read_b128 v[208:211], v181 offset:54272
	ds_read_b128 v[212:215], v181 offset:55296
	ds_read_b128 v[216:219], v181 offset:56320
	global_load_lds_dwordx4 v[156:157], off
	v_lshl_add_u64 v[156:157], v[158:159], 0, s[10:11]
	s_mov_b32 m0, s76
	s_nop 0
	global_load_lds_dwordx4 v[156:157], off
	s_barrier
	s_setprio 1
	s_waitcnt lgkmcnt(6)
	v_mfma_scale_f32_16x16x128_f8f6f4 v[78:81], v[2:9], v[188:195], v[78:81], v222, v222 op_sel_hi:[0,0,0]
	v_mfma_scale_f32_16x16x128_f8f6f4 v[74:77], v[10:17], v[188:195], v[74:77], v222, v222 op_sel_hi:[0,0,0]
	s_waitcnt lgkmcnt(4)
	v_mfma_scale_f32_16x16x128_f8f6f4 v[62:65], v[2:9], v[196:203], v[62:65], v222, v222 op_sel_hi:[0,0,0]
	v_mfma_scale_f32_16x16x128_f8f6f4 v[58:61], v[10:17], v[196:203], v[58:61], v222, v222 op_sel_hi:[0,0,0]
	s_waitcnt lgkmcnt(2)
	v_mfma_scale_f32_16x16x128_f8f6f4 v[46:49], v[2:9], v[204:211], v[46:49], v222, v222 op_sel_hi:[0,0,0]
	v_mfma_scale_f32_16x16x128_f8f6f4 v[42:45], v[10:17], v[204:211], v[42:45], v222, v222 op_sel_hi:[0,0,0]
	s_waitcnt lgkmcnt(0)
	v_mfma_scale_f32_16x16x128_f8f6f4 v[30:33], v[2:9], v[212:219], v[30:33], v222, v222 op_sel_hi:[0,0,0]
	v_mfma_scale_f32_16x16x128_f8f6f4 v[26:29], v[10:17], v[212:219], v[26:29], v222, v222 op_sel_hi:[0,0,0]
	s_setprio 0
	s_barrier
	s_add_u32 s10, s6, 0x20180
	s_addc_u32 s11, s7, 0
	s_mov_b32 m0, s77
	v_lshl_add_u64 v[2:3], s[10:11], 0, v[0:1]
	global_load_lds_dwordx4 v[2:3], off
	v_lshl_add_u64 v[2:3], s[10:11], 0, v[146:147]
	s_mov_b32 m0, s78
	s_nop 0
	global_load_lds_dwordx4 v[2:3], off
	s_waitcnt vmcnt(6)
	s_barrier
	s_setprio 1
	v_mfma_scale_f32_16x16x128_f8f6f4 v[70:73], v[232:239], v[188:195], v[70:73], v222, v222 op_sel_hi:[0,0,0]
	v_mfma_scale_f32_16x16x128_f8f6f4 v[66:69], v[240:247], v[188:195], v[66:69], v222, v222 op_sel_hi:[0,0,0]
	v_mfma_scale_f32_16x16x128_f8f6f4 v[54:57], v[232:239], v[196:203], v[54:57], v222, v222 op_sel_hi:[0,0,0]
	v_mfma_scale_f32_16x16x128_f8f6f4 v[50:53], v[240:247], v[196:203], v[50:53], v222, v222 op_sel_hi:[0,0,0]
	v_mfma_scale_f32_16x16x128_f8f6f4 v[38:41], v[232:239], v[204:211], v[38:41], v222, v222 op_sel_hi:[0,0,0]
	v_mfma_scale_f32_16x16x128_f8f6f4 v[34:37], v[240:247], v[204:211], v[34:37], v222, v222 op_sel_hi:[0,0,0]
	v_mfma_scale_f32_16x16x128_f8f6f4 v[22:25], v[232:239], v[212:219], v[22:25], v222, v222 op_sel_hi:[0,0,0]
	v_mfma_scale_f32_16x16x128_f8f6f4 v[18:21], v[240:247], v[212:219], v[18:21], v222, v222 op_sel_hi:[0,0,0]
	s_setprio 0
	s_add_u32 s8, s8, 0x20180
	s_addc_u32 s9, s9, 0
	s_add_u32 s52, s6, 0x200
	s_addc_u32 s53, s7, 0
	s_mov_b32 s54, 0
	s_barrier
.LBB0_375:
	ds_read_b128 v[10:13], v165
	ds_read_b128 v[14:17], v166
	ds_read_b128 v[156:159], v167
	ds_read_b128 v[160:163], v168
	s_add_u32 s6, s8, 0xfffe0080
	s_addc_u32 s7, s9, -1
	s_cmp_eq_u32 s54, 4
	s_cselect_b32 s11, s12, s7
	s_cselect_b32 s10, s13, s6
	s_cselect_b32 s7, s28, s53
	s_cselect_b32 s6, s43, s52
	s_mov_b32 m0, s45
	v_lshl_add_u64 v[2:3], s[8:9], 0, v[152:153]
	ds_read_b128 v[188:191], v181
	ds_read_b128 v[192:195], v181 offset:1024
	ds_read_b128 v[196:199], v181 offset:2048
	ds_read_b128 v[200:203], v181 offset:3072
	ds_read_b128 v[204:207], v181 offset:4096
	ds_read_b128 v[208:211], v181 offset:5120
	ds_read_b128 v[212:215], v181 offset:6144
	ds_read_b128 v[216:219], v181 offset:7168
	global_load_lds_dwordx4 v[2:3], off
	v_lshl_add_u64 v[2:3], s[8:9], 0, v[154:155]
	s_mov_b32 m0, s47
	s_nop 0
	global_load_lds_dwordx4 v[2:3], off
	s_waitcnt lgkmcnt(8)
	s_barrier
	s_setprio 1
	s_waitcnt lgkmcnt(6)
	v_mfma_scale_f32_16x16x128_f8f6f4 v[142:145], v[10:17], v[188:195], v[142:145], v222, v222 op_sel_hi:[0,0,0]
	v_mfma_scale_f32_16x16x128_f8f6f4 v[138:141], v[156:163], v[188:195], v[138:141], v222, v222 op_sel_hi:[0,0,0]
	s_waitcnt lgkmcnt(4)
	v_mfma_scale_f32_16x16x128_f8f6f4 v[126:129], v[10:17], v[196:203], v[126:129], v222, v222 op_sel_hi:[0,0,0]
	v_mfma_scale_f32_16x16x128_f8f6f4 v[122:125], v[156:163], v[196:203], v[122:125], v222, v222 op_sel_hi:[0,0,0]
	s_waitcnt lgkmcnt(2)
	v_mfma_scale_f32_16x16x128_f8f6f4 v[110:113], v[10:17], v[204:211], v[110:113], v222, v222 op_sel_hi:[0,0,0]
	v_mfma_scale_f32_16x16x128_f8f6f4 v[106:109], v[156:163], v[204:211], v[106:109], v222, v222 op_sel_hi:[0,0,0]
	s_waitcnt lgkmcnt(0)
	v_mfma_scale_f32_16x16x128_f8f6f4 v[94:97], v[10:17], v[212:219], v[94:97], v222, v222 op_sel_hi:[0,0,0]
	v_mfma_scale_f32_16x16x128_f8f6f4 v[90:93], v[156:163], v[212:219], v[90:93], v222, v222 op_sel_hi:[0,0,0]
	s_setprio 0
	s_barrier
	s_mov_b32 m0, s65
	v_lshl_add_u64 v[6:7], s[6:7], 0, v[0:1]
	ds_read_b128 v[232:235], v169
	ds_read_b128 v[236:239], v170
	ds_read_b128 v[240:243], v171
	ds_read_b128 v[244:247], v172
	global_load_lds_dwordx4 v[6:7], off
	v_lshl_add_u64 v[8:9], s[6:7], 0, v[146:147]
	s_mov_b32 m0, s66
	s_nop 0
	global_load_lds_dwordx4 v[8:9], off
	s_barrier
	s_setprio 1
	s_waitcnt lgkmcnt(2)
	v_mfma_scale_f32_16x16x128_f8f6f4 v[134:137], v[232:239], v[188:195], v[134:137], v222, v222 op_sel_hi:[0,0,0]
	v_mfma_scale_f32_16x16x128_f8f6f4 v[118:121], v[232:239], v[196:203], v[118:121], v222, v222 op_sel_hi:[0,0,0]
	v_mfma_scale_f32_16x16x128_f8f6f4 v[102:105], v[232:239], v[204:211], v[102:105], v222, v222 op_sel_hi:[0,0,0]
	v_mfma_scale_f32_16x16x128_f8f6f4 v[86:89], v[232:239], v[212:219], v[86:89], v222, v222 op_sel_hi:[0,0,0]
	s_waitcnt lgkmcnt(0)
	v_mfma_scale_f32_16x16x128_f8f6f4 v[130:133], v[240:247], v[188:195], v[130:133], v222, v222 op_sel_hi:[0,0,0]
	v_mfma_scale_f32_16x16x128_f8f6f4 v[114:117], v[240:247], v[196:203], v[114:117], v222, v222 op_sel_hi:[0,0,0]
	v_mfma_scale_f32_16x16x128_f8f6f4 v[98:101], v[240:247], v[204:211], v[98:101], v222, v222 op_sel_hi:[0,0,0]
	v_mfma_scale_f32_16x16x128_f8f6f4 v[82:85], v[240:247], v[212:219], v[82:85], v222, v222 op_sel_hi:[0,0,0]
	s_setprio 0
	s_mov_b32 m0, s64
	v_lshl_add_u64 v[2:3], s[10:11], 0, v[150:151]
	s_barrier
	ds_read_b128 v[188:191], v181 offset:16384
	ds_read_b128 v[192:195], v181 offset:17408
	ds_read_b128 v[196:199], v181 offset:18432
	ds_read_b128 v[200:203], v181 offset:19456
	ds_read_b128 v[204:207], v181 offset:20480
	ds_read_b128 v[208:211], v181 offset:21504
	ds_read_b128 v[212:215], v181 offset:22528
	ds_read_b128 v[216:219], v181 offset:23552
	global_load_lds_dwordx4 v[2:3], off
	v_lshl_add_u64 v[4:5], s[10:11], 0, v[148:149]
	s_mov_b32 m0, s67
	s_nop 0
	global_load_lds_dwordx4 v[4:5], off
	s_barrier
	s_setprio 1
	s_waitcnt lgkmcnt(6)
	v_mfma_scale_f32_16x16x128_f8f6f4 v[78:81], v[10:17], v[188:195], v[78:81], v222, v222 op_sel_hi:[0,0,0]
	v_mfma_scale_f32_16x16x128_f8f6f4 v[74:77], v[156:163], v[188:195], v[74:77], v222, v222 op_sel_hi:[0,0,0]
	s_waitcnt lgkmcnt(4)
	v_mfma_scale_f32_16x16x128_f8f6f4 v[62:65], v[10:17], v[196:203], v[62:65], v222, v222 op_sel_hi:[0,0,0]
	v_mfma_scale_f32_16x16x128_f8f6f4 v[58:61], v[156:163], v[196:203], v[58:61], v222, v222 op_sel_hi:[0,0,0]
	s_waitcnt lgkmcnt(2)
	v_mfma_scale_f32_16x16x128_f8f6f4 v[46:49], v[10:17], v[204:211], v[46:49], v222, v222 op_sel_hi:[0,0,0]
	v_mfma_scale_f32_16x16x128_f8f6f4 v[42:45], v[156:163], v[204:211], v[42:45], v222, v222 op_sel_hi:[0,0,0]
	s_waitcnt lgkmcnt(0)
	v_mfma_scale_f32_16x16x128_f8f6f4 v[30:33], v[10:17], v[212:219], v[30:33], v222, v222 op_sel_hi:[0,0,0]
	v_mfma_scale_f32_16x16x128_f8f6f4 v[26:29], v[156:163], v[212:219], v[26:29], v222, v222 op_sel_hi:[0,0,0]
	s_setprio 0
	s_barrier
	s_add_u32 s56, s6, 0x20000
	s_addc_u32 s57, s7, 0
	s_mov_b32 m0, s68
	v_lshl_add_u64 v[10:11], s[56:57], 0, v[0:1]
	global_load_lds_dwordx4 v[10:11], off
	v_lshl_add_u64 v[10:11], s[56:57], 0, v[146:147]
	s_mov_b32 m0, s69
	s_nop 0
	global_load_lds_dwordx4 v[10:11], off
	s_waitcnt vmcnt(6)
	s_barrier
	s_setprio 1
	v_mfma_scale_f32_16x16x128_f8f6f4 v[70:73], v[232:239], v[188:195], v[70:73], v222, v222 op_sel_hi:[0,0,0]
	v_mfma_scale_f32_16x16x128_f8f6f4 v[66:69], v[240:247], v[188:195], v[66:69], v222, v222 op_sel_hi:[0,0,0]
	v_mfma_scale_f32_16x16x128_f8f6f4 v[54:57], v[232:239], v[196:203], v[54:57], v222, v222 op_sel_hi:[0,0,0]
	v_mfma_scale_f32_16x16x128_f8f6f4 v[50:53], v[240:247], v[196:203], v[50:53], v222, v222 op_sel_hi:[0,0,0]
	v_mfma_scale_f32_16x16x128_f8f6f4 v[38:41], v[232:239], v[204:211], v[38:41], v222, v222 op_sel_hi:[0,0,0]
	v_mfma_scale_f32_16x16x128_f8f6f4 v[34:37], v[240:247], v[204:211], v[34:37], v222, v222 op_sel_hi:[0,0,0]
	v_mfma_scale_f32_16x16x128_f8f6f4 v[22:25], v[232:239], v[212:219], v[22:25], v222, v222 op_sel_hi:[0,0,0]
	v_mfma_scale_f32_16x16x128_f8f6f4 v[18:21], v[240:247], v[212:219], v[18:21], v222, v222 op_sel_hi:[0,0,0]
	s_setprio 0
	s_barrier
	ds_read_b128 v[10:13], v173
	ds_read_b128 v[14:17], v174
	ds_read_b128 v[156:159], v175
	ds_read_b128 v[160:163], v176
	s_add_u32 s10, s10, 0x20000
	s_addc_u32 s11, s11, 0
	s_mov_b32 m0, s70
	v_lshl_add_u64 v[182:183], s[10:11], 0, v[150:151]
	ds_read_b128 v[188:191], v181 offset:32768
	ds_read_b128 v[192:195], v181 offset:33792
	ds_read_b128 v[196:199], v181 offset:34816
	ds_read_b128 v[200:203], v181 offset:35840
	ds_read_b128 v[204:207], v181 offset:36864
	ds_read_b128 v[208:211], v181 offset:37888
	ds_read_b128 v[212:215], v181 offset:38912
	ds_read_b128 v[216:219], v181 offset:39936
	global_load_lds_dwordx4 v[182:183], off
	v_lshl_add_u64 v[182:183], s[10:11], 0, v[148:149]
	s_mov_b32 m0, s71
	s_nop 0
	global_load_lds_dwordx4 v[182:183], off
	s_waitcnt lgkmcnt(8)
	s_barrier
	s_setprio 1
	s_waitcnt lgkmcnt(6)
	v_mfma_scale_f32_16x16x128_f8f6f4 v[142:145], v[10:17], v[188:195], v[142:145], v222, v222 op_sel_hi:[0,0,0]
	v_mfma_scale_f32_16x16x128_f8f6f4 v[138:141], v[156:163], v[188:195], v[138:141], v222, v222 op_sel_hi:[0,0,0]
	s_waitcnt lgkmcnt(4)
	v_mfma_scale_f32_16x16x128_f8f6f4 v[126:129], v[10:17], v[196:203], v[126:129], v222, v222 op_sel_hi:[0,0,0]
	v_mfma_scale_f32_16x16x128_f8f6f4 v[122:125], v[156:163], v[196:203], v[122:125], v222, v222 op_sel_hi:[0,0,0]
	s_waitcnt lgkmcnt(2)
	v_mfma_scale_f32_16x16x128_f8f6f4 v[110:113], v[10:17], v[204:211], v[110:113], v222, v222 op_sel_hi:[0,0,0]
	v_mfma_scale_f32_16x16x128_f8f6f4 v[106:109], v[156:163], v[204:211], v[106:109], v222, v222 op_sel_hi:[0,0,0]
	s_waitcnt lgkmcnt(0)
	v_mfma_scale_f32_16x16x128_f8f6f4 v[94:97], v[10:17], v[212:219], v[94:97], v222, v222 op_sel_hi:[0,0,0]
	v_mfma_scale_f32_16x16x128_f8f6f4 v[90:93], v[156:163], v[212:219], v[90:93], v222, v222 op_sel_hi:[0,0,0]
	s_setprio 0
	s_barrier
	s_mov_b32 m0, s73
	v_lshl_add_u64 v[6:7], v[6:7], 0, s[24:25]
	ds_read_b128 v[232:235], v177
	ds_read_b128 v[236:239], v178
	ds_read_b128 v[240:243], v179
	ds_read_b128 v[244:247], v180
	global_load_lds_dwordx4 v[6:7], off
	v_lshl_add_u64 v[6:7], v[8:9], 0, s[24:25]
	s_mov_b32 m0, s74
	s_nop 0
	global_load_lds_dwordx4 v[6:7], off
	s_barrier
	s_setprio 1
	s_waitcnt lgkmcnt(2)
	v_mfma_scale_f32_16x16x128_f8f6f4 v[134:137], v[232:239], v[188:195], v[134:137], v222, v222 op_sel_hi:[0,0,0]
	v_mfma_scale_f32_16x16x128_f8f6f4 v[118:121], v[232:239], v[196:203], v[118:121], v222, v222 op_sel_hi:[0,0,0]
	v_mfma_scale_f32_16x16x128_f8f6f4 v[102:105], v[232:239], v[204:211], v[102:105], v222, v222 op_sel_hi:[0,0,0]
	v_mfma_scale_f32_16x16x128_f8f6f4 v[86:89], v[232:239], v[212:219], v[86:89], v222, v222 op_sel_hi:[0,0,0]
	s_waitcnt lgkmcnt(0)
	v_mfma_scale_f32_16x16x128_f8f6f4 v[130:133], v[240:247], v[188:195], v[130:133], v222, v222 op_sel_hi:[0,0,0]
	v_mfma_scale_f32_16x16x128_f8f6f4 v[114:117], v[240:247], v[196:203], v[114:117], v222, v222 op_sel_hi:[0,0,0]
	v_mfma_scale_f32_16x16x128_f8f6f4 v[98:101], v[240:247], v[204:211], v[98:101], v222, v222 op_sel_hi:[0,0,0]
	v_mfma_scale_f32_16x16x128_f8f6f4 v[82:85], v[240:247], v[212:219], v[82:85], v222, v222 op_sel_hi:[0,0,0]
	s_setprio 0
	s_mov_b32 m0, s75
	v_lshl_add_u64 v[2:3], v[2:3], 0, s[24:25]
	s_barrier
	ds_read_b128 v[188:191], v181 offset:49152
	ds_read_b128 v[192:195], v181 offset:50176
	ds_read_b128 v[196:199], v181 offset:51200
	ds_read_b128 v[200:203], v181 offset:52224
	ds_read_b128 v[204:207], v181 offset:53248
	ds_read_b128 v[208:211], v181 offset:54272
	ds_read_b128 v[212:215], v181 offset:55296
	ds_read_b128 v[216:219], v181 offset:56320
	global_load_lds_dwordx4 v[2:3], off
	v_lshl_add_u64 v[2:3], v[4:5], 0, s[24:25]
	s_mov_b32 m0, s76
	s_nop 0
	global_load_lds_dwordx4 v[2:3], off
	s_barrier
	s_setprio 1
	s_waitcnt lgkmcnt(6)
	v_mfma_scale_f32_16x16x128_f8f6f4 v[78:81], v[10:17], v[188:195], v[78:81], v222, v222 op_sel_hi:[0,0,0]
	v_mfma_scale_f32_16x16x128_f8f6f4 v[74:77], v[156:163], v[188:195], v[74:77], v222, v222 op_sel_hi:[0,0,0]
	s_waitcnt lgkmcnt(4)
	v_mfma_scale_f32_16x16x128_f8f6f4 v[62:65], v[10:17], v[196:203], v[62:65], v222, v222 op_sel_hi:[0,0,0]
	v_mfma_scale_f32_16x16x128_f8f6f4 v[58:61], v[156:163], v[196:203], v[58:61], v222, v222 op_sel_hi:[0,0,0]
	s_waitcnt lgkmcnt(2)
	v_mfma_scale_f32_16x16x128_f8f6f4 v[46:49], v[10:17], v[204:211], v[46:49], v222, v222 op_sel_hi:[0,0,0]
	v_mfma_scale_f32_16x16x128_f8f6f4 v[42:45], v[156:163], v[204:211], v[42:45], v222, v222 op_sel_hi:[0,0,0]
	s_waitcnt lgkmcnt(0)
	v_mfma_scale_f32_16x16x128_f8f6f4 v[30:33], v[10:17], v[212:219], v[30:33], v222, v222 op_sel_hi:[0,0,0]
	v_mfma_scale_f32_16x16x128_f8f6f4 v[26:29], v[156:163], v[212:219], v[26:29], v222, v222 op_sel_hi:[0,0,0]
	s_setprio 0
	s_barrier
	s_add_u32 s6, s6, 0x20080
	s_addc_u32 s7, s7, 0
	s_mov_b32 m0, s77
	v_lshl_add_u64 v[2:3], s[6:7], 0, v[0:1]
	global_load_lds_dwordx4 v[2:3], off
	v_lshl_add_u64 v[2:3], s[6:7], 0, v[146:147]
	s_mov_b32 m0, s78
	s_nop 0
	global_load_lds_dwordx4 v[2:3], off
	s_waitcnt vmcnt(6)
	s_barrier
	s_setprio 1
	v_mfma_scale_f32_16x16x128_f8f6f4 v[70:73], v[232:239], v[188:195], v[70:73], v222, v222 op_sel_hi:[0,0,0]
	v_mfma_scale_f32_16x16x128_f8f6f4 v[66:69], v[240:247], v[188:195], v[66:69], v222, v222 op_sel_hi:[0,0,0]
	v_mfma_scale_f32_16x16x128_f8f6f4 v[54:57], v[232:239], v[196:203], v[54:57], v222, v222 op_sel_hi:[0,0,0]
	v_mfma_scale_f32_16x16x128_f8f6f4 v[50:53], v[240:247], v[196:203], v[50:53], v222, v222 op_sel_hi:[0,0,0]
	v_mfma_scale_f32_16x16x128_f8f6f4 v[38:41], v[232:239], v[204:211], v[38:41], v222, v222 op_sel_hi:[0,0,0]
	v_mfma_scale_f32_16x16x128_f8f6f4 v[34:37], v[240:247], v[204:211], v[34:37], v222, v222 op_sel_hi:[0,0,0]
	v_mfma_scale_f32_16x16x128_f8f6f4 v[22:25], v[232:239], v[212:219], v[22:25], v222, v222 op_sel_hi:[0,0,0]
	v_mfma_scale_f32_16x16x128_f8f6f4 v[18:21], v[240:247], v[212:219], v[18:21], v222, v222 op_sel_hi:[0,0,0]
	s_setprio 0
	s_add_i32 s54, s54, 2
	s_add_u32 s8, s8, 0x100
	s_addc_u32 s9, s9, 0
	s_add_u32 s52, s52, 0x100
	s_addc_u32 s53, s53, 0
	s_cmp_gt_u32 s54, 5
	s_barrier
	s_cbranch_scc0 .LBB0_375
	s_and_b32 s43, s82, 3
	s_cmp_lt_i32 s82, 4
	s_cselect_b64 s[6:7], -1, 0
	s_cmp_gt_i32 s82, 3
	s_nop 15
	s_nop 15
	v_mbcnt_lo_u32_b32 v2, -1, 0
	v_mbcnt_hi_u32_b32 v2, -1, v2
	s_cselect_b64 s[58:59], -1, 0
	s_cmp_lt_i32 s82, 8
	s_cselect_b64 s[8:9], -1, 0
	s_cmp_gt_i32 s82, 7
	v_readlane_b32 s47, v252, 51
	v_readlane_b32 s45, v252, 52
	s_cselect_b64 s[12:13], -1, 0
	s_mov_b64 s[10:11], -1
	s_and_b64 vcc, exec, s[58:59]
	s_cbranch_vccz .LBB0_382
	s_and_b64 vcc, exec, s[12:13]
	s_cbranch_vccz .LBB0_379
	s_lshl_b32 s10, s82, 8
	s_add_i32 s28, s10, 0xfffff800
	s_mov_b64 s[10:11], 0

.LBB0_525:
	s_ashr_i32 s9, s8, 31
	v_cmp_lt_i64_e32 vcc, s[10:11], v[248:249]
	s_lshl_b64 s[10:11], s[8:9], 18
	s_add_u32 s10, s44, s10
	s_addc_u32 s11, s45, s11
	s_and_b64 s[12:13], vcc, exec
	ds_read_b128 v[2:5], v165
	ds_read_b128 v[6:9], v166
	ds_read_b128 v[10:13], v167
	ds_read_b128 v[14:17], v168
	s_cselect_b32 s9, s11, s43
	s_cselect_b32 s67, s10, s42
	s_ashr_i32 s7, s6, 31
	s_lshl_b64 s[12:13], s[6:7], 18
	s_add_u32 s12, s27, s12
	s_addc_u32 s13, s60, s13
	s_and_b64 s[20:21], vcc, exec
	s_cselect_b32 s7, s13, s35
	s_cselect_b32 s68, s12, s34
	s_add_u32 s20, s42, 0x20080
	s_addc_u32 s21, s43, 0
	s_add_i32 s69, s46, 0xc000
	v_add_u32_e32 v181, s54, v164
	v_lshl_add_u64 v[42:43], s[20:21], 0, v[150:151]
	s_mov_b32 m0, s69
	s_add_i32 s70, s46, 0xe000
	ds_read_b128 v[18:21], v181
	ds_read_b128 v[22:25], v181 offset:1024
	ds_read_b128 v[26:29], v181 offset:2048
	ds_read_b128 v[30:33], v181 offset:3072
	ds_read_b128 v[34:37], v181 offset:4096
	ds_read_b128 v[38:41], v181 offset:5120
	ds_read_b128 v[50:53], v181 offset:6144
	ds_read_b128 v[54:57], v181 offset:7168
	global_load_lds_dwordx4 v[42:43], off
	v_lshl_add_u64 v[42:43], s[20:21], 0, v[148:149]
	s_mov_b32 m0, s70
	s_nop 0
	global_load_lds_dwordx4 v[42:43], off
	s_waitcnt lgkmcnt(8)
	s_barrier
	s_setprio 1
	s_waitcnt lgkmcnt(6)
	v_mfma_scale_f32_16x16x128_f8f6f4 v[130:133], v[2:9], v[18:25], 0, v222, v222 op_sel_hi:[0,0,0]
	v_mfma_scale_f32_16x16x128_f8f6f4 v[122:125], v[10:17], v[18:25], 0, v222, v222 op_sel_hi:[0,0,0]
	s_waitcnt lgkmcnt(4)
	v_mfma_scale_f32_16x16x128_f8f6f4 v[114:117], v[2:9], v[26:33], 0, v222, v222 op_sel_hi:[0,0,0]
	v_mfma_scale_f32_16x16x128_f8f6f4 v[106:109], v[10:17], v[26:33], 0, v222, v222 op_sel_hi:[0,0,0]
	s_waitcnt lgkmcnt(2)
	v_mfma_scale_f32_16x16x128_f8f6f4 v[98:101], v[2:9], v[34:41], 0, v222, v222 op_sel_hi:[0,0,0]
	v_mfma_scale_f32_16x16x128_f8f6f4 v[90:93], v[10:17], v[34:41], 0, v222, v222 op_sel_hi:[0,0,0]
	s_waitcnt lgkmcnt(0)
	v_mfma_scale_f32_16x16x128_f8f6f4 v[86:89], v[2:9], v[50:57], 0, v222, v222 op_sel_hi:[0,0,0]
	v_mfma_scale_f32_16x16x128_f8f6f4 v[82:85], v[10:17], v[50:57], 0, v222, v222 op_sel_hi:[0,0,0]
	s_setprio 0
	s_barrier
	v_lshl_add_u64 v[160:161], s[34:35], 0, v[0:1]
	s_mov_b64 s[20:21], 0x100
	s_mov_b32 m0, s47
	v_lshl_add_u64 v[42:43], v[160:161], 0, s[20:21]
	v_lshl_add_u64 v[162:163], s[34:35], 0, v[146:147]
	ds_read_b128 v[188:191], v169
	ds_read_b128 v[192:195], v170
	ds_read_b128 v[196:199], v171
	ds_read_b128 v[200:203], v172
	global_load_lds_dwordx4 v[42:43], off
	v_lshl_add_u64 v[42:43], v[162:163], 0, s[20:21]
	s_mov_b32 m0, s48
	s_nop 0
	global_load_lds_dwordx4 v[42:43], off
	s_barrier
	s_setprio 1
	s_waitcnt lgkmcnt(2)
	v_mfma_scale_f32_16x16x128_f8f6f4 v[62:65], v[188:195], v[18:25], 0, v222, v222 op_sel_hi:[0,0,0]
	s_waitcnt lgkmcnt(0)
	v_mfma_scale_f32_16x16x128_f8f6f4 v[58:61], v[196:203], v[18:25], 0, v222, v222 op_sel_hi:[0,0,0]
	v_mfma_scale_f32_16x16x128_f8f6f4 v[46:49], v[188:195], v[26:33], 0, v222, v222 op_sel_hi:[0,0,0]
	v_mfma_scale_f32_16x16x128_f8f6f4 v[42:45], v[196:203], v[26:33], 0, v222, v222 op_sel_hi:[0,0,0]
	v_mfma_scale_f32_16x16x128_f8f6f4 v[30:33], v[188:195], v[34:41], 0, v222, v222 op_sel_hi:[0,0,0]
	v_mfma_scale_f32_16x16x128_f8f6f4 v[26:29], v[196:203], v[34:41], 0, v222, v222 op_sel_hi:[0,0,0]
	v_mfma_scale_f32_16x16x128_f8f6f4 v[22:25], v[188:195], v[50:57], 0, v222, v222 op_sel_hi:[0,0,0]
	v_mfma_scale_f32_16x16x128_f8f6f4 v[18:21], v[196:203], v[50:57], 0, v222, v222 op_sel_hi:[0,0,0]
	s_setprio 0
	v_lshl_add_u64 v[156:157], s[42:43], 0, v[150:151]
	s_mov_b32 m0, s46
	v_lshl_add_u64 v[66:67], v[156:157], 0, s[20:21]
	v_lshl_add_u64 v[158:159], s[42:43], 0, v[148:149]
	s_barrier
	ds_read_b128 v[34:37], v181 offset:16384
	ds_read_b128 v[38:41], v181 offset:17408
	ds_read_b128 v[50:53], v181 offset:18432
	ds_read_b128 v[54:57], v181 offset:19456
	ds_read_b128 v[204:207], v181 offset:20480
	ds_read_b128 v[208:211], v181 offset:21504
	ds_read_b128 v[212:215], v181 offset:22528
	ds_read_b128 v[216:219], v181 offset:23552
	global_load_lds_dwordx4 v[66:67], off
	v_lshl_add_u64 v[66:67], v[158:159], 0, s[20:21]
	s_mov_b32 m0, s49
	s_nop 0
	global_load_lds_dwordx4 v[66:67], off
	s_barrier
	s_setprio 1
	s_waitcnt lgkmcnt(6)
	v_mfma_scale_f32_16x16x128_f8f6f4 v[142:145], v[2:9], v[34:41], 0, v222, v222 op_sel_hi:[0,0,0]
	v_mfma_scale_f32_16x16x128_f8f6f4 v[138:141], v[10:17], v[34:41], 0, v222, v222 op_sel_hi:[0,0,0]
	s_waitcnt lgkmcnt(4)
	v_mfma_scale_f32_16x16x128_f8f6f4 v[134:137], v[2:9], v[50:57], 0, v222, v222 op_sel_hi:[0,0,0]
	v_mfma_scale_f32_16x16x128_f8f6f4 v[126:129], v[10:17], v[50:57], 0, v222, v222 op_sel_hi:[0,0,0]
	s_waitcnt lgkmcnt(2)
	v_mfma_scale_f32_16x16x128_f8f6f4 v[118:121], v[2:9], v[204:211], 0, v222, v222 op_sel_hi:[0,0,0]
	v_mfma_scale_f32_16x16x128_f8f6f4 v[110:113], v[10:17], v[204:211], 0, v222, v222 op_sel_hi:[0,0,0]
	s_waitcnt lgkmcnt(0)
	v_mfma_scale_f32_16x16x128_f8f6f4 v[102:105], v[2:9], v[212:219], 0, v222, v222 op_sel_hi:[0,0,0]
	v_mfma_scale_f32_16x16x128_f8f6f4 v[94:97], v[10:17], v[212:219], 0, v222, v222 op_sel_hi:[0,0,0]
	s_setprio 0
	s_barrier
	s_add_u32 s20, s34, 0x20100
	s_addc_u32 s21, s35, 0
	s_mov_b32 m0, s50
	v_lshl_add_u64 v[2:3], s[20:21], 0, v[0:1]
	global_load_lds_dwordx4 v[2:3], off
	v_lshl_add_u64 v[2:3], s[20:21], 0, v[146:147]
	s_mov_b32 m0, s51
	s_nop 0
	global_load_lds_dwordx4 v[2:3], off
	s_waitcnt vmcnt(6)
	s_barrier
	s_setprio 1
	v_mfma_scale_f32_16x16x128_f8f6f4 v[78:81], v[188:195], v[34:41], 0, v222, v222 op_sel_hi:[0,0,0]
	v_mfma_scale_f32_16x16x128_f8f6f4 v[74:77], v[196:203], v[34:41], 0, v222, v222 op_sel_hi:[0,0,0]
	v_mfma_scale_f32_16x16x128_f8f6f4 v[70:73], v[188:195], v[50:57], 0, v222, v222 op_sel_hi:[0,0,0]
	v_mfma_scale_f32_16x16x128_f8f6f4 v[66:69], v[196:203], v[50:57], 0, v222, v222 op_sel_hi:[0,0,0]
	v_mfma_scale_f32_16x16x128_f8f6f4 v[54:57], v[188:195], v[204:211], 0, v222, v222 op_sel_hi:[0,0,0]
	v_mfma_scale_f32_16x16x128_f8f6f4 v[50:53], v[196:203], v[204:211], 0, v222, v222 op_sel_hi:[0,0,0]
	v_mfma_scale_f32_16x16x128_f8f6f4 v[38:41], v[188:195], v[212:219], 0, v222, v222 op_sel_hi:[0,0,0]
	v_mfma_scale_f32_16x16x128_f8f6f4 v[34:37], v[196:203], v[212:219], 0, v222, v222 op_sel_hi:[0,0,0]
	s_setprio 0
	s_barrier
	ds_read_b128 v[2:5], v173
	ds_read_b128 v[6:9], v174
	ds_read_b128 v[10:13], v175
	ds_read_b128 v[14:17], v176
	s_add_u32 s20, s42, 0x20100
	s_addc_u32 s21, s43, 0
	s_mov_b32 m0, s52
	v_lshl_add_u64 v[182:183], s[20:21], 0, v[150:151]
	ds_read_b128 v[188:191], v181 offset:32768
	ds_read_b128 v[192:195], v181 offset:33792
	ds_read_b128 v[196:199], v181 offset:34816
	ds_read_b128 v[200:203], v181 offset:35840
	ds_read_b128 v[204:207], v181 offset:36864
	ds_read_b128 v[208:211], v181 offset:37888
	ds_read_b128 v[212:215], v181 offset:38912
	ds_read_b128 v[216:219], v181 offset:39936
	global_load_lds_dwordx4 v[182:183], off
	v_lshl_add_u64 v[182:183], s[20:21], 0, v[148:149]
	s_mov_b32 m0, s53
	s_nop 0
	global_load_lds_dwordx4 v[182:183], off
	s_waitcnt lgkmcnt(8)
	s_barrier
	s_setprio 1
	s_waitcnt lgkmcnt(6)
	v_mfma_scale_f32_16x16x128_f8f6f4 v[130:133], v[2:9], v[188:195], v[130:133], v222, v222 op_sel_hi:[0,0,0]
	v_mfma_scale_f32_16x16x128_f8f6f4 v[122:125], v[10:17], v[188:195], v[122:125], v222, v222 op_sel_hi:[0,0,0]
	s_waitcnt lgkmcnt(4)
	v_mfma_scale_f32_16x16x128_f8f6f4 v[114:117], v[2:9], v[196:203], v[114:117], v222, v222 op_sel_hi:[0,0,0]
	v_mfma_scale_f32_16x16x128_f8f6f4 v[106:109], v[10:17], v[196:203], v[106:109], v222, v222 op_sel_hi:[0,0,0]
	s_waitcnt lgkmcnt(2)
	v_mfma_scale_f32_16x16x128_f8f6f4 v[98:101], v[2:9], v[204:211], v[98:101], v222, v222 op_sel_hi:[0,0,0]
	v_mfma_scale_f32_16x16x128_f8f6f4 v[90:93], v[10:17], v[204:211], v[90:93], v222, v222 op_sel_hi:[0,0,0]
	s_waitcnt lgkmcnt(0)
	v_mfma_scale_f32_16x16x128_f8f6f4 v[86:89], v[2:9], v[212:219], v[86:89], v222, v222 op_sel_hi:[0,0,0]
	v_mfma_scale_f32_16x16x128_f8f6f4 v[82:85], v[10:17], v[212:219], v[82:85], v222, v222 op_sel_hi:[0,0,0]
	s_setprio 0
	s_barrier
	s_mov_b64 s[20:21], 0x180
	s_mov_b32 m0, s55
	v_lshl_add_u64 v[160:161], v[160:161], 0, s[20:21]
	ds_read_b128 v[232:235], v177
	ds_read_b128 v[236:239], v178
	ds_read_b128 v[240:243], v179
	ds_read_b128 v[244:247], v180
	global_load_lds_dwordx4 v[160:161], off
	v_lshl_add_u64 v[160:161], v[162:163], 0, s[20:21]
	s_mov_b32 m0, s56
	s_nop 0
	global_load_lds_dwordx4 v[160:161], off
	s_barrier
	s_setprio 1
	s_waitcnt lgkmcnt(2)
	v_mfma_scale_f32_16x16x128_f8f6f4 v[62:65], v[232:239], v[188:195], v[62:65], v222, v222 op_sel_hi:[0,0,0]
	v_mfma_scale_f32_16x16x128_f8f6f4 v[46:49], v[232:239], v[196:203], v[46:49], v222, v222 op_sel_hi:[0,0,0]
	v_mfma_scale_f32_16x16x128_f8f6f4 v[30:33], v[232:239], v[204:211], v[30:33], v222, v222 op_sel_hi:[0,0,0]
	v_mfma_scale_f32_16x16x128_f8f6f4 v[22:25], v[232:239], v[212:219], v[22:25], v222, v222 op_sel_hi:[0,0,0]
	s_waitcnt lgkmcnt(0)
	v_mfma_scale_f32_16x16x128_f8f6f4 v[58:61], v[240:247], v[188:195], v[58:61], v222, v222 op_sel_hi:[0,0,0]
	v_mfma_scale_f32_16x16x128_f8f6f4 v[42:45], v[240:247], v[196:203], v[42:45], v222, v222 op_sel_hi:[0,0,0]
	v_mfma_scale_f32_16x16x128_f8f6f4 v[26:29], v[240:247], v[204:211], v[26:29], v222, v222 op_sel_hi:[0,0,0]
	v_mfma_scale_f32_16x16x128_f8f6f4 v[18:21], v[240:247], v[212:219], v[18:21], v222, v222 op_sel_hi:[0,0,0]
	s_setprio 0
	s_mov_b32 m0, s57
	v_lshl_add_u64 v[156:157], v[156:157], 0, s[20:21]
	s_barrier
	ds_read_b128 v[188:191], v181 offset:49152
	ds_read_b128 v[192:195], v181 offset:50176
	ds_read_b128 v[196:199], v181 offset:51200
	ds_read_b128 v[200:203], v181 offset:52224
	ds_read_b128 v[204:207], v181 offset:53248
	ds_read_b128 v[208:211], v181 offset:54272
	ds_read_b128 v[212:215], v181 offset:55296
	ds_read_b128 v[216:219], v181 offset:56320
	global_load_lds_dwordx4 v[156:157], off
	v_lshl_add_u64 v[156:157], v[158:159], 0, s[20:21]
	s_mov_b32 m0, s58
	s_nop 0
	global_load_lds_dwordx4 v[156:157], off
	s_barrier
	s_setprio 1
	s_waitcnt lgkmcnt(6)
	v_mfma_scale_f32_16x16x128_f8f6f4 v[142:145], v[2:9], v[188:195], v[142:145], v222, v222 op_sel_hi:[0,0,0]
	v_mfma_scale_f32_16x16x128_f8f6f4 v[138:141], v[10:17], v[188:195], v[138:141], v222, v222 op_sel_hi:[0,0,0]
	s_waitcnt lgkmcnt(4)
	v_mfma_scale_f32_16x16x128_f8f6f4 v[134:137], v[2:9], v[196:203], v[134:137], v222, v222 op_sel_hi:[0,0,0]
	v_mfma_scale_f32_16x16x128_f8f6f4 v[126:129], v[10:17], v[196:203], v[126:129], v222, v222 op_sel_hi:[0,0,0]
	s_waitcnt lgkmcnt(2)
	v_mfma_scale_f32_16x16x128_f8f6f4 v[118:121], v[2:9], v[204:211], v[118:121], v222, v222 op_sel_hi:[0,0,0]
	v_mfma_scale_f32_16x16x128_f8f6f4 v[110:113], v[10:17], v[204:211], v[110:113], v222, v222 op_sel_hi:[0,0,0]
	s_waitcnt lgkmcnt(0)
	v_mfma_scale_f32_16x16x128_f8f6f4 v[102:105], v[2:9], v[212:219], v[102:105], v222, v222 op_sel_hi:[0,0,0]
	v_mfma_scale_f32_16x16x128_f8f6f4 v[94:97], v[10:17], v[212:219], v[94:97], v222, v222 op_sel_hi:[0,0,0]
	s_setprio 0
	s_barrier
	s_add_u32 s20, s34, 0x20180
	s_addc_u32 s21, s35, 0
	s_mov_b32 m0, s59
	v_lshl_add_u64 v[2:3], s[20:21], 0, v[0:1]
	global_load_lds_dwordx4 v[2:3], off
	v_lshl_add_u64 v[2:3], s[20:21], 0, v[146:147]
	s_mov_b32 m0, s61
	s_nop 0
	global_load_lds_dwordx4 v[2:3], off
	s_waitcnt vmcnt(6)
	s_barrier
	s_setprio 1
	v_mfma_scale_f32_16x16x128_f8f6f4 v[78:81], v[232:239], v[188:195], v[78:81], v222, v222 op_sel_hi:[0,0,0]
	v_mfma_scale_f32_16x16x128_f8f6f4 v[74:77], v[240:247], v[188:195], v[74:77], v222, v222 op_sel_hi:[0,0,0]
	v_mfma_scale_f32_16x16x128_f8f6f4 v[70:73], v[232:239], v[196:203], v[70:73], v222, v222 op_sel_hi:[0,0,0]
	v_mfma_scale_f32_16x16x128_f8f6f4 v[66:69], v[240:247], v[196:203], v[66:69], v222, v222 op_sel_hi:[0,0,0]
	v_mfma_scale_f32_16x16x128_f8f6f4 v[54:57], v[232:239], v[204:211], v[54:57], v222, v222 op_sel_hi:[0,0,0]
	v_mfma_scale_f32_16x16x128_f8f6f4 v[50:53], v[240:247], v[204:211], v[50:53], v222, v222 op_sel_hi:[0,0,0]
	v_mfma_scale_f32_16x16x128_f8f6f4 v[38:41], v[232:239], v[212:219], v[38:41], v222, v222 op_sel_hi:[0,0,0]
	v_mfma_scale_f32_16x16x128_f8f6f4 v[34:37], v[240:247], v[212:219], v[34:37], v222, v222 op_sel_hi:[0,0,0]
	s_setprio 0
	s_add_u32 s20, s42, 0x20180
	s_addc_u32 s21, s43, 0
	s_add_u32 s71, s34, 0x200
	s_addc_u32 s72, s35, 0
	s_mov_b32 s73, 0
	s_barrier
.LBB0_526:
	ds_read_b128 v[10:13], v165
	ds_read_b128 v[14:17], v166
	ds_read_b128 v[156:159], v167
	ds_read_b128 v[160:163], v168
	s_add_u32 s34, s20, 0xfffe0080
	s_addc_u32 s35, s21, -1
	s_cmp_eq_u32 s73, 4
	s_cselect_b32 s43, s9, s35
	s_cselect_b32 s42, s67, s34
	s_cselect_b32 s35, s7, s72
	s_cselect_b32 s34, s68, s71
	s_mov_b32 m0, s69
	v_lshl_add_u64 v[2:3], s[20:21], 0, v[152:153]
	ds_read_b128 v[188:191], v181
	ds_read_b128 v[192:195], v181 offset:1024
	ds_read_b128 v[196:199], v181 offset:2048
	ds_read_b128 v[200:203], v181 offset:3072
	ds_read_b128 v[204:207], v181 offset:4096
	ds_read_b128 v[208:211], v181 offset:5120
	ds_read_b128 v[212:215], v181 offset:6144
	ds_read_b128 v[216:219], v181 offset:7168
	global_load_lds_dwordx4 v[2:3], off
	v_lshl_add_u64 v[2:3], s[20:21], 0, v[154:155]
	s_mov_b32 m0, s70
	s_nop 0
	global_load_lds_dwordx4 v[2:3], off
	s_waitcnt lgkmcnt(8)
	s_barrier
	s_setprio 1
	s_waitcnt lgkmcnt(6)
	v_mfma_scale_f32_16x16x128_f8f6f4 v[130:133], v[10:17], v[188:195], v[130:133], v222, v222 op_sel_hi:[0,0,0]
	v_mfma_scale_f32_16x16x128_f8f6f4 v[122:125], v[156:163], v[188:195], v[122:125], v222, v222 op_sel_hi:[0,0,0]
	s_waitcnt lgkmcnt(4)
	v_mfma_scale_f32_16x16x128_f8f6f4 v[114:117], v[10:17], v[196:203], v[114:117], v222, v222 op_sel_hi:[0,0,0]
	v_mfma_scale_f32_16x16x128_f8f6f4 v[106:109], v[156:163], v[196:203], v[106:109], v222, v222 op_sel_hi:[0,0,0]
	s_waitcnt lgkmcnt(2)
	v_mfma_scale_f32_16x16x128_f8f6f4 v[98:101], v[10:17], v[204:211], v[98:101], v222, v222 op_sel_hi:[0,0,0]
	v_mfma_scale_f32_16x16x128_f8f6f4 v[90:93], v[156:163], v[204:211], v[90:93], v222, v222 op_sel_hi:[0,0,0]
	s_waitcnt lgkmcnt(0)
	v_mfma_scale_f32_16x16x128_f8f6f4 v[86:89], v[10:17], v[212:219], v[86:89], v222, v222 op_sel_hi:[0,0,0]
	v_mfma_scale_f32_16x16x128_f8f6f4 v[82:85], v[156:163], v[212:219], v[82:85], v222, v222 op_sel_hi:[0,0,0]
	s_setprio 0
	s_barrier
	s_mov_b32 m0, s47
	v_lshl_add_u64 v[6:7], s[34:35], 0, v[0:1]
	ds_read_b128 v[232:235], v169
	ds_read_b128 v[236:239], v170
	ds_read_b128 v[240:243], v171
	ds_read_b128 v[244:247], v172
	global_load_lds_dwordx4 v[6:7], off
	v_lshl_add_u64 v[8:9], s[34:35], 0, v[146:147]
	s_mov_b32 m0, s48
	s_nop 0
	global_load_lds_dwordx4 v[8:9], off
	s_barrier
	s_setprio 1
	s_waitcnt lgkmcnt(2)
	v_mfma_scale_f32_16x16x128_f8f6f4 v[62:65], v[232:239], v[188:195], v[62:65], v222, v222 op_sel_hi:[0,0,0]
	v_mfma_scale_f32_16x16x128_f8f6f4 v[46:49], v[232:239], v[196:203], v[46:49], v222, v222 op_sel_hi:[0,0,0]
	v_mfma_scale_f32_16x16x128_f8f6f4 v[30:33], v[232:239], v[204:211], v[30:33], v222, v222 op_sel_hi:[0,0,0]
	v_mfma_scale_f32_16x16x128_f8f6f4 v[22:25], v[232:239], v[212:219], v[22:25], v222, v222 op_sel_hi:[0,0,0]
	s_waitcnt lgkmcnt(0)
	v_mfma_scale_f32_16x16x128_f8f6f4 v[58:61], v[240:247], v[188:195], v[58:61], v222, v222 op_sel_hi:[0,0,0]
	v_mfma_scale_f32_16x16x128_f8f6f4 v[42:45], v[240:247], v[196:203], v[42:45], v222, v222 op_sel_hi:[0,0,0]
	v_mfma_scale_f32_16x16x128_f8f6f4 v[26:29], v[240:247], v[204:211], v[26:29], v222, v222 op_sel_hi:[0,0,0]
	v_mfma_scale_f32_16x16x128_f8f6f4 v[18:21], v[240:247], v[212:219], v[18:21], v222, v222 op_sel_hi:[0,0,0]
	s_setprio 0
	s_mov_b32 m0, s46
	v_lshl_add_u64 v[2:3], s[42:43], 0, v[150:151]
	s_barrier
	ds_read_b128 v[188:191], v181 offset:16384
	ds_read_b128 v[192:195], v181 offset:17408
	ds_read_b128 v[196:199], v181 offset:18432
	ds_read_b128 v[200:203], v181 offset:19456
	ds_read_b128 v[204:207], v181 offset:20480
	ds_read_b128 v[208:211], v181 offset:21504
	ds_read_b128 v[212:215], v181 offset:22528
	ds_read_b128 v[216:219], v181 offset:23552
	global_load_lds_dwordx4 v[2:3], off
	v_lshl_add_u64 v[4:5], s[42:43], 0, v[148:149]
	s_mov_b32 m0, s49
	s_nop 0
	global_load_lds_dwordx4 v[4:5], off
	s_barrier
	s_setprio 1
	s_waitcnt lgkmcnt(6)
	v_mfma_scale_f32_16x16x128_f8f6f4 v[142:145], v[10:17], v[188:195], v[142:145], v222, v222 op_sel_hi:[0,0,0]
	v_mfma_scale_f32_16x16x128_f8f6f4 v[138:141], v[156:163], v[188:195], v[138:141], v222, v222 op_sel_hi:[0,0,0]
	s_waitcnt lgkmcnt(4)
	v_mfma_scale_f32_16x16x128_f8f6f4 v[134:137], v[10:17], v[196:203], v[134:137], v222, v222 op_sel_hi:[0,0,0]
	v_mfma_scale_f32_16x16x128_f8f6f4 v[126:129], v[156:163], v[196:203], v[126:129], v222, v222 op_sel_hi:[0,0,0]
	s_waitcnt lgkmcnt(2)
	v_mfma_scale_f32_16x16x128_f8f6f4 v[118:121], v[10:17], v[204:211], v[118:121], v222, v222 op_sel_hi:[0,0,0]
	v_mfma_scale_f32_16x16x128_f8f6f4 v[110:113], v[156:163], v[204:211], v[110:113], v222, v222 op_sel_hi:[0,0,0]
	s_waitcnt lgkmcnt(0)
	v_mfma_scale_f32_16x16x128_f8f6f4 v[102:105], v[10:17], v[212:219], v[102:105], v222, v222 op_sel_hi:[0,0,0]
	v_mfma_scale_f32_16x16x128_f8f6f4 v[94:97], v[156:163], v[212:219], v[94:97], v222, v222 op_sel_hi:[0,0,0]
	s_setprio 0
	s_barrier
	s_add_u32 s74, s34, 0x20000
	s_addc_u32 s75, s35, 0
	s_mov_b32 m0, s50
	v_lshl_add_u64 v[10:11], s[74:75], 0, v[0:1]
	global_load_lds_dwordx4 v[10:11], off
	v_lshl_add_u64 v[10:11], s[74:75], 0, v[146:147]
	s_mov_b32 m0, s51
	s_nop 0
	global_load_lds_dwordx4 v[10:11], off
	s_waitcnt vmcnt(6)
	s_barrier
	s_setprio 1
	v_mfma_scale_f32_16x16x128_f8f6f4 v[78:81], v[232:239], v[188:195], v[78:81], v222, v222 op_sel_hi:[0,0,0]
	v_mfma_scale_f32_16x16x128_f8f6f4 v[74:77], v[240:247], v[188:195], v[74:77], v222, v222 op_sel_hi:[0,0,0]
	v_mfma_scale_f32_16x16x128_f8f6f4 v[70:73], v[232:239], v[196:203], v[70:73], v222, v222 op_sel_hi:[0,0,0]
	v_mfma_scale_f32_16x16x128_f8f6f4 v[66:69], v[240:247], v[196:203], v[66:69], v222, v222 op_sel_hi:[0,0,0]
	v_mfma_scale_f32_16x16x128_f8f6f4 v[54:57], v[232:239], v[204:211], v[54:57], v222, v222 op_sel_hi:[0,0,0]
	v_mfma_scale_f32_16x16x128_f8f6f4 v[50:53], v[240:247], v[204:211], v[50:53], v222, v222 op_sel_hi:[0,0,0]
	v_mfma_scale_f32_16x16x128_f8f6f4 v[38:41], v[232:239], v[212:219], v[38:41], v222, v222 op_sel_hi:[0,0,0]
	v_mfma_scale_f32_16x16x128_f8f6f4 v[34:37], v[240:247], v[212:219], v[34:37], v222, v222 op_sel_hi:[0,0,0]
	s_setprio 0
	s_barrier
	ds_read_b128 v[10:13], v173
	ds_read_b128 v[14:17], v174
	ds_read_b128 v[156:159], v175
	ds_read_b128 v[160:163], v176
	s_add_u32 s42, s42, 0x20000
	s_addc_u32 s43, s43, 0
	s_mov_b32 m0, s52
	v_lshl_add_u64 v[182:183], s[42:43], 0, v[150:151]
	ds_read_b128 v[188:191], v181 offset:32768
	ds_read_b128 v[192:195], v181 offset:33792
	ds_read_b128 v[196:199], v181 offset:34816
	ds_read_b128 v[200:203], v181 offset:35840
	ds_read_b128 v[204:207], v181 offset:36864
	ds_read_b128 v[208:211], v181 offset:37888
	ds_read_b128 v[212:215], v181 offset:38912
	ds_read_b128 v[216:219], v181 offset:39936
	global_load_lds_dwordx4 v[182:183], off
	v_lshl_add_u64 v[182:183], s[42:43], 0, v[148:149]
	s_mov_b32 m0, s53
	s_nop 0
	global_load_lds_dwordx4 v[182:183], off
	s_waitcnt lgkmcnt(8)
	s_barrier
	s_setprio 1
	s_waitcnt lgkmcnt(6)
	v_mfma_scale_f32_16x16x128_f8f6f4 v[130:133], v[10:17], v[188:195], v[130:133], v222, v222 op_sel_hi:[0,0,0]
	v_mfma_scale_f32_16x16x128_f8f6f4 v[122:125], v[156:163], v[188:195], v[122:125], v222, v222 op_sel_hi:[0,0,0]
	s_waitcnt lgkmcnt(4)
	v_mfma_scale_f32_16x16x128_f8f6f4 v[114:117], v[10:17], v[196:203], v[114:117], v222, v222 op_sel_hi:[0,0,0]
	v_mfma_scale_f32_16x16x128_f8f6f4 v[106:109], v[156:163], v[196:203], v[106:109], v222, v222 op_sel_hi:[0,0,0]
	s_waitcnt lgkmcnt(2)
	v_mfma_scale_f32_16x16x128_f8f6f4 v[98:101], v[10:17], v[204:211], v[98:101], v222, v222 op_sel_hi:[0,0,0]
	v_mfma_scale_f32_16x16x128_f8f6f4 v[90:93], v[156:163], v[204:211], v[90:93], v222, v222 op_sel_hi:[0,0,0]
	s_waitcnt lgkmcnt(0)
	v_mfma_scale_f32_16x16x128_f8f6f4 v[86:89], v[10:17], v[212:219], v[86:89], v222, v222 op_sel_hi:[0,0,0]
	v_mfma_scale_f32_16x16x128_f8f6f4 v[82:85], v[156:163], v[212:219], v[82:85], v222, v222 op_sel_hi:[0,0,0]
	s_setprio 0
	s_barrier
	s_mov_b32 m0, s55
	v_lshl_add_u64 v[6:7], v[6:7], 0, s[24:25]
	ds_read_b128 v[232:235], v177
	ds_read_b128 v[236:239], v178
	ds_read_b128 v[240:243], v179
	ds_read_b128 v[244:247], v180
	global_load_lds_dwordx4 v[6:7], off
	v_lshl_add_u64 v[6:7], v[8:9], 0, s[24:25]
	s_mov_b32 m0, s56
	s_nop 0
	global_load_lds_dwordx4 v[6:7], off
	s_barrier
	s_setprio 1
	s_waitcnt lgkmcnt(2)
	v_mfma_scale_f32_16x16x128_f8f6f4 v[62:65], v[232:239], v[188:195], v[62:65], v222, v222 op_sel_hi:[0,0,0]
	v_mfma_scale_f32_16x16x128_f8f6f4 v[46:49], v[232:239], v[196:203], v[46:49], v222, v222 op_sel_hi:[0,0,0]
	v_mfma_scale_f32_16x16x128_f8f6f4 v[30:33], v[232:239], v[204:211], v[30:33], v222, v222 op_sel_hi:[0,0,0]
	v_mfma_scale_f32_16x16x128_f8f6f4 v[22:25], v[232:239], v[212:219], v[22:25], v222, v222 op_sel_hi:[0,0,0]
	s_waitcnt lgkmcnt(0)
	v_mfma_scale_f32_16x16x128_f8f6f4 v[58:61], v[240:247], v[188:195], v[58:61], v222, v222 op_sel_hi:[0,0,0]
	v_mfma_scale_f32_16x16x128_f8f6f4 v[42:45], v[240:247], v[196:203], v[42:45], v222, v222 op_sel_hi:[0,0,0]
	v_mfma_scale_f32_16x16x128_f8f6f4 v[26:29], v[240:247], v[204:211], v[26:29], v222, v222 op_sel_hi:[0,0,0]
	v_mfma_scale_f32_16x16x128_f8f6f4 v[18:21], v[240:247], v[212:219], v[18:21], v222, v222 op_sel_hi:[0,0,0]
	s_setprio 0
	s_mov_b32 m0, s57
	v_lshl_add_u64 v[2:3], v[2:3], 0, s[24:25]
	s_barrier
	ds_read_b128 v[188:191], v181 offset:49152
	ds_read_b128 v[192:195], v181 offset:50176
	ds_read_b128 v[196:199], v181 offset:51200
	ds_read_b128 v[200:203], v181 offset:52224
	ds_read_b128 v[204:207], v181 offset:53248
	ds_read_b128 v[208:211], v181 offset:54272
	ds_read_b128 v[212:215], v181 offset:55296
	ds_read_b128 v[216:219], v181 offset:56320
	global_load_lds_dwordx4 v[2:3], off
	v_lshl_add_u64 v[2:3], v[4:5], 0, s[24:25]
	s_mov_b32 m0, s58
	s_nop 0
	global_load_lds_dwordx4 v[2:3], off
	s_barrier
	s_setprio 1
	s_waitcnt lgkmcnt(6)
	v_mfma_scale_f32_16x16x128_f8f6f4 v[142:145], v[10:17], v[188:195], v[142:145], v222, v222 op_sel_hi:[0,0,0]
	v_mfma_scale_f32_16x16x128_f8f6f4 v[138:141], v[156:163], v[188:195], v[138:141], v222, v222 op_sel_hi:[0,0,0]
	s_waitcnt lgkmcnt(4)
	v_mfma_scale_f32_16x16x128_f8f6f4 v[134:137], v[10:17], v[196:203], v[134:137], v222, v222 op_sel_hi:[0,0,0]
	v_mfma_scale_f32_16x16x128_f8f6f4 v[126:129], v[156:163], v[196:203], v[126:129], v222, v222 op_sel_hi:[0,0,0]
	s_waitcnt lgkmcnt(2)
	v_mfma_scale_f32_16x16x128_f8f6f4 v[118:121], v[10:17], v[204:211], v[118:121], v222, v222 op_sel_hi:[0,0,0]
	v_mfma_scale_f32_16x16x128_f8f6f4 v[110:113], v[156:163], v[204:211], v[110:113], v222, v222 op_sel_hi:[0,0,0]
	s_waitcnt lgkmcnt(0)
	v_mfma_scale_f32_16x16x128_f8f6f4 v[102:105], v[10:17], v[212:219], v[102:105], v222, v222 op_sel_hi:[0,0,0]
	v_mfma_scale_f32_16x16x128_f8f6f4 v[94:97], v[156:163], v[212:219], v[94:97], v222, v222 op_sel_hi:[0,0,0]
	s_setprio 0
	s_barrier
	s_add_u32 s34, s34, 0x20080
	s_addc_u32 s35, s35, 0
	s_mov_b32 m0, s59
	v_lshl_add_u64 v[2:3], s[34:35], 0, v[0:1]
	global_load_lds_dwordx4 v[2:3], off
	v_lshl_add_u64 v[2:3], s[34:35], 0, v[146:147]
	s_mov_b32 m0, s61
	s_nop 0
	global_load_lds_dwordx4 v[2:3], off
	s_waitcnt vmcnt(6)
	s_barrier
	s_setprio 1
	v_mfma_scale_f32_16x16x128_f8f6f4 v[78:81], v[232:239], v[188:195], v[78:81], v222, v222 op_sel_hi:[0,0,0]
	v_mfma_scale_f32_16x16x128_f8f6f4 v[74:77], v[240:247], v[188:195], v[74:77], v222, v222 op_sel_hi:[0,0,0]
	v_mfma_scale_f32_16x16x128_f8f6f4 v[70:73], v[232:239], v[196:203], v[70:73], v222, v222 op_sel_hi:[0,0,0]
	v_mfma_scale_f32_16x16x128_f8f6f4 v[66:69], v[240:247], v[196:203], v[66:69], v222, v222 op_sel_hi:[0,0,0]
	v_mfma_scale_f32_16x16x128_f8f6f4 v[54:57], v[232:239], v[204:211], v[54:57], v222, v222 op_sel_hi:[0,0,0]
	v_mfma_scale_f32_16x16x128_f8f6f4 v[50:53], v[240:247], v[204:211], v[50:53], v222, v222 op_sel_hi:[0,0,0]
	v_mfma_scale_f32_16x16x128_f8f6f4 v[38:41], v[232:239], v[212:219], v[38:41], v222, v222 op_sel_hi:[0,0,0]
	v_mfma_scale_f32_16x16x128_f8f6f4 v[34:37], v[240:247], v[212:219], v[34:37], v222, v222 op_sel_hi:[0,0,0]
	s_setprio 0
	s_add_i32 s73, s73, 2
	s_add_u32 s20, s20, 0x100
	s_addc_u32 s21, s21, 0
	s_add_u32 s71, s71, 0x100
	s_addc_u32 s72, s72, 0
	s_cmp_gt_u32 s73, 5
	s_barrier
	s_cbranch_scc0 .LBB0_526
	s_ashr_i32 s21, s66, 1
	s_ashr_i32 s20, s65, 1
	s_and_b32 s21, s21, -4
	s_add_i32 s20, s21, s20
	s_ashr_i32 s21, s20, 31
	s_lshl_b64 s[20:21], s[20:21], 22
	s_add_u32 s20, s62, s20
	s_addc_u32 s21, s63, s21
	s_lshl_b32 s34, s66, 19
	s_and_b32 s34, s34, 0x380000
	s_nop 15
	s_nop 15
	v_mbcnt_lo_u32_b32 v2, -1, 0
	v_mbcnt_hi_u32_b32 v2, -1, v2
	s_add_u32 s20, s20, s34
	v_and_b32_e32 v3, 15, v2
	s_addc_u32 s21, s21, 0
	s_lshl_b32 s34, s65, 18
	v_lshrrev_b32_e32 v2, 1, v2
	v_readlane_b32 s7, v252, 51
	v_readlane_b32 s9, v252, 52
	s_and_b32 s34, s34, 0x40000
	v_and_b32_e32 v2, 24, v2
	s_add_u32 s20, s20, s34
	v_lshl_or_b32 v6, s9, 5, v2
	v_lshl_or_b32 v8, s7, 6, v3
	s_addc_u32 s21, s21, 0
	v_ashrrev_i32_e32 v7, 31, v6
	v_pk_mul_f32 v[4:5], v[132:133], s[22:23] op_sel_hi:[1,0]
	v_pk_mul_f32 v[2:3], v[130:131], s[22:23] op_sel_hi:[1,0]
	v_pk_mul_f32 v[12:13], v[124:125], s[22:23] op_sel_hi:[1,0]
	v_ashrrev_i32_e32 v9, 31, v8
	v_lshl_add_u64 v[10:11], v[6:7], 1, s[20:21]
	v_pk_mul_f32 v[14:15], v[122:123], s[22:23] op_sel_hi:[1,0]
	v_cvt_pk_bf16_f32 v2, v2, v3
	v_cvt_pk_bf16_f32 v3, v4, v5
	v_cvt_pk_bf16_f32 v5, v12, v13
	v_lshlrev_b64 v[12:13], 10, v[8:9]
	v_cvt_pk_bf16_f32 v4, v14, v15
	v_lshl_add_u64 v[14:15], v[10:11], 0, v[12:13]
	global_store_dwordx4 v[14:15], v[2:5], off
	v_pk_mul_f32 v[14:15], v[108:109], s[22:23] op_sel_hi:[1,0]
	v_pk_mul_f32 v[16:17], v[106:107], s[22:23] op_sel_hi:[1,0]
	v_pk_mul_f32 v[4:5], v[116:117], s[22:23] op_sel_hi:[1,0]
	v_pk_mul_f32 v[2:3], v[114:115], s[22:23] op_sel_hi:[1,0]
	v_pk_mul_f32 v[90:91], v[90:91], s[22:23] op_sel_hi:[1,0]
	v_cvt_pk_bf16_f32 v2, v2, v3
	v_cvt_pk_bf16_f32 v3, v4, v5
	v_cvt_pk_bf16_f32 v5, v14, v15
	v_or_b32_e32 v14, 16, v8
	v_ashrrev_i32_e32 v15, 31, v14
	v_lshlrev_b64 v[14:15], 10, v[14:15]
	v_cvt_pk_bf16_f32 v4, v16, v17
	v_lshl_add_u64 v[16:17], v[10:11], 0, v[14:15]
	global_store_dwordx4 v[16:17], v[2:5], off
	v_pk_mul_f32 v[16:17], v[92:93], s[22:23] op_sel_hi:[1,0]
	v_pk_mul_f32 v[82:83], v[82:83], s[22:23] op_sel_hi:[1,0]
	v_pk_mul_f32 v[4:5], v[100:101], s[22:23] op_sel_hi:[1,0]
	v_pk_mul_f32 v[2:3], v[98:99], s[22:23] op_sel_hi:[1,0]
	v_pk_mul_f32 v[84:85], v[84:85], s[22:23] op_sel_hi:[1,0]
	v_cvt_pk_bf16_f32 v2, v2, v3
	v_cvt_pk_bf16_f32 v3, v4, v5
	v_cvt_pk_bf16_f32 v5, v16, v17
	v_or_b32_e32 v16, 32, v8
	v_ashrrev_i32_e32 v17, 31, v16
	v_lshlrev_b64 v[16:17], 10, v[16:17]
	v_cvt_pk_bf16_f32 v4, v90, v91
	v_lshl_add_u64 v[90:91], v[10:11], 0, v[16:17]
	global_store_dwordx4 v[90:91], v[2:5], off
	v_pk_mul_f32 v[90:91], v[110:111], s[22:23] op_sel_hi:[1,0]
	v_pk_mul_f32 v[92:93], v[94:95], s[22:23] op_sel_hi:[1,0]
	v_pk_mul_f32 v[4:5], v[88:89], s[22:23] op_sel_hi:[1,0]
	v_pk_mul_f32 v[2:3], v[86:87], s[22:23] op_sel_hi:[1,0]
	v_pk_mul_f32 v[86:87], v[140:141], s[22:23] op_sel_hi:[1,0]
	v_cvt_pk_bf16_f32 v2, v2, v3
	v_cvt_pk_bf16_f32 v3, v4, v5
	v_cvt_pk_bf16_f32 v4, v82, v83
	v_or_b32_e32 v82, 48, v8
	v_ashrrev_i32_e32 v83, 31, v82
	v_lshlrev_b64 v[82:83], 10, v[82:83]
	v_cvt_pk_bf16_f32 v5, v84, v85
	v_lshl_add_u64 v[84:85], v[10:11], 0, v[82:83]
	global_store_dwordx4 v[84:85], v[2:5], off
	v_add_u32_e32 v84, 0x80, v8
	v_ashrrev_i32_e32 v85, 31, v84
	v_pk_mul_f32 v[4:5], v[144:145], s[22:23] op_sel_hi:[1,0]
	v_pk_mul_f32 v[2:3], v[142:143], s[22:23] op_sel_hi:[1,0]
	v_pk_mul_f32 v[88:89], v[138:139], s[22:23] op_sel_hi:[1,0]
	v_lshlrev_b64 v[84:85], 10, v[84:85]
	v_cvt_pk_bf16_f32 v2, v2, v3
	v_cvt_pk_bf16_f32 v3, v4, v5
	v_cvt_pk_bf16_f32 v4, v88, v89
	v_cvt_pk_bf16_f32 v5, v86, v87
	v_lshl_add_u64 v[86:87], v[10:11], 0, v[84:85]
	global_store_dwordx4 v[86:87], v[2:5], off
	v_pk_mul_f32 v[86:87], v[128:129], s[22:23] op_sel_hi:[1,0]
	v_pk_mul_f32 v[88:89], v[126:127], s[22:23] op_sel_hi:[1,0]
	v_pk_mul_f32 v[4:5], v[136:137], s[22:23] op_sel_hi:[1,0]
	v_pk_mul_f32 v[2:3], v[134:135], s[22:23] op_sel_hi:[1,0]
	v_pk_mul_f32 v[58:59], v[58:59], s[22:23] op_sel_hi:[1,0]
	v_cvt_pk_bf16_f32 v2, v2, v3
	v_cvt_pk_bf16_f32 v3, v4, v5
	v_cvt_pk_bf16_f32 v5, v86, v87
	v_add_u32_e32 v86, 0x90, v8
	v_ashrrev_i32_e32 v87, 31, v86
	v_lshlrev_b64 v[86:87], 10, v[86:87]
	v_cvt_pk_bf16_f32 v4, v88, v89
	v_lshl_add_u64 v[88:89], v[10:11], 0, v[86:87]
	global_store_dwordx4 v[88:89], v[2:5], off
	v_pk_mul_f32 v[88:89], v[112:113], s[22:23] op_sel_hi:[1,0]
	s_and_b64 vcc, exec, s[4:5]
	v_pk_mul_f32 v[4:5], v[120:121], s[22:23] op_sel_hi:[1,0]
	v_pk_mul_f32 v[2:3], v[118:119], s[22:23] op_sel_hi:[1,0]
	s_mov_b32 s66, s6
	v_cvt_pk_bf16_f32 v2, v2, v3
	v_cvt_pk_bf16_f32 v3, v4, v5
	v_cvt_pk_bf16_f32 v5, v88, v89
	v_add_u32_e32 v88, 0xa0, v8
	v_ashrrev_i32_e32 v89, 31, v88
	v_lshlrev_b64 v[88:89], 10, v[88:89]
	v_add_u32_e32 v8, 0xb0, v8
	v_cvt_pk_bf16_f32 v4, v90, v91
	v_lshl_add_u64 v[90:91], v[10:11], 0, v[88:89]
	v_ashrrev_i32_e32 v9, 31, v8
	global_store_dwordx4 v[90:91], v[2:5], off
	v_pk_mul_f32 v[90:91], v[96:97], s[22:23] op_sel_hi:[1,0]
	v_lshlrev_b64 v[8:9], 10, v[8:9]
	v_pk_mul_f32 v[4:5], v[104:105], s[22:23] op_sel_hi:[1,0]
	v_pk_mul_f32 v[2:3], v[102:103], s[22:23] op_sel_hi:[1,0]
	v_lshl_add_u64 v[10:11], v[10:11], 0, v[8:9]
	v_cvt_pk_bf16_f32 v2, v2, v3
	v_cvt_pk_bf16_f32 v3, v4, v5
	v_cvt_pk_bf16_f32 v4, v92, v93
	v_cvt_pk_bf16_f32 v5, v90, v91
	global_store_dwordx4 v[10:11], v[2:5], off
	v_pk_mul_f32 v[10:11], v[60:61], s[22:23] op_sel_hi:[1,0]
	s_mov_b32 s65, s8
	v_add_u32_e32 v2, 0x80, v6
	v_ashrrev_i32_e32 v3, 31, v2
	v_lshl_add_u64 v[6:7], v[2:3], 1, s[20:21]
	v_pk_mul_f32 v[4:5], v[64:65], s[22:23] op_sel_hi:[1,0]
	v_pk_mul_f32 v[2:3], v[62:63], s[22:23] op_sel_hi:[1,0]
	s_mov_b64 s[34:35], s[12:13]
	v_cvt_pk_bf16_f32 v2, v2, v3
	v_cvt_pk_bf16_f32 v3, v4, v5
	v_cvt_pk_bf16_f32 v4, v58, v59
	v_cvt_pk_bf16_f32 v5, v10, v11
	v_lshl_add_u64 v[10:11], v[6:7], 0, v[12:13]
	global_store_dwordx4 v[10:11], v[2:5], off
	v_pk_mul_f32 v[10:11], v[44:45], s[22:23] op_sel_hi:[1,0]
	v_pk_mul_f32 v[12:13], v[42:43], s[22:23] op_sel_hi:[1,0]
	v_pk_mul_f32 v[4:5], v[48:49], s[22:23] op_sel_hi:[1,0]
	v_pk_mul_f32 v[2:3], v[46:47], s[22:23] op_sel_hi:[1,0]
	s_mov_b64 s[42:43], s[10:11]
	v_cvt_pk_bf16_f32 v2, v2, v3
	v_cvt_pk_bf16_f32 v3, v4, v5
	v_cvt_pk_bf16_f32 v4, v12, v13
	v_cvt_pk_bf16_f32 v5, v10, v11
	v_lshl_add_u64 v[10:11], v[6:7], 0, v[14:15]
	global_store_dwordx4 v[10:11], v[2:5], off
	v_pk_mul_f32 v[10:11], v[28:29], s[22:23] op_sel_hi:[1,0]
	v_pk_mul_f32 v[12:13], v[26:27], s[22:23] op_sel_hi:[1,0]
	v_pk_mul_f32 v[4:5], v[32:33], s[22:23] op_sel_hi:[1,0]
	v_pk_mul_f32 v[2:3], v[30:31], s[22:23] op_sel_hi:[1,0]
	s_nop 0
	v_cvt_pk_bf16_f32 v2, v2, v3
	v_cvt_pk_bf16_f32 v3, v4, v5
	v_cvt_pk_bf16_f32 v4, v12, v13
	v_cvt_pk_bf16_f32 v5, v10, v11
	v_lshl_add_u64 v[10:11], v[6:7], 0, v[16:17]
	global_store_dwordx4 v[10:11], v[2:5], off
	v_pk_mul_f32 v[10:11], v[20:21], s[22:23] op_sel_hi:[1,0]
	v_pk_mul_f32 v[12:13], v[18:19], s[22:23] op_sel_hi:[1,0]
	v_pk_mul_f32 v[4:5], v[24:25], s[22:23] op_sel_hi:[1,0]
	v_pk_mul_f32 v[2:3], v[22:23], s[22:23] op_sel_hi:[1,0]
	s_nop 0
	v_cvt_pk_bf16_f32 v2, v2, v3
	v_cvt_pk_bf16_f32 v3, v4, v5
	v_cvt_pk_bf16_f32 v4, v12, v13
	v_cvt_pk_bf16_f32 v5, v10, v11
	v_lshl_add_u64 v[10:11], v[6:7], 0, v[82:83]
	global_store_dwordx4 v[10:11], v[2:5], off
	v_pk_mul_f32 v[10:11], v[76:77], s[22:23] op_sel_hi:[1,0]
	v_pk_mul_f32 v[12:13], v[74:75], s[22:23] op_sel_hi:[1,0]
	v_pk_mul_f32 v[4:5], v[80:81], s[22:23] op_sel_hi:[1,0]
	v_pk_mul_f32 v[2:3], v[78:79], s[22:23] op_sel_hi:[1,0]
	s_nop 0
	v_cvt_pk_bf16_f32 v2, v2, v3
	v_cvt_pk_bf16_f32 v3, v4, v5
	v_cvt_pk_bf16_f32 v4, v12, v13
	v_cvt_pk_bf16_f32 v5, v10, v11
	v_lshl_add_u64 v[10:11], v[6:7], 0, v[84:85]
	global_store_dwordx4 v[10:11], v[2:5], off
	v_pk_mul_f32 v[10:11], v[68:69], s[22:23] op_sel_hi:[1,0]
	v_pk_mul_f32 v[12:13], v[66:67], s[22:23] op_sel_hi:[1,0]
	v_pk_mul_f32 v[4:5], v[72:73], s[22:23] op_sel_hi:[1,0]
	v_pk_mul_f32 v[2:3], v[70:71], s[22:23] op_sel_hi:[1,0]
	s_nop 0
	v_cvt_pk_bf16_f32 v2, v2, v3
	v_cvt_pk_bf16_f32 v3, v4, v5
	v_cvt_pk_bf16_f32 v4, v12, v13
	v_cvt_pk_bf16_f32 v5, v10, v11
	v_lshl_add_u64 v[10:11], v[6:7], 0, v[86:87]
	global_store_dwordx4 v[10:11], v[2:5], off
	v_pk_mul_f32 v[10:11], v[52:53], s[22:23] op_sel_hi:[1,0]
	v_pk_mul_f32 v[12:13], v[50:51], s[22:23] op_sel_hi:[1,0]
	v_pk_mul_f32 v[4:5], v[56:57], s[22:23] op_sel_hi:[1,0]
	v_pk_mul_f32 v[2:3], v[54:55], s[22:23] op_sel_hi:[1,0]
	s_nop 0
	v_cvt_pk_bf16_f32 v2, v2, v3
	v_cvt_pk_bf16_f32 v3, v4, v5
	v_cvt_pk_bf16_f32 v4, v12, v13
	v_cvt_pk_bf16_f32 v5, v10, v11
	v_lshl_add_u64 v[10:11], v[6:7], 0, v[88:89]
	global_store_dwordx4 v[10:11], v[2:5], off
	v_pk_mul_f32 v[10:11], v[36:37], s[22:23] op_sel_hi:[1,0]
	v_pk_mul_f32 v[12:13], v[34:35], s[22:23] op_sel_hi:[1,0]
	v_pk_mul_f32 v[4:5], v[40:41], s[22:23] op_sel_hi:[1,0]
	v_pk_mul_f32 v[2:3], v[38:39], s[22:23] op_sel_hi:[1,0]
	v_lshl_add_u64 v[6:7], v[6:7], 0, v[8:9]
	v_cvt_pk_bf16_f32 v2, v2, v3
	v_cvt_pk_bf16_f32 v3, v4, v5
	v_cvt_pk_bf16_f32 v4, v12, v13
	v_cvt_pk_bf16_f32 v5, v10, v11
	global_store_dwordx4 v[6:7], v[2:5], off
	s_cbranch_vccz .LBB0_519
	s_waitcnt vmcnt(0)
	s_cmpk_gt_u32 s28, 0xff
	s_cbranch_scc1 .LBB0_530
	s_barrier

.LBB0_585:
	s_add_u32 s47, s20, s46
	s_addc_u32 s77, s21, 0
	s_add_u32 s50, s47, 0x100
	s_addc_u32 s51, s77, 0
	s_and_b64 s[48:49], s[44:45], exec
	s_cselect_b32 s51, s73, s51
	s_cselect_b32 s50, s74, s50
	s_add_u32 s46, s34, s46
	s_addc_u32 s48, s35, 0
	s_add_u32 s46, s46, 0x100
	s_addc_u32 s48, s48, 0
	s_and_b64 s[44:45], s[44:45], exec
	s_cselect_b32 s53, s75, s48
	s_cselect_b32 s52, s76, s46
	s_add_u32 s78, s47, 0x20080
	s_addc_u32 s79, s77, 0
	s_add_i32 m0, s55, 0xc000
	s_add_i32 s77, s55, 0xe000
	ds_read_b128 v[140:143], v149
	ds_read_b128 v[144:147], v150
	ds_read_b128 v[166:169], v151
	ds_read_b128 v[170:173], v152
	s_add_u32 s48, s52, 0x10000
	s_addc_u32 s49, s53, 0
	s_add_u32 s46, s50, 0x20000
	s_addc_u32 s47, s51, 0
	s_add_u32 s44, s52, 0x10080
	s_addc_u32 s45, s53, 0
	v_add_u32_e32 v0, s63, v148
	v_lshl_add_u64 v[2:3], s[78:79], 0, v[138:139]
	ds_read_b128 v[174:177], v0
	ds_read_b128 v[178:181], v0 offset:1024
	ds_read_b128 v[182:185], v0 offset:2048
	ds_read_b128 v[188:191], v0 offset:3072
	ds_read_b128 v[192:195], v0 offset:4096
	ds_read_b128 v[196:199], v0 offset:5120
	ds_read_b128 v[200:203], v0 offset:6144
	ds_read_b128 v[204:207], v0 offset:7168
	global_load_lds_dwordx4 v[2:3], off
	v_lshl_add_u64 v[2:3], s[78:79], 0, v[134:135]
	s_mov_b32 m0, s77
	s_nop 0
	global_load_lds_dwordx4 v[2:3], off
	s_waitcnt lgkmcnt(8)
	s_barrier
	s_setprio 1
	s_waitcnt lgkmcnt(7)
	v_mfma_f32_16x16x32_bf16 v[128:131], v[140:143], v[174:177], v[128:131]
	v_mfma_f32_16x16x32_bf16 v[124:127], v[166:169], v[174:177], v[124:127]
	s_waitcnt lgkmcnt(6)
	v_mfma_f32_16x16x32_bf16 v[128:131], v[144:147], v[178:181], v[128:131]
	v_mfma_f32_16x16x32_bf16 v[124:127], v[170:173], v[178:181], v[124:127]
	s_waitcnt lgkmcnt(5)
	v_mfma_f32_16x16x32_bf16 v[120:123], v[140:143], v[182:185], v[120:123]
	v_mfma_f32_16x16x32_bf16 v[116:119], v[166:169], v[182:185], v[116:119]
	s_waitcnt lgkmcnt(4)
	v_mfma_f32_16x16x32_bf16 v[120:123], v[144:147], v[188:191], v[120:123]
	v_mfma_f32_16x16x32_bf16 v[116:119], v[170:173], v[188:191], v[116:119]
	s_waitcnt lgkmcnt(3)
	v_mfma_f32_16x16x32_bf16 v[112:115], v[140:143], v[192:195], v[112:115]
	v_mfma_f32_16x16x32_bf16 v[108:111], v[166:169], v[192:195], v[108:111]
	s_waitcnt lgkmcnt(2)
	v_mfma_f32_16x16x32_bf16 v[112:115], v[144:147], v[196:199], v[112:115]
	v_mfma_f32_16x16x32_bf16 v[108:111], v[170:173], v[196:199], v[108:111]
	s_waitcnt lgkmcnt(1)
	v_mfma_f32_16x16x32_bf16 v[104:107], v[140:143], v[200:203], v[104:107]
	v_mfma_f32_16x16x32_bf16 v[100:103], v[166:169], v[200:203], v[100:103]
	s_waitcnt lgkmcnt(0)
	v_mfma_f32_16x16x32_bf16 v[104:107], v[144:147], v[204:207], v[104:107]
	v_mfma_f32_16x16x32_bf16 v[100:103], v[170:173], v[204:207], v[100:103]
	s_setprio 0
	s_barrier
	s_mov_b32 m0, s56
	v_lshl_add_u64 v[220:221], s[52:53], 0, v[136:137]
	ds_read_b128 v[208:211], v153
	ds_read_b128 v[212:215], v154
	ds_read_b128 v[216:219], v155
	ds_read_b128 v[232:235], v156
	global_load_lds_dwordx4 v[220:221], off
	v_lshl_add_u64 v[226:227], s[52:53], 0, v[132:133]
	s_mov_b32 m0, s57
	s_nop 0
	global_load_lds_dwordx4 v[226:227], off
	s_barrier
	s_setprio 1
	s_waitcnt lgkmcnt(3)
	v_mfma_f32_16x16x32_bf16 v[96:99], v[208:211], v[174:177], v[96:99]
	v_mfma_f32_16x16x32_bf16 v[88:91], v[208:211], v[182:185], v[88:91]
	v_mfma_f32_16x16x32_bf16 v[80:83], v[208:211], v[192:195], v[80:83]
	v_mfma_f32_16x16x32_bf16 v[72:75], v[208:211], v[200:203], v[72:75]
	s_waitcnt lgkmcnt(2)
	v_mfma_f32_16x16x32_bf16 v[96:99], v[212:215], v[178:181], v[96:99]
	v_mfma_f32_16x16x32_bf16 v[88:91], v[212:215], v[188:191], v[88:91]
	v_mfma_f32_16x16x32_bf16 v[80:83], v[212:215], v[196:199], v[80:83]
	v_mfma_f32_16x16x32_bf16 v[72:75], v[212:215], v[204:207], v[72:75]
	s_waitcnt lgkmcnt(1)
	v_mfma_f32_16x16x32_bf16 v[92:95], v[216:219], v[174:177], v[92:95]
	v_mfma_f32_16x16x32_bf16 v[84:87], v[216:219], v[182:185], v[84:87]
	v_mfma_f32_16x16x32_bf16 v[76:79], v[216:219], v[192:195], v[76:79]
	v_mfma_f32_16x16x32_bf16 v[68:71], v[216:219], v[200:203], v[68:71]
	s_waitcnt lgkmcnt(0)
	v_mfma_f32_16x16x32_bf16 v[92:95], v[232:235], v[178:181], v[92:95]
	v_mfma_f32_16x16x32_bf16 v[84:87], v[232:235], v[188:191], v[84:87]
	v_mfma_f32_16x16x32_bf16 v[76:79], v[232:235], v[196:199], v[76:79]
	v_mfma_f32_16x16x32_bf16 v[68:71], v[232:235], v[204:207], v[68:71]
	s_setprio 0
	s_mov_b32 m0, s55
	v_lshl_add_u64 v[236:237], s[50:51], 0, v[138:139]
	s_barrier
	ds_read_b128 v[174:177], v0 offset:16384
	ds_read_b128 v[178:181], v0 offset:17408
	ds_read_b128 v[182:185], v0 offset:18432
	ds_read_b128 v[188:191], v0 offset:19456
	ds_read_b128 v[192:195], v0 offset:20480
	ds_read_b128 v[196:199], v0 offset:21504
	ds_read_b128 v[200:203], v0 offset:22528
	ds_read_b128 v[204:207], v0 offset:23552
	global_load_lds_dwordx4 v[236:237], off
	v_lshl_add_u64 v[238:239], s[50:51], 0, v[134:135]
	s_mov_b32 m0, s58
	s_nop 0
	global_load_lds_dwordx4 v[238:239], off
	s_barrier
	s_setprio 1
	s_waitcnt lgkmcnt(7)
	v_mfma_f32_16x16x32_bf16 v[64:67], v[140:143], v[174:177], v[64:67]
	v_mfma_f32_16x16x32_bf16 v[60:63], v[166:169], v[174:177], v[60:63]
	s_waitcnt lgkmcnt(6)
	v_mfma_f32_16x16x32_bf16 v[64:67], v[144:147], v[178:181], v[64:67]
	v_mfma_f32_16x16x32_bf16 v[60:63], v[170:173], v[178:181], v[60:63]
	s_waitcnt lgkmcnt(5)
	v_mfma_f32_16x16x32_bf16 v[56:59], v[140:143], v[182:185], v[56:59]
	v_mfma_f32_16x16x32_bf16 v[52:55], v[166:169], v[182:185], v[52:55]
	s_waitcnt lgkmcnt(4)
	v_mfma_f32_16x16x32_bf16 v[56:59], v[144:147], v[188:191], v[56:59]
	v_mfma_f32_16x16x32_bf16 v[52:55], v[170:173], v[188:191], v[52:55]
	s_waitcnt lgkmcnt(3)
	v_mfma_f32_16x16x32_bf16 v[48:51], v[140:143], v[192:195], v[48:51]
	v_mfma_f32_16x16x32_bf16 v[44:47], v[166:169], v[192:195], v[44:47]
	s_waitcnt lgkmcnt(2)
	v_mfma_f32_16x16x32_bf16 v[48:51], v[144:147], v[196:199], v[48:51]
	v_mfma_f32_16x16x32_bf16 v[44:47], v[170:173], v[196:199], v[44:47]
	s_waitcnt lgkmcnt(1)
	v_mfma_f32_16x16x32_bf16 v[40:43], v[140:143], v[200:203], v[40:43]
	v_mfma_f32_16x16x32_bf16 v[36:39], v[166:169], v[200:203], v[36:39]
	s_waitcnt lgkmcnt(0)
	v_mfma_f32_16x16x32_bf16 v[40:43], v[144:147], v[204:207], v[40:43]
	v_mfma_f32_16x16x32_bf16 v[36:39], v[170:173], v[204:207], v[36:39]
	s_setprio 0
	s_barrier
	s_mov_b32 m0, s59
	v_lshl_add_u64 v[2:3], s[48:49], 0, v[136:137]
	global_load_lds_dwordx4 v[2:3], off
	v_lshl_add_u64 v[2:3], s[48:49], 0, v[132:133]
	s_mov_b32 m0, s60
	s_nop 0
	global_load_lds_dwordx4 v[2:3], off
	s_waitcnt vmcnt(6)
	s_barrier
	s_setprio 1
	v_mfma_f32_16x16x32_bf16 v[32:35], v[208:211], v[174:177], v[32:35]
	v_mfma_f32_16x16x32_bf16 v[28:31], v[216:219], v[174:177], v[28:31]
	v_mfma_f32_16x16x32_bf16 v[24:27], v[208:211], v[182:185], v[24:27]
	v_mfma_f32_16x16x32_bf16 v[20:23], v[216:219], v[182:185], v[20:23]
	v_mfma_f32_16x16x32_bf16 v[16:19], v[208:211], v[192:195], v[16:19]
	v_mfma_f32_16x16x32_bf16 v[12:15], v[216:219], v[192:195], v[12:15]
	v_mfma_f32_16x16x32_bf16 v[8:11], v[208:211], v[200:203], v[8:11]
	v_mfma_f32_16x16x32_bf16 v[2:5], v[216:219], v[200:203], v[4:7]
	v_mfma_f32_16x16x32_bf16 v[32:35], v[212:215], v[178:181], v[32:35]
	v_mfma_f32_16x16x32_bf16 v[28:31], v[232:235], v[178:181], v[28:31]
	v_mfma_f32_16x16x32_bf16 v[24:27], v[212:215], v[188:191], v[24:27]
	v_mfma_f32_16x16x32_bf16 v[20:23], v[232:235], v[188:191], v[20:23]
	v_mfma_f32_16x16x32_bf16 v[16:19], v[212:215], v[196:199], v[16:19]
	v_mfma_f32_16x16x32_bf16 v[12:15], v[232:235], v[196:199], v[12:15]
	v_mfma_f32_16x16x32_bf16 v[8:11], v[212:215], v[204:207], v[8:11]
	v_mfma_f32_16x16x32_bf16 v[2:5], v[232:235], v[204:207], v[2:5]
	s_setprio 0
	s_barrier
	ds_read_b128 v[140:143], v157
	ds_read_b128 v[144:147], v158
	ds_read_b128 v[166:169], v159
	ds_read_b128 v[170:173], v160
	s_mov_b32 m0, s61
	v_lshl_add_u64 v[6:7], s[46:47], 0, v[138:139]
	ds_read_b128 v[174:177], v0 offset:32768
	ds_read_b128 v[178:181], v0 offset:33792
	ds_read_b128 v[182:185], v0 offset:34816
	ds_read_b128 v[188:191], v0 offset:35840
	ds_read_b128 v[192:195], v0 offset:36864
	ds_read_b128 v[196:199], v0 offset:37888
	ds_read_b128 v[200:203], v0 offset:38912
	ds_read_b128 v[204:207], v0 offset:39936
	global_load_lds_dwordx4 v[6:7], off
	v_lshl_add_u64 v[6:7], s[46:47], 0, v[134:135]
	s_mov_b32 m0, s62
	s_nop 0
	global_load_lds_dwordx4 v[6:7], off
	s_waitcnt lgkmcnt(8)
	s_barrier
	s_setprio 1
	s_waitcnt lgkmcnt(7)
	v_mfma_f32_16x16x32_bf16 v[128:131], v[140:143], v[174:177], v[128:131]
	v_mfma_f32_16x16x32_bf16 v[124:127], v[166:169], v[174:177], v[124:127]
	s_waitcnt lgkmcnt(6)
	v_mfma_f32_16x16x32_bf16 v[128:131], v[144:147], v[178:181], v[128:131]
	v_mfma_f32_16x16x32_bf16 v[124:127], v[170:173], v[178:181], v[124:127]
	s_waitcnt lgkmcnt(5)
	v_mfma_f32_16x16x32_bf16 v[120:123], v[140:143], v[182:185], v[120:123]
	v_mfma_f32_16x16x32_bf16 v[116:119], v[166:169], v[182:185], v[116:119]
	s_waitcnt lgkmcnt(4)
	v_mfma_f32_16x16x32_bf16 v[120:123], v[144:147], v[188:191], v[120:123]
	v_mfma_f32_16x16x32_bf16 v[116:119], v[170:173], v[188:191], v[116:119]
	s_waitcnt lgkmcnt(3)
	v_mfma_f32_16x16x32_bf16 v[112:115], v[140:143], v[192:195], v[112:115]
	v_mfma_f32_16x16x32_bf16 v[108:111], v[166:169], v[192:195], v[108:111]
	s_waitcnt lgkmcnt(2)
	v_mfma_f32_16x16x32_bf16 v[112:115], v[144:147], v[196:199], v[112:115]
	v_mfma_f32_16x16x32_bf16 v[108:111], v[170:173], v[196:199], v[108:111]
	s_waitcnt lgkmcnt(1)
	v_mfma_f32_16x16x32_bf16 v[104:107], v[140:143], v[200:203], v[104:107]
	v_mfma_f32_16x16x32_bf16 v[100:103], v[166:169], v[200:203], v[100:103]
	s_waitcnt lgkmcnt(0)
	v_mfma_f32_16x16x32_bf16 v[104:107], v[144:147], v[204:207], v[104:107]
	v_mfma_f32_16x16x32_bf16 v[100:103], v[170:173], v[204:207], v[100:103]
	s_setprio 0
	s_barrier
	s_mov_b32 m0, s64
	v_lshl_add_u64 v[6:7], v[220:221], 0, s[24:25]
	ds_read_b128 v[208:211], v161
	ds_read_b128 v[212:215], v162
	ds_read_b128 v[216:219], v163
	ds_read_b128 v[232:235], v164
	global_load_lds_dwordx4 v[6:7], off
	v_lshl_add_u64 v[6:7], v[226:227], 0, s[24:25]
	s_mov_b32 m0, s65
	s_nop 0
	global_load_lds_dwordx4 v[6:7], off
	s_barrier
	s_setprio 1
	s_waitcnt lgkmcnt(3)
	v_mfma_f32_16x16x32_bf16 v[96:99], v[208:211], v[174:177], v[96:99]
	v_mfma_f32_16x16x32_bf16 v[88:91], v[208:211], v[182:185], v[88:91]
	v_mfma_f32_16x16x32_bf16 v[80:83], v[208:211], v[192:195], v[80:83]
	v_mfma_f32_16x16x32_bf16 v[72:75], v[208:211], v[200:203], v[72:75]
	s_waitcnt lgkmcnt(2)
	v_mfma_f32_16x16x32_bf16 v[96:99], v[212:215], v[178:181], v[96:99]
	v_mfma_f32_16x16x32_bf16 v[88:91], v[212:215], v[188:191], v[88:91]
	v_mfma_f32_16x16x32_bf16 v[80:83], v[212:215], v[196:199], v[80:83]
	v_mfma_f32_16x16x32_bf16 v[72:75], v[212:215], v[204:207], v[72:75]
	s_waitcnt lgkmcnt(1)
	v_mfma_f32_16x16x32_bf16 v[92:95], v[216:219], v[174:177], v[92:95]
	v_mfma_f32_16x16x32_bf16 v[84:87], v[216:219], v[182:185], v[84:87]
	v_mfma_f32_16x16x32_bf16 v[76:79], v[216:219], v[192:195], v[76:79]
	v_mfma_f32_16x16x32_bf16 v[68:71], v[216:219], v[200:203], v[68:71]
	s_waitcnt lgkmcnt(0)
	v_mfma_f32_16x16x32_bf16 v[92:95], v[232:235], v[178:181], v[92:95]
	v_mfma_f32_16x16x32_bf16 v[84:87], v[232:235], v[188:191], v[84:87]
	v_mfma_f32_16x16x32_bf16 v[76:79], v[232:235], v[196:199], v[76:79]
	v_mfma_f32_16x16x32_bf16 v[68:71], v[232:235], v[204:207], v[68:71]
	s_setprio 0
	s_mov_b32 m0, s66
	v_lshl_add_u64 v[6:7], v[236:237], 0, s[24:25]
	s_barrier
	ds_read_b128 v[174:177], v0 offset:49152
	ds_read_b128 v[178:181], v0 offset:50176
	ds_read_b128 v[182:185], v0 offset:51200
	ds_read_b128 v[188:191], v0 offset:52224
	ds_read_b128 v[192:195], v0 offset:53248
	ds_read_b128 v[196:199], v0 offset:54272
	ds_read_b128 v[200:203], v0 offset:55296
	ds_read_b128 v[204:207], v0 offset:56320
	global_load_lds_dwordx4 v[6:7], off
	v_lshl_add_u64 v[6:7], v[238:239], 0, s[24:25]
	s_mov_b32 m0, s67
	s_nop 0
	global_load_lds_dwordx4 v[6:7], off
	s_barrier
	s_setprio 1
	s_waitcnt lgkmcnt(7)
	v_mfma_f32_16x16x32_bf16 v[64:67], v[140:143], v[174:177], v[64:67]
	v_mfma_f32_16x16x32_bf16 v[60:63], v[166:169], v[174:177], v[60:63]
	s_waitcnt lgkmcnt(6)
	v_mfma_f32_16x16x32_bf16 v[64:67], v[144:147], v[178:181], v[64:67]
	v_mfma_f32_16x16x32_bf16 v[60:63], v[170:173], v[178:181], v[60:63]
	s_waitcnt lgkmcnt(5)
	v_mfma_f32_16x16x32_bf16 v[56:59], v[140:143], v[182:185], v[56:59]
	v_mfma_f32_16x16x32_bf16 v[52:55], v[166:169], v[182:185], v[52:55]
	s_waitcnt lgkmcnt(4)
	v_mfma_f32_16x16x32_bf16 v[56:59], v[144:147], v[188:191], v[56:59]
	v_mfma_f32_16x16x32_bf16 v[52:55], v[170:173], v[188:191], v[52:55]
	s_waitcnt lgkmcnt(3)
	v_mfma_f32_16x16x32_bf16 v[48:51], v[140:143], v[192:195], v[48:51]
	v_mfma_f32_16x16x32_bf16 v[44:47], v[166:169], v[192:195], v[44:47]
	s_waitcnt lgkmcnt(2)
	v_mfma_f32_16x16x32_bf16 v[48:51], v[144:147], v[196:199], v[48:51]
	v_mfma_f32_16x16x32_bf16 v[44:47], v[170:173], v[196:199], v[44:47]
	s_waitcnt lgkmcnt(1)
	v_mfma_f32_16x16x32_bf16 v[40:43], v[140:143], v[200:203], v[40:43]
	v_mfma_f32_16x16x32_bf16 v[36:39], v[166:169], v[200:203], v[36:39]
	s_waitcnt lgkmcnt(0)
	v_mfma_f32_16x16x32_bf16 v[40:43], v[144:147], v[204:207], v[40:43]
	v_mfma_f32_16x16x32_bf16 v[36:39], v[170:173], v[204:207], v[36:39]
	s_setprio 0
	s_barrier
	s_mov_b32 m0, s68
	v_lshl_add_u64 v[6:7], s[44:45], 0, v[136:137]
	global_load_lds_dwordx4 v[6:7], off
	v_lshl_add_u64 v[6:7], s[44:45], 0, v[132:133]
	s_mov_b32 m0, s69
	s_nop 0
	global_load_lds_dwordx4 v[6:7], off
	s_waitcnt vmcnt(6)
	s_barrier
	s_setprio 1
	v_mfma_f32_16x16x32_bf16 v[32:35], v[208:211], v[174:177], v[32:35]
	v_mfma_f32_16x16x32_bf16 v[28:31], v[216:219], v[174:177], v[28:31]
	v_mfma_f32_16x16x32_bf16 v[24:27], v[208:211], v[182:185], v[24:27]
	v_mfma_f32_16x16x32_bf16 v[20:23], v[216:219], v[182:185], v[20:23]
	v_mfma_f32_16x16x32_bf16 v[16:19], v[208:211], v[192:195], v[16:19]
	v_mfma_f32_16x16x32_bf16 v[12:15], v[216:219], v[192:195], v[12:15]
	v_mfma_f32_16x16x32_bf16 v[6:9], v[208:211], v[200:203], v[8:11]
	v_mfma_f32_16x16x32_bf16 v[2:5], v[216:219], v[200:203], v[2:5]
	v_mfma_f32_16x16x32_bf16 v[32:35], v[212:215], v[178:181], v[32:35]
	v_mfma_f32_16x16x32_bf16 v[28:31], v[232:235], v[178:181], v[28:31]
	v_mfma_f32_16x16x32_bf16 v[24:27], v[212:215], v[188:191], v[24:27]
	v_mfma_f32_16x16x32_bf16 v[20:23], v[232:235], v[188:191], v[20:23]
	v_mfma_f32_16x16x32_bf16 v[16:19], v[212:215], v[196:199], v[16:19]
	v_mfma_f32_16x16x32_bf16 v[12:15], v[232:235], v[196:199], v[12:15]
	v_mfma_f32_16x16x32_bf16 v[8:11], v[212:215], v[204:207], v[6:9]
	v_mfma_f32_16x16x32_bf16 v[4:7], v[232:235], v[204:207], v[2:5]
	s_setprio 0
	s_movk_i32 s46, 0x100
	s_andn2_b64 vcc, exec, s[42:43]
	s_mov_b64 s[44:45], -1
	s_mov_b64 s[42:43], 0
	s_barrier
	s_cbranch_vccz .LBB0_585
	s_bfe_u32 s42, s72, 0x20004
	v_cvt_f32_ubyte0_e32 v2, s42
	v_sub_f32_e32 v2, 0xc0a00000, v2
	s_mov_b32 s46, 0xc2fc0000
	v_cmp_gt_f32_e32 vcc, s46, v2
	s_ashr_i32 s20, s72, 1
	s_ashr_i32 s21, s20, 31
	v_cndmask_b32_e32 v3, 0, v224, vcc
	v_add_f32_e32 v2, v2, v3
	v_exp_f32_e32 v2, v2
	s_and_b32 s42, s20, 7
	s_and_b64 s[44:45], vcc, exec
	s_cselect_b32 s43, 0xffffffc0, 0
	v_ldexp_f32 v2, v2, s43
	v_sub_f32_e32 v2, 1.0, v2
	v_log_f32_e32 v2, v2
	v_readlane_b32 s34, v252, 51
	v_readlane_b32 s35, v252, 52
	v_mbcnt_lo_u32_b32 v0, -1, 0
	v_mbcnt_hi_u32_b32 v0, -1, v0
	v_mul_f32_e32 v3, 0x43800000, v2
	v_cmp_gt_f32_e32 vcc, s46, v3
	s_and_b64 s[44:45], vcc, exec
	s_cselect_b32 s43, 0xffffffc0, 0
	v_cndmask_b32_e32 v3, 0, v224, vcc
	v_fmac_f32_e32 v3, 0x43800000, v2
	v_exp_f32_e32 v2, v3
	v_and_b32_e32 v3, 15, v0
	s_lshl_b64 s[20:21], s[20:21], 9
	v_ldexp_f32 v2, v2, s43
	s_lshl_b32 s43, s72, 8
	s_and_b32 s43, s43, 0x100
	v_lshl_or_b32 v142, s34, 6, v3
	s_lshl_b32 s34, s35, 5
	v_lshrrev_b32_e32 v0, 1, v0
	s_or_b32 s20, s20, s43
	s_ashr_i32 s35, s34, 31
	v_and_b32_e32 v0, 24, v0
	v_mov_b32_e32 v140, v2
	v_mov_b32_e32 v141, v2
	s_cmp_gt_i32 s42, 6
	v_lshlrev_b32_e32 v0, 1, v0
	s_cbranch_scc1 .LBB0_611
	v_ashrrev_i32_e32 v143, 31, v142
	v_lshl_add_u64 v[144:145], s[20:21], 0, v[142:143]
	v_lshlrev_b64 v[144:145], 10, v[144:145]
	v_lshl_add_u64 v[144:145], s[6:7], 0, v[144:145]
	v_lshl_add_u64 v[144:145], s[34:35], 1, v[144:145]
	v_lshl_add_u64 v[146:147], v[144:145], 0, v[0:1]
	s_mov_b64 s[44:45], 0x200
	s_cmp_lg_u32 s42, 0
	v_lshl_add_u64 v[144:145], v[146:147], 0, s[44:45]
	s_cbranch_scc1 .LBB0_589
	v_mov_b32 v166, 0
	s_nop 0
	v_mov_b32_e32 v167, v166
	v_mov_b32_e32 v168, v166
	v_mov_b32_e32 v169, v166
	global_store_dwordx4 v[144:145], v[166:169], off

.LBB0_648:
	s_add_u32 s45, s20, s44
	s_addc_u32 s53, s21, 0
	s_add_u32 s48, s45, 0x100
	s_addc_u32 s49, s53, 0
	s_and_b64 s[46:47], s[42:43], exec
	s_cselect_b32 s49, s9, s49
	s_cselect_b32 s48, s8, s48
	s_add_u32 s44, s12, s44
	s_addc_u32 s46, s13, 0
	s_add_u32 s44, s44, 0x100
	s_addc_u32 s46, s46, 0
	s_and_b64 s[42:43], s[42:43], exec
	s_cselect_b32 s51, s73, s46
	s_cselect_b32 s50, s74, s44
	s_add_u32 s52, s45, 0x80080
	s_addc_u32 s53, s53, 0
	s_add_i32 m0, s56, 0xc000
	s_add_i32 s75, s56, 0xe000
	ds_read_b128 v[136:139], v141
	ds_read_b128 v[158:161], v142
	ds_read_b128 v[162:165], v143
	ds_read_b128 v[166:169], v144
	s_add_u32 s46, s50, 0x40000
	s_addc_u32 s47, s51, 0
	s_add_u32 s44, s48, 0x80000
	s_addc_u32 s45, s49, 0
	s_add_u32 s42, s50, 0x40080
	s_addc_u32 s43, s51, 0
	v_add_u32_e32 v157, s64, v140
	v_lshl_add_u64 v[204:205], s[52:53], 0, v[134:135]
	ds_read_b128 v[170:173], v157
	ds_read_b128 v[174:177], v157 offset:1024
	ds_read_b128 v[178:181], v157 offset:2048
	ds_read_b128 v[182:185], v157 offset:3072
	ds_read_b128 v[188:191], v157 offset:4096
	ds_read_b128 v[192:195], v157 offset:5120
	ds_read_b128 v[196:199], v157 offset:6144
	ds_read_b128 v[200:203], v157 offset:7168
	global_load_lds_dwordx4 v[204:205], off
	v_lshl_add_u64 v[204:205], s[52:53], 0, v[132:133]
	s_mov_b32 m0, s75
	s_nop 0
	global_load_lds_dwordx4 v[204:205], off
	s_waitcnt lgkmcnt(8)
	s_barrier
	s_setprio 1
	s_waitcnt lgkmcnt(7)
	v_mfma_f32_16x16x32_bf16 v[126:129], v[136:139], v[170:173], v[126:129]
	v_mfma_f32_16x16x32_bf16 v[122:125], v[162:165], v[170:173], v[122:125]
	s_waitcnt lgkmcnt(6)
	v_mfma_f32_16x16x32_bf16 v[126:129], v[158:161], v[174:177], v[126:129]
	v_mfma_f32_16x16x32_bf16 v[122:125], v[166:169], v[174:177], v[122:125]
	s_waitcnt lgkmcnt(5)
	v_mfma_f32_16x16x32_bf16 v[110:113], v[136:139], v[178:181], v[110:113]
	v_mfma_f32_16x16x32_bf16 v[106:109], v[162:165], v[178:181], v[106:109]
	s_waitcnt lgkmcnt(4)
	v_mfma_f32_16x16x32_bf16 v[110:113], v[158:161], v[182:185], v[110:113]
	v_mfma_f32_16x16x32_bf16 v[106:109], v[166:169], v[182:185], v[106:109]
	s_waitcnt lgkmcnt(3)
	v_mfma_f32_16x16x32_bf16 v[94:97], v[136:139], v[188:191], v[94:97]
	v_mfma_f32_16x16x32_bf16 v[90:93], v[162:165], v[188:191], v[90:93]
	s_waitcnt lgkmcnt(2)
	v_mfma_f32_16x16x32_bf16 v[94:97], v[158:161], v[192:195], v[94:97]
	v_mfma_f32_16x16x32_bf16 v[90:93], v[166:169], v[192:195], v[90:93]
	s_waitcnt lgkmcnt(1)
	v_mfma_f32_16x16x32_bf16 v[78:81], v[136:139], v[196:199], v[78:81]
	v_mfma_f32_16x16x32_bf16 v[74:77], v[162:165], v[196:199], v[74:77]
	s_waitcnt lgkmcnt(0)
	v_mfma_f32_16x16x32_bf16 v[78:81], v[158:161], v[200:203], v[78:81]
	v_mfma_f32_16x16x32_bf16 v[74:77], v[166:169], v[200:203], v[74:77]
	s_setprio 0
	s_barrier
	s_mov_b32 m0, s57
	v_lshl_add_u64 v[220:221], s[50:51], 0, v[0:1]
	ds_read_b128 v[204:207], v145
	ds_read_b128 v[208:211], v146
	ds_read_b128 v[212:215], v147
	ds_read_b128 v[216:219], v148
	global_load_lds_dwordx4 v[220:221], off
	v_lshl_add_u64 v[226:227], s[50:51], 0, v[130:131]
	s_mov_b32 m0, s58
	s_nop 0
	global_load_lds_dwordx4 v[226:227], off
	s_barrier
	s_setprio 1
	s_waitcnt lgkmcnt(3)
	v_mfma_f32_16x16x32_bf16 v[118:121], v[204:207], v[170:173], v[118:121]
	v_mfma_f32_16x16x32_bf16 v[102:105], v[204:207], v[178:181], v[102:105]
	v_mfma_f32_16x16x32_bf16 v[86:89], v[204:207], v[188:191], v[86:89]
	v_mfma_f32_16x16x32_bf16 v[70:73], v[204:207], v[196:199], v[70:73]
	s_waitcnt lgkmcnt(2)
	v_mfma_f32_16x16x32_bf16 v[118:121], v[208:211], v[174:177], v[118:121]
	v_mfma_f32_16x16x32_bf16 v[102:105], v[208:211], v[182:185], v[102:105]
	v_mfma_f32_16x16x32_bf16 v[86:89], v[208:211], v[192:195], v[86:89]
	v_mfma_f32_16x16x32_bf16 v[70:73], v[208:211], v[200:203], v[70:73]
	s_waitcnt lgkmcnt(1)
	v_mfma_f32_16x16x32_bf16 v[114:117], v[212:215], v[170:173], v[114:117]
	v_mfma_f32_16x16x32_bf16 v[98:101], v[212:215], v[178:181], v[98:101]
	v_mfma_f32_16x16x32_bf16 v[82:85], v[212:215], v[188:191], v[82:85]
	v_mfma_f32_16x16x32_bf16 v[66:69], v[212:215], v[196:199], v[66:69]
	s_waitcnt lgkmcnt(0)
	v_mfma_f32_16x16x32_bf16 v[114:117], v[216:219], v[174:177], v[114:117]
	v_mfma_f32_16x16x32_bf16 v[98:101], v[216:219], v[182:185], v[98:101]
	v_mfma_f32_16x16x32_bf16 v[82:85], v[216:219], v[192:195], v[82:85]
	v_mfma_f32_16x16x32_bf16 v[66:69], v[216:219], v[200:203], v[66:69]
	s_setprio 0
	s_mov_b32 m0, s56
	v_lshl_add_u64 v[232:233], s[48:49], 0, v[134:135]
	s_barrier
	ds_read_b128 v[170:173], v157 offset:16384
	ds_read_b128 v[174:177], v157 offset:17408
	ds_read_b128 v[178:181], v157 offset:18432
	ds_read_b128 v[182:185], v157 offset:19456
	ds_read_b128 v[188:191], v157 offset:20480
	ds_read_b128 v[192:195], v157 offset:21504
	ds_read_b128 v[196:199], v157 offset:22528
	ds_read_b128 v[200:203], v157 offset:23552
	global_load_lds_dwordx4 v[232:233], off
	v_lshl_add_u64 v[234:235], s[48:49], 0, v[132:133]
	s_mov_b32 m0, s59
	s_nop 0
	global_load_lds_dwordx4 v[234:235], off
	s_barrier
	s_setprio 1
	s_waitcnt lgkmcnt(7)
	v_mfma_f32_16x16x32_bf16 v[62:65], v[136:139], v[170:173], v[62:65]
	v_mfma_f32_16x16x32_bf16 v[58:61], v[162:165], v[170:173], v[58:61]
	s_waitcnt lgkmcnt(6)
	v_mfma_f32_16x16x32_bf16 v[62:65], v[158:161], v[174:177], v[62:65]
	v_mfma_f32_16x16x32_bf16 v[58:61], v[166:169], v[174:177], v[58:61]
	s_waitcnt lgkmcnt(5)
	v_mfma_f32_16x16x32_bf16 v[46:49], v[136:139], v[178:181], v[46:49]
	v_mfma_f32_16x16x32_bf16 v[42:45], v[162:165], v[178:181], v[42:45]
	s_waitcnt lgkmcnt(4)
	v_mfma_f32_16x16x32_bf16 v[46:49], v[158:161], v[182:185], v[46:49]
	v_mfma_f32_16x16x32_bf16 v[42:45], v[166:169], v[182:185], v[42:45]
	s_waitcnt lgkmcnt(3)
	v_mfma_f32_16x16x32_bf16 v[30:33], v[136:139], v[188:191], v[30:33]
	v_mfma_f32_16x16x32_bf16 v[26:29], v[162:165], v[188:191], v[26:29]
	s_waitcnt lgkmcnt(2)
	v_mfma_f32_16x16x32_bf16 v[30:33], v[158:161], v[192:195], v[30:33]
	v_mfma_f32_16x16x32_bf16 v[26:29], v[166:169], v[192:195], v[26:29]
	s_waitcnt lgkmcnt(1)
	v_mfma_f32_16x16x32_bf16 v[14:17], v[136:139], v[196:199], v[14:17]
	v_mfma_f32_16x16x32_bf16 v[10:13], v[162:165], v[196:199], v[10:13]
	s_waitcnt lgkmcnt(0)
	v_mfma_f32_16x16x32_bf16 v[14:17], v[158:161], v[200:203], v[14:17]
	v_mfma_f32_16x16x32_bf16 v[10:13], v[166:169], v[200:203], v[10:13]
	s_setprio 0
	s_barrier
	s_mov_b32 m0, s60
	v_lshl_add_u64 v[136:137], s[46:47], 0, v[0:1]
	global_load_lds_dwordx4 v[136:137], off
	v_lshl_add_u64 v[136:137], s[46:47], 0, v[130:131]
	s_mov_b32 m0, s61
	s_nop 0
	global_load_lds_dwordx4 v[136:137], off
	s_waitcnt vmcnt(6)
	s_barrier
	s_setprio 1
	v_mfma_f32_16x16x32_bf16 v[54:57], v[204:207], v[170:173], v[54:57]
	v_mfma_f32_16x16x32_bf16 v[50:53], v[212:215], v[170:173], v[50:53]
	v_mfma_f32_16x16x32_bf16 v[38:41], v[204:207], v[178:181], v[38:41]
	v_mfma_f32_16x16x32_bf16 v[34:37], v[212:215], v[178:181], v[34:37]
	v_mfma_f32_16x16x32_bf16 v[22:25], v[204:207], v[188:191], v[22:25]
	v_mfma_f32_16x16x32_bf16 v[18:21], v[212:215], v[188:191], v[18:21]
	v_mfma_f32_16x16x32_bf16 v[6:9], v[204:207], v[196:199], v[6:9]
	v_mfma_f32_16x16x32_bf16 v[2:5], v[212:215], v[196:199], v[2:5]
	v_mfma_f32_16x16x32_bf16 v[54:57], v[208:211], v[174:177], v[54:57]
	v_mfma_f32_16x16x32_bf16 v[50:53], v[216:219], v[174:177], v[50:53]
	v_mfma_f32_16x16x32_bf16 v[38:41], v[208:211], v[182:185], v[38:41]
	v_mfma_f32_16x16x32_bf16 v[34:37], v[216:219], v[182:185], v[34:37]
	v_mfma_f32_16x16x32_bf16 v[22:25], v[208:211], v[192:195], v[22:25]
	v_mfma_f32_16x16x32_bf16 v[18:21], v[216:219], v[192:195], v[18:21]
	v_mfma_f32_16x16x32_bf16 v[6:9], v[208:211], v[200:203], v[6:9]
	v_mfma_f32_16x16x32_bf16 v[2:5], v[216:219], v[200:203], v[2:5]
	s_setprio 0
	s_barrier
	ds_read_b128 v[136:139], v149
	ds_read_b128 v[158:161], v150
	ds_read_b128 v[162:165], v151
	ds_read_b128 v[166:169], v152
	s_mov_b32 m0, s62
	v_lshl_add_u64 v[204:205], s[44:45], 0, v[134:135]
	ds_read_b128 v[170:173], v157 offset:32768
	ds_read_b128 v[174:177], v157 offset:33792
	ds_read_b128 v[178:181], v157 offset:34816
	ds_read_b128 v[182:185], v157 offset:35840
	ds_read_b128 v[188:191], v157 offset:36864
	ds_read_b128 v[192:195], v157 offset:37888
	ds_read_b128 v[196:199], v157 offset:38912
	ds_read_b128 v[200:203], v157 offset:39936
	global_load_lds_dwordx4 v[204:205], off
	v_lshl_add_u64 v[204:205], s[44:45], 0, v[132:133]
	s_mov_b32 m0, s63
	s_nop 0
	global_load_lds_dwordx4 v[204:205], off
	s_waitcnt lgkmcnt(8)
	s_barrier
	s_setprio 1
	s_waitcnt lgkmcnt(7)
	v_mfma_f32_16x16x32_bf16 v[126:129], v[136:139], v[170:173], v[126:129]
	v_mfma_f32_16x16x32_bf16 v[122:125], v[162:165], v[170:173], v[122:125]
	s_waitcnt lgkmcnt(6)
	v_mfma_f32_16x16x32_bf16 v[126:129], v[158:161], v[174:177], v[126:129]
	v_mfma_f32_16x16x32_bf16 v[122:125], v[166:169], v[174:177], v[122:125]
	s_waitcnt lgkmcnt(5)
	v_mfma_f32_16x16x32_bf16 v[110:113], v[136:139], v[178:181], v[110:113]
	v_mfma_f32_16x16x32_bf16 v[106:109], v[162:165], v[178:181], v[106:109]
	s_waitcnt lgkmcnt(4)
	v_mfma_f32_16x16x32_bf16 v[110:113], v[158:161], v[182:185], v[110:113]
	v_mfma_f32_16x16x32_bf16 v[106:109], v[166:169], v[182:185], v[106:109]
	s_waitcnt lgkmcnt(3)
	v_mfma_f32_16x16x32_bf16 v[94:97], v[136:139], v[188:191], v[94:97]
	v_mfma_f32_16x16x32_bf16 v[90:93], v[162:165], v[188:191], v[90:93]
	s_waitcnt lgkmcnt(2)
	v_mfma_f32_16x16x32_bf16 v[94:97], v[158:161], v[192:195], v[94:97]
	v_mfma_f32_16x16x32_bf16 v[90:93], v[166:169], v[192:195], v[90:93]
	s_waitcnt lgkmcnt(1)
	v_mfma_f32_16x16x32_bf16 v[78:81], v[136:139], v[196:199], v[78:81]
	v_mfma_f32_16x16x32_bf16 v[74:77], v[162:165], v[196:199], v[74:77]
	s_waitcnt lgkmcnt(0)
	v_mfma_f32_16x16x32_bf16 v[78:81], v[158:161], v[200:203], v[78:81]
	v_mfma_f32_16x16x32_bf16 v[74:77], v[166:169], v[200:203], v[74:77]
	s_setprio 0
	s_barrier
	s_mov_b32 m0, s65
	v_lshl_add_u64 v[220:221], v[220:221], 0, s[24:25]
	ds_read_b128 v[204:207], v153
	ds_read_b128 v[208:211], v154
	ds_read_b128 v[212:215], v155
	ds_read_b128 v[216:219], v156
	global_load_lds_dwordx4 v[220:221], off
	v_lshl_add_u64 v[220:221], v[226:227], 0, s[24:25]
	s_mov_b32 m0, s66
	s_nop 0
	global_load_lds_dwordx4 v[220:221], off
	s_barrier
	s_setprio 1
	s_waitcnt lgkmcnt(3)
	v_mfma_f32_16x16x32_bf16 v[118:121], v[204:207], v[170:173], v[118:121]
	v_mfma_f32_16x16x32_bf16 v[102:105], v[204:207], v[178:181], v[102:105]
	v_mfma_f32_16x16x32_bf16 v[86:89], v[204:207], v[188:191], v[86:89]
	v_mfma_f32_16x16x32_bf16 v[70:73], v[204:207], v[196:199], v[70:73]
	s_waitcnt lgkmcnt(2)
	v_mfma_f32_16x16x32_bf16 v[118:121], v[208:211], v[174:177], v[118:121]
	v_mfma_f32_16x16x32_bf16 v[102:105], v[208:211], v[182:185], v[102:105]
	v_mfma_f32_16x16x32_bf16 v[86:89], v[208:211], v[192:195], v[86:89]
	v_mfma_f32_16x16x32_bf16 v[70:73], v[208:211], v[200:203], v[70:73]
	s_waitcnt lgkmcnt(1)
	v_mfma_f32_16x16x32_bf16 v[114:117], v[212:215], v[170:173], v[114:117]
	v_mfma_f32_16x16x32_bf16 v[98:101], v[212:215], v[178:181], v[98:101]
	v_mfma_f32_16x16x32_bf16 v[82:85], v[212:215], v[188:191], v[82:85]
	v_mfma_f32_16x16x32_bf16 v[66:69], v[212:215], v[196:199], v[66:69]
	s_waitcnt lgkmcnt(0)
	v_mfma_f32_16x16x32_bf16 v[114:117], v[216:219], v[174:177], v[114:117]
	v_mfma_f32_16x16x32_bf16 v[98:101], v[216:219], v[182:185], v[98:101]
	v_mfma_f32_16x16x32_bf16 v[82:85], v[216:219], v[192:195], v[82:85]
	v_mfma_f32_16x16x32_bf16 v[66:69], v[216:219], v[200:203], v[66:69]
	s_setprio 0
	s_mov_b32 m0, s67
	v_lshl_add_u64 v[220:221], v[232:233], 0, s[24:25]
	s_barrier
	ds_read_b128 v[170:173], v157 offset:49152
	ds_read_b128 v[174:177], v157 offset:50176
	ds_read_b128 v[178:181], v157 offset:51200
	ds_read_b128 v[182:185], v157 offset:52224
	ds_read_b128 v[188:191], v157 offset:53248
	ds_read_b128 v[192:195], v157 offset:54272
	ds_read_b128 v[196:199], v157 offset:55296
	ds_read_b128 v[200:203], v157 offset:56320
	global_load_lds_dwordx4 v[220:221], off
	v_lshl_add_u64 v[220:221], v[234:235], 0, s[24:25]
	s_mov_b32 m0, s68
	s_nop 0
	global_load_lds_dwordx4 v[220:221], off
	s_barrier
	s_setprio 1
	s_waitcnt lgkmcnt(7)
	v_mfma_f32_16x16x32_bf16 v[62:65], v[136:139], v[170:173], v[62:65]
	v_mfma_f32_16x16x32_bf16 v[58:61], v[162:165], v[170:173], v[58:61]
	s_waitcnt lgkmcnt(6)
	v_mfma_f32_16x16x32_bf16 v[62:65], v[158:161], v[174:177], v[62:65]
	v_mfma_f32_16x16x32_bf16 v[58:61], v[166:169], v[174:177], v[58:61]
	s_waitcnt lgkmcnt(5)
	v_mfma_f32_16x16x32_bf16 v[46:49], v[136:139], v[178:181], v[46:49]
	v_mfma_f32_16x16x32_bf16 v[42:45], v[162:165], v[178:181], v[42:45]
	s_waitcnt lgkmcnt(4)
	v_mfma_f32_16x16x32_bf16 v[46:49], v[158:161], v[182:185], v[46:49]
	v_mfma_f32_16x16x32_bf16 v[42:45], v[166:169], v[182:185], v[42:45]
	s_waitcnt lgkmcnt(3)
	v_mfma_f32_16x16x32_bf16 v[30:33], v[136:139], v[188:191], v[30:33]
	v_mfma_f32_16x16x32_bf16 v[26:29], v[162:165], v[188:191], v[26:29]
	s_waitcnt lgkmcnt(2)
	v_mfma_f32_16x16x32_bf16 v[30:33], v[158:161], v[192:195], v[30:33]
	v_mfma_f32_16x16x32_bf16 v[26:29], v[166:169], v[192:195], v[26:29]
	s_waitcnt lgkmcnt(1)
	v_mfma_f32_16x16x32_bf16 v[14:17], v[136:139], v[196:199], v[14:17]
	v_mfma_f32_16x16x32_bf16 v[10:13], v[162:165], v[196:199], v[10:13]
	s_waitcnt lgkmcnt(0)
	v_mfma_f32_16x16x32_bf16 v[14:17], v[158:161], v[200:203], v[14:17]
	v_mfma_f32_16x16x32_bf16 v[10:13], v[166:169], v[200:203], v[10:13]
	s_setprio 0
	s_barrier
	s_mov_b32 m0, s69
	v_lshl_add_u64 v[136:137], s[42:43], 0, v[0:1]
	global_load_lds_dwordx4 v[136:137], off
	v_lshl_add_u64 v[136:137], s[42:43], 0, v[130:131]
	s_mov_b32 m0, s70
	s_nop 0
	global_load_lds_dwordx4 v[136:137], off
	s_waitcnt vmcnt(6)
	s_barrier
	s_setprio 1
	v_mfma_f32_16x16x32_bf16 v[54:57], v[204:207], v[170:173], v[54:57]
	v_mfma_f32_16x16x32_bf16 v[50:53], v[212:215], v[170:173], v[50:53]
	v_mfma_f32_16x16x32_bf16 v[38:41], v[204:207], v[178:181], v[38:41]
	v_mfma_f32_16x16x32_bf16 v[34:37], v[212:215], v[178:181], v[34:37]
	v_mfma_f32_16x16x32_bf16 v[22:25], v[204:207], v[188:191], v[22:25]
	v_mfma_f32_16x16x32_bf16 v[18:21], v[212:215], v[188:191], v[18:21]
	v_mfma_f32_16x16x32_bf16 v[6:9], v[204:207], v[196:199], v[6:9]
	v_mfma_f32_16x16x32_bf16 v[2:5], v[212:215], v[196:199], v[2:5]
	v_mfma_f32_16x16x32_bf16 v[54:57], v[208:211], v[174:177], v[54:57]
	v_mfma_f32_16x16x32_bf16 v[50:53], v[216:219], v[174:177], v[50:53]
	v_mfma_f32_16x16x32_bf16 v[38:41], v[208:211], v[182:185], v[38:41]
	v_mfma_f32_16x16x32_bf16 v[34:37], v[216:219], v[182:185], v[34:37]
	v_mfma_f32_16x16x32_bf16 v[22:25], v[208:211], v[192:195], v[22:25]
	v_mfma_f32_16x16x32_bf16 v[18:21], v[216:219], v[192:195], v[18:21]
	v_mfma_f32_16x16x32_bf16 v[6:9], v[208:211], v[200:203], v[6:9]
	v_mfma_f32_16x16x32_bf16 v[2:5], v[216:219], v[200:203], v[2:5]
	s_setprio 0
	s_movk_i32 s44, 0x100
	s_andn2_b64 vcc, exec, s[34:35]
	s_mov_b64 s[42:43], -1
	s_mov_b64 s[34:35], 0
	s_barrier
	s_cbranch_vccz .LBB0_648
	v_mbcnt_lo_u32_b32 v136, -1, 0
	v_mbcnt_hi_u32_b32 v136, -1, v136
	s_ashr_i32 s12, s28, 5
	v_readlane_b32 s20, v252, 51
	v_readlane_b32 s21, v252, 52
	v_and_b32_e32 v137, 15, v136
	s_ashr_i32 s13, s12, 31
	s_lshl_b32 s34, s28, 8
	v_lshrrev_b32_e32 v136, 1, v136
	s_lshl_b64 s[12:13], s[12:13], 11
	s_and_b32 s34, s34, 0x700
	v_lshl_or_b32 v138, s20, 6, v137
	v_and_b32_e32 v136, 24, v136
	s_or_b32 s12, s12, s34
	v_lshl_or_b32 v136, s21, 5, v136
	v_ashrrev_i32_e32 v139, 31, v138
	v_lshl_add_u64 v[158:159], s[12:13], 0, v[138:139]
	v_cmp_ge_i32_e32 vcc, v138, v136
	v_or_b32_e32 v139, 4, v136
	v_or_b32_e32 v157, 5, v136
	v_cndmask_b32_e32 v126, 0, v126, vcc
	v_cmp_ge_i32_e32 vcc, v138, v139
	v_or_b32_e32 v160, 2, v136
	v_or_b32_e32 v161, 6, v136
	v_cndmask_b32_e32 v122, 0, v122, vcc
	v_cmp_gt_i32_e32 vcc, v138, v136
	v_or_b32_e32 v162, 3, v136
	v_or_b32_e32 v163, 7, v136
	v_cndmask_b32_e32 v127, 0, v127, vcc
	v_cmp_ge_i32_e32 vcc, v138, v157
	v_lshlrev_b64 v[158:159], 12, v[158:159]
	s_lshl_b32 s20, s28, 7
	v_cndmask_b32_e32 v123, 0, v123, vcc
	v_cmp_ge_i32_e32 vcc, v138, v160
	s_and_b32 s28, s20, 0xc00
	s_mov_b64 s[20:21], s[8:9]
	v_cndmask_b32_e32 v128, 0, v128, vcc
	v_cmp_ge_i32_e32 vcc, v138, v161
	s_nop 1
	v_cndmask_b32_e32 v137, 0, v124, vcc
	v_cmp_ge_i32_e32 vcc, v138, v162
	v_cvt_pk_bf16_f32 v124, v126, v127
	v_cvt_pk_bf16_f32 v126, v122, v123
	v_cndmask_b32_e32 v129, 0, v129, vcc
	v_cmp_ge_i32_e32 vcc, v138, v163
	v_lshl_add_u64 v[122:123], s[6:7], 0, v[158:159]
	v_add_u32_e32 v159, 0x83, v136
	v_cndmask_b32_e32 v164, 0, v125, vcc
	v_cvt_pk_bf16_f32 v127, v137, v164
	v_ashrrev_i32_e32 v137, 31, v136
	v_cvt_pk_bf16_f32 v125, v128, v129
	v_lshl_add_u64 v[128:129], v[122:123], 0, s[28:29]
	v_lshlrev_b64 v[122:123], 1, v[136:137]
	v_lshl_add_u64 v[128:129], v[128:129], 0, v[122:123]
	global_store_dwordx4 v[128:129], v[124:127], off
	v_add_u32_e32 v137, 0x82, v136
	s_nop 0
	v_add_u32_e32 v124, 0x80, v136
	v_cmp_ge_i32_e32 vcc, v138, v124
	v_add_u32_e32 v125, 0x84, v136
	s_nop 0
	v_cndmask_b32_e32 v118, 0, v118, vcc
	v_cmp_ge_i32_e32 vcc, v138, v125
	s_nop 1
	v_cndmask_b32_e32 v126, 0, v114, vcc
	v_cmp_gt_i32_e32 vcc, v138, v124
	s_nop 1
	v_cndmask_b32_e32 v114, 0, v119, vcc
	v_add_u32_e32 v119, 0x85, v136
	v_cmp_ge_i32_e32 vcc, v138, v119
	v_cvt_pk_bf16_f32 v114, v118, v114
	s_nop 0
	v_cndmask_b32_e32 v127, 0, v115, vcc
	v_cmp_ge_i32_e32 vcc, v138, v137
	s_nop 1
	v_cndmask_b32_e32 v115, 0, v120, vcc
	v_add_u32_e32 v120, 0x86, v136
	v_cmp_ge_i32_e32 vcc, v138, v120
	s_nop 1
	v_cndmask_b32_e32 v158, 0, v116, vcc
	v_cmp_ge_i32_e32 vcc, v138, v159
	s_nop 1
	v_cndmask_b32_e32 v116, 0, v121, vcc
	v_add_u32_e32 v121, 0x87, v136
	v_cmp_ge_i32_e32 vcc, v138, v121
	v_cvt_pk_bf16_f32 v115, v115, v116
	v_cvt_pk_bf16_f32 v116, v126, v127
	v_cndmask_b32_e32 v117, 0, v117, vcc
	v_cvt_pk_bf16_f32 v117, v158, v117
	global_store_dwordx4 v[128:129], v[114:117], off offset:256
	s_nop 1
	v_or_b32_e32 v114, 16, v138
	v_cmp_ge_i32_e32 vcc, v114, v136
	v_ashrrev_i32_e32 v115, 31, v114
	v_lshl_add_u64 v[116:117], s[12:13], 0, v[114:115]
	v_cndmask_b32_e32 v110, 0, v110, vcc
	v_cmp_ge_i32_e32 vcc, v114, v139
	v_lshlrev_b64 v[116:117], 12, v[116:117]
	s_nop 0
	v_cndmask_b32_e32 v115, 0, v106, vcc
	v_cmp_gt_i32_e32 vcc, v114, v136
	s_nop 1
	v_cndmask_b32_e32 v106, 0, v111, vcc
	v_cmp_ge_i32_e32 vcc, v114, v157
	v_cvt_pk_bf16_f32 v106, v110, v106
	s_nop 0
	v_cndmask_b32_e32 v111, 0, v107, vcc
	v_cmp_ge_i32_e32 vcc, v114, v160
	s_nop 1
	v_cndmask_b32_e32 v107, 0, v112, vcc
	v_cmp_ge_i32_e32 vcc, v114, v161
	s_nop 1
	v_cndmask_b32_e32 v112, 0, v108, vcc
	v_cmp_ge_i32_e32 vcc, v114, v162
	s_nop 1
	v_cndmask_b32_e32 v108, 0, v113, vcc
	v_cmp_ge_i32_e32 vcc, v114, v163
	v_cvt_pk_bf16_f32 v107, v107, v108
	v_cvt_pk_bf16_f32 v108, v115, v111
	v_lshl_add_u64 v[110:111], s[6:7], 0, v[116:117]
	v_cndmask_b32_e32 v109, 0, v109, vcc
	v_lshl_add_u64 v[110:111], v[110:111], 0, s[28:29]
	v_cmp_ge_i32_e32 vcc, v114, v124
	v_cvt_pk_bf16_f32 v109, v112, v109
	v_lshl_add_u64 v[110:111], v[110:111], 0, v[122:123]
	v_cndmask_b32_e32 v102, 0, v102, vcc
	v_cmp_ge_i32_e32 vcc, v114, v125
	global_store_dwordx4 v[110:111], v[106:109], off
	s_nop 1
	v_cndmask_b32_e32 v106, 0, v98, vcc
	v_cmp_gt_i32_e32 vcc, v114, v124
	s_nop 1
	v_cndmask_b32_e32 v98, 0, v103, vcc
	v_cmp_ge_i32_e32 vcc, v114, v119
	v_cvt_pk_bf16_f32 v98, v102, v98
	s_nop 0
	v_cndmask_b32_e32 v103, 0, v99, vcc
	v_cmp_ge_i32_e32 vcc, v114, v137
	s_nop 1
	v_cndmask_b32_e32 v99, 0, v104, vcc
	v_cmp_ge_i32_e32 vcc, v114, v120
	s_nop 1
	v_cndmask_b32_e32 v104, 0, v100, vcc
	v_cmp_ge_i32_e32 vcc, v114, v159
	s_nop 1
	v_cndmask_b32_e32 v100, 0, v105, vcc
	v_cmp_ge_i32_e32 vcc, v114, v121
	v_cvt_pk_bf16_f32 v99, v99, v100
	v_cvt_pk_bf16_f32 v100, v106, v103
	v_cndmask_b32_e32 v101, 0, v101, vcc
	v_cvt_pk_bf16_f32 v101, v104, v101
	global_store_dwordx4 v[110:111], v[98:101], off offset:256
	s_nop 1
	v_or_b32_e32 v98, 32, v138
	v_cmp_ge_i32_e32 vcc, v98, v136
	v_ashrrev_i32_e32 v99, 31, v98
	v_lshl_add_u64 v[100:101], s[12:13], 0, v[98:99]
	v_cndmask_b32_e32 v94, 0, v94, vcc
	v_cmp_ge_i32_e32 vcc, v98, v139
	v_lshlrev_b64 v[100:101], 12, v[100:101]
	s_nop 0
	v_cndmask_b32_e32 v99, 0, v90, vcc
	v_cmp_gt_i32_e32 vcc, v98, v136
	s_nop 1
	v_cndmask_b32_e32 v90, 0, v95, vcc
	v_cmp_ge_i32_e32 vcc, v98, v157
	v_cvt_pk_bf16_f32 v90, v94, v90
	s_nop 0
	v_cndmask_b32_e32 v95, 0, v91, vcc
	v_cmp_ge_i32_e32 vcc, v98, v160
	s_nop 1
	v_cndmask_b32_e32 v91, 0, v96, vcc
	v_cmp_ge_i32_e32 vcc, v98, v161
	s_nop 1
	v_cndmask_b32_e32 v96, 0, v92, vcc
	v_cmp_ge_i32_e32 vcc, v98, v162
	s_nop 1
	v_cndmask_b32_e32 v92, 0, v97, vcc
	v_cmp_ge_i32_e32 vcc, v98, v163
	v_cvt_pk_bf16_f32 v91, v91, v92
	v_cvt_pk_bf16_f32 v92, v99, v95
	v_lshl_add_u64 v[94:95], s[6:7], 0, v[100:101]
	v_cndmask_b32_e32 v93, 0, v93, vcc
	v_lshl_add_u64 v[94:95], v[94:95], 0, s[28:29]
	v_cmp_ge_i32_e32 vcc, v98, v124
	v_cvt_pk_bf16_f32 v93, v96, v93
	v_lshl_add_u64 v[94:95], v[94:95], 0, v[122:123]
	v_cndmask_b32_e32 v86, 0, v86, vcc
	v_cmp_ge_i32_e32 vcc, v98, v125
	global_store_dwordx4 v[94:95], v[90:93], off
	s_nop 1
	v_cndmask_b32_e32 v90, 0, v82, vcc
	v_cmp_gt_i32_e32 vcc, v98, v124
	s_nop 1
	v_cndmask_b32_e32 v82, 0, v87, vcc
	v_cmp_ge_i32_e32 vcc, v98, v119
	v_cvt_pk_bf16_f32 v82, v86, v82
	s_nop 0
	v_cndmask_b32_e32 v87, 0, v83, vcc
	v_cmp_ge_i32_e32 vcc, v98, v137
	s_nop 1
	v_cndmask_b32_e32 v83, 0, v88, vcc
	v_cmp_ge_i32_e32 vcc, v98, v120
	s_nop 1
	v_cndmask_b32_e32 v88, 0, v84, vcc
	v_cmp_ge_i32_e32 vcc, v98, v159
	s_nop 1
	v_cndmask_b32_e32 v84, 0, v89, vcc
	v_cmp_ge_i32_e32 vcc, v98, v121
	v_cvt_pk_bf16_f32 v83, v83, v84
	v_cvt_pk_bf16_f32 v84, v90, v87
	v_cndmask_b32_e32 v85, 0, v85, vcc
	v_cvt_pk_bf16_f32 v85, v88, v85
	global_store_dwordx4 v[94:95], v[82:85], off offset:256
	s_nop 1
	v_or_b32_e32 v82, 48, v138
	v_cmp_ge_i32_e32 vcc, v82, v136
	v_ashrrev_i32_e32 v83, 31, v82
	v_lshl_add_u64 v[84:85], s[12:13], 0, v[82:83]
	v_cndmask_b32_e32 v78, 0, v78, vcc
	v_cmp_ge_i32_e32 vcc, v82, v139
	v_lshlrev_b64 v[84:85], 12, v[84:85]
	s_nop 0
	v_cndmask_b32_e32 v83, 0, v74, vcc
	v_cmp_gt_i32_e32 vcc, v82, v136
	s_nop 1
	v_cndmask_b32_e32 v74, 0, v79, vcc
	v_cmp_ge_i32_e32 vcc, v82, v157
	v_cvt_pk_bf16_f32 v74, v78, v74
	s_nop 0
	v_cndmask_b32_e32 v79, 0, v75, vcc
	v_cmp_ge_i32_e32 vcc, v82, v160
	s_nop 1
	v_cndmask_b32_e32 v75, 0, v80, vcc
	v_cmp_ge_i32_e32 vcc, v82, v161
	s_nop 1
	v_cndmask_b32_e32 v80, 0, v76, vcc
	v_cmp_ge_i32_e32 vcc, v82, v162
	s_nop 1
	v_cndmask_b32_e32 v76, 0, v81, vcc
	v_cmp_ge_i32_e32 vcc, v82, v163
	v_cvt_pk_bf16_f32 v75, v75, v76
	v_cvt_pk_bf16_f32 v76, v83, v79
	v_lshl_add_u64 v[78:79], s[6:7], 0, v[84:85]
	v_cndmask_b32_e32 v77, 0, v77, vcc
	v_lshl_add_u64 v[78:79], v[78:79], 0, s[28:29]
	v_cmp_ge_i32_e32 vcc, v82, v124
	v_cvt_pk_bf16_f32 v77, v80, v77
	v_lshl_add_u64 v[78:79], v[78:79], 0, v[122:123]
	v_cndmask_b32_e32 v70, 0, v70, vcc
	v_cmp_ge_i32_e32 vcc, v82, v125
	global_store_dwordx4 v[78:79], v[74:77], off
	s_nop 1
	v_cndmask_b32_e32 v74, 0, v66, vcc
	v_cmp_gt_i32_e32 vcc, v82, v124
	s_nop 1
	v_cndmask_b32_e32 v66, 0, v71, vcc
	v_cmp_ge_i32_e32 vcc, v82, v119
	v_cvt_pk_bf16_f32 v66, v70, v66
	s_nop 0
	v_cndmask_b32_e32 v71, 0, v67, vcc
	v_cmp_ge_i32_e32 vcc, v82, v137
	s_nop 1
	v_cndmask_b32_e32 v67, 0, v72, vcc
	v_cmp_ge_i32_e32 vcc, v82, v120
	s_nop 1
	v_cndmask_b32_e32 v72, 0, v68, vcc
	v_cmp_ge_i32_e32 vcc, v82, v159
	s_nop 1
	v_cndmask_b32_e32 v68, 0, v73, vcc
	v_cmp_ge_i32_e32 vcc, v82, v121
	v_cvt_pk_bf16_f32 v67, v67, v68
	v_cvt_pk_bf16_f32 v68, v74, v71
	v_cndmask_b32_e32 v69, 0, v69, vcc
	v_cvt_pk_bf16_f32 v69, v72, v69
	global_store_dwordx4 v[78:79], v[66:69], off offset:256
	s_nop 1
	v_add_u32_e32 v66, 0x80, v138
	v_cmp_ge_i32_e32 vcc, v66, v136
	v_ashrrev_i32_e32 v67, 31, v66
	v_lshl_add_u64 v[68:69], s[12:13], 0, v[66:67]
	v_cndmask_b32_e32 v62, 0, v62, vcc
	v_cmp_ge_i32_e32 vcc, v66, v139
	v_lshlrev_b64 v[68:69], 12, v[68:69]
	s_nop 0
	v_cndmask_b32_e32 v67, 0, v58, vcc
	v_cmp_gt_i32_e32 vcc, v66, v136
	s_nop 1
	v_cndmask_b32_e32 v58, 0, v63, vcc
	v_cmp_ge_i32_e32 vcc, v66, v157
	v_cvt_pk_bf16_f32 v58, v62, v58
	s_nop 0
	v_cndmask_b32_e32 v63, 0, v59, vcc
	v_cmp_ge_i32_e32 vcc, v66, v160
	s_nop 1
	v_cndmask_b32_e32 v59, 0, v64, vcc
	v_cmp_ge_i32_e32 vcc, v66, v161
	s_nop 1
	v_cndmask_b32_e32 v64, 0, v60, vcc
	v_cmp_ge_i32_e32 vcc, v66, v162
	s_nop 1
	v_cndmask_b32_e32 v60, 0, v65, vcc
	v_cmp_ge_i32_e32 vcc, v66, v163
	v_cvt_pk_bf16_f32 v59, v59, v60
	v_cvt_pk_bf16_f32 v60, v67, v63
	v_lshl_add_u64 v[62:63], s[6:7], 0, v[68:69]
	v_cndmask_b32_e32 v61, 0, v61, vcc
	v_lshl_add_u64 v[62:63], v[62:63], 0, s[28:29]
	v_cmp_ge_i32_e32 vcc, v66, v124
	v_cvt_pk_bf16_f32 v61, v64, v61
	v_lshl_add_u64 v[62:63], v[62:63], 0, v[122:123]
	v_cndmask_b32_e32 v54, 0, v54, vcc
	v_cmp_ge_i32_e32 vcc, v66, v125
	global_store_dwordx4 v[62:63], v[58:61], off
	s_nop 1
	v_cndmask_b32_e32 v58, 0, v50, vcc
	v_cmp_gt_i32_e32 vcc, v66, v124
	s_nop 1
	v_cndmask_b32_e32 v50, 0, v55, vcc
	v_cmp_ge_i32_e32 vcc, v66, v119
	v_cvt_pk_bf16_f32 v50, v54, v50
	s_nop 0
	v_cndmask_b32_e32 v55, 0, v51, vcc
	v_cmp_ge_i32_e32 vcc, v66, v137
	s_nop 1
	v_cndmask_b32_e32 v51, 0, v56, vcc
	v_cmp_ge_i32_e32 vcc, v66, v120
	s_nop 1
	v_cndmask_b32_e32 v56, 0, v52, vcc
	v_cmp_ge_i32_e32 vcc, v66, v159
	s_nop 1
	v_cndmask_b32_e32 v52, 0, v57, vcc
	v_cmp_ge_i32_e32 vcc, v66, v121
	v_cvt_pk_bf16_f32 v51, v51, v52
	v_cvt_pk_bf16_f32 v52, v58, v55
	v_cndmask_b32_e32 v53, 0, v53, vcc
	v_cvt_pk_bf16_f32 v53, v56, v53
	global_store_dwordx4 v[62:63], v[50:53], off offset:256
	s_nop 1
	v_add_u32_e32 v50, 0x90, v138
	v_cmp_ge_i32_e32 vcc, v50, v136
	v_ashrrev_i32_e32 v51, 31, v50
	v_lshl_add_u64 v[52:53], s[12:13], 0, v[50:51]
	v_cndmask_b32_e32 v46, 0, v46, vcc
	v_cmp_ge_i32_e32 vcc, v50, v139
	v_lshlrev_b64 v[52:53], 12, v[52:53]
	s_nop 0
	v_cndmask_b32_e32 v51, 0, v42, vcc
	v_cmp_gt_i32_e32 vcc, v50, v136
	s_nop 1
	v_cndmask_b32_e32 v42, 0, v47, vcc
	v_cmp_ge_i32_e32 vcc, v50, v157
	v_cvt_pk_bf16_f32 v42, v46, v42
	s_nop 0
	v_cndmask_b32_e32 v47, 0, v43, vcc
	v_cmp_ge_i32_e32 vcc, v50, v160
	s_nop 1
	v_cndmask_b32_e32 v43, 0, v48, vcc
	v_cmp_ge_i32_e32 vcc, v50, v161
	s_nop 1
	v_cndmask_b32_e32 v48, 0, v44, vcc
	v_cmp_ge_i32_e32 vcc, v50, v162
	s_nop 1
	v_cndmask_b32_e32 v44, 0, v49, vcc
	v_cmp_ge_i32_e32 vcc, v50, v163
	v_cvt_pk_bf16_f32 v43, v43, v44
	v_cvt_pk_bf16_f32 v44, v51, v47
	v_lshl_add_u64 v[46:47], s[6:7], 0, v[52:53]
	v_cndmask_b32_e32 v45, 0, v45, vcc
	v_lshl_add_u64 v[46:47], v[46:47], 0, s[28:29]
	v_cmp_ge_i32_e32 vcc, v50, v124
	v_cvt_pk_bf16_f32 v45, v48, v45
	v_lshl_add_u64 v[46:47], v[46:47], 0, v[122:123]
	v_cndmask_b32_e32 v38, 0, v38, vcc
	v_cmp_ge_i32_e32 vcc, v50, v125
	global_store_dwordx4 v[46:47], v[42:45], off
	s_nop 1
	v_cndmask_b32_e32 v42, 0, v34, vcc
	v_cmp_gt_i32_e32 vcc, v50, v124
	s_nop 1
	v_cndmask_b32_e32 v34, 0, v39, vcc
	v_cmp_ge_i32_e32 vcc, v50, v119
	v_cvt_pk_bf16_f32 v34, v38, v34
	s_nop 0
	v_cndmask_b32_e32 v39, 0, v35, vcc
	v_cmp_ge_i32_e32 vcc, v50, v137
	s_nop 1
	v_cndmask_b32_e32 v35, 0, v40, vcc
	v_cmp_ge_i32_e32 vcc, v50, v120
	s_nop 1
	v_cndmask_b32_e32 v40, 0, v36, vcc
	v_cmp_ge_i32_e32 vcc, v50, v159
	s_nop 1
	v_cndmask_b32_e32 v36, 0, v41, vcc
	v_cmp_ge_i32_e32 vcc, v50, v121
	v_cvt_pk_bf16_f32 v35, v35, v36
	v_cvt_pk_bf16_f32 v36, v42, v39
	v_cndmask_b32_e32 v37, 0, v37, vcc
	v_cvt_pk_bf16_f32 v37, v40, v37
	global_store_dwordx4 v[46:47], v[34:37], off offset:256
	s_nop 1
	v_add_u32_e32 v34, 0xa0, v138
	v_cmp_ge_i32_e32 vcc, v34, v136
	v_ashrrev_i32_e32 v35, 31, v34
	v_lshl_add_u64 v[36:37], s[12:13], 0, v[34:35]
	v_cndmask_b32_e32 v30, 0, v30, vcc
	v_cmp_ge_i32_e32 vcc, v34, v139
	v_lshlrev_b64 v[36:37], 12, v[36:37]
	s_nop 0
	v_cndmask_b32_e32 v35, 0, v26, vcc
	v_cmp_gt_i32_e32 vcc, v34, v136
	s_nop 1
	v_cndmask_b32_e32 v26, 0, v31, vcc
	v_cmp_ge_i32_e32 vcc, v34, v157
	v_cvt_pk_bf16_f32 v26, v30, v26
	s_nop 0
	v_cndmask_b32_e32 v31, 0, v27, vcc
	v_cmp_ge_i32_e32 vcc, v34, v160
	s_nop 1
	v_cndmask_b32_e32 v27, 0, v32, vcc
	v_cmp_ge_i32_e32 vcc, v34, v161
	s_nop 1
	v_cndmask_b32_e32 v32, 0, v28, vcc
	v_cmp_ge_i32_e32 vcc, v34, v162
	s_nop 1
	v_cndmask_b32_e32 v28, 0, v33, vcc
	v_cmp_ge_i32_e32 vcc, v34, v163
	v_cvt_pk_bf16_f32 v27, v27, v28
	v_cvt_pk_bf16_f32 v28, v35, v31
	v_lshl_add_u64 v[30:31], s[6:7], 0, v[36:37]
	v_cndmask_b32_e32 v29, 0, v29, vcc
	v_lshl_add_u64 v[30:31], v[30:31], 0, s[28:29]
	v_cmp_ge_i32_e32 vcc, v34, v124
	v_cvt_pk_bf16_f32 v29, v32, v29
	v_lshl_add_u64 v[30:31], v[30:31], 0, v[122:123]
	v_cndmask_b32_e32 v22, 0, v22, vcc
	v_cmp_ge_i32_e32 vcc, v34, v125
	global_store_dwordx4 v[30:31], v[26:29], off
	s_nop 1
	v_cndmask_b32_e32 v26, 0, v18, vcc
	v_cmp_gt_i32_e32 vcc, v34, v124
	s_nop 1
	v_cndmask_b32_e32 v18, 0, v23, vcc
	v_cmp_ge_i32_e32 vcc, v34, v119
	v_cvt_pk_bf16_f32 v18, v22, v18
	s_nop 0
	v_cndmask_b32_e32 v23, 0, v19, vcc
	v_cmp_ge_i32_e32 vcc, v34, v137
	s_nop 1
	v_cndmask_b32_e32 v19, 0, v24, vcc
	v_cmp_ge_i32_e32 vcc, v34, v120
	s_nop 1
	v_cndmask_b32_e32 v24, 0, v20, vcc
	v_cmp_ge_i32_e32 vcc, v34, v159
	s_nop 1
	v_cndmask_b32_e32 v20, 0, v25, vcc
	v_cmp_ge_i32_e32 vcc, v34, v121
	v_cvt_pk_bf16_f32 v19, v19, v20
	v_cvt_pk_bf16_f32 v20, v26, v23
	v_cndmask_b32_e32 v21, 0, v21, vcc
	v_cvt_pk_bf16_f32 v21, v24, v21
	global_store_dwordx4 v[30:31], v[18:21], off offset:256
	s_nop 1
	v_add_u32_e32 v18, 0xb0, v138
	v_cmp_ge_i32_e32 vcc, v18, v136
	v_ashrrev_i32_e32 v19, 31, v18
	v_lshl_add_u64 v[20:21], s[12:13], 0, v[18:19]
	v_cndmask_b32_e32 v14, 0, v14, vcc
	v_cmp_ge_i32_e32 vcc, v18, v139
	v_lshlrev_b64 v[20:21], 12, v[20:21]
	s_mov_b64 s[12:13], s[10:11]
	v_cndmask_b32_e32 v19, 0, v10, vcc
	v_cmp_gt_i32_e32 vcc, v18, v136
	s_nop 1
	v_cndmask_b32_e32 v10, 0, v15, vcc
	v_cmp_ge_i32_e32 vcc, v18, v157
	v_cvt_pk_bf16_f32 v10, v14, v10
	s_nop 0
	v_cndmask_b32_e32 v15, 0, v11, vcc
	v_cmp_ge_i32_e32 vcc, v18, v160
	s_nop 1
	v_cndmask_b32_e32 v11, 0, v16, vcc
	v_cmp_ge_i32_e32 vcc, v18, v161
	s_nop 1
	v_cndmask_b32_e32 v16, 0, v12, vcc
	v_cmp_ge_i32_e32 vcc, v18, v162
	s_nop 1
	v_cndmask_b32_e32 v12, 0, v17, vcc
	v_cmp_ge_i32_e32 vcc, v18, v163
	v_cvt_pk_bf16_f32 v11, v11, v12
	v_cvt_pk_bf16_f32 v12, v19, v15
	v_lshl_add_u64 v[14:15], s[6:7], 0, v[20:21]
	v_cndmask_b32_e32 v13, 0, v13, vcc
	v_lshl_add_u64 v[14:15], v[14:15], 0, s[28:29]
	v_cmp_ge_i32_e32 vcc, v18, v124
	v_cvt_pk_bf16_f32 v13, v16, v13
	v_lshl_add_u64 v[14:15], v[14:15], 0, v[122:123]
	v_cndmask_b32_e32 v6, 0, v6, vcc
	v_cmp_ge_i32_e32 vcc, v18, v125
	global_store_dwordx4 v[14:15], v[10:13], off
	s_mov_b32 s28, s72
	s_nop 0
	v_cndmask_b32_e32 v10, 0, v2, vcc
	v_cmp_gt_i32_e32 vcc, v18, v124
	s_nop 1
	v_cndmask_b32_e32 v2, 0, v7, vcc
	v_cmp_ge_i32_e32 vcc, v18, v119
	v_cvt_pk_bf16_f32 v2, v6, v2
	s_nop 0
	v_cndmask_b32_e32 v7, 0, v3, vcc
	v_cmp_ge_i32_e32 vcc, v18, v137
	s_nop 1
	v_cndmask_b32_e32 v3, 0, v8, vcc
	v_cmp_ge_i32_e32 vcc, v18, v120
	s_nop 1
	v_cndmask_b32_e32 v8, 0, v4, vcc
	v_cmp_ge_i32_e32 vcc, v18, v159
	s_nop 1
	v_cndmask_b32_e32 v4, 0, v9, vcc
	v_cmp_ge_i32_e32 vcc, v18, v121
	v_cvt_pk_bf16_f32 v3, v3, v4
	v_cvt_pk_bf16_f32 v4, v10, v7
	v_cndmask_b32_e32 v5, 0, v5, vcc
	v_cvt_pk_bf16_f32 v5, v8, v5
	s_and_b64 vcc, exec, s[4:5]
	global_store_dwordx4 v[14:15], v[2:5], off offset:256
	s_cbranch_vccz .LBB0_643
	s_branch .LBB0_652

.LBB0_716:
	ds_read_b128 v[162:165], v145
	ds_read_b128 v[166:169], v146
	ds_read_b128 v[170:173], v147
	ds_read_b128 v[174:177], v148
	s_add_u32 s42, s6, 0xfff80080
	s_addc_u32 s43, s7, -1
	s_cmp_eq_u32 s69, 4
	s_cselect_b32 s45, s21, s43
	s_cselect_b32 s44, s20, s42
	s_cselect_b32 s43, s11, s68
	s_cselect_b32 s42, s13, s67
	v_add_u32_e32 v0, s58, v144
	v_lshl_add_u64 v[142:143], s[6:7], 0, v[138:139]
	s_add_i32 m0, s50, 0xc000
	ds_read_b128 v[178:181], v0
	ds_read_b128 v[182:185], v0 offset:1024
	ds_read_b128 v[188:191], v0 offset:2048
	ds_read_b128 v[192:195], v0 offset:3072
	ds_read_b128 v[196:199], v0 offset:4096
	ds_read_b128 v[200:203], v0 offset:5120
	ds_read_b128 v[204:207], v0 offset:6144
	ds_read_b128 v[208:211], v0 offset:7168
	global_load_lds_dwordx4 v[142:143], off
	v_lshl_add_u64 v[142:143], s[6:7], 0, v[140:141]
	s_add_i32 m0, s50, 0xe000
	s_nop 0
	global_load_lds_dwordx4 v[142:143], off
	s_waitcnt lgkmcnt(8)
	s_barrier
	s_setprio 1
	s_waitcnt lgkmcnt(7)
	v_mfma_f32_16x16x32_bf16 v[126:129], v[162:165], v[178:181], v[126:129]
	v_mfma_f32_16x16x32_bf16 v[122:125], v[170:173], v[178:181], v[122:125]
	s_waitcnt lgkmcnt(6)
	v_mfma_f32_16x16x32_bf16 v[126:129], v[166:169], v[182:185], v[126:129]
	v_mfma_f32_16x16x32_bf16 v[122:125], v[174:177], v[182:185], v[122:125]
	s_waitcnt lgkmcnt(5)
	v_mfma_f32_16x16x32_bf16 v[110:113], v[162:165], v[188:191], v[110:113]
	v_mfma_f32_16x16x32_bf16 v[106:109], v[170:173], v[188:191], v[106:109]
	s_waitcnt lgkmcnt(4)
	v_mfma_f32_16x16x32_bf16 v[110:113], v[166:169], v[192:195], v[110:113]
	v_mfma_f32_16x16x32_bf16 v[106:109], v[174:177], v[192:195], v[106:109]
	s_waitcnt lgkmcnt(3)
	v_mfma_f32_16x16x32_bf16 v[94:97], v[162:165], v[196:199], v[94:97]
	v_mfma_f32_16x16x32_bf16 v[90:93], v[170:173], v[196:199], v[90:93]
	s_waitcnt lgkmcnt(2)
	v_mfma_f32_16x16x32_bf16 v[94:97], v[166:169], v[200:203], v[94:97]
	v_mfma_f32_16x16x32_bf16 v[90:93], v[174:177], v[200:203], v[90:93]
	s_waitcnt lgkmcnt(1)
	v_mfma_f32_16x16x32_bf16 v[78:81], v[162:165], v[204:207], v[78:81]
	v_mfma_f32_16x16x32_bf16 v[74:77], v[170:173], v[204:207], v[74:77]
	s_waitcnt lgkmcnt(0)
	v_mfma_f32_16x16x32_bf16 v[78:81], v[166:169], v[208:211], v[78:81]
	v_mfma_f32_16x16x32_bf16 v[74:77], v[174:177], v[208:211], v[74:77]
	s_setprio 0
	s_barrier
	s_mov_b32 m0, s51
	v_lshl_add_u64 v[142:143], s[42:43], 0, v[134:135]
	ds_read_b128 v[212:215], v149
	ds_read_b128 v[216:219], v150
	ds_read_b128 v[232:235], v151
	ds_read_b128 v[236:239], v152
	global_load_lds_dwordx4 v[142:143], off
	v_lshl_add_u64 v[220:221], s[42:43], 0, v[130:131]
	s_mov_b32 m0, s52
	s_nop 0
	global_load_lds_dwordx4 v[220:221], off
	s_barrier
	s_setprio 1
	s_waitcnt lgkmcnt(3)
	v_mfma_f32_16x16x32_bf16 v[118:121], v[212:215], v[178:181], v[118:121]
	v_mfma_f32_16x16x32_bf16 v[102:105], v[212:215], v[188:191], v[102:105]
	v_mfma_f32_16x16x32_bf16 v[86:89], v[212:215], v[196:199], v[86:89]
	v_mfma_f32_16x16x32_bf16 v[70:73], v[212:215], v[204:207], v[70:73]
	s_waitcnt lgkmcnt(2)
	v_mfma_f32_16x16x32_bf16 v[118:121], v[216:219], v[182:185], v[118:121]
	v_mfma_f32_16x16x32_bf16 v[102:105], v[216:219], v[192:195], v[102:105]
	v_mfma_f32_16x16x32_bf16 v[86:89], v[216:219], v[200:203], v[86:89]
	v_mfma_f32_16x16x32_bf16 v[70:73], v[216:219], v[208:211], v[70:73]
	s_waitcnt lgkmcnt(1)
	v_mfma_f32_16x16x32_bf16 v[114:117], v[232:235], v[178:181], v[114:117]
	v_mfma_f32_16x16x32_bf16 v[98:101], v[232:235], v[188:191], v[98:101]
	v_mfma_f32_16x16x32_bf16 v[82:85], v[232:235], v[196:199], v[82:85]
	v_mfma_f32_16x16x32_bf16 v[66:69], v[232:235], v[204:207], v[66:69]
	s_waitcnt lgkmcnt(0)
	v_mfma_f32_16x16x32_bf16 v[114:117], v[236:239], v[182:185], v[114:117]
	v_mfma_f32_16x16x32_bf16 v[98:101], v[236:239], v[192:195], v[98:101]
	v_mfma_f32_16x16x32_bf16 v[82:85], v[236:239], v[200:203], v[82:85]
	v_mfma_f32_16x16x32_bf16 v[66:69], v[236:239], v[208:211], v[66:69]
	s_setprio 0
	s_mov_b32 m0, s50
	v_lshl_add_u64 v[226:227], s[44:45], 0, v[136:137]
	s_barrier
	ds_read_b128 v[178:181], v0 offset:16384
	ds_read_b128 v[182:185], v0 offset:17408
	ds_read_b128 v[188:191], v0 offset:18432
	ds_read_b128 v[192:195], v0 offset:19456
	ds_read_b128 v[196:199], v0 offset:20480
	ds_read_b128 v[200:203], v0 offset:21504
	ds_read_b128 v[204:207], v0 offset:22528
	ds_read_b128 v[208:211], v0 offset:23552
	global_load_lds_dwordx4 v[226:227], off
	v_lshl_add_u64 v[240:241], s[44:45], 0, v[132:133]
	s_mov_b32 m0, s53
	s_nop 0
	global_load_lds_dwordx4 v[240:241], off
	s_barrier
	s_setprio 1
	s_waitcnt lgkmcnt(7)
	v_mfma_f32_16x16x32_bf16 v[62:65], v[162:165], v[178:181], v[62:65]
	v_mfma_f32_16x16x32_bf16 v[58:61], v[170:173], v[178:181], v[58:61]
	s_waitcnt lgkmcnt(6)
	v_mfma_f32_16x16x32_bf16 v[62:65], v[166:169], v[182:185], v[62:65]
	v_mfma_f32_16x16x32_bf16 v[58:61], v[174:177], v[182:185], v[58:61]
	s_waitcnt lgkmcnt(5)
	v_mfma_f32_16x16x32_bf16 v[46:49], v[162:165], v[188:191], v[46:49]
	v_mfma_f32_16x16x32_bf16 v[42:45], v[170:173], v[188:191], v[42:45]
	s_waitcnt lgkmcnt(4)
	v_mfma_f32_16x16x32_bf16 v[46:49], v[166:169], v[192:195], v[46:49]
	v_mfma_f32_16x16x32_bf16 v[42:45], v[174:177], v[192:195], v[42:45]
	s_waitcnt lgkmcnt(3)
	v_mfma_f32_16x16x32_bf16 v[30:33], v[162:165], v[196:199], v[30:33]
	v_mfma_f32_16x16x32_bf16 v[26:29], v[170:173], v[196:199], v[26:29]
	s_waitcnt lgkmcnt(2)
	v_mfma_f32_16x16x32_bf16 v[30:33], v[166:169], v[200:203], v[30:33]
	v_mfma_f32_16x16x32_bf16 v[26:29], v[174:177], v[200:203], v[26:29]
	s_waitcnt lgkmcnt(1)
	v_mfma_f32_16x16x32_bf16 v[14:17], v[162:165], v[204:207], v[14:17]
	v_mfma_f32_16x16x32_bf16 v[10:13], v[170:173], v[204:207], v[10:13]
	s_waitcnt lgkmcnt(0)
	v_mfma_f32_16x16x32_bf16 v[14:17], v[166:169], v[208:211], v[14:17]
	v_mfma_f32_16x16x32_bf16 v[10:13], v[174:177], v[208:211], v[10:13]
	s_setprio 0
	s_barrier
	s_add_u32 s70, s42, 0x20000
	s_addc_u32 s71, s43, 0
	s_mov_b32 m0, s54
	v_lshl_add_u64 v[162:163], s[70:71], 0, v[134:135]
	global_load_lds_dwordx4 v[162:163], off
	v_lshl_add_u64 v[162:163], s[70:71], 0, v[130:131]
	s_mov_b32 m0, s55
	s_nop 0
	global_load_lds_dwordx4 v[162:163], off
	s_waitcnt vmcnt(6)
	s_barrier
	s_setprio 1
	v_mfma_f32_16x16x32_bf16 v[54:57], v[212:215], v[178:181], v[54:57]
	v_mfma_f32_16x16x32_bf16 v[50:53], v[232:235], v[178:181], v[50:53]
	v_mfma_f32_16x16x32_bf16 v[38:41], v[212:215], v[188:191], v[38:41]
	v_mfma_f32_16x16x32_bf16 v[34:37], v[232:235], v[188:191], v[34:37]
	v_mfma_f32_16x16x32_bf16 v[22:25], v[212:215], v[196:199], v[22:25]
	v_mfma_f32_16x16x32_bf16 v[18:21], v[232:235], v[196:199], v[18:21]
	v_mfma_f32_16x16x32_bf16 v[6:9], v[212:215], v[204:207], v[6:9]
	v_mfma_f32_16x16x32_bf16 v[2:5], v[232:235], v[204:207], v[2:5]
	v_mfma_f32_16x16x32_bf16 v[54:57], v[216:219], v[182:185], v[54:57]
	v_mfma_f32_16x16x32_bf16 v[50:53], v[236:239], v[182:185], v[50:53]
	v_mfma_f32_16x16x32_bf16 v[38:41], v[216:219], v[192:195], v[38:41]
	v_mfma_f32_16x16x32_bf16 v[34:37], v[236:239], v[192:195], v[34:37]
	v_mfma_f32_16x16x32_bf16 v[22:25], v[216:219], v[200:203], v[22:25]
	v_mfma_f32_16x16x32_bf16 v[18:21], v[236:239], v[200:203], v[18:21]
	v_mfma_f32_16x16x32_bf16 v[6:9], v[216:219], v[208:211], v[6:9]
	v_mfma_f32_16x16x32_bf16 v[2:5], v[236:239], v[208:211], v[2:5]
	s_setprio 0
	s_barrier
	ds_read_b128 v[162:165], v153
	ds_read_b128 v[166:169], v154
	ds_read_b128 v[170:173], v155
	ds_read_b128 v[174:177], v156
	s_add_u32 s44, s44, 0x80000
	s_addc_u32 s45, s45, 0
	s_mov_b32 m0, s56
	v_lshl_add_u64 v[212:213], s[44:45], 0, v[136:137]
	ds_read_b128 v[178:181], v0 offset:32768
	ds_read_b128 v[182:185], v0 offset:33792
	ds_read_b128 v[188:191], v0 offset:34816
	ds_read_b128 v[192:195], v0 offset:35840
	ds_read_b128 v[196:199], v0 offset:36864
	ds_read_b128 v[200:203], v0 offset:37888
	ds_read_b128 v[204:207], v0 offset:38912
	ds_read_b128 v[208:211], v0 offset:39936
	global_load_lds_dwordx4 v[212:213], off
	v_lshl_add_u64 v[212:213], s[44:45], 0, v[132:133]
	s_mov_b32 m0, s57
	s_nop 0
	global_load_lds_dwordx4 v[212:213], off
	s_waitcnt lgkmcnt(8)
	s_barrier
	s_setprio 1
	s_waitcnt lgkmcnt(7)
	v_mfma_f32_16x16x32_bf16 v[126:129], v[162:165], v[178:181], v[126:129]
	v_mfma_f32_16x16x32_bf16 v[122:125], v[170:173], v[178:181], v[122:125]
	s_waitcnt lgkmcnt(6)
	v_mfma_f32_16x16x32_bf16 v[126:129], v[166:169], v[182:185], v[126:129]
	v_mfma_f32_16x16x32_bf16 v[122:125], v[174:177], v[182:185], v[122:125]
	s_waitcnt lgkmcnt(5)
	v_mfma_f32_16x16x32_bf16 v[110:113], v[162:165], v[188:191], v[110:113]
	v_mfma_f32_16x16x32_bf16 v[106:109], v[170:173], v[188:191], v[106:109]
	s_waitcnt lgkmcnt(4)
	v_mfma_f32_16x16x32_bf16 v[110:113], v[166:169], v[192:195], v[110:113]
	v_mfma_f32_16x16x32_bf16 v[106:109], v[174:177], v[192:195], v[106:109]
	s_waitcnt lgkmcnt(3)
	v_mfma_f32_16x16x32_bf16 v[94:97], v[162:165], v[196:199], v[94:97]
	v_mfma_f32_16x16x32_bf16 v[90:93], v[170:173], v[196:199], v[90:93]
	s_waitcnt lgkmcnt(2)
	v_mfma_f32_16x16x32_bf16 v[94:97], v[166:169], v[200:203], v[94:97]
	v_mfma_f32_16x16x32_bf16 v[90:93], v[174:177], v[200:203], v[90:93]
	s_waitcnt lgkmcnt(1)
	v_mfma_f32_16x16x32_bf16 v[78:81], v[162:165], v[204:207], v[78:81]
	v_mfma_f32_16x16x32_bf16 v[74:77], v[170:173], v[204:207], v[74:77]
	s_waitcnt lgkmcnt(0)
	v_mfma_f32_16x16x32_bf16 v[78:81], v[166:169], v[208:211], v[78:81]
	v_mfma_f32_16x16x32_bf16 v[74:77], v[174:177], v[208:211], v[74:77]
	s_setprio 0
	s_barrier
	s_mov_b32 m0, s59
	v_lshl_add_u64 v[142:143], v[142:143], 0, s[24:25]
	ds_read_b128 v[212:215], v157
	ds_read_b128 v[216:219], v158
	ds_read_b128 v[232:235], v159
	ds_read_b128 v[236:239], v160
	global_load_lds_dwordx4 v[142:143], off
	v_lshl_add_u64 v[142:143], v[220:221], 0, s[24:25]
	s_mov_b32 m0, s60
	s_nop 0
	global_load_lds_dwordx4 v[142:143], off
	s_barrier
	s_setprio 1
	s_waitcnt lgkmcnt(3)
	v_mfma_f32_16x16x32_bf16 v[118:121], v[212:215], v[178:181], v[118:121]
	v_mfma_f32_16x16x32_bf16 v[102:105], v[212:215], v[188:191], v[102:105]
	v_mfma_f32_16x16x32_bf16 v[86:89], v[212:215], v[196:199], v[86:89]
	v_mfma_f32_16x16x32_bf16 v[70:73], v[212:215], v[204:207], v[70:73]
	s_waitcnt lgkmcnt(2)
	v_mfma_f32_16x16x32_bf16 v[118:121], v[216:219], v[182:185], v[118:121]
	v_mfma_f32_16x16x32_bf16 v[102:105], v[216:219], v[192:195], v[102:105]
	v_mfma_f32_16x16x32_bf16 v[86:89], v[216:219], v[200:203], v[86:89]
	v_mfma_f32_16x16x32_bf16 v[70:73], v[216:219], v[208:211], v[70:73]
	s_waitcnt lgkmcnt(1)
	v_mfma_f32_16x16x32_bf16 v[114:117], v[232:235], v[178:181], v[114:117]
	v_mfma_f32_16x16x32_bf16 v[98:101], v[232:235], v[188:191], v[98:101]
	v_mfma_f32_16x16x32_bf16 v[82:85], v[232:235], v[196:199], v[82:85]
	v_mfma_f32_16x16x32_bf16 v[66:69], v[232:235], v[204:207], v[66:69]
	s_waitcnt lgkmcnt(0)
	v_mfma_f32_16x16x32_bf16 v[114:117], v[236:239], v[182:185], v[114:117]
	v_mfma_f32_16x16x32_bf16 v[98:101], v[236:239], v[192:195], v[98:101]
	v_mfma_f32_16x16x32_bf16 v[82:85], v[236:239], v[200:203], v[82:85]
	v_mfma_f32_16x16x32_bf16 v[66:69], v[236:239], v[208:211], v[66:69]
	s_setprio 0
	s_mov_b32 m0, s61
	v_lshl_add_u64 v[142:143], v[226:227], 0, s[24:25]
	s_barrier
	ds_read_b128 v[178:181], v0 offset:49152
	ds_read_b128 v[182:185], v0 offset:50176
	ds_read_b128 v[188:191], v0 offset:51200
	ds_read_b128 v[192:195], v0 offset:52224
	ds_read_b128 v[196:199], v0 offset:53248
	ds_read_b128 v[200:203], v0 offset:54272
	ds_read_b128 v[204:207], v0 offset:55296
	ds_read_b128 v[208:211], v0 offset:56320
	global_load_lds_dwordx4 v[142:143], off
	v_lshl_add_u64 v[142:143], v[240:241], 0, s[24:25]
	s_mov_b32 m0, s62
	s_nop 0
	global_load_lds_dwordx4 v[142:143], off
	s_barrier
	s_setprio 1
	s_waitcnt lgkmcnt(7)
	v_mfma_f32_16x16x32_bf16 v[62:65], v[162:165], v[178:181], v[62:65]
	v_mfma_f32_16x16x32_bf16 v[58:61], v[170:173], v[178:181], v[58:61]
	s_waitcnt lgkmcnt(6)
	v_mfma_f32_16x16x32_bf16 v[62:65], v[166:169], v[182:185], v[62:65]
	v_mfma_f32_16x16x32_bf16 v[58:61], v[174:177], v[182:185], v[58:61]
	s_waitcnt lgkmcnt(5)
	v_mfma_f32_16x16x32_bf16 v[46:49], v[162:165], v[188:191], v[46:49]
	v_mfma_f32_16x16x32_bf16 v[42:45], v[170:173], v[188:191], v[42:45]
	s_waitcnt lgkmcnt(4)
	v_mfma_f32_16x16x32_bf16 v[46:49], v[166:169], v[192:195], v[46:49]
	v_mfma_f32_16x16x32_bf16 v[42:45], v[174:177], v[192:195], v[42:45]
	s_waitcnt lgkmcnt(3)
	v_mfma_f32_16x16x32_bf16 v[30:33], v[162:165], v[196:199], v[30:33]
	v_mfma_f32_16x16x32_bf16 v[26:29], v[170:173], v[196:199], v[26:29]
	s_waitcnt lgkmcnt(2)
	v_mfma_f32_16x16x32_bf16 v[30:33], v[166:169], v[200:203], v[30:33]
	v_mfma_f32_16x16x32_bf16 v[26:29], v[174:177], v[200:203], v[26:29]
	s_waitcnt lgkmcnt(1)
	v_mfma_f32_16x16x32_bf16 v[14:17], v[162:165], v[204:207], v[14:17]
	v_mfma_f32_16x16x32_bf16 v[10:13], v[170:173], v[204:207], v[10:13]
	s_waitcnt lgkmcnt(0)
	v_mfma_f32_16x16x32_bf16 v[14:17], v[166:169], v[208:211], v[14:17]
	v_mfma_f32_16x16x32_bf16 v[10:13], v[174:177], v[208:211], v[10:13]
	s_setprio 0
	s_barrier
	s_add_u32 s42, s42, 0x20080
	s_addc_u32 s43, s43, 0
	s_mov_b32 m0, s63
	v_lshl_add_u64 v[142:143], s[42:43], 0, v[134:135]
	global_load_lds_dwordx4 v[142:143], off
	v_lshl_add_u64 v[142:143], s[42:43], 0, v[130:131]
	s_mov_b32 m0, s64
	s_nop 0
	global_load_lds_dwordx4 v[142:143], off
	s_waitcnt vmcnt(6)
	s_barrier
	s_setprio 1
	v_mfma_f32_16x16x32_bf16 v[54:57], v[212:215], v[178:181], v[54:57]
	v_mfma_f32_16x16x32_bf16 v[50:53], v[232:235], v[178:181], v[50:53]
	v_mfma_f32_16x16x32_bf16 v[38:41], v[212:215], v[188:191], v[38:41]
	v_mfma_f32_16x16x32_bf16 v[34:37], v[232:235], v[188:191], v[34:37]
	v_mfma_f32_16x16x32_bf16 v[22:25], v[212:215], v[196:199], v[22:25]
	v_mfma_f32_16x16x32_bf16 v[18:21], v[232:235], v[196:199], v[18:21]
	v_mfma_f32_16x16x32_bf16 v[6:9], v[212:215], v[204:207], v[6:9]
	v_mfma_f32_16x16x32_bf16 v[2:5], v[232:235], v[204:207], v[2:5]
	v_mfma_f32_16x16x32_bf16 v[54:57], v[216:219], v[182:185], v[54:57]
	v_mfma_f32_16x16x32_bf16 v[50:53], v[236:239], v[182:185], v[50:53]
	v_mfma_f32_16x16x32_bf16 v[38:41], v[216:219], v[192:195], v[38:41]
	v_mfma_f32_16x16x32_bf16 v[34:37], v[236:239], v[192:195], v[34:37]
	v_mfma_f32_16x16x32_bf16 v[22:25], v[216:219], v[200:203], v[22:25]
	v_mfma_f32_16x16x32_bf16 v[18:21], v[236:239], v[200:203], v[18:21]
	v_mfma_f32_16x16x32_bf16 v[6:9], v[216:219], v[208:211], v[6:9]
	v_mfma_f32_16x16x32_bf16 v[2:5], v[236:239], v[208:211], v[2:5]
	s_setprio 0
	s_add_i32 s69, s69, 2
	s_add_u32 s6, s6, 0x100
	s_addc_u32 s7, s7, 0
	s_add_u32 s67, s67, 0x100
	s_addc_u32 s68, s68, 0
	s_cmp_gt_u32 s69, 5
	s_barrier
	s_cbranch_scc0 .LBB0_716
	v_pk_mul_f32 v[122:123], v[122:123], 4.0 op_sel_hi:[1,0]
	v_mov_b32_e32 v165, v1
	v_cvt_pk_fp8_f32 v165, v122, v123
	v_pk_mul_f32 v[114:115], v[114:115], 4.0 op_sel_hi:[1,0]
	v_mov_b32_e32 v123, v1
	v_cvt_pk_fp8_f32 v123, v114, v115
	v_pk_mul_f32 v[116:117], v[116:117], 4.0 op_sel_hi:[1,0]
	v_pk_mul_f32 v[106:107], v[106:107], 4.0 op_sel_hi:[1,0]
	v_pk_mul_f32 v[98:99], v[98:99], 4.0 op_sel_hi:[1,0]
	v_cvt_pk_fp8_f32 v123, v116, v117 op_sel:[0,0,1]
	v_mov_b32_e32 v117, v1
	v_cvt_pk_fp8_f32 v117, v106, v107
	v_mov_b32_e32 v107, v1
	v_cvt_pk_fp8_f32 v107, v98, v99
	v_pk_mul_f32 v[100:101], v[100:101], 4.0 op_sel_hi:[1,0]
	v_pk_mul_f32 v[90:91], v[90:91], 4.0 op_sel_hi:[1,0]
	v_pk_mul_f32 v[82:83], v[82:83], 4.0 op_sel_hi:[1,0]
	v_cvt_pk_fp8_f32 v107, v100, v101 op_sel:[0,0,1]
	v_mov_b32_e32 v101, v1
	v_cvt_pk_fp8_f32 v101, v90, v91
	v_mov_b32_e32 v91, v1
	v_cvt_pk_fp8_f32 v91, v82, v83
	v_pk_mul_f32 v[84:85], v[84:85], 4.0 op_sel_hi:[1,0]
	v_pk_mul_f32 v[74:75], v[74:75], 4.0 op_sel_hi:[1,0]
	v_pk_mul_f32 v[66:67], v[66:67], 4.0 op_sel_hi:[1,0]
	v_cvt_pk_fp8_f32 v91, v84, v85 op_sel:[0,0,1]
	v_mov_b32_e32 v85, v1
	v_cvt_pk_fp8_f32 v85, v74, v75
	v_mov_b32_e32 v75, v1
	v_cvt_pk_fp8_f32 v75, v66, v67
	v_pk_mul_f32 v[68:69], v[68:69], 4.0 op_sel_hi:[1,0]
	v_pk_mul_f32 v[58:59], v[58:59], 4.0 op_sel_hi:[1,0]
	v_pk_mul_f32 v[50:51], v[50:51], 4.0 op_sel_hi:[1,0]
	v_cvt_pk_fp8_f32 v75, v68, v69 op_sel:[0,0,1]
	v_mov_b32_e32 v69, v1
	v_cvt_pk_fp8_f32 v69, v58, v59
	v_mov_b32_e32 v59, v1
	v_cvt_pk_fp8_f32 v59, v50, v51
	v_pk_mul_f32 v[52:53], v[52:53], 4.0 op_sel_hi:[1,0]
	v_pk_mul_f32 v[42:43], v[42:43], 4.0 op_sel_hi:[1,0]
	v_pk_mul_f32 v[34:35], v[34:35], 4.0 op_sel_hi:[1,0]
	v_cvt_pk_fp8_f32 v59, v52, v53 op_sel:[0,0,1]
	v_mov_b32_e32 v53, v1
	v_cvt_pk_fp8_f32 v53, v42, v43
	v_mov_b32_e32 v43, v1
	v_cvt_pk_fp8_f32 v43, v34, v35
	v_pk_mul_f32 v[36:37], v[36:37], 4.0 op_sel_hi:[1,0]
	v_pk_mul_f32 v[26:27], v[26:27], 4.0 op_sel_hi:[1,0]
	v_pk_mul_f32 v[18:19], v[18:19], 4.0 op_sel_hi:[1,0]
	v_cvt_pk_fp8_f32 v43, v36, v37 op_sel:[0,0,1]
	v_mov_b32_e32 v37, v1
	v_cvt_pk_fp8_f32 v37, v26, v27
	v_mov_b32_e32 v27, v1
	v_cvt_pk_fp8_f32 v27, v18, v19
	v_mbcnt_lo_u32_b32 v0, -1, 0
	v_mbcnt_hi_u32_b32 v0, -1, v0
	v_readlane_b32 s11, v252, 51
	v_and_b32_e32 v142, 15, v0
	v_readlane_b32 s13, v252, 52
	s_ashr_i32 s6, s28, 5
	v_pk_mul_f32 v[20:21], v[20:21], 4.0 op_sel_hi:[1,0]
	s_ashr_i32 s7, s6, 31
	s_lshl_b32 s42, s28, 8
	v_lshl_or_b32 v142, s11, 6, v142
	v_cvt_pk_fp8_f32 v27, v20, v21 op_sel:[0,0,1]
	v_pk_mul_f32 v[10:11], v[10:11], 4.0 op_sel_hi:[1,0]
	v_mov_b32_e32 v21, v1
	s_lshl_b64 s[6:7], s[6:7], 11
	s_and_b32 s42, s42, 0x700
	v_pk_mul_f32 v[126:127], v[126:127], 4.0 op_sel_hi:[1,0]
	v_mov_b32_e32 v164, v1
	v_pk_mul_f32 v[118:119], v[118:119], 4.0 op_sel_hi:[1,0]
	v_mov_b32_e32 v122, v1
	v_or_b32_e32 v114, 16, v142
	v_pk_mul_f32 v[110:111], v[110:111], 4.0 op_sel_hi:[1,0]
	v_mov_b32_e32 v116, v1
	v_pk_mul_f32 v[102:103], v[102:103], 4.0 op_sel_hi:[1,0]
	v_mov_b32_e32 v106, v1
	v_or_b32_e32 v98, 32, v142
	v_pk_mul_f32 v[94:95], v[94:95], 4.0 op_sel_hi:[1,0]
	v_mov_b32_e32 v100, v1
	v_pk_mul_f32 v[86:87], v[86:87], 4.0 op_sel_hi:[1,0]
	v_mov_b32_e32 v90, v1
	v_or_b32_e32 v82, 48, v142
	v_pk_mul_f32 v[78:79], v[78:79], 4.0 op_sel_hi:[1,0]
	v_mov_b32_e32 v84, v1
	v_pk_mul_f32 v[70:71], v[70:71], 4.0 op_sel_hi:[1,0]
	v_mov_b32_e32 v74, v1
	v_add_u32_e32 v66, 0x80, v142
	v_pk_mul_f32 v[62:63], v[62:63], 4.0 op_sel_hi:[1,0]
	v_mov_b32_e32 v68, v1
	v_pk_mul_f32 v[54:55], v[54:55], 4.0 op_sel_hi:[1,0]
	v_mov_b32_e32 v58, v1
	v_add_u32_e32 v50, 0x90, v142
	v_pk_mul_f32 v[46:47], v[46:47], 4.0 op_sel_hi:[1,0]
	v_mov_b32_e32 v52, v1
	v_pk_mul_f32 v[38:39], v[38:39], 4.0 op_sel_hi:[1,0]
	v_mov_b32_e32 v42, v1
	v_add_u32_e32 v34, 0xa0, v142
	v_pk_mul_f32 v[30:31], v[30:31], 4.0 op_sel_hi:[1,0]
	v_mov_b32_e32 v36, v1
	v_pk_mul_f32 v[22:23], v[22:23], 4.0 op_sel_hi:[1,0]
	v_mov_b32_e32 v26, v1
	v_add_u32_e32 v18, 0xb0, v142
	v_pk_mul_f32 v[14:15], v[14:15], 4.0 op_sel_hi:[1,0]
	v_mov_b32_e32 v20, v1
	v_cvt_pk_fp8_f32 v21, v10, v11
	v_pk_mul_f32 v[6:7], v[6:7], 4.0 op_sel_hi:[1,0]
	v_pk_mul_f32 v[2:3], v[2:3], 4.0 op_sel_hi:[1,0]
	v_mov_b32_e32 v10, v1
	v_mov_b32_e32 v11, v1
	s_or_b32 s6, s6, s42
	v_ashrrev_i32_e32 v143, 31, v142
	v_cvt_pk_fp8_f32 v164, v126, v127
	v_cvt_pk_fp8_f32 v122, v118, v119
	v_ashrrev_i32_e32 v115, 31, v114
	v_cvt_pk_fp8_f32 v116, v110, v111
	v_cvt_pk_fp8_f32 v106, v102, v103
	v_ashrrev_i32_e32 v99, 31, v98
	v_cvt_pk_fp8_f32 v100, v94, v95
	v_cvt_pk_fp8_f32 v90, v86, v87
	v_ashrrev_i32_e32 v83, 31, v82
	v_cvt_pk_fp8_f32 v84, v78, v79
	v_cvt_pk_fp8_f32 v74, v70, v71
	v_ashrrev_i32_e32 v67, 31, v66
	v_cvt_pk_fp8_f32 v68, v62, v63
	v_cvt_pk_fp8_f32 v58, v54, v55
	v_ashrrev_i32_e32 v51, 31, v50
	v_cvt_pk_fp8_f32 v52, v46, v47
	v_cvt_pk_fp8_f32 v42, v38, v39
	v_ashrrev_i32_e32 v35, 31, v34
	v_cvt_pk_fp8_f32 v36, v30, v31
	v_cvt_pk_fp8_f32 v26, v22, v23
	v_ashrrev_i32_e32 v19, 31, v18
	v_cvt_pk_fp8_f32 v20, v14, v15
	v_cvt_pk_fp8_f32 v10, v6, v7
	v_cvt_pk_fp8_f32 v11, v2, v3
	v_lshl_add_u64 v[162:163], s[6:7], 0, v[142:143]
	v_lshl_add_u64 v[114:115], s[6:7], 0, v[114:115]
	v_lshl_add_u64 v[98:99], s[6:7], 0, v[98:99]
	v_lshl_add_u64 v[82:83], s[6:7], 0, v[82:83]
	v_lshl_add_u64 v[66:67], s[6:7], 0, v[66:67]
	v_lshl_add_u64 v[50:51], s[6:7], 0, v[50:51]
	v_lshl_add_u64 v[34:35], s[6:7], 0, v[34:35]
	v_lshl_add_u64 v[18:19], s[6:7], 0, v[18:19]
	s_lshl_b32 s11, s28, 6
	v_lshlrev_b64 v[162:163], 11, v[162:163]
	v_lshlrev_b64 v[114:115], 11, v[114:115]
	v_lshlrev_b64 v[98:99], 11, v[98:99]
	v_lshlrev_b64 v[82:83], 11, v[82:83]
	v_lshlrev_b64 v[66:67], 11, v[66:67]
	v_lshlrev_b64 v[50:51], 11, v[50:51]
	v_lshlrev_b64 v[34:35], 11, v[34:35]
	v_lshlrev_b64 v[18:19], 11, v[18:19]
	s_and_b32 s28, s11, 0x600
	v_lshl_add_u64 v[162:163], s[8:9], 0, v[162:163]
	s_lshl_b32 s44, s66, 8
	v_pk_mul_f32 v[128:129], v[128:129], 4.0 op_sel_hi:[1,0]
	v_pk_mul_f32 v[124:125], v[124:125], 4.0 op_sel_hi:[1,0]
	v_pk_mul_f32 v[120:121], v[120:121], 4.0 op_sel_hi:[1,0]
	v_lshl_add_u64 v[114:115], s[8:9], 0, v[114:115]
	v_pk_mul_f32 v[112:113], v[112:113], 4.0 op_sel_hi:[1,0]
	v_pk_mul_f32 v[108:109], v[108:109], 4.0 op_sel_hi:[1,0]
	v_pk_mul_f32 v[104:105], v[104:105], 4.0 op_sel_hi:[1,0]
	v_lshl_add_u64 v[98:99], s[8:9], 0, v[98:99]
	v_pk_mul_f32 v[96:97], v[96:97], 4.0 op_sel_hi:[1,0]
	v_pk_mul_f32 v[92:93], v[92:93], 4.0 op_sel_hi:[1,0]
	v_pk_mul_f32 v[88:89], v[88:89], 4.0 op_sel_hi:[1,0]
	v_lshl_add_u64 v[82:83], s[8:9], 0, v[82:83]
	v_pk_mul_f32 v[80:81], v[80:81], 4.0 op_sel_hi:[1,0]
	v_pk_mul_f32 v[76:77], v[76:77], 4.0 op_sel_hi:[1,0]
	v_pk_mul_f32 v[72:73], v[72:73], 4.0 op_sel_hi:[1,0]
	v_lshl_add_u64 v[66:67], s[8:9], 0, v[66:67]
	v_pk_mul_f32 v[64:65], v[64:65], 4.0 op_sel_hi:[1,0]
	v_pk_mul_f32 v[60:61], v[60:61], 4.0 op_sel_hi:[1,0]
	v_pk_mul_f32 v[56:57], v[56:57], 4.0 op_sel_hi:[1,0]
	v_lshl_add_u64 v[50:51], s[8:9], 0, v[50:51]
	v_pk_mul_f32 v[48:49], v[48:49], 4.0 op_sel_hi:[1,0]
	v_pk_mul_f32 v[44:45], v[44:45], 4.0 op_sel_hi:[1,0]
	v_pk_mul_f32 v[40:41], v[40:41], 4.0 op_sel_hi:[1,0]
	v_lshl_add_u64 v[34:35], s[8:9], 0, v[34:35]
	v_pk_mul_f32 v[32:33], v[32:33], 4.0 op_sel_hi:[1,0]
	v_pk_mul_f32 v[28:29], v[28:29], 4.0 op_sel_hi:[1,0]
	v_pk_mul_f32 v[24:25], v[24:25], 4.0 op_sel_hi:[1,0]
	v_lshl_add_u64 v[18:19], s[8:9], 0, v[18:19]
	v_pk_mul_f32 v[16:17], v[16:17], 4.0 op_sel_hi:[1,0]
	v_pk_mul_f32 v[12:13], v[12:13], 4.0 op_sel_hi:[1,0]
	v_pk_mul_f32 v[8:9], v[8:9], 4.0 op_sel_hi:[1,0]
	v_pk_mul_f32 v[4:5], v[4:5], 4.0 op_sel_hi:[1,0]
	s_lshl_b32 s42, s13, 5
	v_lshl_add_u64 v[162:163], v[162:163], 0, s[28:29]
	s_ashr_i32 s45, s44, 31
	v_cvt_pk_fp8_f32 v164, v128, v129 op_sel:[0,0,1]
	v_cvt_pk_fp8_f32 v165, v124, v125 op_sel:[0,0,1]
	v_cvt_pk_fp8_f32 v122, v120, v121 op_sel:[0,0,1]
	v_lshl_add_u64 v[114:115], v[114:115], 0, s[28:29]
	v_cvt_pk_fp8_f32 v116, v112, v113 op_sel:[0,0,1]
	v_cvt_pk_fp8_f32 v117, v108, v109 op_sel:[0,0,1]
	v_cvt_pk_fp8_f32 v106, v104, v105 op_sel:[0,0,1]
	v_lshl_add_u64 v[98:99], v[98:99], 0, s[28:29]
	v_cvt_pk_fp8_f32 v100, v96, v97 op_sel:[0,0,1]
	v_cvt_pk_fp8_f32 v101, v92, v93 op_sel:[0,0,1]
	v_cvt_pk_fp8_f32 v90, v88, v89 op_sel:[0,0,1]
	v_lshl_add_u64 v[82:83], v[82:83], 0, s[28:29]
	v_cvt_pk_fp8_f32 v84, v80, v81 op_sel:[0,0,1]
	v_cvt_pk_fp8_f32 v85, v76, v77 op_sel:[0,0,1]
	v_cvt_pk_fp8_f32 v74, v72, v73 op_sel:[0,0,1]
	v_lshl_add_u64 v[66:67], v[66:67], 0, s[28:29]
	v_cvt_pk_fp8_f32 v68, v64, v65 op_sel:[0,0,1]
	v_cvt_pk_fp8_f32 v69, v60, v61 op_sel:[0,0,1]
	v_cvt_pk_fp8_f32 v58, v56, v57 op_sel:[0,0,1]
	v_lshl_add_u64 v[50:51], v[50:51], 0, s[28:29]
	v_cvt_pk_fp8_f32 v52, v48, v49 op_sel:[0,0,1]
	v_cvt_pk_fp8_f32 v53, v44, v45 op_sel:[0,0,1]
	v_cvt_pk_fp8_f32 v42, v40, v41 op_sel:[0,0,1]
	v_lshl_add_u64 v[34:35], v[34:35], 0, s[28:29]
	v_cvt_pk_fp8_f32 v36, v32, v33 op_sel:[0,0,1]
	v_cvt_pk_fp8_f32 v37, v28, v29 op_sel:[0,0,1]
	v_cvt_pk_fp8_f32 v26, v24, v25 op_sel:[0,0,1]
	v_lshl_add_u64 v[18:19], v[18:19], 0, s[28:29]
	v_cvt_pk_fp8_f32 v20, v16, v17 op_sel:[0,0,1]
	v_cvt_pk_fp8_f32 v21, v12, v13 op_sel:[0,0,1]
	v_cvt_pk_fp8_f32 v10, v8, v9 op_sel:[0,0,1]
	v_cvt_pk_fp8_f32 v11, v4, v5 op_sel:[0,0,1]
	s_ashr_i32 s43, s42, 31
	v_lshrrev_b32_e32 v0, 1, v0
	v_lshl_add_u64 v[162:163], v[162:163], 0, s[44:45]
	v_lshl_add_u64 v[114:115], v[114:115], 0, s[44:45]
	v_lshl_add_u64 v[98:99], v[98:99], 0, s[44:45]
	v_lshl_add_u64 v[82:83], v[82:83], 0, s[44:45]
	v_lshl_add_u64 v[66:67], v[66:67], 0, s[44:45]
	v_lshl_add_u64 v[50:51], v[50:51], 0, s[44:45]
	v_lshl_add_u64 v[34:35], v[34:35], 0, s[44:45]
	v_lshl_add_u64 v[18:19], v[18:19], 0, s[44:45]
	v_and_b32_e32 v0, 24, v0
	v_lshl_add_u64 v[162:163], v[162:163], 0, s[42:43]
	v_lshl_add_u64 v[114:115], v[114:115], 0, s[42:43]
	v_lshl_add_u64 v[98:99], v[98:99], 0, s[42:43]
	v_lshl_add_u64 v[82:83], v[82:83], 0, s[42:43]
	v_lshl_add_u64 v[66:67], v[66:67], 0, s[42:43]
	v_lshl_add_u64 v[50:51], v[50:51], 0, s[42:43]
	v_lshl_add_u64 v[34:35], v[34:35], 0, s[42:43]
	v_lshl_add_u64 v[18:19], v[18:19], 0, s[42:43]
	v_lshl_add_u64 v[162:163], v[162:163], 0, v[0:1]
	v_lshl_add_u64 v[114:115], v[114:115], 0, v[0:1]
	v_lshl_add_u64 v[98:99], v[98:99], 0, v[0:1]
	v_lshl_add_u64 v[82:83], v[82:83], 0, v[0:1]
	v_lshl_add_u64 v[66:67], v[66:67], 0, v[0:1]
	v_lshl_add_u64 v[50:51], v[50:51], 0, v[0:1]
	v_lshl_add_u64 v[34:35], v[34:35], 0, v[0:1]
	v_lshl_add_u64 v[18:19], v[18:19], 0, v[0:1]
	s_and_b64 vcc, exec, s[4:5]
	s_mov_b32 s66, s10
	s_mov_b32 s28, s12
	s_mov_b64 s[42:43], s[34:35]
	s_mov_b64 s[44:45], s[20:21]
	global_store_dwordx2 v[162:163], v[164:165], off
	global_store_dwordx2 v[162:163], v[122:123], off offset:128
	global_store_dwordx2 v[114:115], v[116:117], off
	global_store_dwordx2 v[114:115], v[106:107], off offset:128
	global_store_dwordx2 v[98:99], v[100:101], off
	global_store_dwordx2 v[98:99], v[90:91], off offset:128
	global_store_dwordx2 v[82:83], v[84:85], off
	global_store_dwordx2 v[82:83], v[74:75], off offset:128
	global_store_dwordx2 v[66:67], v[68:69], off
	global_store_dwordx2 v[66:67], v[58:59], off offset:128
	global_store_dwordx2 v[50:51], v[52:53], off
	global_store_dwordx2 v[50:51], v[42:43], off offset:128
	global_store_dwordx2 v[34:35], v[36:37], off
	global_store_dwordx2 v[34:35], v[26:27], off offset:128
	global_store_dwordx2 v[18:19], v[20:21], off
	global_store_dwordx2 v[18:19], v[10:11], off offset:128
	s_cbranch_vccz .LBB0_707
	s_waitcnt vmcnt(0)
	s_cmpk_gt_u32 s27, 0xff
	s_cbranch_scc1 .LBB0_720
	s_barrier

.LBB0_833:
	v_mov_b64_e32 v[2:3], 0x200
	s_ashr_i32 s21, s20, 31
	v_cmp_lt_i64_e32 vcc, s[34:35], v[2:3]
	s_lshl_b64 s[34:35], s[20:21], 19
	s_add_u32 s34, s28, s34
	s_addc_u32 s35, s50, s35
	s_and_b64 s[42:43], vcc, exec
	ds_read_b128 v[2:5], v175
	ds_read_b128 v[6:9], v176
	ds_read_b128 v[10:13], v177
	ds_read_b128 v[14:17], v178
	s_cselect_b32 s21, s35, s47
	s_cselect_b32 s71, s34, s46
	s_ashr_i32 s13, s12, 31
	s_lshl_b64 s[42:43], s[12:13], 19
	s_add_u32 s42, s51, s42
	s_addc_u32 s43, s52, s43
	s_and_b64 s[48:49], vcc, exec
	s_cselect_b32 s13, s43, s45
	s_cselect_b32 s72, s42, s44
	s_add_u32 s48, s46, 0x40080
	s_addc_u32 s49, s47, 0
	s_add_i32 s73, s53, 0xc000
	v_add_u32_e32 v0, s61, v174
	v_lshl_add_u64 v[50:51], s[48:49], 0, v[164:165]
	s_mov_b32 m0, s73
	s_add_i32 s74, s53, 0xe000
	ds_read_b128 v[18:21], v0
	ds_read_b128 v[22:25], v0 offset:1024
	ds_read_b128 v[26:29], v0 offset:2048
	ds_read_b128 v[30:33], v0 offset:3072
	ds_read_b128 v[34:37], v0 offset:4096
	ds_read_b128 v[38:41], v0 offset:5120
	ds_read_b128 v[42:45], v0 offset:6144
	ds_read_b128 v[46:49], v0 offset:7168
	global_load_lds_dwordx4 v[50:51], off
	v_lshl_add_u64 v[50:51], s[48:49], 0, v[160:161]
	s_mov_b32 m0, s74
	s_nop 0
	global_load_lds_dwordx4 v[50:51], off
	s_waitcnt lgkmcnt(8)
	s_barrier
	s_setprio 1
	s_waitcnt lgkmcnt(6)
	v_mfma_scale_f32_16x16x128_f8f6f4 v[134:137], v[2:9], v[18:25], 0, v222, v222 op_sel_hi:[0,0,0]
	v_mfma_scale_f32_16x16x128_f8f6f4 v[130:133], v[10:17], v[18:25], 0, v222, v222 op_sel_hi:[0,0,0]
	s_waitcnt lgkmcnt(4)
	v_mfma_scale_f32_16x16x128_f8f6f4 v[118:121], v[2:9], v[26:33], 0, v222, v222 op_sel_hi:[0,0,0]
	v_mfma_scale_f32_16x16x128_f8f6f4 v[114:117], v[10:17], v[26:33], 0, v222, v222 op_sel_hi:[0,0,0]
	s_waitcnt lgkmcnt(2)
	v_mfma_scale_f32_16x16x128_f8f6f4 v[102:105], v[2:9], v[34:41], 0, v222, v222 op_sel_hi:[0,0,0]
	v_mfma_scale_f32_16x16x128_f8f6f4 v[98:101], v[10:17], v[34:41], 0, v222, v222 op_sel_hi:[0,0,0]
	s_waitcnt lgkmcnt(0)
	v_mfma_scale_f32_16x16x128_f8f6f4 v[74:77], v[2:9], v[42:49], 0, v222, v222 op_sel_hi:[0,0,0]
	v_mfma_scale_f32_16x16x128_f8f6f4 v[66:69], v[10:17], v[42:49], 0, v222, v222 op_sel_hi:[0,0,0]
	s_setprio 0
	s_barrier
	v_lshl_add_u64 v[150:151], s[44:45], 0, v[162:163]
	s_mov_b64 s[48:49], 0x100
	s_mov_b32 m0, s54
	v_lshl_add_u64 v[50:51], v[150:151], 0, s[48:49]
	v_lshl_add_u64 v[152:153], s[44:45], 0, v[158:159]
	ds_read_b128 v[188:191], v179
	ds_read_b128 v[192:195], v180
	ds_read_b128 v[202:205], v181
	ds_read_b128 v[206:209], v182
	global_load_lds_dwordx4 v[50:51], off
	v_lshl_add_u64 v[50:51], v[152:153], 0, s[48:49]
	s_mov_b32 m0, s55
	s_nop 0
	global_load_lds_dwordx4 v[50:51], off
	s_barrier
	s_setprio 1
	s_waitcnt lgkmcnt(2)
	v_mfma_scale_f32_16x16x128_f8f6f4 v[142:145], v[188:195], v[18:25], 0, v222, v222 op_sel_hi:[0,0,0]
	v_mfma_scale_f32_16x16x128_f8f6f4 v[126:129], v[188:195], v[26:33], 0, v222, v222 op_sel_hi:[0,0,0]
	v_mfma_scale_f32_16x16x128_f8f6f4 v[110:113], v[188:195], v[34:41], 0, v222, v222 op_sel_hi:[0,0,0]
	v_mfma_scale_f32_16x16x128_f8f6f4 v[78:81], v[188:195], v[42:49], 0, v222, v222 op_sel_hi:[0,0,0]
	s_waitcnt lgkmcnt(0)
	v_mfma_scale_f32_16x16x128_f8f6f4 v[138:141], v[202:209], v[18:25], 0, v222, v222 op_sel_hi:[0,0,0]
	v_mfma_scale_f32_16x16x128_f8f6f4 v[122:125], v[202:209], v[26:33], 0, v222, v222 op_sel_hi:[0,0,0]
	v_mfma_scale_f32_16x16x128_f8f6f4 v[106:109], v[202:209], v[34:41], 0, v222, v222 op_sel_hi:[0,0,0]
	v_mfma_scale_f32_16x16x128_f8f6f4 v[70:73], v[202:209], v[42:49], 0, v222, v222 op_sel_hi:[0,0,0]
	s_setprio 0
	v_lshl_add_u64 v[146:147], s[46:47], 0, v[164:165]
	s_mov_b32 m0, s53
	v_lshl_add_u64 v[18:19], v[146:147], 0, s[48:49]
	v_lshl_add_u64 v[148:149], s[46:47], 0, v[160:161]
	s_barrier
	ds_read_b128 v[26:29], v0 offset:16384
	ds_read_b128 v[30:33], v0 offset:17408
	ds_read_b128 v[34:37], v0 offset:18432
	ds_read_b128 v[38:41], v0 offset:19456
	ds_read_b128 v[210:213], v0 offset:20480
	ds_read_b128 v[214:217], v0 offset:21504
	ds_read_b128 v[232:235], v0 offset:22528
	ds_read_b128 v[236:239], v0 offset:23552
	global_load_lds_dwordx4 v[18:19], off
	v_lshl_add_u64 v[18:19], v[148:149], 0, s[48:49]
	s_mov_b32 m0, s56
	s_nop 0
	global_load_lds_dwordx4 v[18:19], off
	s_barrier
	s_setprio 1
	s_waitcnt lgkmcnt(6)
	v_mfma_scale_f32_16x16x128_f8f6f4 v[94:97], v[2:9], v[26:33], 0, v222, v222 op_sel_hi:[0,0,0]
	v_mfma_scale_f32_16x16x128_f8f6f4 v[90:93], v[10:17], v[26:33], 0, v222, v222 op_sel_hi:[0,0,0]
	s_waitcnt lgkmcnt(4)
	v_mfma_scale_f32_16x16x128_f8f6f4 v[62:65], v[2:9], v[34:41], 0, v222, v222 op_sel_hi:[0,0,0]
	v_mfma_scale_f32_16x16x128_f8f6f4 v[58:61], v[10:17], v[34:41], 0, v222, v222 op_sel_hi:[0,0,0]
	s_waitcnt lgkmcnt(2)
	v_mfma_scale_f32_16x16x128_f8f6f4 v[46:49], v[2:9], v[210:217], 0, v222, v222 op_sel_hi:[0,0,0]
	v_mfma_scale_f32_16x16x128_f8f6f4 v[42:45], v[10:17], v[210:217], 0, v222, v222 op_sel_hi:[0,0,0]
	s_waitcnt lgkmcnt(0)
	v_mfma_scale_f32_16x16x128_f8f6f4 v[22:25], v[2:9], v[232:239], 0, v222, v222 op_sel_hi:[0,0,0]
	v_mfma_scale_f32_16x16x128_f8f6f4 v[18:21], v[10:17], v[232:239], 0, v222, v222 op_sel_hi:[0,0,0]
	s_setprio 0
	s_barrier
	s_add_u32 s48, s44, 0x40100
	s_addc_u32 s49, s45, 0
	s_mov_b32 m0, s57
	v_lshl_add_u64 v[2:3], s[48:49], 0, v[162:163]
	global_load_lds_dwordx4 v[2:3], off
	v_lshl_add_u64 v[2:3], s[48:49], 0, v[158:159]
	s_mov_b32 m0, s58
	s_nop 0
	global_load_lds_dwordx4 v[2:3], off
	s_waitcnt vmcnt(6)
	s_barrier
	s_setprio 1
	v_mfma_scale_f32_16x16x128_f8f6f4 v[86:89], v[188:195], v[26:33], 0, v222, v222 op_sel_hi:[0,0,0]
	v_mfma_scale_f32_16x16x128_f8f6f4 v[82:85], v[202:209], v[26:33], 0, v222, v222 op_sel_hi:[0,0,0]
	v_mfma_scale_f32_16x16x128_f8f6f4 v[54:57], v[188:195], v[34:41], 0, v222, v222 op_sel_hi:[0,0,0]
	v_mfma_scale_f32_16x16x128_f8f6f4 v[50:53], v[202:209], v[34:41], 0, v222, v222 op_sel_hi:[0,0,0]
	v_mfma_scale_f32_16x16x128_f8f6f4 v[38:41], v[188:195], v[210:217], 0, v222, v222 op_sel_hi:[0,0,0]
	v_mfma_scale_f32_16x16x128_f8f6f4 v[34:37], v[202:209], v[210:217], 0, v222, v222 op_sel_hi:[0,0,0]
	v_mfma_scale_f32_16x16x128_f8f6f4 v[30:33], v[188:195], v[232:239], 0, v222, v222 op_sel_hi:[0,0,0]
	v_mfma_scale_f32_16x16x128_f8f6f4 v[26:29], v[202:209], v[232:239], 0, v222, v222 op_sel_hi:[0,0,0]
	s_setprio 0
	s_barrier
	ds_read_b128 v[2:5], v183
	ds_read_b128 v[6:9], v184
	ds_read_b128 v[10:13], v185
	ds_read_b128 v[14:17], v196
	s_add_u32 s48, s46, 0x40100
	s_addc_u32 s49, s47, 0
	s_mov_b32 m0, s59
	v_lshl_add_u64 v[154:155], s[48:49], 0, v[164:165]
	ds_read_b128 v[188:191], v0 offset:32768
	ds_read_b128 v[192:195], v0 offset:33792
	ds_read_b128 v[202:205], v0 offset:34816
	ds_read_b128 v[206:209], v0 offset:35840
	ds_read_b128 v[210:213], v0 offset:36864
	ds_read_b128 v[214:217], v0 offset:37888
	ds_read_b128 v[232:235], v0 offset:38912
	ds_read_b128 v[236:239], v0 offset:39936
	global_load_lds_dwordx4 v[154:155], off
	v_lshl_add_u64 v[154:155], s[48:49], 0, v[160:161]
	s_mov_b32 m0, s60
	s_nop 0
	global_load_lds_dwordx4 v[154:155], off
	s_waitcnt lgkmcnt(8)
	s_barrier
	s_setprio 1
	s_waitcnt lgkmcnt(6)
	v_mfma_scale_f32_16x16x128_f8f6f4 v[134:137], v[2:9], v[188:195], v[134:137], v222, v222 op_sel_hi:[0,0,0]
	v_mfma_scale_f32_16x16x128_f8f6f4 v[130:133], v[10:17], v[188:195], v[130:133], v222, v222 op_sel_hi:[0,0,0]
	s_waitcnt lgkmcnt(4)
	v_mfma_scale_f32_16x16x128_f8f6f4 v[118:121], v[2:9], v[202:209], v[118:121], v222, v222 op_sel_hi:[0,0,0]
	v_mfma_scale_f32_16x16x128_f8f6f4 v[114:117], v[10:17], v[202:209], v[114:117], v222, v222 op_sel_hi:[0,0,0]
	s_waitcnt lgkmcnt(2)
	v_mfma_scale_f32_16x16x128_f8f6f4 v[102:105], v[2:9], v[210:217], v[102:105], v222, v222 op_sel_hi:[0,0,0]
	v_mfma_scale_f32_16x16x128_f8f6f4 v[98:101], v[10:17], v[210:217], v[98:101], v222, v222 op_sel_hi:[0,0,0]
	s_waitcnt lgkmcnt(0)
	v_mfma_scale_f32_16x16x128_f8f6f4 v[74:77], v[2:9], v[232:239], v[74:77], v222, v222 op_sel_hi:[0,0,0]
	v_mfma_scale_f32_16x16x128_f8f6f4 v[66:69], v[10:17], v[232:239], v[66:69], v222, v222 op_sel_hi:[0,0,0]
	s_setprio 0
	s_barrier
	s_mov_b64 s[48:49], 0x180
	s_mov_b32 m0, s62
	v_lshl_add_u64 v[150:151], v[150:151], 0, s[48:49]
	ds_read_b128 v[240:243], v197
	ds_read_b128 v[244:247], v198
	ds_read_b128 v[166:169], v199
	ds_read_b128 v[170:173], v200
	global_load_lds_dwordx4 v[150:151], off
	v_lshl_add_u64 v[150:151], v[152:153], 0, s[48:49]
	s_mov_b32 m0, s63
	s_nop 0
	global_load_lds_dwordx4 v[150:151], off
	s_barrier
	s_setprio 1
	s_waitcnt lgkmcnt(2)
	v_mfma_scale_f32_16x16x128_f8f6f4 v[142:145], v[240:247], v[188:195], v[142:145], v222, v222 op_sel_hi:[0,0,0]
	v_mfma_scale_f32_16x16x128_f8f6f4 v[126:129], v[240:247], v[202:209], v[126:129], v222, v222 op_sel_hi:[0,0,0]
	v_mfma_scale_f32_16x16x128_f8f6f4 v[110:113], v[240:247], v[210:217], v[110:113], v222, v222 op_sel_hi:[0,0,0]
	v_mfma_scale_f32_16x16x128_f8f6f4 v[78:81], v[240:247], v[232:239], v[78:81], v222, v222 op_sel_hi:[0,0,0]
	s_waitcnt lgkmcnt(0)
	v_mfma_scale_f32_16x16x128_f8f6f4 v[138:141], v[166:173], v[188:195], v[138:141], v222, v222 op_sel_hi:[0,0,0]
	v_mfma_scale_f32_16x16x128_f8f6f4 v[122:125], v[166:173], v[202:209], v[122:125], v222, v222 op_sel_hi:[0,0,0]
	v_mfma_scale_f32_16x16x128_f8f6f4 v[106:109], v[166:173], v[210:217], v[106:109], v222, v222 op_sel_hi:[0,0,0]
	v_mfma_scale_f32_16x16x128_f8f6f4 v[70:73], v[166:173], v[232:239], v[70:73], v222, v222 op_sel_hi:[0,0,0]
	s_setprio 0
	s_mov_b32 m0, s64
	v_lshl_add_u64 v[146:147], v[146:147], 0, s[48:49]
	s_barrier
	ds_read_b128 v[150:153], v0 offset:49152
	ds_read_b128 v[154:157], v0 offset:50176
	ds_read_b128 v[188:191], v0 offset:51200
	ds_read_b128 v[192:195], v0 offset:52224
	ds_read_b128 v[202:205], v0 offset:53248
	ds_read_b128 v[206:209], v0 offset:54272
	ds_read_b128 v[210:213], v0 offset:55296
	ds_read_b128 v[214:217], v0 offset:56320
	global_load_lds_dwordx4 v[146:147], off
	v_lshl_add_u64 v[146:147], v[148:149], 0, s[48:49]
	s_mov_b32 m0, s65
	s_nop 0
	global_load_lds_dwordx4 v[146:147], off
	s_barrier
	s_setprio 1
	s_waitcnt lgkmcnt(6)
	v_mfma_scale_f32_16x16x128_f8f6f4 v[94:97], v[2:9], v[150:157], v[94:97], v222, v222 op_sel_hi:[0,0,0]
	v_mfma_scale_f32_16x16x128_f8f6f4 v[90:93], v[10:17], v[150:157], v[90:93], v222, v222 op_sel_hi:[0,0,0]
	s_waitcnt lgkmcnt(4)
	v_mfma_scale_f32_16x16x128_f8f6f4 v[62:65], v[2:9], v[188:195], v[62:65], v222, v222 op_sel_hi:[0,0,0]
	v_mfma_scale_f32_16x16x128_f8f6f4 v[58:61], v[10:17], v[188:195], v[58:61], v222, v222 op_sel_hi:[0,0,0]
	s_waitcnt lgkmcnt(2)
	v_mfma_scale_f32_16x16x128_f8f6f4 v[46:49], v[2:9], v[202:209], v[46:49], v222, v222 op_sel_hi:[0,0,0]
	v_mfma_scale_f32_16x16x128_f8f6f4 v[42:45], v[10:17], v[202:209], v[42:45], v222, v222 op_sel_hi:[0,0,0]
	s_waitcnt lgkmcnt(0)
	v_mfma_scale_f32_16x16x128_f8f6f4 v[22:25], v[2:9], v[210:217], v[22:25], v222, v222 op_sel_hi:[0,0,0]
	v_mfma_scale_f32_16x16x128_f8f6f4 v[18:21], v[10:17], v[210:217], v[18:21], v222, v222 op_sel_hi:[0,0,0]
	s_setprio 0
	s_barrier
	s_add_u32 s48, s44, 0x40180
	s_addc_u32 s49, s45, 0
	s_mov_b32 m0, s66
	v_lshl_add_u64 v[2:3], s[48:49], 0, v[162:163]
	global_load_lds_dwordx4 v[2:3], off
	v_lshl_add_u64 v[2:3], s[48:49], 0, v[158:159]
	s_mov_b32 m0, s67
	s_nop 0
	global_load_lds_dwordx4 v[2:3], off
	s_waitcnt vmcnt(6)
	s_barrier
	s_setprio 1
	v_mfma_scale_f32_16x16x128_f8f6f4 v[86:89], v[240:247], v[150:157], v[86:89], v222, v222 op_sel_hi:[0,0,0]
	v_mfma_scale_f32_16x16x128_f8f6f4 v[82:85], v[166:173], v[150:157], v[82:85], v222, v222 op_sel_hi:[0,0,0]
	v_mfma_scale_f32_16x16x128_f8f6f4 v[54:57], v[240:247], v[188:195], v[54:57], v222, v222 op_sel_hi:[0,0,0]
	v_mfma_scale_f32_16x16x128_f8f6f4 v[50:53], v[166:173], v[188:195], v[50:53], v222, v222 op_sel_hi:[0,0,0]
	v_mfma_scale_f32_16x16x128_f8f6f4 v[38:41], v[240:247], v[202:209], v[38:41], v222, v222 op_sel_hi:[0,0,0]
	v_mfma_scale_f32_16x16x128_f8f6f4 v[34:37], v[166:173], v[202:209], v[34:37], v222, v222 op_sel_hi:[0,0,0]
	v_mfma_scale_f32_16x16x128_f8f6f4 v[30:33], v[240:247], v[210:217], v[30:33], v222, v222 op_sel_hi:[0,0,0]
	v_mfma_scale_f32_16x16x128_f8f6f4 v[26:29], v[166:173], v[210:217], v[26:29], v222, v222 op_sel_hi:[0,0,0]
	s_setprio 0
	s_add_u32 s46, s46, 0x40180
	s_addc_u32 s47, s47, 0
	s_add_u32 s75, s44, 0x200
	s_addc_u32 s76, s45, 0
	s_mov_b32 s77, 0
	s_barrier
.LBB0_834:
	ds_read_b128 v[10:13], v175
	ds_read_b128 v[14:17], v176
	ds_read_b128 v[146:149], v177
	ds_read_b128 v[150:153], v178
	s_add_u32 s44, s46, 0xfffc0080
	s_addc_u32 s45, s47, -1
	s_cmp_eq_u32 s77, 12
	s_cselect_b32 s49, s21, s45
	s_cselect_b32 s48, s71, s44
	s_cselect_b32 s45, s13, s76
	s_cselect_b32 s44, s72, s75
	s_mov_b32 m0, s73
	v_lshl_add_u64 v[2:3], s[46:47], 0, v[218:219]
	ds_read_b128 v[166:169], v0
	ds_read_b128 v[170:173], v0 offset:1024
	ds_read_b128 v[188:191], v0 offset:2048
	ds_read_b128 v[192:195], v0 offset:3072
	ds_read_b128 v[202:205], v0 offset:4096
	ds_read_b128 v[206:209], v0 offset:5120
	ds_read_b128 v[210:213], v0 offset:6144
	ds_read_b128 v[214:217], v0 offset:7168
	global_load_lds_dwordx4 v[2:3], off
	v_lshl_add_u64 v[2:3], s[46:47], 0, v[220:221]
	s_mov_b32 m0, s74
	s_nop 0
	global_load_lds_dwordx4 v[2:3], off
	s_waitcnt lgkmcnt(8)
	s_barrier
	s_setprio 1
	s_waitcnt lgkmcnt(6)
	v_mfma_scale_f32_16x16x128_f8f6f4 v[134:137], v[10:17], v[166:173], v[134:137], v222, v222 op_sel_hi:[0,0,0]
	v_mfma_scale_f32_16x16x128_f8f6f4 v[130:133], v[146:153], v[166:173], v[130:133], v222, v222 op_sel_hi:[0,0,0]
	s_waitcnt lgkmcnt(4)
	v_mfma_scale_f32_16x16x128_f8f6f4 v[118:121], v[10:17], v[188:195], v[118:121], v222, v222 op_sel_hi:[0,0,0]
	v_mfma_scale_f32_16x16x128_f8f6f4 v[114:117], v[146:153], v[188:195], v[114:117], v222, v222 op_sel_hi:[0,0,0]
	s_waitcnt lgkmcnt(2)
	v_mfma_scale_f32_16x16x128_f8f6f4 v[102:105], v[10:17], v[202:209], v[102:105], v222, v222 op_sel_hi:[0,0,0]
	v_mfma_scale_f32_16x16x128_f8f6f4 v[98:101], v[146:153], v[202:209], v[98:101], v222, v222 op_sel_hi:[0,0,0]
	s_waitcnt lgkmcnt(0)
	v_mfma_scale_f32_16x16x128_f8f6f4 v[74:77], v[10:17], v[210:217], v[74:77], v222, v222 op_sel_hi:[0,0,0]
	v_mfma_scale_f32_16x16x128_f8f6f4 v[66:69], v[146:153], v[210:217], v[66:69], v222, v222 op_sel_hi:[0,0,0]
	s_setprio 0
	s_barrier
	s_mov_b32 m0, s54
	v_lshl_add_u64 v[6:7], s[44:45], 0, v[162:163]
	ds_read_b128 v[232:235], v179
	ds_read_b128 v[236:239], v180
	ds_read_b128 v[240:243], v181
	ds_read_b128 v[244:247], v182
	global_load_lds_dwordx4 v[6:7], off
	v_lshl_add_u64 v[8:9], s[44:45], 0, v[158:159]
	s_mov_b32 m0, s55
	s_nop 0
	global_load_lds_dwordx4 v[8:9], off
	s_barrier
	s_setprio 1
	s_waitcnt lgkmcnt(2)
	v_mfma_scale_f32_16x16x128_f8f6f4 v[142:145], v[232:239], v[166:173], v[142:145], v222, v222 op_sel_hi:[0,0,0]
	v_mfma_scale_f32_16x16x128_f8f6f4 v[126:129], v[232:239], v[188:195], v[126:129], v222, v222 op_sel_hi:[0,0,0]
	v_mfma_scale_f32_16x16x128_f8f6f4 v[110:113], v[232:239], v[202:209], v[110:113], v222, v222 op_sel_hi:[0,0,0]
	v_mfma_scale_f32_16x16x128_f8f6f4 v[78:81], v[232:239], v[210:217], v[78:81], v222, v222 op_sel_hi:[0,0,0]
	s_waitcnt lgkmcnt(0)
	v_mfma_scale_f32_16x16x128_f8f6f4 v[138:141], v[240:247], v[166:173], v[138:141], v222, v222 op_sel_hi:[0,0,0]
	v_mfma_scale_f32_16x16x128_f8f6f4 v[122:125], v[240:247], v[188:195], v[122:125], v222, v222 op_sel_hi:[0,0,0]
	v_mfma_scale_f32_16x16x128_f8f6f4 v[106:109], v[240:247], v[202:209], v[106:109], v222, v222 op_sel_hi:[0,0,0]
	v_mfma_scale_f32_16x16x128_f8f6f4 v[70:73], v[240:247], v[210:217], v[70:73], v222, v222 op_sel_hi:[0,0,0]
	s_setprio 0
	s_mov_b32 m0, s53
	v_lshl_add_u64 v[2:3], s[48:49], 0, v[164:165]
	s_barrier
	ds_read_b128 v[166:169], v0 offset:16384
	ds_read_b128 v[170:173], v0 offset:17408
	ds_read_b128 v[188:191], v0 offset:18432
	ds_read_b128 v[192:195], v0 offset:19456
	ds_read_b128 v[202:205], v0 offset:20480
	ds_read_b128 v[206:209], v0 offset:21504
	ds_read_b128 v[210:213], v0 offset:22528
	ds_read_b128 v[214:217], v0 offset:23552
	global_load_lds_dwordx4 v[2:3], off
	v_lshl_add_u64 v[4:5], s[48:49], 0, v[160:161]
	s_mov_b32 m0, s56
	s_nop 0
	global_load_lds_dwordx4 v[4:5], off
	s_barrier
	s_setprio 1
	s_waitcnt lgkmcnt(6)
	v_mfma_scale_f32_16x16x128_f8f6f4 v[94:97], v[10:17], v[166:173], v[94:97], v222, v222 op_sel_hi:[0,0,0]
	v_mfma_scale_f32_16x16x128_f8f6f4 v[90:93], v[146:153], v[166:173], v[90:93], v222, v222 op_sel_hi:[0,0,0]
	s_waitcnt lgkmcnt(4)
	v_mfma_scale_f32_16x16x128_f8f6f4 v[62:65], v[10:17], v[188:195], v[62:65], v222, v222 op_sel_hi:[0,0,0]
	v_mfma_scale_f32_16x16x128_f8f6f4 v[58:61], v[146:153], v[188:195], v[58:61], v222, v222 op_sel_hi:[0,0,0]
	s_waitcnt lgkmcnt(2)
	v_mfma_scale_f32_16x16x128_f8f6f4 v[46:49], v[10:17], v[202:209], v[46:49], v222, v222 op_sel_hi:[0,0,0]
	v_mfma_scale_f32_16x16x128_f8f6f4 v[42:45], v[146:153], v[202:209], v[42:45], v222, v222 op_sel_hi:[0,0,0]
	s_waitcnt lgkmcnt(0)
	v_mfma_scale_f32_16x16x128_f8f6f4 v[22:25], v[10:17], v[210:217], v[22:25], v222, v222 op_sel_hi:[0,0,0]
	v_mfma_scale_f32_16x16x128_f8f6f4 v[18:21], v[146:153], v[210:217], v[18:21], v222, v222 op_sel_hi:[0,0,0]
	s_setprio 0
	s_barrier
	s_add_u32 s78, s44, 0x40000
	s_addc_u32 s79, s45, 0
	s_mov_b32 m0, s57
	v_lshl_add_u64 v[10:11], s[78:79], 0, v[162:163]
	global_load_lds_dwordx4 v[10:11], off
	v_lshl_add_u64 v[10:11], s[78:79], 0, v[158:159]
	s_mov_b32 m0, s58
	s_nop 0
	global_load_lds_dwordx4 v[10:11], off
	s_waitcnt vmcnt(6)
	s_barrier
	s_setprio 1
	v_mfma_scale_f32_16x16x128_f8f6f4 v[86:89], v[232:239], v[166:173], v[86:89], v222, v222 op_sel_hi:[0,0,0]
	v_mfma_scale_f32_16x16x128_f8f6f4 v[82:85], v[240:247], v[166:173], v[82:85], v222, v222 op_sel_hi:[0,0,0]
	v_mfma_scale_f32_16x16x128_f8f6f4 v[54:57], v[232:239], v[188:195], v[54:57], v222, v222 op_sel_hi:[0,0,0]
	v_mfma_scale_f32_16x16x128_f8f6f4 v[50:53], v[240:247], v[188:195], v[50:53], v222, v222 op_sel_hi:[0,0,0]
	v_mfma_scale_f32_16x16x128_f8f6f4 v[38:41], v[232:239], v[202:209], v[38:41], v222, v222 op_sel_hi:[0,0,0]
	v_mfma_scale_f32_16x16x128_f8f6f4 v[34:37], v[240:247], v[202:209], v[34:37], v222, v222 op_sel_hi:[0,0,0]
	v_mfma_scale_f32_16x16x128_f8f6f4 v[30:33], v[232:239], v[210:217], v[30:33], v222, v222 op_sel_hi:[0,0,0]
	v_mfma_scale_f32_16x16x128_f8f6f4 v[26:29], v[240:247], v[210:217], v[26:29], v222, v222 op_sel_hi:[0,0,0]
	s_setprio 0
	s_barrier
	ds_read_b128 v[10:13], v183
	ds_read_b128 v[14:17], v184
	ds_read_b128 v[146:149], v185
	ds_read_b128 v[150:153], v196
	s_add_u32 s48, s48, 0x40000
	s_addc_u32 s49, s49, 0
	s_mov_b32 m0, s59
	v_lshl_add_u64 v[154:155], s[48:49], 0, v[164:165]
	ds_read_b128 v[166:169], v0 offset:32768
	ds_read_b128 v[170:173], v0 offset:33792
	ds_read_b128 v[188:191], v0 offset:34816
	ds_read_b128 v[192:195], v0 offset:35840
	ds_read_b128 v[202:205], v0 offset:36864
	ds_read_b128 v[206:209], v0 offset:37888
	ds_read_b128 v[210:213], v0 offset:38912
	ds_read_b128 v[214:217], v0 offset:39936
	global_load_lds_dwordx4 v[154:155], off
	v_lshl_add_u64 v[154:155], s[48:49], 0, v[160:161]
	s_mov_b32 m0, s60
	s_nop 0
	global_load_lds_dwordx4 v[154:155], off
	s_waitcnt lgkmcnt(8)
	s_barrier
	s_setprio 1
	s_waitcnt lgkmcnt(6)
	v_mfma_scale_f32_16x16x128_f8f6f4 v[134:137], v[10:17], v[166:173], v[134:137], v222, v222 op_sel_hi:[0,0,0]
	v_mfma_scale_f32_16x16x128_f8f6f4 v[130:133], v[146:153], v[166:173], v[130:133], v222, v222 op_sel_hi:[0,0,0]
	s_waitcnt lgkmcnt(4)
	v_mfma_scale_f32_16x16x128_f8f6f4 v[118:121], v[10:17], v[188:195], v[118:121], v222, v222 op_sel_hi:[0,0,0]
	v_mfma_scale_f32_16x16x128_f8f6f4 v[114:117], v[146:153], v[188:195], v[114:117], v222, v222 op_sel_hi:[0,0,0]
	s_waitcnt lgkmcnt(2)
	v_mfma_scale_f32_16x16x128_f8f6f4 v[102:105], v[10:17], v[202:209], v[102:105], v222, v222 op_sel_hi:[0,0,0]
	v_mfma_scale_f32_16x16x128_f8f6f4 v[98:101], v[146:153], v[202:209], v[98:101], v222, v222 op_sel_hi:[0,0,0]
	s_waitcnt lgkmcnt(0)
	v_mfma_scale_f32_16x16x128_f8f6f4 v[74:77], v[10:17], v[210:217], v[74:77], v222, v222 op_sel_hi:[0,0,0]
	v_mfma_scale_f32_16x16x128_f8f6f4 v[66:69], v[146:153], v[210:217], v[66:69], v222, v222 op_sel_hi:[0,0,0]
	s_setprio 0
	s_barrier
	s_mov_b32 m0, s62
	v_lshl_add_u64 v[6:7], v[6:7], 0, s[24:25]
	ds_read_b128 v[232:235], v197
	ds_read_b128 v[236:239], v198
	ds_read_b128 v[240:243], v199
	ds_read_b128 v[244:247], v200
	global_load_lds_dwordx4 v[6:7], off
	v_lshl_add_u64 v[6:7], v[8:9], 0, s[24:25]
	s_mov_b32 m0, s63
	s_nop 0
	global_load_lds_dwordx4 v[6:7], off
	s_barrier
	s_setprio 1
	s_waitcnt lgkmcnt(2)
	v_mfma_scale_f32_16x16x128_f8f6f4 v[142:145], v[232:239], v[166:173], v[142:145], v222, v222 op_sel_hi:[0,0,0]
	v_mfma_scale_f32_16x16x128_f8f6f4 v[126:129], v[232:239], v[188:195], v[126:129], v222, v222 op_sel_hi:[0,0,0]
	v_mfma_scale_f32_16x16x128_f8f6f4 v[110:113], v[232:239], v[202:209], v[110:113], v222, v222 op_sel_hi:[0,0,0]
	v_mfma_scale_f32_16x16x128_f8f6f4 v[78:81], v[232:239], v[210:217], v[78:81], v222, v222 op_sel_hi:[0,0,0]
	s_waitcnt lgkmcnt(0)
	v_mfma_scale_f32_16x16x128_f8f6f4 v[138:141], v[240:247], v[166:173], v[138:141], v222, v222 op_sel_hi:[0,0,0]
	v_mfma_scale_f32_16x16x128_f8f6f4 v[122:125], v[240:247], v[188:195], v[122:125], v222, v222 op_sel_hi:[0,0,0]
	v_mfma_scale_f32_16x16x128_f8f6f4 v[106:109], v[240:247], v[202:209], v[106:109], v222, v222 op_sel_hi:[0,0,0]
	v_mfma_scale_f32_16x16x128_f8f6f4 v[70:73], v[240:247], v[210:217], v[70:73], v222, v222 op_sel_hi:[0,0,0]
	s_setprio 0
	s_mov_b32 m0, s64
	v_lshl_add_u64 v[2:3], v[2:3], 0, s[24:25]
	s_barrier
	ds_read_b128 v[166:169], v0 offset:49152
	ds_read_b128 v[170:173], v0 offset:50176
	ds_read_b128 v[188:191], v0 offset:51200
	ds_read_b128 v[192:195], v0 offset:52224
	ds_read_b128 v[202:205], v0 offset:53248
	ds_read_b128 v[206:209], v0 offset:54272
	ds_read_b128 v[210:213], v0 offset:55296
	ds_read_b128 v[214:217], v0 offset:56320
	global_load_lds_dwordx4 v[2:3], off
	v_lshl_add_u64 v[2:3], v[4:5], 0, s[24:25]
	s_mov_b32 m0, s65
	s_nop 0
	global_load_lds_dwordx4 v[2:3], off
	s_barrier
	s_setprio 1
	s_waitcnt lgkmcnt(6)
	v_mfma_scale_f32_16x16x128_f8f6f4 v[94:97], v[10:17], v[166:173], v[94:97], v222, v222 op_sel_hi:[0,0,0]
	v_mfma_scale_f32_16x16x128_f8f6f4 v[90:93], v[146:153], v[166:173], v[90:93], v222, v222 op_sel_hi:[0,0,0]
	s_waitcnt lgkmcnt(4)
	v_mfma_scale_f32_16x16x128_f8f6f4 v[62:65], v[10:17], v[188:195], v[62:65], v222, v222 op_sel_hi:[0,0,0]
	v_mfma_scale_f32_16x16x128_f8f6f4 v[58:61], v[146:153], v[188:195], v[58:61], v222, v222 op_sel_hi:[0,0,0]
	s_waitcnt lgkmcnt(2)
	v_mfma_scale_f32_16x16x128_f8f6f4 v[46:49], v[10:17], v[202:209], v[46:49], v222, v222 op_sel_hi:[0,0,0]
	v_mfma_scale_f32_16x16x128_f8f6f4 v[42:45], v[146:153], v[202:209], v[42:45], v222, v222 op_sel_hi:[0,0,0]
	s_waitcnt lgkmcnt(0)
	v_mfma_scale_f32_16x16x128_f8f6f4 v[22:25], v[10:17], v[210:217], v[22:25], v222, v222 op_sel_hi:[0,0,0]
	v_mfma_scale_f32_16x16x128_f8f6f4 v[18:21], v[146:153], v[210:217], v[18:21], v222, v222 op_sel_hi:[0,0,0]
	s_setprio 0
	s_barrier
	s_add_u32 s44, s44, 0x40080
	s_addc_u32 s45, s45, 0
	s_mov_b32 m0, s66
	v_lshl_add_u64 v[2:3], s[44:45], 0, v[162:163]
	global_load_lds_dwordx4 v[2:3], off
	v_lshl_add_u64 v[2:3], s[44:45], 0, v[158:159]
	s_mov_b32 m0, s67
	s_nop 0
	global_load_lds_dwordx4 v[2:3], off
	s_waitcnt vmcnt(6)
	s_barrier
	s_setprio 1
	v_mfma_scale_f32_16x16x128_f8f6f4 v[86:89], v[232:239], v[166:173], v[86:89], v222, v222 op_sel_hi:[0,0,0]
	v_mfma_scale_f32_16x16x128_f8f6f4 v[82:85], v[240:247], v[166:173], v[82:85], v222, v222 op_sel_hi:[0,0,0]
	v_mfma_scale_f32_16x16x128_f8f6f4 v[54:57], v[232:239], v[188:195], v[54:57], v222, v222 op_sel_hi:[0,0,0]
	v_mfma_scale_f32_16x16x128_f8f6f4 v[50:53], v[240:247], v[188:195], v[50:53], v222, v222 op_sel_hi:[0,0,0]
	v_mfma_scale_f32_16x16x128_f8f6f4 v[38:41], v[232:239], v[202:209], v[38:41], v222, v222 op_sel_hi:[0,0,0]
	v_mfma_scale_f32_16x16x128_f8f6f4 v[34:37], v[240:247], v[202:209], v[34:37], v222, v222 op_sel_hi:[0,0,0]
	v_mfma_scale_f32_16x16x128_f8f6f4 v[30:33], v[232:239], v[210:217], v[30:33], v222, v222 op_sel_hi:[0,0,0]
	v_mfma_scale_f32_16x16x128_f8f6f4 v[26:29], v[240:247], v[210:217], v[26:29], v222, v222 op_sel_hi:[0,0,0]
	s_setprio 0
	s_add_i32 s77, s77, 2
	s_add_u32 s46, s46, 0x100
	s_addc_u32 s47, s47, 0
	s_add_u32 s75, s75, 0x100
	s_addc_u32 s76, s76, 0
	s_cmp_gt_u32 s77, 13
	s_barrier
	s_cbranch_scc0 .LBB0_834
	s_nop 15
	s_nop 15
	v_mbcnt_lo_u32_b32 v0, -1, 0
	v_mbcnt_hi_u32_b32 v0, -1, v0
	v_readlane_b32 s13, v252, 51
	v_and_b32_e32 v202, 15, v0
	v_bfe_u32 v201, v0, 4, 2
	v_readlane_b32 s21, v252, 52
	s_mov_b64 s[44:45], -1
	s_and_b64 vcc, exec, s[8:9]
	s_cbranch_vccz .LBB0_837
	s_lshl_b32 s44, s69, 8
	s_ashr_i32 s45, s44, 31
	s_lshl_b32 s46, s21, 5
	s_lshl_b32 s48, s70, 8
	s_lshl_b32 s49, s13, 6
	s_ashr_i32 s47, s46, 31
	s_lshl_b64 s[44:45], s[44:45], 1
	s_add_u32 s71, s10, s44
	v_or_b32_e32 v5, s48, v202
	s_addc_u32 s73, s11, s45
	s_lshl_b64 s[46:47], s[46:47], 1
	s_add_u32 s72, s71, s46
	v_or_b32_e32 v203, s49, v202
	v_add_u32_e32 v6, s49, v5
	s_addc_u32 s73, s73, s47
	v_lshlrev_b32_e32 v0, 4, v201
	v_add_u32_e32 v188, s48, v203
	v_ashrrev_i32_e32 v7, 31, v6
	v_lshl_add_u64 v[2:3], s[72:73], 0, v[0:1]
	v_or_b32_e32 v4, 32, v188
	v_lshlrev_b64 v[8:9], 11, v[6:7]
	v_lshl_add_u64 v[8:9], v[2:3], 0, v[8:9]
	v_ashrrev_i32_e32 v5, 31, v4
	global_load_dwordx4 v[166:169], v[8:9], off
	v_lshlrev_b64 v[170:171], 11, v[4:5]
	v_lshl_add_u64 v[4:5], v[2:3], 0, v[170:171]
	global_load_dwordx4 v[14:17], v[4:5], off
	global_load_dwordx4 v[154:157], v[8:9], off offset:256
	global_load_dwordx4 v[10:13], v[4:5], off offset:256
	v_or_b32_e32 v4, 16, v6
	v_ashrrev_i32_e32 v5, 31, v4
	v_lshlrev_b64 v[4:5], 11, v[4:5]
	v_lshl_add_u64 v[4:5], v[2:3], 0, v[4:5]
	global_load_dwordx4 v[150:153], v[4:5], off
	v_or_b32_e32 v6, 48, v188
	v_ashrrev_i32_e32 v7, 31, v6
	v_lshlrev_b64 v[6:7], 11, v[6:7]
	v_lshl_add_u64 v[2:3], v[2:3], 0, v[6:7]
	global_load_dwordx4 v[6:9], v[2:3], off
	global_load_dwordx4 v[146:149], v[4:5], off offset:256
	s_nop 0
	global_load_dwordx4 v[2:5], v[2:3], off offset:256
	v_ashrrev_i32_e32 v189, 31, v188
	v_lshlrev_b64 v[188:189], 11, v[188:189]
	v_lshl_add_u64 v[188:189], s[6:7], 0, v[188:189]
	v_lshl_add_u64 v[188:189], v[188:189], 0, s[44:45]
	v_lshl_add_u64 v[188:189], v[188:189], 0, s[46:47]
	v_lshl_add_u64 v[188:189], v[188:189], 0, v[0:1]
	s_add_u32 s72, s10, s46
	s_addc_u32 s73, s11, s47
	s_or_b32 s71, s48, 16
	s_add_i32 s49, s48, s49
	v_or_b32_e32 v204, s49, v202
	v_lshl_add_u64 v[172:173], s[72:73], 0, v[0:1]
	v_lshl_add_u64 v[172:173], v[172:173], 0, s[44:45]
	v_lshl_add_u64 v[170:171], s[6:7], 0, v[170:171]
	v_lshl_add_u64 v[170:171], v[170:171], 0, s[44:45]
	v_lshl_add_u64 v[170:171], v[170:171], 0, s[46:47]
	v_lshl_add_u64 v[170:171], v[170:171], 0, v[0:1]
	s_or_b32 s49, s48, 48
	s_waitcnt vmcnt(0)
	v_lshlrev_b32_e32 v190, 16, v166
	v_and_b32_e32 v191, 0xffff0000, v166
	v_lshlrev_b32_e32 v166, 16, v167
	v_and_b32_e32 v167, 0xffff0000, v167
	v_lshlrev_b32_e32 v192, 16, v168
	v_and_b32_e32 v193, 0xffff0000, v168
	v_lshlrev_b32_e32 v168, 16, v169
	v_and_b32_e32 v169, 0xffff0000, v169
	v_pk_fma_f32 v[194:195], v[136:137], s[16:17], v[166:167] op_sel_hi:[1,0,1]
	v_pk_fma_f32 v[166:167], v[134:135], s[16:17], v[190:191] op_sel_hi:[1,0,1]
	v_pk_fma_f32 v[190:191], v[132:133], s[16:17], v[168:169] op_sel_hi:[1,0,1]
	v_pk_fma_f32 v[168:169], v[130:131], s[16:17], v[192:193] op_sel_hi:[1,0,1]
	v_cvt_pk_bf16_f32 v166, v166, v167
	v_cvt_pk_bf16_f32 v167, v194, v195
	v_cvt_pk_bf16_f32 v168, v168, v169
	v_cvt_pk_bf16_f32 v169, v190, v191
	global_store_dwordx4 v[188:189], v[166:169], off
	v_lshlrev_b32_e32 v192, 16, v16
	v_and_b32_e32 v193, 0xffff0000, v16
	v_lshlrev_b32_e32 v166, 16, v154
	v_and_b32_e32 v167, 0xffff0000, v154
	v_lshlrev_b32_e32 v154, 16, v155
	v_and_b32_e32 v155, 0xffff0000, v155
	v_lshlrev_b32_e32 v168, 16, v156
	v_and_b32_e32 v169, 0xffff0000, v156
	v_lshlrev_b32_e32 v156, 16, v157
	v_and_b32_e32 v157, 0xffff0000, v157
	v_pk_fma_f32 v[190:191], v[144:145], s[16:17], v[154:155] op_sel_hi:[1,0,1]
	v_pk_fma_f32 v[154:155], v[142:143], s[16:17], v[166:167] op_sel_hi:[1,0,1]
	v_pk_fma_f32 v[166:167], v[140:141], s[16:17], v[156:157] op_sel_hi:[1,0,1]
	v_pk_fma_f32 v[156:157], v[138:139], s[16:17], v[168:169] op_sel_hi:[1,0,1]
	v_cvt_pk_bf16_f32 v154, v154, v155
	v_cvt_pk_bf16_f32 v155, v190, v191
	v_cvt_pk_bf16_f32 v156, v156, v157
	v_cvt_pk_bf16_f32 v157, v166, v167
	global_store_dwordx4 v[188:189], v[154:157], off offset:256
	v_lshlrev_b32_e32 v190, 16, v14
	v_and_b32_e32 v191, 0xffff0000, v14
	v_lshlrev_b32_e32 v154, 16, v150
	v_and_b32_e32 v155, 0xffff0000, v150
	v_lshlrev_b32_e32 v150, 16, v151
	v_and_b32_e32 v151, 0xffff0000, v151
	v_lshlrev_b32_e32 v156, 16, v152
	v_and_b32_e32 v157, 0xffff0000, v152
	v_lshlrev_b32_e32 v152, 16, v153
	v_and_b32_e32 v153, 0xffff0000, v153
	v_pk_fma_f32 v[166:167], v[120:121], s[16:17], v[150:151] op_sel_hi:[1,0,1]
	v_pk_fma_f32 v[150:151], v[118:119], s[16:17], v[154:155] op_sel_hi:[1,0,1]
	v_pk_fma_f32 v[154:155], v[116:117], s[16:17], v[152:153] op_sel_hi:[1,0,1]
	v_pk_fma_f32 v[152:153], v[114:115], s[16:17], v[156:157] op_sel_hi:[1,0,1]
	v_cvt_pk_bf16_f32 v150, v150, v151
	v_cvt_pk_bf16_f32 v152, v152, v153
	v_cvt_pk_bf16_f32 v153, v154, v155
	v_add_u32_e32 v154, s71, v203
	v_ashrrev_i32_e32 v155, 31, v154
	v_lshlrev_b64 v[154:155], 11, v[154:155]
	v_lshl_add_u64 v[154:155], s[6:7], 0, v[154:155]
	v_lshl_add_u64 v[154:155], v[154:155], 0, s[44:45]
	v_lshl_add_u64 v[154:155], v[154:155], 0, s[46:47]
	v_cvt_pk_bf16_f32 v151, v166, v167
	v_lshl_add_u64 v[154:155], v[154:155], 0, v[0:1]
	global_store_dwordx4 v[154:155], v[150:153], off
	v_lshlrev_b32_e32 v14, 16, v15
	v_and_b32_e32 v15, 0xffff0000, v15
	v_lshlrev_b32_e32 v150, 16, v146
	v_and_b32_e32 v151, 0xffff0000, v146
	v_lshlrev_b32_e32 v146, 16, v147
	v_and_b32_e32 v147, 0xffff0000, v147
	v_lshlrev_b32_e32 v152, 16, v148
	v_and_b32_e32 v153, 0xffff0000, v148
	v_lshlrev_b32_e32 v148, 16, v149
	v_and_b32_e32 v149, 0xffff0000, v149
	v_pk_fma_f32 v[156:157], v[128:129], s[16:17], v[146:147] op_sel_hi:[1,0,1]
	v_pk_fma_f32 v[146:147], v[126:127], s[16:17], v[150:151] op_sel_hi:[1,0,1]
	v_pk_fma_f32 v[150:151], v[124:125], s[16:17], v[148:149] op_sel_hi:[1,0,1]
	v_pk_fma_f32 v[148:149], v[122:123], s[16:17], v[152:153] op_sel_hi:[1,0,1]
	v_cvt_pk_bf16_f32 v146, v146, v147
	v_cvt_pk_bf16_f32 v147, v156, v157
	v_cvt_pk_bf16_f32 v148, v148, v149
	v_cvt_pk_bf16_f32 v149, v150, v151
	global_store_dwordx4 v[154:155], v[146:149], off offset:256
	v_lshlrev_b32_e32 v16, 16, v17
	v_and_b32_e32 v17, 0xffff0000, v17
	v_add_u32_e32 v146, 0x80, v204
	v_ashrrev_i32_e32 v147, 31, v146
	v_lshlrev_b64 v[188:189], 11, v[146:147]
	v_lshl_add_u64 v[146:147], v[172:173], 0, v[188:189]
	global_load_dwordx4 v[150:153], v[146:147], off
	global_load_dwordx4 v[154:157], v[146:147], off offset:256
	v_add_u32_e32 v146, 0x90, v204
	v_ashrrev_i32_e32 v147, 31, v146
	v_lshlrev_b64 v[146:147], 11, v[146:147]
	v_pk_fma_f32 v[194:195], v[104:105], s[16:17], v[14:15] op_sel_hi:[1,0,1]
	v_pk_fma_f32 v[14:15], v[102:103], s[16:17], v[190:191] op_sel_hi:[1,0,1]
	v_pk_fma_f32 v[190:191], v[100:101], s[16:17], v[16:17] op_sel_hi:[1,0,1]
	v_pk_fma_f32 v[16:17], v[98:99], s[16:17], v[192:193] op_sel_hi:[1,0,1]
	v_lshl_add_u64 v[146:147], v[172:173], 0, v[146:147]
	v_cvt_pk_bf16_f32 v14, v14, v15
	v_cvt_pk_bf16_f32 v15, v194, v195
	v_cvt_pk_bf16_f32 v16, v16, v17
	v_cvt_pk_bf16_f32 v17, v190, v191
	global_load_dwordx4 v[166:169], v[146:147], off
	s_nop 0
	global_load_dwordx4 v[146:149], v[146:147], off offset:256
	global_store_dwordx4 v[170:171], v[14:17], off
	v_add_u32_e32 v192, 0x80, v203
	s_nop 0
	v_lshlrev_b32_e32 v14, 16, v10
	v_and_b32_e32 v15, 0xffff0000, v10
	v_lshlrev_b32_e32 v10, 16, v11
	v_and_b32_e32 v11, 0xffff0000, v11
	v_lshlrev_b32_e32 v16, 16, v12
	v_and_b32_e32 v17, 0xffff0000, v12
	v_lshlrev_b32_e32 v12, 16, v13
	v_and_b32_e32 v13, 0xffff0000, v13
	v_pk_fma_f32 v[190:191], v[112:113], s[16:17], v[10:11] op_sel_hi:[1,0,1]
	v_pk_fma_f32 v[10:11], v[110:111], s[16:17], v[14:15] op_sel_hi:[1,0,1]
	v_pk_fma_f32 v[14:15], v[108:109], s[16:17], v[12:13] op_sel_hi:[1,0,1]
	v_pk_fma_f32 v[12:13], v[106:107], s[16:17], v[16:17] op_sel_hi:[1,0,1]
	v_cvt_pk_bf16_f32 v10, v10, v11
	v_cvt_pk_bf16_f32 v11, v190, v191
	v_cvt_pk_bf16_f32 v12, v12, v13
	v_cvt_pk_bf16_f32 v13, v14, v15
	global_store_dwordx4 v[170:171], v[10:13], off offset:256
	s_waitcnt vmcnt(0)
	v_lshlrev_b32_e32 v170, 16, v150
	v_lshlrev_b32_e32 v10, 16, v6
	v_and_b32_e32 v11, 0xffff0000, v6
	v_lshlrev_b32_e32 v6, 16, v7
	v_and_b32_e32 v7, 0xffff0000, v7
	v_lshlrev_b32_e32 v12, 16, v8
	v_and_b32_e32 v13, 0xffff0000, v8
	v_lshlrev_b32_e32 v8, 16, v9
	v_and_b32_e32 v9, 0xffff0000, v9
	v_pk_fma_f32 v[14:15], v[76:77], s[16:17], v[6:7] op_sel_hi:[1,0,1]
	v_pk_fma_f32 v[6:7], v[74:75], s[16:17], v[10:11] op_sel_hi:[1,0,1]
	v_pk_fma_f32 v[10:11], v[68:69], s[16:17], v[8:9] op_sel_hi:[1,0,1]
	v_pk_fma_f32 v[8:9], v[66:67], s[16:17], v[12:13] op_sel_hi:[1,0,1]
	v_cvt_pk_bf16_f32 v6, v6, v7
	v_cvt_pk_bf16_f32 v8, v8, v9
	v_cvt_pk_bf16_f32 v9, v10, v11
	v_add_u32_e32 v10, s49, v203
	v_ashrrev_i32_e32 v11, 31, v10
	v_lshlrev_b64 v[10:11], 11, v[10:11]
	v_lshl_add_u64 v[10:11], s[6:7], 0, v[10:11]
	v_lshl_add_u64 v[10:11], v[10:11], 0, s[44:45]
	v_lshl_add_u64 v[10:11], v[10:11], 0, s[46:47]
	v_cvt_pk_bf16_f32 v7, v14, v15
	v_lshl_add_u64 v[10:11], v[10:11], 0, v[0:1]
	global_store_dwordx4 v[10:11], v[6:9], off
	v_and_b32_e32 v171, 0xffff0000, v150
	v_lshlrev_b32_e32 v150, 16, v151
	v_lshlrev_b32_e32 v6, 16, v2
	v_and_b32_e32 v7, 0xffff0000, v2
	v_lshlrev_b32_e32 v2, 16, v3
	v_and_b32_e32 v3, 0xffff0000, v3
	v_lshlrev_b32_e32 v8, 16, v4
	v_and_b32_e32 v9, 0xffff0000, v4
	v_lshlrev_b32_e32 v4, 16, v5
	v_and_b32_e32 v5, 0xffff0000, v5
	v_pk_fma_f32 v[12:13], v[80:81], s[16:17], v[2:3] op_sel_hi:[1,0,1]
	v_pk_fma_f32 v[2:3], v[78:79], s[16:17], v[6:7] op_sel_hi:[1,0,1]
	v_pk_fma_f32 v[6:7], v[72:73], s[16:17], v[4:5] op_sel_hi:[1,0,1]
	v_pk_fma_f32 v[4:5], v[70:71], s[16:17], v[8:9] op_sel_hi:[1,0,1]
	v_cvt_pk_bf16_f32 v2, v2, v3
	v_cvt_pk_bf16_f32 v3, v12, v13
	v_cvt_pk_bf16_f32 v4, v4, v5
	v_cvt_pk_bf16_f32 v5, v6, v7
	global_store_dwordx4 v[10:11], v[2:5], off offset:256
	v_and_b32_e32 v151, 0xffff0000, v151
	v_pk_fma_f32 v[190:191], v[96:97], s[16:17], v[150:151] op_sel_hi:[1,0,1]
	v_add_u32_e32 v2, 0xa0, v204
	v_ashrrev_i32_e32 v3, 31, v2
	v_lshlrev_b64 v[2:3], 11, v[2:3]
	v_lshl_add_u64 v[2:3], v[172:173], 0, v[2:3]
	global_load_dwordx4 v[6:9], v[2:3], off
	global_load_dwordx4 v[10:13], v[2:3], off offset:256
	v_add_u32_e32 v2, 0xb0, v204
	v_ashrrev_i32_e32 v3, 31, v2
	v_lshlrev_b64 v[2:3], 11, v[2:3]
	v_lshl_add_u64 v[2:3], v[172:173], 0, v[2:3]
	global_load_dwordx4 v[14:17], v[2:3], off
	s_nop 0
	global_load_dwordx4 v[2:5], v[2:3], off offset:256
	v_lshlrev_b32_e32 v172, 16, v152
	v_and_b32_e32 v173, 0xffff0000, v152
	v_lshlrev_b32_e32 v152, 16, v153
	v_and_b32_e32 v153, 0xffff0000, v153
	v_pk_fma_f32 v[150:151], v[94:95], s[16:17], v[170:171] op_sel_hi:[1,0,1]
	v_pk_fma_f32 v[170:171], v[92:93], s[16:17], v[152:153] op_sel_hi:[1,0,1]
	v_pk_fma_f32 v[152:153], v[90:91], s[16:17], v[172:173] op_sel_hi:[1,0,1]
	v_cvt_pk_bf16_f32 v150, v150, v151
	v_cvt_pk_bf16_f32 v152, v152, v153
	v_cvt_pk_bf16_f32 v153, v170, v171
	v_lshl_add_u64 v[170:171], s[6:7], 0, v[188:189]
	v_lshl_add_u64 v[170:171], v[170:171], 0, s[44:45]
	v_lshl_add_u64 v[170:171], v[170:171], 0, s[46:47]
	v_cvt_pk_bf16_f32 v151, v190, v191
	v_lshl_add_u64 v[170:171], v[170:171], 0, v[0:1]
	global_store_dwordx4 v[170:171], v[150:153], off
	s_nop 1
	v_lshlrev_b32_e32 v150, 16, v154
	v_and_b32_e32 v151, 0xffff0000, v154
	v_lshlrev_b32_e32 v152, 16, v155
	v_and_b32_e32 v153, 0xffff0000, v155
	v_lshlrev_b32_e32 v154, 16, v156
	v_and_b32_e32 v155, 0xffff0000, v156
	v_lshlrev_b32_e32 v156, 16, v157
	v_and_b32_e32 v157, 0xffff0000, v157
	v_pk_fma_f32 v[152:153], v[88:89], s[16:17], v[152:153] op_sel_hi:[1,0,1]
	v_pk_fma_f32 v[150:151], v[86:87], s[16:17], v[150:151] op_sel_hi:[1,0,1]
	v_pk_fma_f32 v[156:157], v[84:85], s[16:17], v[156:157] op_sel_hi:[1,0,1]
	v_pk_fma_f32 v[154:155], v[82:83], s[16:17], v[154:155] op_sel_hi:[1,0,1]
	v_cvt_pk_bf16_f32 v150, v150, v151
	v_cvt_pk_bf16_f32 v151, v152, v153
	v_cvt_pk_bf16_f32 v152, v154, v155
	v_cvt_pk_bf16_f32 v153, v156, v157
	global_store_dwordx4 v[170:171], v[150:153], off offset:256
	v_lshlrev_b32_e32 v154, 16, v168
	v_and_b32_e32 v155, 0xffff0000, v168
	v_lshlrev_b32_e32 v150, 16, v166
	v_and_b32_e32 v151, 0xffff0000, v166
	v_lshlrev_b32_e32 v152, 16, v167
	v_and_b32_e32 v153, 0xffff0000, v167
	v_pk_fma_f32 v[152:153], v[64:65], s[16:17], v[152:153] op_sel_hi:[1,0,1]
	v_pk_fma_f32 v[150:151], v[62:63], s[16:17], v[150:151] op_sel_hi:[1,0,1]
	v_pk_fma_f32 v[154:155], v[58:59], s[16:17], v[154:155] op_sel_hi:[1,0,1]
	v_cvt_pk_bf16_f32 v150, v150, v151
	v_cvt_pk_bf16_f32 v151, v152, v153
	v_cvt_pk_bf16_f32 v152, v154, v155
	v_add_u32_e32 v154, s71, v192
	v_ashrrev_i32_e32 v155, 31, v154
	v_lshlrev_b64 v[154:155], 11, v[154:155]
	v_lshl_add_u64 v[154:155], s[6:7], 0, v[154:155]
	v_lshlrev_b32_e32 v156, 16, v169
	v_and_b32_e32 v157, 0xffff0000, v169
	v_lshl_add_u64 v[154:155], v[154:155], 0, s[44:45]
	v_pk_fma_f32 v[156:157], v[60:61], s[16:17], v[156:157] op_sel_hi:[1,0,1]
	v_lshl_add_u64 v[154:155], v[154:155], 0, s[46:47]
	v_cvt_pk_bf16_f32 v153, v156, v157
	v_lshl_add_u64 v[154:155], v[154:155], 0, v[0:1]
	global_store_dwordx4 v[154:155], v[150:153], off
	s_nop 1
	v_lshlrev_b32_e32 v150, 16, v146
	v_and_b32_e32 v151, 0xffff0000, v146
	v_lshlrev_b32_e32 v146, 16, v147
	v_and_b32_e32 v147, 0xffff0000, v147
	v_lshlrev_b32_e32 v152, 16, v148
	v_and_b32_e32 v153, 0xffff0000, v148
	v_lshlrev_b32_e32 v148, 16, v149
	v_and_b32_e32 v149, 0xffff0000, v149
	v_pk_fma_f32 v[156:157], v[56:57], s[16:17], v[146:147] op_sel_hi:[1,0,1]
	v_pk_fma_f32 v[146:147], v[54:55], s[16:17], v[150:151] op_sel_hi:[1,0,1]
	v_pk_fma_f32 v[150:151], v[52:53], s[16:17], v[148:149] op_sel_hi:[1,0,1]
	v_pk_fma_f32 v[148:149], v[50:51], s[16:17], v[152:153] op_sel_hi:[1,0,1]
	v_cvt_pk_bf16_f32 v146, v146, v147
	v_cvt_pk_bf16_f32 v147, v156, v157
	v_cvt_pk_bf16_f32 v148, v148, v149
	v_cvt_pk_bf16_f32 v149, v150, v151
	global_store_dwordx4 v[154:155], v[146:149], off offset:256
	s_waitcnt vmcnt(0)
	s_nop 0
	v_lshlrev_b32_e32 v146, 16, v6
	v_and_b32_e32 v147, 0xffff0000, v6
	v_lshlrev_b32_e32 v6, 16, v7
	v_and_b32_e32 v7, 0xffff0000, v7
	v_lshlrev_b32_e32 v148, 16, v8
	v_and_b32_e32 v149, 0xffff0000, v8
	v_lshlrev_b32_e32 v8, 16, v9
	v_and_b32_e32 v9, 0xffff0000, v9
	v_pk_fma_f32 v[150:151], v[48:49], s[16:17], v[6:7] op_sel_hi:[1,0,1]
	v_pk_fma_f32 v[6:7], v[46:47], s[16:17], v[146:147] op_sel_hi:[1,0,1]
	v_pk_fma_f32 v[146:147], v[44:45], s[16:17], v[8:9] op_sel_hi:[1,0,1]
	v_pk_fma_f32 v[8:9], v[42:43], s[16:17], v[148:149] op_sel_hi:[1,0,1]
	v_cvt_pk_bf16_f32 v6, v6, v7
	v_cvt_pk_bf16_f32 v8, v8, v9
	v_cvt_pk_bf16_f32 v9, v146, v147
	v_add_u32_e32 v146, s48, v192
	v_or_b32_e32 v146, 32, v146
	v_ashrrev_i32_e32 v147, 31, v146
	v_lshlrev_b64 v[146:147], 11, v[146:147]
	v_lshl_add_u64 v[146:147], s[6:7], 0, v[146:147]
	v_lshl_add_u64 v[146:147], v[146:147], 0, s[44:45]
	v_lshl_add_u64 v[146:147], v[146:147], 0, s[46:47]
	v_cvt_pk_bf16_f32 v7, v150, v151
	v_lshl_add_u64 v[146:147], v[146:147], 0, v[0:1]
	global_store_dwordx4 v[146:147], v[6:9], off
	s_nop 1
	v_lshlrev_b32_e32 v6, 16, v10
	v_and_b32_e32 v7, 0xffff0000, v10
	v_lshlrev_b32_e32 v8, 16, v11
	v_and_b32_e32 v9, 0xffff0000, v11
	v_lshlrev_b32_e32 v10, 16, v12
	v_and_b32_e32 v11, 0xffff0000, v12
	v_lshlrev_b32_e32 v12, 16, v13
	v_and_b32_e32 v13, 0xffff0000, v13
	v_pk_fma_f32 v[8:9], v[40:41], s[16:17], v[8:9] op_sel_hi:[1,0,1]
	v_pk_fma_f32 v[6:7], v[38:39], s[16:17], v[6:7] op_sel_hi:[1,0,1]
	v_pk_fma_f32 v[12:13], v[36:37], s[16:17], v[12:13] op_sel_hi:[1,0,1]
	v_pk_fma_f32 v[10:11], v[34:35], s[16:17], v[10:11] op_sel_hi:[1,0,1]
	v_cvt_pk_bf16_f32 v6, v6, v7
	v_cvt_pk_bf16_f32 v7, v8, v9
	v_cvt_pk_bf16_f32 v8, v10, v11
	v_cvt_pk_bf16_f32 v9, v12, v13
	global_store_dwordx4 v[146:147], v[6:9], off offset:256
	v_lshlrev_b32_e32 v10, 16, v16
	v_and_b32_e32 v11, 0xffff0000, v16
	v_lshlrev_b32_e32 v6, 16, v14
	v_and_b32_e32 v7, 0xffff0000, v14
	v_lshlrev_b32_e32 v8, 16, v15
	v_and_b32_e32 v9, 0xffff0000, v15
	v_pk_fma_f32 v[8:9], v[24:25], s[16:17], v[8:9] op_sel_hi:[1,0,1]
	v_pk_fma_f32 v[6:7], v[22:23], s[16:17], v[6:7] op_sel_hi:[1,0,1]
	v_pk_fma_f32 v[10:11], v[18:19], s[16:17], v[10:11] op_sel_hi:[1,0,1]
	v_cvt_pk_bf16_f32 v6, v6, v7
	v_cvt_pk_bf16_f32 v7, v8, v9
	v_cvt_pk_bf16_f32 v8, v10, v11
	v_add_u32_e32 v10, s49, v192
	v_ashrrev_i32_e32 v11, 31, v10
	v_lshlrev_b64 v[10:11], 11, v[10:11]
	v_lshl_add_u64 v[10:11], s[6:7], 0, v[10:11]
	v_lshlrev_b32_e32 v12, 16, v17
	v_and_b32_e32 v13, 0xffff0000, v17
	v_lshl_add_u64 v[10:11], v[10:11], 0, s[44:45]
	v_pk_fma_f32 v[12:13], v[20:21], s[16:17], v[12:13] op_sel_hi:[1,0,1]
	v_lshl_add_u64 v[10:11], v[10:11], 0, s[46:47]
	v_cvt_pk_bf16_f32 v9, v12, v13
	v_lshl_add_u64 v[10:11], v[10:11], 0, v[0:1]
	global_store_dwordx4 v[10:11], v[6:9], off
	s_mov_b64 s[44:45], 0
	s_nop 0
	v_lshlrev_b32_e32 v6, 16, v2
	v_and_b32_e32 v7, 0xffff0000, v2
	v_lshlrev_b32_e32 v2, 16, v3
	v_and_b32_e32 v3, 0xffff0000, v3
	v_lshlrev_b32_e32 v8, 16, v4
	v_and_b32_e32 v9, 0xffff0000, v4
	v_lshlrev_b32_e32 v4, 16, v5
	v_and_b32_e32 v5, 0xffff0000, v5
	v_pk_fma_f32 v[12:13], v[32:33], s[16:17], v[2:3] op_sel_hi:[1,0,1]
	v_pk_fma_f32 v[2:3], v[30:31], s[16:17], v[6:7] op_sel_hi:[1,0,1]
	v_pk_fma_f32 v[6:7], v[28:29], s[16:17], v[4:5] op_sel_hi:[1,0,1]
	v_pk_fma_f32 v[4:5], v[26:27], s[16:17], v[8:9] op_sel_hi:[1,0,1]
	v_cvt_pk_bf16_f32 v2, v2, v3
	v_cvt_pk_bf16_f32 v3, v12, v13
	v_cvt_pk_bf16_f32 v4, v4, v5
	v_cvt_pk_bf16_f32 v5, v6, v7
	global_store_dwordx4 v[10:11], v[2:5], off offset:256

.LBB0_973:
	ds_read_b128 v[90:93], v166
	ds_read_b128 v[94:97], v167
	ds_read_b128 v[98:101], v168
	ds_read_b128 v[102:105], v169
	s_add_u32 s8, s6, 0xfffc0080
	s_addc_u32 s9, s7, -1
	s_cmp_eq_u32 s44, 12
	s_cselect_b32 s39, s15, s9
	s_cselect_b32 s38, s28, s8
	s_cselect_b32 s9, s13, s42
	s_cselect_b32 s8, s40, s41
	v_add_u32_e32 v0, s68, v163
	v_lshl_add_u64 v[164:165], s[6:7], 0, v[154:155]
	s_add_i32 m0, s58, 0xc000
	ds_read_b128 v[158:161], v0
	ds_read_b128 v[182:185], v0 offset:1024
	ds_read_b128 v[188:191], v0 offset:2048
	ds_read_b128 v[192:195], v0 offset:3072
	ds_read_b128 v[196:199], v0 offset:4096
	ds_read_b128 v[200:203], v0 offset:5120
	ds_read_b128 v[204:207], v0 offset:6144
	ds_read_b128 v[208:211], v0 offset:7168
	global_load_lds_dwordx4 v[164:165], off
	v_lshl_add_u64 v[164:165], s[6:7], 0, v[156:157]
	s_add_i32 m0, s58, 0xe000
	s_nop 0
	global_load_lds_dwordx4 v[164:165], off
	s_waitcnt lgkmcnt(8)
	s_barrier
	s_setprio 1
	s_waitcnt lgkmcnt(7)
	v_mfma_f32_16x16x32_bf16 v[142:145], v[90:93], v[158:161], v[142:145]
	v_mfma_f32_16x16x32_bf16 v[138:141], v[98:101], v[158:161], v[138:141]
	s_waitcnt lgkmcnt(6)
	v_mfma_f32_16x16x32_bf16 v[142:145], v[94:97], v[182:185], v[142:145]
	v_mfma_f32_16x16x32_bf16 v[138:141], v[102:105], v[182:185], v[138:141]
	s_waitcnt lgkmcnt(5)
	v_mfma_f32_16x16x32_bf16 v[126:129], v[90:93], v[188:191], v[126:129]
	v_mfma_f32_16x16x32_bf16 v[122:125], v[98:101], v[188:191], v[122:125]
	s_waitcnt lgkmcnt(4)
	v_mfma_f32_16x16x32_bf16 v[126:129], v[94:97], v[192:195], v[126:129]
	v_mfma_f32_16x16x32_bf16 v[122:125], v[102:105], v[192:195], v[122:125]
	s_waitcnt lgkmcnt(3)
	v_mfma_f32_16x16x32_bf16 v[110:113], v[90:93], v[196:199], v[110:113]
	v_mfma_f32_16x16x32_bf16 v[106:109], v[98:101], v[196:199], v[106:109]
	s_waitcnt lgkmcnt(2)
	v_mfma_f32_16x16x32_bf16 v[110:113], v[94:97], v[200:203], v[110:113]
	v_mfma_f32_16x16x32_bf16 v[106:109], v[102:105], v[200:203], v[106:109]
	s_waitcnt lgkmcnt(1)
	v_mfma_f32_16x16x32_bf16 v[78:81], v[90:93], v[204:207], v[78:81]
	v_mfma_f32_16x16x32_bf16 v[74:77], v[98:101], v[204:207], v[74:77]
	s_waitcnt lgkmcnt(0)
	v_mfma_f32_16x16x32_bf16 v[78:81], v[94:97], v[208:211], v[78:81]
	v_mfma_f32_16x16x32_bf16 v[74:77], v[102:105], v[208:211], v[74:77]
	s_setprio 0
	s_barrier
	s_mov_b32 m0, s59
	v_lshl_add_u64 v[164:165], s[8:9], 0, v[150:151]
	ds_read_b128 v[212:215], v170
	ds_read_b128 v[216:219], v171
	ds_read_b128 v[232:235], v172
	ds_read_b128 v[236:239], v173
	global_load_lds_dwordx4 v[164:165], off
	v_lshl_add_u64 v[220:221], s[8:9], 0, v[146:147]
	s_mov_b32 m0, s60
	s_nop 0
	global_load_lds_dwordx4 v[220:221], off
	s_barrier
	s_setprio 1
	s_waitcnt lgkmcnt(3)
	v_mfma_f32_16x16x32_bf16 v[134:137], v[212:215], v[158:161], v[134:137]
	v_mfma_f32_16x16x32_bf16 v[118:121], v[212:215], v[188:191], v[118:121]
	v_mfma_f32_16x16x32_bf16 v[86:89], v[212:215], v[196:199], v[86:89]
	v_mfma_f32_16x16x32_bf16 v[70:73], v[212:215], v[204:207], v[70:73]
	s_waitcnt lgkmcnt(2)
	v_mfma_f32_16x16x32_bf16 v[134:137], v[216:219], v[182:185], v[134:137]
	v_mfma_f32_16x16x32_bf16 v[118:121], v[216:219], v[192:195], v[118:121]
	v_mfma_f32_16x16x32_bf16 v[86:89], v[216:219], v[200:203], v[86:89]
	v_mfma_f32_16x16x32_bf16 v[70:73], v[216:219], v[208:211], v[70:73]
	s_waitcnt lgkmcnt(1)
	v_mfma_f32_16x16x32_bf16 v[130:133], v[232:235], v[158:161], v[130:133]
	v_mfma_f32_16x16x32_bf16 v[114:117], v[232:235], v[188:191], v[114:117]
	v_mfma_f32_16x16x32_bf16 v[82:85], v[232:235], v[196:199], v[82:85]
	v_mfma_f32_16x16x32_bf16 v[66:69], v[232:235], v[204:207], v[66:69]
	s_waitcnt lgkmcnt(0)
	v_mfma_f32_16x16x32_bf16 v[130:133], v[236:239], v[182:185], v[130:133]
	v_mfma_f32_16x16x32_bf16 v[114:117], v[236:239], v[192:195], v[114:117]
	v_mfma_f32_16x16x32_bf16 v[82:85], v[236:239], v[200:203], v[82:85]
	v_mfma_f32_16x16x32_bf16 v[66:69], v[236:239], v[208:211], v[66:69]
	s_setprio 0
	s_mov_b32 m0, s58
	v_lshl_add_u64 v[240:241], s[38:39], 0, v[152:153]
	s_barrier
	ds_read_b128 v[158:161], v0 offset:16384
	ds_read_b128 v[182:185], v0 offset:17408
	ds_read_b128 v[188:191], v0 offset:18432
	ds_read_b128 v[192:195], v0 offset:19456
	ds_read_b128 v[196:199], v0 offset:20480
	ds_read_b128 v[200:203], v0 offset:21504
	ds_read_b128 v[204:207], v0 offset:22528
	ds_read_b128 v[208:211], v0 offset:23552
	global_load_lds_dwordx4 v[240:241], off
	v_lshl_add_u64 v[242:243], s[38:39], 0, v[148:149]
	s_mov_b32 m0, s61
	s_nop 0
	global_load_lds_dwordx4 v[242:243], off
	s_barrier
	s_setprio 1
	s_waitcnt lgkmcnt(7)
	v_mfma_f32_16x16x32_bf16 v[62:65], v[90:93], v[158:161], v[62:65]
	v_mfma_f32_16x16x32_bf16 v[58:61], v[98:101], v[158:161], v[58:61]
	s_waitcnt lgkmcnt(6)
	v_mfma_f32_16x16x32_bf16 v[62:65], v[94:97], v[182:185], v[62:65]
	v_mfma_f32_16x16x32_bf16 v[58:61], v[102:105], v[182:185], v[58:61]
	s_waitcnt lgkmcnt(5)
	v_mfma_f32_16x16x32_bf16 v[46:49], v[90:93], v[188:191], v[46:49]
	v_mfma_f32_16x16x32_bf16 v[42:45], v[98:101], v[188:191], v[42:45]
	s_waitcnt lgkmcnt(4)
	v_mfma_f32_16x16x32_bf16 v[46:49], v[94:97], v[192:195], v[46:49]
	v_mfma_f32_16x16x32_bf16 v[42:45], v[102:105], v[192:195], v[42:45]
	s_waitcnt lgkmcnt(3)
	v_mfma_f32_16x16x32_bf16 v[30:33], v[90:93], v[196:199], v[30:33]
	v_mfma_f32_16x16x32_bf16 v[26:29], v[98:101], v[196:199], v[26:29]
	s_waitcnt lgkmcnt(2)
	v_mfma_f32_16x16x32_bf16 v[30:33], v[94:97], v[200:203], v[30:33]
	v_mfma_f32_16x16x32_bf16 v[26:29], v[102:105], v[200:203], v[26:29]
	s_waitcnt lgkmcnt(1)
	v_mfma_f32_16x16x32_bf16 v[14:17], v[90:93], v[204:207], v[14:17]
	v_mfma_f32_16x16x32_bf16 v[10:13], v[98:101], v[204:207], v[10:13]
	s_waitcnt lgkmcnt(0)
	v_mfma_f32_16x16x32_bf16 v[14:17], v[94:97], v[208:211], v[14:17]
	v_mfma_f32_16x16x32_bf16 v[10:13], v[102:105], v[208:211], v[10:13]
	s_setprio 0
	s_barrier
	s_add_u32 s46, s8, 0x40000
	s_addc_u32 s47, s9, 0
	s_mov_b32 m0, s62
	v_lshl_add_u64 v[90:91], s[46:47], 0, v[150:151]
	global_load_lds_dwordx4 v[90:91], off
	v_lshl_add_u64 v[90:91], s[46:47], 0, v[146:147]
	s_mov_b32 m0, s63
	s_nop 0
	global_load_lds_dwordx4 v[90:91], off
	s_waitcnt vmcnt(6)
	s_barrier
	s_setprio 1
	v_mfma_f32_16x16x32_bf16 v[54:57], v[212:215], v[158:161], v[54:57]
	v_mfma_f32_16x16x32_bf16 v[50:53], v[232:235], v[158:161], v[50:53]
	v_mfma_f32_16x16x32_bf16 v[38:41], v[212:215], v[188:191], v[38:41]
	v_mfma_f32_16x16x32_bf16 v[34:37], v[232:235], v[188:191], v[34:37]
	v_mfma_f32_16x16x32_bf16 v[22:25], v[212:215], v[196:199], v[22:25]
	v_mfma_f32_16x16x32_bf16 v[18:21], v[232:235], v[196:199], v[18:21]
	v_mfma_f32_16x16x32_bf16 v[6:9], v[212:215], v[204:207], v[6:9]
	v_mfma_f32_16x16x32_bf16 v[2:5], v[232:235], v[204:207], v[2:5]
	v_mfma_f32_16x16x32_bf16 v[54:57], v[216:219], v[182:185], v[54:57]
	v_mfma_f32_16x16x32_bf16 v[50:53], v[236:239], v[182:185], v[50:53]
	v_mfma_f32_16x16x32_bf16 v[38:41], v[216:219], v[192:195], v[38:41]
	v_mfma_f32_16x16x32_bf16 v[34:37], v[236:239], v[192:195], v[34:37]
	v_mfma_f32_16x16x32_bf16 v[22:25], v[216:219], v[200:203], v[22:25]
	v_mfma_f32_16x16x32_bf16 v[18:21], v[236:239], v[200:203], v[18:21]
	v_mfma_f32_16x16x32_bf16 v[6:9], v[216:219], v[208:211], v[6:9]
	v_mfma_f32_16x16x32_bf16 v[2:5], v[236:239], v[208:211], v[2:5]
	s_setprio 0
	s_barrier
	ds_read_b128 v[90:93], v174
	ds_read_b128 v[94:97], v175
	ds_read_b128 v[98:101], v176
	ds_read_b128 v[102:105], v177
	s_add_u32 s38, s38, 0x40000
	s_addc_u32 s39, s39, 0
	s_mov_b32 m0, s64
	v_lshl_add_u64 v[212:213], s[38:39], 0, v[152:153]
	ds_read_b128 v[158:161], v0 offset:32768
	ds_read_b128 v[182:185], v0 offset:33792
	ds_read_b128 v[188:191], v0 offset:34816
	ds_read_b128 v[192:195], v0 offset:35840
	ds_read_b128 v[196:199], v0 offset:36864
	ds_read_b128 v[200:203], v0 offset:37888
	ds_read_b128 v[204:207], v0 offset:38912
	ds_read_b128 v[208:211], v0 offset:39936
	global_load_lds_dwordx4 v[212:213], off
	v_lshl_add_u64 v[212:213], s[38:39], 0, v[148:149]
	s_mov_b32 m0, s65
	s_nop 0
	global_load_lds_dwordx4 v[212:213], off
	s_waitcnt lgkmcnt(8)
	s_barrier
	s_setprio 1
	s_waitcnt lgkmcnt(7)
	v_mfma_f32_16x16x32_bf16 v[142:145], v[90:93], v[158:161], v[142:145]
	v_mfma_f32_16x16x32_bf16 v[138:141], v[98:101], v[158:161], v[138:141]
	s_waitcnt lgkmcnt(6)
	v_mfma_f32_16x16x32_bf16 v[142:145], v[94:97], v[182:185], v[142:145]
	v_mfma_f32_16x16x32_bf16 v[138:141], v[102:105], v[182:185], v[138:141]
	s_waitcnt lgkmcnt(5)
	v_mfma_f32_16x16x32_bf16 v[126:129], v[90:93], v[188:191], v[126:129]
	v_mfma_f32_16x16x32_bf16 v[122:125], v[98:101], v[188:191], v[122:125]
	s_waitcnt lgkmcnt(4)
	v_mfma_f32_16x16x32_bf16 v[126:129], v[94:97], v[192:195], v[126:129]
	v_mfma_f32_16x16x32_bf16 v[122:125], v[102:105], v[192:195], v[122:125]
	s_waitcnt lgkmcnt(3)
	v_mfma_f32_16x16x32_bf16 v[110:113], v[90:93], v[196:199], v[110:113]
	v_mfma_f32_16x16x32_bf16 v[106:109], v[98:101], v[196:199], v[106:109]
	s_waitcnt lgkmcnt(2)
	v_mfma_f32_16x16x32_bf16 v[110:113], v[94:97], v[200:203], v[110:113]
	v_mfma_f32_16x16x32_bf16 v[106:109], v[102:105], v[200:203], v[106:109]
	s_waitcnt lgkmcnt(1)
	v_mfma_f32_16x16x32_bf16 v[78:81], v[90:93], v[204:207], v[78:81]
	v_mfma_f32_16x16x32_bf16 v[74:77], v[98:101], v[204:207], v[74:77]
	s_waitcnt lgkmcnt(0)
	v_mfma_f32_16x16x32_bf16 v[78:81], v[94:97], v[208:211], v[78:81]
	v_mfma_f32_16x16x32_bf16 v[74:77], v[102:105], v[208:211], v[74:77]
	s_setprio 0
	s_barrier
	s_mov_b32 m0, s69
	v_lshl_add_u64 v[164:165], v[164:165], 0, s[24:25]
	ds_read_b128 v[212:215], v178
	ds_read_b128 v[216:219], v179
	ds_read_b128 v[232:235], v180
	ds_read_b128 v[236:239], v181
	global_load_lds_dwordx4 v[164:165], off
	v_lshl_add_u64 v[164:165], v[220:221], 0, s[24:25]
	s_mov_b32 m0, s70
	s_nop 0
	global_load_lds_dwordx4 v[164:165], off
	s_barrier
	s_setprio 1
	s_waitcnt lgkmcnt(3)
	v_mfma_f32_16x16x32_bf16 v[134:137], v[212:215], v[158:161], v[134:137]
	v_mfma_f32_16x16x32_bf16 v[118:121], v[212:215], v[188:191], v[118:121]
	v_mfma_f32_16x16x32_bf16 v[86:89], v[212:215], v[196:199], v[86:89]
	v_mfma_f32_16x16x32_bf16 v[70:73], v[212:215], v[204:207], v[70:73]
	s_waitcnt lgkmcnt(2)
	v_mfma_f32_16x16x32_bf16 v[134:137], v[216:219], v[182:185], v[134:137]
	v_mfma_f32_16x16x32_bf16 v[118:121], v[216:219], v[192:195], v[118:121]
	v_mfma_f32_16x16x32_bf16 v[86:89], v[216:219], v[200:203], v[86:89]
	v_mfma_f32_16x16x32_bf16 v[70:73], v[216:219], v[208:211], v[70:73]
	s_waitcnt lgkmcnt(1)
	v_mfma_f32_16x16x32_bf16 v[130:133], v[232:235], v[158:161], v[130:133]
	v_mfma_f32_16x16x32_bf16 v[114:117], v[232:235], v[188:191], v[114:117]
	v_mfma_f32_16x16x32_bf16 v[82:85], v[232:235], v[196:199], v[82:85]
	v_mfma_f32_16x16x32_bf16 v[66:69], v[232:235], v[204:207], v[66:69]
	s_waitcnt lgkmcnt(0)
	v_mfma_f32_16x16x32_bf16 v[130:133], v[236:239], v[182:185], v[130:133]
	v_mfma_f32_16x16x32_bf16 v[114:117], v[236:239], v[192:195], v[114:117]
	v_mfma_f32_16x16x32_bf16 v[82:85], v[236:239], v[200:203], v[82:85]
	v_mfma_f32_16x16x32_bf16 v[66:69], v[236:239], v[208:211], v[66:69]
	s_setprio 0
	s_mov_b32 m0, s71
	v_lshl_add_u64 v[164:165], v[240:241], 0, s[24:25]
	s_barrier
	ds_read_b128 v[158:161], v0 offset:49152
	ds_read_b128 v[182:185], v0 offset:50176
	ds_read_b128 v[188:191], v0 offset:51200
	ds_read_b128 v[192:195], v0 offset:52224
	ds_read_b128 v[196:199], v0 offset:53248
	ds_read_b128 v[200:203], v0 offset:54272
	ds_read_b128 v[204:207], v0 offset:55296
	ds_read_b128 v[208:211], v0 offset:56320
	global_load_lds_dwordx4 v[164:165], off
	v_lshl_add_u64 v[164:165], v[242:243], 0, s[24:25]
	s_mov_b32 m0, s72
	s_nop 0
	global_load_lds_dwordx4 v[164:165], off
	s_barrier
	s_setprio 1
	s_waitcnt lgkmcnt(7)
	v_mfma_f32_16x16x32_bf16 v[62:65], v[90:93], v[158:161], v[62:65]
	v_mfma_f32_16x16x32_bf16 v[58:61], v[98:101], v[158:161], v[58:61]
	s_waitcnt lgkmcnt(6)
	v_mfma_f32_16x16x32_bf16 v[62:65], v[94:97], v[182:185], v[62:65]
	v_mfma_f32_16x16x32_bf16 v[58:61], v[102:105], v[182:185], v[58:61]
	s_waitcnt lgkmcnt(5)
	v_mfma_f32_16x16x32_bf16 v[46:49], v[90:93], v[188:191], v[46:49]
	v_mfma_f32_16x16x32_bf16 v[42:45], v[98:101], v[188:191], v[42:45]
	s_waitcnt lgkmcnt(4)
	v_mfma_f32_16x16x32_bf16 v[46:49], v[94:97], v[192:195], v[46:49]
	v_mfma_f32_16x16x32_bf16 v[42:45], v[102:105], v[192:195], v[42:45]
	s_waitcnt lgkmcnt(3)
	v_mfma_f32_16x16x32_bf16 v[30:33], v[90:93], v[196:199], v[30:33]
	v_mfma_f32_16x16x32_bf16 v[26:29], v[98:101], v[196:199], v[26:29]
	s_waitcnt lgkmcnt(2)
	v_mfma_f32_16x16x32_bf16 v[30:33], v[94:97], v[200:203], v[30:33]
	v_mfma_f32_16x16x32_bf16 v[26:29], v[102:105], v[200:203], v[26:29]
	s_waitcnt lgkmcnt(1)
	v_mfma_f32_16x16x32_bf16 v[14:17], v[90:93], v[204:207], v[14:17]
	v_mfma_f32_16x16x32_bf16 v[10:13], v[98:101], v[204:207], v[10:13]
	s_waitcnt lgkmcnt(0)
	v_mfma_f32_16x16x32_bf16 v[14:17], v[94:97], v[208:211], v[14:17]
	v_mfma_f32_16x16x32_bf16 v[10:13], v[102:105], v[208:211], v[10:13]
	s_setprio 0
	s_barrier
	s_add_u32 s8, s8, 0x40080
	s_addc_u32 s9, s9, 0
	s_mov_b32 m0, s73
	v_lshl_add_u64 v[90:91], s[8:9], 0, v[150:151]
	global_load_lds_dwordx4 v[90:91], off
	v_lshl_add_u64 v[90:91], s[8:9], 0, v[146:147]
	s_mov_b32 m0, s74
	s_nop 0
	global_load_lds_dwordx4 v[90:91], off
	s_waitcnt vmcnt(6)
	s_barrier
	s_setprio 1
	v_mfma_f32_16x16x32_bf16 v[54:57], v[212:215], v[158:161], v[54:57]
	v_mfma_f32_16x16x32_bf16 v[50:53], v[232:235], v[158:161], v[50:53]
	v_mfma_f32_16x16x32_bf16 v[38:41], v[212:215], v[188:191], v[38:41]
	v_mfma_f32_16x16x32_bf16 v[34:37], v[232:235], v[188:191], v[34:37]
	v_mfma_f32_16x16x32_bf16 v[22:25], v[212:215], v[196:199], v[22:25]
	v_mfma_f32_16x16x32_bf16 v[18:21], v[232:235], v[196:199], v[18:21]
	v_mfma_f32_16x16x32_bf16 v[6:9], v[212:215], v[204:207], v[6:9]
	v_mfma_f32_16x16x32_bf16 v[2:5], v[232:235], v[204:207], v[2:5]
	v_mfma_f32_16x16x32_bf16 v[54:57], v[216:219], v[182:185], v[54:57]
	v_mfma_f32_16x16x32_bf16 v[50:53], v[236:239], v[182:185], v[50:53]
	v_mfma_f32_16x16x32_bf16 v[38:41], v[216:219], v[192:195], v[38:41]
	v_mfma_f32_16x16x32_bf16 v[34:37], v[236:239], v[192:195], v[34:37]
	v_mfma_f32_16x16x32_bf16 v[22:25], v[216:219], v[200:203], v[22:25]
	v_mfma_f32_16x16x32_bf16 v[18:21], v[236:239], v[200:203], v[18:21]
	v_mfma_f32_16x16x32_bf16 v[6:9], v[216:219], v[208:211], v[6:9]
	v_mfma_f32_16x16x32_bf16 v[2:5], v[236:239], v[208:211], v[2:5]
	s_setprio 0
	s_add_i32 s44, s44, 2
	s_add_u32 s6, s6, 0x100
	s_addc_u32 s7, s7, 0
	s_add_u32 s41, s41, 0x100
	s_addc_u32 s42, s42, 0
	s_cmp_gt_u32 s44, 13
	s_barrier
	s_cbranch_scc0 .LBB0_973
	s_cmp_eq_u32 s76, 6
	s_cselect_b64 s[46:47], -1, 0
	s_cmp_lg_u32 s76, 6
	s_cselect_b64 s[40:41], -1, 0
	s_cmp_gt_i32 s76, 1
	s_cselect_b64 s[38:39], -1, 0
	s_cmp_gt_u32 s76, 5
	s_cselect_b64 s[48:49], -1, 0
	s_cmp_lt_u32 s76, 6
	s_movk_i32 s6, 0xc0
	s_cselect_b32 s8, 0x80, s6
	s_cmp_gt_u32 s76, 3
	s_cselect_b64 s[50:51], -1, 0
	s_and_b64 s[6:7], s[50:51], exec
	s_cselect_b32 s28, s8, 64
	s_cmp_lt_i32 s76, 2
	s_cselect_b64 s[8:9], -1, 0
	s_and_b64 s[6:7], s[8:9], exec
	s_cselect_b32 s6, 0, s28
	v_mbcnt_lo_u32_b32 v161, -1, 0
	v_mbcnt_hi_u32_b32 v161, -1, v161
	s_lshl_b32 s6, s6, 2
	v_lshrrev_b32_e32 v0, 1, v161
	s_add_u32 s6, s66, s6
	v_and_b32_e32 v160, 24, v0
	s_addc_u32 s7, s67, 0
	v_lshlrev_b32_e32 v0, 2, v160
	v_mov_b32_e32 v90, 1.0
	v_readlane_b32 s15, v252, 51
	v_readlane_b32 s13, v252, 52
	v_lshl_add_u64 v[158:159], s[6:7], 0, v[0:1]
	s_and_b64 vcc, exec, s[46:47]
	v_mov_b32_e32 v94, 1.0
	v_mov_b32_e32 v95, v90
	v_mov_b32_e32 v96, 1.0
	v_mov_b32_e32 v97, 1.0
	s_cbranch_vccnz .LBB0_976
	global_load_dwordx4 v[94:97], v[158:159], off

.LBB0_1055:
	ds_read_b128 v[142:145], v149
	ds_read_b128 v[166:169], v150
	ds_read_b128 v[170:173], v151
	ds_read_b128 v[174:177], v152
	s_add_u32 s40, s38, 0xfffc0080
	s_addc_u32 s41, s39, -1
	s_cmp_eq_u32 s65, 12
	s_cselect_b32 s43, s7, s41
	s_cselect_b32 s42, s15, s40
	s_cselect_b32 s41, s13, s64
	s_cselect_b32 s40, s62, s63
	v_add_u32_e32 v0, s53, v148
	v_lshl_add_u64 v[146:147], s[38:39], 0, v[138:139]
	s_add_i32 m0, s46, 0xc000
	ds_read_b128 v[178:181], v0
	ds_read_b128 v[182:185], v0 offset:1024
	ds_read_b128 v[188:191], v0 offset:2048
	ds_read_b128 v[192:195], v0 offset:3072
	ds_read_b128 v[196:199], v0 offset:4096
	ds_read_b128 v[200:203], v0 offset:5120
	ds_read_b128 v[204:207], v0 offset:6144
	ds_read_b128 v[208:211], v0 offset:7168
	global_load_lds_dwordx4 v[146:147], off
	v_lshl_add_u64 v[146:147], s[38:39], 0, v[140:141]
	s_add_i32 m0, s46, 0xe000
	s_nop 0
	global_load_lds_dwordx4 v[146:147], off
	s_waitcnt lgkmcnt(8)
	s_barrier
	s_setprio 1
	s_waitcnt lgkmcnt(7)
	v_mfma_f32_16x16x32_bf16 v[126:129], v[142:145], v[178:181], v[126:129]
	v_mfma_f32_16x16x32_bf16 v[122:125], v[170:173], v[178:181], v[122:125]
	s_waitcnt lgkmcnt(6)
	v_mfma_f32_16x16x32_bf16 v[126:129], v[166:169], v[182:185], v[126:129]
	v_mfma_f32_16x16x32_bf16 v[122:125], v[174:177], v[182:185], v[122:125]
	s_waitcnt lgkmcnt(5)
	v_mfma_f32_16x16x32_bf16 v[110:113], v[142:145], v[188:191], v[110:113]
	v_mfma_f32_16x16x32_bf16 v[106:109], v[170:173], v[188:191], v[106:109]
	s_waitcnt lgkmcnt(4)
	v_mfma_f32_16x16x32_bf16 v[110:113], v[166:169], v[192:195], v[110:113]
	v_mfma_f32_16x16x32_bf16 v[106:109], v[174:177], v[192:195], v[106:109]
	s_waitcnt lgkmcnt(3)
	v_mfma_f32_16x16x32_bf16 v[94:97], v[142:145], v[196:199], v[94:97]
	v_mfma_f32_16x16x32_bf16 v[90:93], v[170:173], v[196:199], v[90:93]
	s_waitcnt lgkmcnt(2)
	v_mfma_f32_16x16x32_bf16 v[94:97], v[166:169], v[200:203], v[94:97]
	v_mfma_f32_16x16x32_bf16 v[90:93], v[174:177], v[200:203], v[90:93]
	s_waitcnt lgkmcnt(1)
	v_mfma_f32_16x16x32_bf16 v[78:81], v[142:145], v[204:207], v[78:81]
	v_mfma_f32_16x16x32_bf16 v[74:77], v[170:173], v[204:207], v[74:77]
	s_waitcnt lgkmcnt(0)
	v_mfma_f32_16x16x32_bf16 v[78:81], v[166:169], v[208:211], v[78:81]
	v_mfma_f32_16x16x32_bf16 v[74:77], v[174:177], v[208:211], v[74:77]
	s_setprio 0
	s_barrier
	s_mov_b32 m0, s47
	v_lshl_add_u64 v[146:147], s[40:41], 0, v[132:133]
	ds_read_b128 v[212:215], v153
	ds_read_b128 v[216:219], v154
	ds_read_b128 v[232:235], v155
	ds_read_b128 v[236:239], v156
	global_load_lds_dwordx4 v[146:147], off
	v_lshl_add_u64 v[220:221], s[40:41], 0, v[136:137]
	s_mov_b32 m0, s48
	s_nop 0
	global_load_lds_dwordx4 v[220:221], off
	s_barrier
	s_setprio 1
	s_waitcnt lgkmcnt(3)
	v_mfma_f32_16x16x32_bf16 v[118:121], v[212:215], v[178:181], v[118:121]
	v_mfma_f32_16x16x32_bf16 v[102:105], v[212:215], v[188:191], v[102:105]
	v_mfma_f32_16x16x32_bf16 v[86:89], v[212:215], v[196:199], v[86:89]
	v_mfma_f32_16x16x32_bf16 v[70:73], v[212:215], v[204:207], v[70:73]
	s_waitcnt lgkmcnt(2)
	v_mfma_f32_16x16x32_bf16 v[118:121], v[216:219], v[182:185], v[118:121]
	v_mfma_f32_16x16x32_bf16 v[102:105], v[216:219], v[192:195], v[102:105]
	v_mfma_f32_16x16x32_bf16 v[86:89], v[216:219], v[200:203], v[86:89]
	v_mfma_f32_16x16x32_bf16 v[70:73], v[216:219], v[208:211], v[70:73]
	s_waitcnt lgkmcnt(1)
	v_mfma_f32_16x16x32_bf16 v[114:117], v[232:235], v[178:181], v[114:117]
	v_mfma_f32_16x16x32_bf16 v[98:101], v[232:235], v[188:191], v[98:101]
	v_mfma_f32_16x16x32_bf16 v[82:85], v[232:235], v[196:199], v[82:85]
	v_mfma_f32_16x16x32_bf16 v[66:69], v[232:235], v[204:207], v[66:69]
	s_waitcnt lgkmcnt(0)
	v_mfma_f32_16x16x32_bf16 v[114:117], v[236:239], v[182:185], v[114:117]
	v_mfma_f32_16x16x32_bf16 v[98:101], v[236:239], v[192:195], v[98:101]
	v_mfma_f32_16x16x32_bf16 v[82:85], v[236:239], v[200:203], v[82:85]
	v_mfma_f32_16x16x32_bf16 v[66:69], v[236:239], v[208:211], v[66:69]
	s_setprio 0
	s_mov_b32 m0, s46
	v_lshl_add_u64 v[240:241], s[42:43], 0, v[130:131]
	s_barrier
	ds_read_b128 v[178:181], v0 offset:16384
	ds_read_b128 v[182:185], v0 offset:17408
	ds_read_b128 v[188:191], v0 offset:18432
	ds_read_b128 v[192:195], v0 offset:19456
	ds_read_b128 v[196:199], v0 offset:20480
	ds_read_b128 v[200:203], v0 offset:21504
	ds_read_b128 v[204:207], v0 offset:22528
	ds_read_b128 v[208:211], v0 offset:23552
	global_load_lds_dwordx4 v[240:241], off
	v_lshl_add_u64 v[242:243], s[42:43], 0, v[134:135]
	s_mov_b32 m0, s9
	s_nop 0
	global_load_lds_dwordx4 v[242:243], off
	s_barrier
	s_setprio 1
	s_waitcnt lgkmcnt(7)
	v_mfma_f32_16x16x32_bf16 v[62:65], v[142:145], v[178:181], v[62:65]
	v_mfma_f32_16x16x32_bf16 v[58:61], v[170:173], v[178:181], v[58:61]
	s_waitcnt lgkmcnt(6)
	v_mfma_f32_16x16x32_bf16 v[62:65], v[166:169], v[182:185], v[62:65]
	v_mfma_f32_16x16x32_bf16 v[58:61], v[174:177], v[182:185], v[58:61]
	s_waitcnt lgkmcnt(5)
	v_mfma_f32_16x16x32_bf16 v[46:49], v[142:145], v[188:191], v[46:49]
	v_mfma_f32_16x16x32_bf16 v[42:45], v[170:173], v[188:191], v[42:45]
	s_waitcnt lgkmcnt(4)
	v_mfma_f32_16x16x32_bf16 v[46:49], v[166:169], v[192:195], v[46:49]
	v_mfma_f32_16x16x32_bf16 v[42:45], v[174:177], v[192:195], v[42:45]
	s_waitcnt lgkmcnt(3)
	v_mfma_f32_16x16x32_bf16 v[30:33], v[142:145], v[196:199], v[30:33]
	v_mfma_f32_16x16x32_bf16 v[26:29], v[170:173], v[196:199], v[26:29]
	s_waitcnt lgkmcnt(2)
	v_mfma_f32_16x16x32_bf16 v[30:33], v[166:169], v[200:203], v[30:33]
	v_mfma_f32_16x16x32_bf16 v[26:29], v[174:177], v[200:203], v[26:29]
	s_waitcnt lgkmcnt(1)
	v_mfma_f32_16x16x32_bf16 v[14:17], v[142:145], v[204:207], v[14:17]
	v_mfma_f32_16x16x32_bf16 v[10:13], v[170:173], v[204:207], v[10:13]
	s_waitcnt lgkmcnt(0)
	v_mfma_f32_16x16x32_bf16 v[14:17], v[166:169], v[208:211], v[14:17]
	v_mfma_f32_16x16x32_bf16 v[10:13], v[174:177], v[208:211], v[10:13]
	s_setprio 0
	s_barrier
	s_add_u32 s66, s40, 0x40000
	s_addc_u32 s67, s41, 0
	s_mov_b32 m0, s49
	v_lshl_add_u64 v[142:143], s[66:67], 0, v[132:133]
	global_load_lds_dwordx4 v[142:143], off
	v_lshl_add_u64 v[142:143], s[66:67], 0, v[136:137]
	s_mov_b32 m0, s50
	s_nop 0
	global_load_lds_dwordx4 v[142:143], off
	s_waitcnt vmcnt(6)
	s_barrier
	s_setprio 1
	v_mfma_f32_16x16x32_bf16 v[54:57], v[212:215], v[178:181], v[54:57]
	v_mfma_f32_16x16x32_bf16 v[50:53], v[232:235], v[178:181], v[50:53]
	v_mfma_f32_16x16x32_bf16 v[38:41], v[212:215], v[188:191], v[38:41]
	v_mfma_f32_16x16x32_bf16 v[34:37], v[232:235], v[188:191], v[34:37]
	v_mfma_f32_16x16x32_bf16 v[22:25], v[212:215], v[196:199], v[22:25]
	v_mfma_f32_16x16x32_bf16 v[18:21], v[232:235], v[196:199], v[18:21]
	v_mfma_f32_16x16x32_bf16 v[6:9], v[212:215], v[204:207], v[6:9]
	v_mfma_f32_16x16x32_bf16 v[2:5], v[232:235], v[204:207], v[2:5]
	v_mfma_f32_16x16x32_bf16 v[54:57], v[216:219], v[182:185], v[54:57]
	v_mfma_f32_16x16x32_bf16 v[50:53], v[236:239], v[182:185], v[50:53]
	v_mfma_f32_16x16x32_bf16 v[38:41], v[216:219], v[192:195], v[38:41]
	v_mfma_f32_16x16x32_bf16 v[34:37], v[236:239], v[192:195], v[34:37]
	v_mfma_f32_16x16x32_bf16 v[22:25], v[216:219], v[200:203], v[22:25]
	v_mfma_f32_16x16x32_bf16 v[18:21], v[236:239], v[200:203], v[18:21]
	v_mfma_f32_16x16x32_bf16 v[6:9], v[216:219], v[208:211], v[6:9]
	v_mfma_f32_16x16x32_bf16 v[2:5], v[236:239], v[208:211], v[2:5]
	s_setprio 0
	s_barrier
	ds_read_b128 v[142:145], v157
	ds_read_b128 v[166:169], v158
	ds_read_b128 v[170:173], v159
	ds_read_b128 v[174:177], v160
	s_add_u32 s42, s42, 0x40000
	s_addc_u32 s43, s43, 0
	s_mov_b32 m0, s51
	v_lshl_add_u64 v[212:213], s[42:43], 0, v[130:131]
	ds_read_b128 v[178:181], v0 offset:32768
	ds_read_b128 v[182:185], v0 offset:33792
	ds_read_b128 v[188:191], v0 offset:34816
	ds_read_b128 v[192:195], v0 offset:35840
	ds_read_b128 v[196:199], v0 offset:36864
	ds_read_b128 v[200:203], v0 offset:37888
	ds_read_b128 v[204:207], v0 offset:38912
	ds_read_b128 v[208:211], v0 offset:39936
	global_load_lds_dwordx4 v[212:213], off
	v_lshl_add_u64 v[212:213], s[42:43], 0, v[134:135]
	s_mov_b32 m0, s52
	s_nop 0
	global_load_lds_dwordx4 v[212:213], off
	s_waitcnt lgkmcnt(8)
	s_barrier
	s_setprio 1
	s_waitcnt lgkmcnt(7)
	v_mfma_f32_16x16x32_bf16 v[126:129], v[142:145], v[178:181], v[126:129]
	v_mfma_f32_16x16x32_bf16 v[122:125], v[170:173], v[178:181], v[122:125]
	s_waitcnt lgkmcnt(6)
	v_mfma_f32_16x16x32_bf16 v[126:129], v[166:169], v[182:185], v[126:129]
	v_mfma_f32_16x16x32_bf16 v[122:125], v[174:177], v[182:185], v[122:125]
	s_waitcnt lgkmcnt(5)
	v_mfma_f32_16x16x32_bf16 v[110:113], v[142:145], v[188:191], v[110:113]
	v_mfma_f32_16x16x32_bf16 v[106:109], v[170:173], v[188:191], v[106:109]
	s_waitcnt lgkmcnt(4)
	v_mfma_f32_16x16x32_bf16 v[110:113], v[166:169], v[192:195], v[110:113]
	v_mfma_f32_16x16x32_bf16 v[106:109], v[174:177], v[192:195], v[106:109]
	s_waitcnt lgkmcnt(3)
	v_mfma_f32_16x16x32_bf16 v[94:97], v[142:145], v[196:199], v[94:97]
	v_mfma_f32_16x16x32_bf16 v[90:93], v[170:173], v[196:199], v[90:93]
	s_waitcnt lgkmcnt(2)
	v_mfma_f32_16x16x32_bf16 v[94:97], v[166:169], v[200:203], v[94:97]
	v_mfma_f32_16x16x32_bf16 v[90:93], v[174:177], v[200:203], v[90:93]
	s_waitcnt lgkmcnt(1)
	v_mfma_f32_16x16x32_bf16 v[78:81], v[142:145], v[204:207], v[78:81]
	v_mfma_f32_16x16x32_bf16 v[74:77], v[170:173], v[204:207], v[74:77]
	s_waitcnt lgkmcnt(0)
	v_mfma_f32_16x16x32_bf16 v[78:81], v[166:169], v[208:211], v[78:81]
	v_mfma_f32_16x16x32_bf16 v[74:77], v[174:177], v[208:211], v[74:77]
	s_setprio 0
	s_barrier
	s_mov_b32 m0, s55
	v_lshl_add_u64 v[146:147], v[146:147], 0, s[24:25]
	ds_read_b128 v[212:215], v161
	ds_read_b128 v[216:219], v162
	ds_read_b128 v[232:235], v163
	ds_read_b128 v[236:239], v164
	global_load_lds_dwordx4 v[146:147], off
	v_lshl_add_u64 v[146:147], v[220:221], 0, s[24:25]
	s_mov_b32 m0, s56
	s_nop 0
	global_load_lds_dwordx4 v[146:147], off
	s_barrier
	s_setprio 1
	s_waitcnt lgkmcnt(3)
	v_mfma_f32_16x16x32_bf16 v[118:121], v[212:215], v[178:181], v[118:121]
	v_mfma_f32_16x16x32_bf16 v[102:105], v[212:215], v[188:191], v[102:105]
	v_mfma_f32_16x16x32_bf16 v[86:89], v[212:215], v[196:199], v[86:89]
	v_mfma_f32_16x16x32_bf16 v[70:73], v[212:215], v[204:207], v[70:73]
	s_waitcnt lgkmcnt(2)
	v_mfma_f32_16x16x32_bf16 v[118:121], v[216:219], v[182:185], v[118:121]
	v_mfma_f32_16x16x32_bf16 v[102:105], v[216:219], v[192:195], v[102:105]
	v_mfma_f32_16x16x32_bf16 v[86:89], v[216:219], v[200:203], v[86:89]
	v_mfma_f32_16x16x32_bf16 v[70:73], v[216:219], v[208:211], v[70:73]
	s_waitcnt lgkmcnt(1)
	v_mfma_f32_16x16x32_bf16 v[114:117], v[232:235], v[178:181], v[114:117]
	v_mfma_f32_16x16x32_bf16 v[98:101], v[232:235], v[188:191], v[98:101]
	v_mfma_f32_16x16x32_bf16 v[82:85], v[232:235], v[196:199], v[82:85]
	v_mfma_f32_16x16x32_bf16 v[66:69], v[232:235], v[204:207], v[66:69]
	s_waitcnt lgkmcnt(0)
	v_mfma_f32_16x16x32_bf16 v[114:117], v[236:239], v[182:185], v[114:117]
	v_mfma_f32_16x16x32_bf16 v[98:101], v[236:239], v[192:195], v[98:101]
	v_mfma_f32_16x16x32_bf16 v[82:85], v[236:239], v[200:203], v[82:85]
	v_mfma_f32_16x16x32_bf16 v[66:69], v[236:239], v[208:211], v[66:69]
	s_setprio 0
	s_mov_b32 m0, s57
	v_lshl_add_u64 v[146:147], v[240:241], 0, s[24:25]
	s_barrier
	ds_read_b128 v[178:181], v0 offset:49152
	ds_read_b128 v[182:185], v0 offset:50176
	ds_read_b128 v[188:191], v0 offset:51200
	ds_read_b128 v[192:195], v0 offset:52224
	ds_read_b128 v[196:199], v0 offset:53248
	ds_read_b128 v[200:203], v0 offset:54272
	ds_read_b128 v[204:207], v0 offset:55296
	ds_read_b128 v[208:211], v0 offset:56320
	global_load_lds_dwordx4 v[146:147], off
	v_lshl_add_u64 v[146:147], v[242:243], 0, s[24:25]
	s_mov_b32 m0, s58
	s_nop 0
	global_load_lds_dwordx4 v[146:147], off
	s_barrier
	s_setprio 1
	s_waitcnt lgkmcnt(7)
	v_mfma_f32_16x16x32_bf16 v[62:65], v[142:145], v[178:181], v[62:65]
	v_mfma_f32_16x16x32_bf16 v[58:61], v[170:173], v[178:181], v[58:61]
	s_waitcnt lgkmcnt(6)
	v_mfma_f32_16x16x32_bf16 v[62:65], v[166:169], v[182:185], v[62:65]
	v_mfma_f32_16x16x32_bf16 v[58:61], v[174:177], v[182:185], v[58:61]
	s_waitcnt lgkmcnt(5)
	v_mfma_f32_16x16x32_bf16 v[46:49], v[142:145], v[188:191], v[46:49]
	v_mfma_f32_16x16x32_bf16 v[42:45], v[170:173], v[188:191], v[42:45]
	s_waitcnt lgkmcnt(4)
	v_mfma_f32_16x16x32_bf16 v[46:49], v[166:169], v[192:195], v[46:49]
	v_mfma_f32_16x16x32_bf16 v[42:45], v[174:177], v[192:195], v[42:45]
	s_waitcnt lgkmcnt(3)
	v_mfma_f32_16x16x32_bf16 v[30:33], v[142:145], v[196:199], v[30:33]
	v_mfma_f32_16x16x32_bf16 v[26:29], v[170:173], v[196:199], v[26:29]
	s_waitcnt lgkmcnt(2)
	v_mfma_f32_16x16x32_bf16 v[30:33], v[166:169], v[200:203], v[30:33]
	v_mfma_f32_16x16x32_bf16 v[26:29], v[174:177], v[200:203], v[26:29]
	s_waitcnt lgkmcnt(1)
	v_mfma_f32_16x16x32_bf16 v[14:17], v[142:145], v[204:207], v[14:17]
	v_mfma_f32_16x16x32_bf16 v[10:13], v[170:173], v[204:207], v[10:13]
	s_waitcnt lgkmcnt(0)
	v_mfma_f32_16x16x32_bf16 v[14:17], v[166:169], v[208:211], v[14:17]
	v_mfma_f32_16x16x32_bf16 v[10:13], v[174:177], v[208:211], v[10:13]
	s_setprio 0
	s_barrier
	s_add_u32 s40, s40, 0x40080
	s_addc_u32 s41, s41, 0
	s_mov_b32 m0, s59
	v_lshl_add_u64 v[142:143], s[40:41], 0, v[132:133]
	global_load_lds_dwordx4 v[142:143], off
	v_lshl_add_u64 v[142:143], s[40:41], 0, v[136:137]
	s_mov_b32 m0, s60
	s_nop 0
	global_load_lds_dwordx4 v[142:143], off
	s_waitcnt vmcnt(6)
	s_barrier
	s_setprio 1
	v_mfma_f32_16x16x32_bf16 v[54:57], v[212:215], v[178:181], v[54:57]
	v_mfma_f32_16x16x32_bf16 v[50:53], v[232:235], v[178:181], v[50:53]
	v_mfma_f32_16x16x32_bf16 v[38:41], v[212:215], v[188:191], v[38:41]
	v_mfma_f32_16x16x32_bf16 v[34:37], v[232:235], v[188:191], v[34:37]
	v_mfma_f32_16x16x32_bf16 v[22:25], v[212:215], v[196:199], v[22:25]
	v_mfma_f32_16x16x32_bf16 v[18:21], v[232:235], v[196:199], v[18:21]
	v_mfma_f32_16x16x32_bf16 v[6:9], v[212:215], v[204:207], v[6:9]
	v_mfma_f32_16x16x32_bf16 v[2:5], v[232:235], v[204:207], v[2:5]
	v_mfma_f32_16x16x32_bf16 v[54:57], v[216:219], v[182:185], v[54:57]
	v_mfma_f32_16x16x32_bf16 v[50:53], v[236:239], v[182:185], v[50:53]
	v_mfma_f32_16x16x32_bf16 v[38:41], v[216:219], v[192:195], v[38:41]
	v_mfma_f32_16x16x32_bf16 v[34:37], v[236:239], v[192:195], v[34:37]
	v_mfma_f32_16x16x32_bf16 v[22:25], v[216:219], v[200:203], v[22:25]
	v_mfma_f32_16x16x32_bf16 v[18:21], v[236:239], v[200:203], v[18:21]
	v_mfma_f32_16x16x32_bf16 v[6:9], v[216:219], v[208:211], v[6:9]
	v_mfma_f32_16x16x32_bf16 v[2:5], v[236:239], v[208:211], v[2:5]
	s_setprio 0
	s_add_i32 s65, s65, 2
	s_add_u32 s38, s38, 0x100
	s_addc_u32 s39, s39, 0
	s_add_u32 s63, s63, 0x100
	s_addc_u32 s64, s64, 0
	s_cmp_gt_u32 s65, 13
	s_barrier
	s_cbranch_scc0 .LBB0_1055
	v_readlane_b32 s13, v252, 51
	v_readlane_b32 s7, v252, 52
	v_mbcnt_lo_u32_b32 v143, -1, 0
	v_mbcnt_hi_u32_b32 v143, -1, v143
	s_lshl_b32 s15, s13, 6
	s_cmp_gt_i32 s8, 1
	v_and_b32_e32 v144, 15, v143
	s_cselect_b64 s[40:41], -1, 0
	v_or_b32_e32 v142, s15, v144
	s_mov_b64 s[42:43], -1
	s_and_b64 vcc, exec, s[40:41]
	s_cbranch_vccz .LBB0_1058
	s_movk_i32 s38, 0x80
	v_cmp_gt_i32_e32 vcc, s38, v142
	s_mov_b64 s[42:43], 0
	s_nop 0
	v_cndmask_b32_e32 v0, v187, v223, vcc
	v_mov_b64_e32 v[146:147], v[0:1]

.LBB0_1150:
	ds_read_b128 v[102:105], v155
	ds_read_b128 v[110:113], v156
	ds_read_b128 v[148:151], v157
	ds_read_b128 v[172:175], v158
	s_add_u32 s34, s20, 0xfffc0080
	s_addc_u32 s35, s21, -1
	s_cmp_eq_u32 s71, 28
	s_cselect_b32 s39, s65, s35
	s_cselect_b32 s38, s66, s34
	s_cselect_b32 s35, s67, s70
	s_cselect_b32 s34, s68, s69
	v_add_u32_e32 v171, s55, v154
	v_lshl_add_u64 v[152:153], s[20:21], 0, v[144:145]
	s_add_i32 m0, s46, 0xc000
	ds_read_b128 v[176:179], v171
	ds_read_b128 v[180:183], v171 offset:1024
	ds_read_b128 v[188:191], v171 offset:2048
	ds_read_b128 v[192:195], v171 offset:3072
	ds_read_b128 v[196:199], v171 offset:4096
	ds_read_b128 v[200:203], v171 offset:5120
	ds_read_b128 v[204:207], v171 offset:6144
	ds_read_b128 v[208:211], v171 offset:7168
	global_load_lds_dwordx4 v[152:153], off
	v_lshl_add_u64 v[152:153], s[20:21], 0, v[146:147]
	s_add_i32 m0, s46, 0xe000
	s_nop 0
	global_load_lds_dwordx4 v[152:153], off
	s_waitcnt lgkmcnt(8)
	s_barrier
	s_setprio 1
	s_waitcnt lgkmcnt(7)
	v_mfma_f32_16x16x32_bf16 v[134:137], v[102:105], v[176:179], v[134:137]
	v_mfma_f32_16x16x32_bf16 v[130:133], v[148:151], v[176:179], v[130:133]
	s_waitcnt lgkmcnt(6)
	v_mfma_f32_16x16x32_bf16 v[134:137], v[110:113], v[180:183], v[134:137]
	v_mfma_f32_16x16x32_bf16 v[130:133], v[172:175], v[180:183], v[130:133]
	s_waitcnt lgkmcnt(5)
	v_mfma_f32_16x16x32_bf16 v[126:129], v[102:105], v[188:191], v[126:129]
	v_mfma_f32_16x16x32_bf16 v[122:125], v[148:151], v[188:191], v[122:125]
	s_waitcnt lgkmcnt(4)
	v_mfma_f32_16x16x32_bf16 v[126:129], v[110:113], v[192:195], v[126:129]
	v_mfma_f32_16x16x32_bf16 v[122:125], v[172:175], v[192:195], v[122:125]
	s_waitcnt lgkmcnt(3)
	v_mfma_f32_16x16x32_bf16 v[118:121], v[102:105], v[196:199], v[118:121]
	v_mfma_f32_16x16x32_bf16 v[114:117], v[148:151], v[196:199], v[114:117]
	s_waitcnt lgkmcnt(2)
	v_mfma_f32_16x16x32_bf16 v[118:121], v[110:113], v[200:203], v[118:121]
	v_mfma_f32_16x16x32_bf16 v[114:117], v[172:175], v[200:203], v[114:117]
	s_waitcnt lgkmcnt(1)
	v_mfma_f32_16x16x32_bf16 v[106:109], v[102:105], v[204:207], v[106:109]
	v_mfma_f32_16x16x32_bf16 v[98:101], v[148:151], v[204:207], v[98:101]
	s_waitcnt lgkmcnt(0)
	v_mfma_f32_16x16x32_bf16 v[106:109], v[110:113], v[208:211], v[106:109]
	v_mfma_f32_16x16x32_bf16 v[98:101], v[172:175], v[208:211], v[98:101]
	s_setprio 0
	s_barrier
	s_mov_b32 m0, s47
	v_lshl_add_u64 v[152:153], s[34:35], 0, v[0:1]
	ds_read_b128 v[212:215], v159
	ds_read_b128 v[216:219], v160
	ds_read_b128 v[232:235], v161
	ds_read_b128 v[236:239], v162
	global_load_lds_dwordx4 v[152:153], off
	v_lshl_add_u64 v[184:185], s[34:35], 0, v[138:139]
	s_mov_b32 m0, s48
	s_nop 0
	global_load_lds_dwordx4 v[184:185], off
	s_barrier
	s_setprio 1
	s_waitcnt lgkmcnt(3)
	v_mfma_f32_16x16x32_bf16 v[62:65], v[212:215], v[176:179], v[62:65]
	v_mfma_f32_16x16x32_bf16 v[54:57], v[212:215], v[188:191], v[54:57]
	v_mfma_f32_16x16x32_bf16 v[46:49], v[212:215], v[196:199], v[46:49]
	v_mfma_f32_16x16x32_bf16 v[38:41], v[212:215], v[204:207], v[38:41]
	s_waitcnt lgkmcnt(2)
	v_mfma_f32_16x16x32_bf16 v[62:65], v[216:219], v[180:183], v[62:65]
	v_mfma_f32_16x16x32_bf16 v[54:57], v[216:219], v[192:195], v[54:57]
	v_mfma_f32_16x16x32_bf16 v[46:49], v[216:219], v[200:203], v[46:49]
	v_mfma_f32_16x16x32_bf16 v[38:41], v[216:219], v[208:211], v[38:41]
	s_waitcnt lgkmcnt(1)
	v_mfma_f32_16x16x32_bf16 v[58:61], v[232:235], v[176:179], v[58:61]
	v_mfma_f32_16x16x32_bf16 v[50:53], v[232:235], v[188:191], v[50:53]
	v_mfma_f32_16x16x32_bf16 v[42:45], v[232:235], v[196:199], v[42:45]
	v_mfma_f32_16x16x32_bf16 v[34:37], v[232:235], v[204:207], v[34:37]
	s_waitcnt lgkmcnt(0)
	v_mfma_f32_16x16x32_bf16 v[58:61], v[236:239], v[180:183], v[58:61]
	v_mfma_f32_16x16x32_bf16 v[50:53], v[236:239], v[192:195], v[50:53]
	v_mfma_f32_16x16x32_bf16 v[42:45], v[236:239], v[200:203], v[42:45]
	v_mfma_f32_16x16x32_bf16 v[34:37], v[236:239], v[208:211], v[34:37]
	s_setprio 0
	s_mov_b32 m0, s46
	v_lshl_add_u64 v[220:221], s[38:39], 0, v[142:143]
	s_barrier
	ds_read_b128 v[176:179], v171 offset:16384
	ds_read_b128 v[180:183], v171 offset:17408
	ds_read_b128 v[188:191], v171 offset:18432
	ds_read_b128 v[192:195], v171 offset:19456
	ds_read_b128 v[196:199], v171 offset:20480
	ds_read_b128 v[200:203], v171 offset:21504
	ds_read_b128 v[204:207], v171 offset:22528
	ds_read_b128 v[208:211], v171 offset:23552
	global_load_lds_dwordx4 v[220:221], off
	v_lshl_add_u64 v[240:241], s[38:39], 0, v[140:141]
	s_mov_b32 m0, s49
	s_nop 0
	global_load_lds_dwordx4 v[240:241], off
	s_barrier
	s_setprio 1
	s_waitcnt lgkmcnt(7)
	v_mfma_f32_16x16x32_bf16 v[94:97], v[102:105], v[176:179], v[94:97]
	v_mfma_f32_16x16x32_bf16 v[90:93], v[148:151], v[176:179], v[90:93]
	s_waitcnt lgkmcnt(6)
	v_mfma_f32_16x16x32_bf16 v[94:97], v[110:113], v[180:183], v[94:97]
	v_mfma_f32_16x16x32_bf16 v[90:93], v[172:175], v[180:183], v[90:93]
	s_waitcnt lgkmcnt(5)
	v_mfma_f32_16x16x32_bf16 v[86:89], v[102:105], v[188:191], v[86:89]
	v_mfma_f32_16x16x32_bf16 v[82:85], v[148:151], v[188:191], v[82:85]
	s_waitcnt lgkmcnt(4)
	v_mfma_f32_16x16x32_bf16 v[86:89], v[110:113], v[192:195], v[86:89]
	v_mfma_f32_16x16x32_bf16 v[82:85], v[172:175], v[192:195], v[82:85]
	s_waitcnt lgkmcnt(3)
	v_mfma_f32_16x16x32_bf16 v[78:81], v[102:105], v[196:199], v[78:81]
	v_mfma_f32_16x16x32_bf16 v[74:77], v[148:151], v[196:199], v[74:77]
	s_waitcnt lgkmcnt(2)
	v_mfma_f32_16x16x32_bf16 v[78:81], v[110:113], v[200:203], v[78:81]
	v_mfma_f32_16x16x32_bf16 v[74:77], v[172:175], v[200:203], v[74:77]
	s_waitcnt lgkmcnt(1)
	v_mfma_f32_16x16x32_bf16 v[70:73], v[102:105], v[204:207], v[70:73]
	v_mfma_f32_16x16x32_bf16 v[66:69], v[148:151], v[204:207], v[66:69]
	s_waitcnt lgkmcnt(0)
	v_mfma_f32_16x16x32_bf16 v[70:73], v[110:113], v[208:211], v[70:73]
	v_mfma_f32_16x16x32_bf16 v[66:69], v[172:175], v[208:211], v[66:69]
	s_setprio 0
	s_barrier
	s_add_u32 s72, s34, 0x80000
	s_addc_u32 s73, s35, 0
	s_mov_b32 m0, s50
	v_lshl_add_u64 v[102:103], s[72:73], 0, v[0:1]
	global_load_lds_dwordx4 v[102:103], off
	v_lshl_add_u64 v[102:103], s[72:73], 0, v[138:139]
	s_mov_b32 m0, s51
	s_nop 0
	global_load_lds_dwordx4 v[102:103], off
	s_waitcnt vmcnt(6)
	s_barrier
	s_setprio 1
	v_mfma_f32_16x16x32_bf16 v[30:33], v[212:215], v[176:179], v[30:33]
	v_mfma_f32_16x16x32_bf16 v[26:29], v[232:235], v[176:179], v[26:29]
	v_mfma_f32_16x16x32_bf16 v[22:25], v[212:215], v[188:191], v[22:25]
	v_mfma_f32_16x16x32_bf16 v[18:21], v[232:235], v[188:191], v[18:21]
	v_mfma_f32_16x16x32_bf16 v[14:17], v[212:215], v[196:199], v[14:17]
	v_mfma_f32_16x16x32_bf16 v[10:13], v[232:235], v[196:199], v[10:13]
	v_mfma_f32_16x16x32_bf16 v[6:9], v[212:215], v[204:207], v[6:9]
	v_mfma_f32_16x16x32_bf16 v[2:5], v[232:235], v[204:207], v[2:5]
	v_mfma_f32_16x16x32_bf16 v[30:33], v[216:219], v[180:183], v[30:33]
	v_mfma_f32_16x16x32_bf16 v[26:29], v[236:239], v[180:183], v[26:29]
	v_mfma_f32_16x16x32_bf16 v[22:25], v[216:219], v[192:195], v[22:25]
	v_mfma_f32_16x16x32_bf16 v[18:21], v[236:239], v[192:195], v[18:21]
	v_mfma_f32_16x16x32_bf16 v[14:17], v[216:219], v[200:203], v[14:17]
	v_mfma_f32_16x16x32_bf16 v[10:13], v[236:239], v[200:203], v[10:13]
	v_mfma_f32_16x16x32_bf16 v[6:9], v[216:219], v[208:211], v[6:9]
	v_mfma_f32_16x16x32_bf16 v[2:5], v[236:239], v[208:211], v[2:5]
	s_setprio 0
	s_barrier
	ds_read_b128 v[102:105], v163
	ds_read_b128 v[110:113], v164
	ds_read_b128 v[148:151], v165
	ds_read_b128 v[172:175], v166
	s_add_u32 s38, s38, 0x40000
	s_addc_u32 s39, s39, 0
	s_mov_b32 m0, s52
	v_lshl_add_u64 v[212:213], s[38:39], 0, v[142:143]
	ds_read_b128 v[176:179], v171 offset:32768
	ds_read_b128 v[180:183], v171 offset:33792
	ds_read_b128 v[188:191], v171 offset:34816
	ds_read_b128 v[192:195], v171 offset:35840
	ds_read_b128 v[196:199], v171 offset:36864
	ds_read_b128 v[200:203], v171 offset:37888
	ds_read_b128 v[204:207], v171 offset:38912
	ds_read_b128 v[208:211], v171 offset:39936
	global_load_lds_dwordx4 v[212:213], off
	v_lshl_add_u64 v[212:213], s[38:39], 0, v[140:141]
	s_mov_b32 m0, s53
	s_nop 0
	global_load_lds_dwordx4 v[212:213], off
	s_waitcnt lgkmcnt(8)
	s_barrier
	s_setprio 1
	s_waitcnt lgkmcnt(7)
	v_mfma_f32_16x16x32_bf16 v[134:137], v[102:105], v[176:179], v[134:137]
	v_mfma_f32_16x16x32_bf16 v[130:133], v[148:151], v[176:179], v[130:133]
	s_waitcnt lgkmcnt(6)
	v_mfma_f32_16x16x32_bf16 v[134:137], v[110:113], v[180:183], v[134:137]
	v_mfma_f32_16x16x32_bf16 v[130:133], v[172:175], v[180:183], v[130:133]
	s_waitcnt lgkmcnt(5)
	v_mfma_f32_16x16x32_bf16 v[126:129], v[102:105], v[188:191], v[126:129]
	v_mfma_f32_16x16x32_bf16 v[122:125], v[148:151], v[188:191], v[122:125]
	s_waitcnt lgkmcnt(4)
	v_mfma_f32_16x16x32_bf16 v[126:129], v[110:113], v[192:195], v[126:129]
	v_mfma_f32_16x16x32_bf16 v[122:125], v[172:175], v[192:195], v[122:125]
	s_waitcnt lgkmcnt(3)
	v_mfma_f32_16x16x32_bf16 v[118:121], v[102:105], v[196:199], v[118:121]
	v_mfma_f32_16x16x32_bf16 v[114:117], v[148:151], v[196:199], v[114:117]
	s_waitcnt lgkmcnt(2)
	v_mfma_f32_16x16x32_bf16 v[118:121], v[110:113], v[200:203], v[118:121]
	v_mfma_f32_16x16x32_bf16 v[114:117], v[172:175], v[200:203], v[114:117]
	s_waitcnt lgkmcnt(1)
	v_mfma_f32_16x16x32_bf16 v[106:109], v[102:105], v[204:207], v[106:109]
	v_mfma_f32_16x16x32_bf16 v[98:101], v[148:151], v[204:207], v[98:101]
	s_waitcnt lgkmcnt(0)
	v_mfma_f32_16x16x32_bf16 v[106:109], v[110:113], v[208:211], v[106:109]
	v_mfma_f32_16x16x32_bf16 v[98:101], v[172:175], v[208:211], v[98:101]
	s_setprio 0
	s_barrier
	s_mov_b32 m0, s56
	v_lshl_add_u64 v[152:153], v[152:153], 0, s[24:25]
	ds_read_b128 v[212:215], v167
	ds_read_b128 v[216:219], v168
	ds_read_b128 v[232:235], v169
	ds_read_b128 v[236:239], v170
	global_load_lds_dwordx4 v[152:153], off
	v_lshl_add_u64 v[152:153], v[184:185], 0, s[24:25]
	s_mov_b32 m0, s57
	s_nop 0
	global_load_lds_dwordx4 v[152:153], off
	s_barrier
	s_setprio 1
	s_waitcnt lgkmcnt(3)
	v_mfma_f32_16x16x32_bf16 v[62:65], v[212:215], v[176:179], v[62:65]
	v_mfma_f32_16x16x32_bf16 v[54:57], v[212:215], v[188:191], v[54:57]
	v_mfma_f32_16x16x32_bf16 v[46:49], v[212:215], v[196:199], v[46:49]
	v_mfma_f32_16x16x32_bf16 v[38:41], v[212:215], v[204:207], v[38:41]
	s_waitcnt lgkmcnt(2)
	v_mfma_f32_16x16x32_bf16 v[62:65], v[216:219], v[180:183], v[62:65]
	v_mfma_f32_16x16x32_bf16 v[54:57], v[216:219], v[192:195], v[54:57]
	v_mfma_f32_16x16x32_bf16 v[46:49], v[216:219], v[200:203], v[46:49]
	v_mfma_f32_16x16x32_bf16 v[38:41], v[216:219], v[208:211], v[38:41]
	s_waitcnt lgkmcnt(1)
	v_mfma_f32_16x16x32_bf16 v[58:61], v[232:235], v[176:179], v[58:61]
	v_mfma_f32_16x16x32_bf16 v[50:53], v[232:235], v[188:191], v[50:53]
	v_mfma_f32_16x16x32_bf16 v[42:45], v[232:235], v[196:199], v[42:45]
	v_mfma_f32_16x16x32_bf16 v[34:37], v[232:235], v[204:207], v[34:37]
	s_waitcnt lgkmcnt(0)
	v_mfma_f32_16x16x32_bf16 v[58:61], v[236:239], v[180:183], v[58:61]
	v_mfma_f32_16x16x32_bf16 v[50:53], v[236:239], v[192:195], v[50:53]
	v_mfma_f32_16x16x32_bf16 v[42:45], v[236:239], v[200:203], v[42:45]
	v_mfma_f32_16x16x32_bf16 v[34:37], v[236:239], v[208:211], v[34:37]
	s_setprio 0
	s_mov_b32 m0, s58
	v_lshl_add_u64 v[152:153], v[220:221], 0, s[24:25]
	s_barrier
	ds_read_b128 v[176:179], v171 offset:49152
	ds_read_b128 v[180:183], v171 offset:50176
	ds_read_b128 v[188:191], v171 offset:51200
	ds_read_b128 v[192:195], v171 offset:52224
	ds_read_b128 v[196:199], v171 offset:53248
	ds_read_b128 v[200:203], v171 offset:54272
	ds_read_b128 v[204:207], v171 offset:55296
	ds_read_b128 v[208:211], v171 offset:56320
	global_load_lds_dwordx4 v[152:153], off
	v_lshl_add_u64 v[152:153], v[240:241], 0, s[24:25]
	s_mov_b32 m0, s59
	s_nop 0
	global_load_lds_dwordx4 v[152:153], off
	s_barrier
	s_setprio 1
	s_waitcnt lgkmcnt(7)
	v_mfma_f32_16x16x32_bf16 v[94:97], v[102:105], v[176:179], v[94:97]
	v_mfma_f32_16x16x32_bf16 v[90:93], v[148:151], v[176:179], v[90:93]
	s_waitcnt lgkmcnt(6)
	v_mfma_f32_16x16x32_bf16 v[94:97], v[110:113], v[180:183], v[94:97]
	v_mfma_f32_16x16x32_bf16 v[90:93], v[172:175], v[180:183], v[90:93]
	s_waitcnt lgkmcnt(5)
	v_mfma_f32_16x16x32_bf16 v[86:89], v[102:105], v[188:191], v[86:89]
	v_mfma_f32_16x16x32_bf16 v[82:85], v[148:151], v[188:191], v[82:85]
	s_waitcnt lgkmcnt(4)
	v_mfma_f32_16x16x32_bf16 v[86:89], v[110:113], v[192:195], v[86:89]
	v_mfma_f32_16x16x32_bf16 v[82:85], v[172:175], v[192:195], v[82:85]
	s_waitcnt lgkmcnt(3)
	v_mfma_f32_16x16x32_bf16 v[78:81], v[102:105], v[196:199], v[78:81]
	v_mfma_f32_16x16x32_bf16 v[74:77], v[148:151], v[196:199], v[74:77]
	s_waitcnt lgkmcnt(2)
	v_mfma_f32_16x16x32_bf16 v[78:81], v[110:113], v[200:203], v[78:81]
	v_mfma_f32_16x16x32_bf16 v[74:77], v[172:175], v[200:203], v[74:77]
	s_waitcnt lgkmcnt(1)
	v_mfma_f32_16x16x32_bf16 v[70:73], v[102:105], v[204:207], v[70:73]
	v_mfma_f32_16x16x32_bf16 v[66:69], v[148:151], v[204:207], v[66:69]
	s_waitcnt lgkmcnt(0)
	v_mfma_f32_16x16x32_bf16 v[70:73], v[110:113], v[208:211], v[70:73]
	v_mfma_f32_16x16x32_bf16 v[66:69], v[172:175], v[208:211], v[66:69]
	s_setprio 0
	s_barrier
	s_add_u32 s34, s34, 0x80080
	s_addc_u32 s35, s35, 0
	s_mov_b32 m0, s60
	v_lshl_add_u64 v[102:103], s[34:35], 0, v[0:1]
	global_load_lds_dwordx4 v[102:103], off
	v_lshl_add_u64 v[102:103], s[34:35], 0, v[138:139]
	s_mov_b32 m0, s61
	s_nop 0
	global_load_lds_dwordx4 v[102:103], off
	s_waitcnt vmcnt(6)
	s_barrier
	s_setprio 1
	v_mfma_f32_16x16x32_bf16 v[30:33], v[212:215], v[176:179], v[30:33]
	v_mfma_f32_16x16x32_bf16 v[26:29], v[232:235], v[176:179], v[26:29]
	v_mfma_f32_16x16x32_bf16 v[22:25], v[212:215], v[188:191], v[22:25]
	v_mfma_f32_16x16x32_bf16 v[18:21], v[232:235], v[188:191], v[18:21]
	v_mfma_f32_16x16x32_bf16 v[14:17], v[212:215], v[196:199], v[14:17]
	v_mfma_f32_16x16x32_bf16 v[10:13], v[232:235], v[196:199], v[10:13]
	v_mfma_f32_16x16x32_bf16 v[6:9], v[212:215], v[204:207], v[6:9]
	v_mfma_f32_16x16x32_bf16 v[2:5], v[232:235], v[204:207], v[2:5]
	v_mfma_f32_16x16x32_bf16 v[30:33], v[216:219], v[180:183], v[30:33]
	v_mfma_f32_16x16x32_bf16 v[26:29], v[236:239], v[180:183], v[26:29]
	v_mfma_f32_16x16x32_bf16 v[22:25], v[216:219], v[192:195], v[22:25]
	v_mfma_f32_16x16x32_bf16 v[18:21], v[236:239], v[192:195], v[18:21]
	v_mfma_f32_16x16x32_bf16 v[14:17], v[216:219], v[200:203], v[14:17]
	v_mfma_f32_16x16x32_bf16 v[10:13], v[236:239], v[200:203], v[10:13]
	v_mfma_f32_16x16x32_bf16 v[6:9], v[216:219], v[208:211], v[6:9]
	v_mfma_f32_16x16x32_bf16 v[2:5], v[236:239], v[208:211], v[2:5]
	s_setprio 0
	s_add_i32 s71, s71, 2
	s_add_u32 s20, s20, 0x100
	s_addc_u32 s21, s21, 0
	s_add_u32 s69, s69, 0x100
	s_addc_u32 s70, s70, 0
	s_cmp_gt_u32 s71, 29
	s_barrier
	s_cbranch_scc0 .LBB0_1150
	v_mbcnt_lo_u32_b32 v102, -1, 0
	v_mbcnt_hi_u32_b32 v102, -1, v102
	v_readlane_b32 s38, v252, 51
	v_and_b32_e32 v103, 15, v102
	v_readlane_b32 s21, v252, 52
	v_lshrrev_b32_e32 v102, 1, v102
	s_ashr_i32 s20, s64, 4
	v_and_b32_e32 v102, 24, v102
	v_lshl_or_b32 v152, s21, 5, v102
	s_lshl_b32 s34, s20, 8
	s_ashr_i32 s21, s20, 31
	s_lshl_b32 s39, s64, 8
	s_ashr_i32 s35, s34, 31
	s_lshl_b64 s[20:21], s[20:21], 12
	s_and_b32 s39, s39, 0xf00
	s_or_b32 s20, s20, s39
	s_lshl_b64 s[34:35], s[34:35], 2
	s_add_u32 s34, s28, s34
	s_addc_u32 s35, s54, s35
	v_ashrrev_i32_e32 v153, 31, v152
	v_lshl_add_u64 v[150:151], v[152:153], 2, s[34:35]
	v_lshl_or_b32 v148, s38, 6, v103
	global_load_dwordx4 v[102:105], v[150:151], off offset:16
	global_load_dwordx4 v[110:113], v[150:151], off
	s_and_b64 vcc, exec, s[6:7]
	s_mov_b32 s64, s63
	s_mov_b64 s[34:35], s[14:15]
	s_waitcnt vmcnt(0)
	v_pk_add_f32 v[130:131], v[130:131], v[102:103]
	v_pk_add_f32 v[134:135], v[134:135], v[110:111]
	v_pk_add_f32 v[136:137], v[136:137], v[112:113]
	v_mul_f32_e32 v149, 0xbfb8aa3b, v134
	v_exp_f32_e32 v149, v149
	v_pk_add_f32 v[132:133], v[132:133], v[104:105]
	v_pk_add_f32 v[126:127], v[126:127], v[110:111]
	v_pk_add_f32 v[128:129], v[128:129], v[112:113]
	v_add_f32_e32 v149, 1.0, v149
	v_rcp_f32_e32 v172, v149
	v_mul_f32_e32 v149, 0xbfb8aa3b, v130
	v_exp_f32_e32 v149, v149
	v_pk_add_f32 v[124:125], v[124:125], v[104:105]
	v_pk_add_f32 v[114:115], v[114:115], v[102:103]
	v_pk_add_f32 v[118:119], v[118:119], v[110:111]
	v_add_f32_e32 v149, 1.0, v149
	v_rcp_f32_e32 v174, v149
	v_mul_f32_e32 v149, 0xbfb8aa3b, v135
	v_exp_f32_e32 v149, v149
	v_pk_add_f32 v[116:117], v[116:117], v[104:105]
	v_pk_add_f32 v[120:121], v[120:121], v[112:113]
	v_pk_add_f32 v[98:99], v[98:99], v[102:103]
	v_add_f32_e32 v149, 1.0, v149
	v_rcp_f32_e32 v173, v149
	v_mul_f32_e32 v149, 0xbfb8aa3b, v131
	v_exp_f32_e32 v149, v149
	v_pk_add_f32 v[106:107], v[106:107], v[110:111]
	v_pk_mul_f32 v[134:135], v[134:135], v[172:173]
	v_pk_add_f32 v[100:101], v[100:101], v[104:105]
	v_add_f32_e32 v149, 1.0, v149
	v_rcp_f32_e32 v175, v149
	v_mul_f32_e32 v149, 0xbfb8aa3b, v136
	v_exp_f32_e32 v149, v149
	v_cvt_pk_bf16_f32 v134, v134, v135
	v_pk_mul_f32 v[130:131], v[130:131], v[174:175]
	v_pk_add_f32 v[108:109], v[108:109], v[112:113]
	v_add_f32_e32 v149, 1.0, v149
	v_rcp_f32_e32 v172, v149
	v_mul_f32_e32 v149, 0xbfb8aa3b, v132
	v_exp_f32_e32 v149, v149
	v_pk_add_f32 v[94:95], v[94:95], v[110:111]
	v_pk_add_f32 v[90:91], v[90:91], v[102:103]
	v_pk_add_f32 v[96:97], v[96:97], v[112:113]
	v_add_f32_e32 v149, 1.0, v149
	v_rcp_f32_e32 v174, v149
	v_mul_f32_e32 v149, 0xbfb8aa3b, v137
	v_exp_f32_e32 v149, v149
	v_pk_add_f32 v[92:93], v[92:93], v[104:105]
	v_pk_add_f32 v[82:83], v[82:83], v[102:103]
	v_pk_add_f32 v[86:87], v[86:87], v[110:111]
	v_add_f32_e32 v149, 1.0, v149
	v_rcp_f32_e32 v173, v149
	v_mul_f32_e32 v149, 0xbfb8aa3b, v133
	v_exp_f32_e32 v149, v149
	v_pk_add_f32 v[84:85], v[84:85], v[104:105]
	v_pk_mul_f32 v[136:137], v[136:137], v[172:173]
	v_pk_add_f32 v[88:89], v[88:89], v[112:113]
	v_add_f32_e32 v149, 1.0, v149
	v_rcp_f32_e32 v175, v149
	v_ashrrev_i32_e32 v149, 31, v148
	v_cvt_pk_bf16_f32 v135, v136, v137
	v_cvt_pk_bf16_f32 v136, v130, v131
	v_lshl_add_u64 v[130:131], s[20:21], 0, v[148:149]
	v_pk_mul_f32 v[132:133], v[132:133], v[174:175]
	v_lshlrev_b64 v[130:131], 9, v[130:131]
	v_cvt_pk_bf16_f32 v137, v132, v133
	v_lshl_add_u64 v[130:131], s[4:5], 0, v[130:131]
	v_lshlrev_b64 v[132:133], 1, v[152:153]
	v_lshl_add_u64 v[130:131], v[130:131], 0, v[132:133]
	global_store_dwordx4 v[130:131], v[134:137], off
	v_pk_add_f32 v[74:75], v[74:75], v[102:103]
	v_pk_add_f32 v[78:79], v[78:79], v[110:111]
	v_pk_add_f32 v[134:135], v[122:123], v[102:103]
	v_mul_f32_e32 v122, 0xbfb8aa3b, v126
	v_mul_f32_e32 v123, 0xbfb8aa3b, v134
	v_exp_f32_e32 v123, v123
	v_exp_f32_e32 v122, v122
	v_pk_add_f32 v[76:77], v[76:77], v[104:105]
	v_pk_add_f32 v[80:81], v[80:81], v[112:113]
	v_add_f32_e32 v123, 1.0, v123
	v_rcp_f32_e32 v136, v123
	v_mul_f32_e32 v123, 0xbfb8aa3b, v127
	v_exp_f32_e32 v123, v123
	v_add_f32_e32 v122, 1.0, v122
	v_rcp_f32_e32 v122, v122
	v_pk_add_f32 v[66:67], v[66:67], v[102:103]
	v_add_f32_e32 v123, 1.0, v123
	v_rcp_f32_e32 v123, v123
	v_pk_add_f32 v[70:71], v[70:71], v[110:111]
	v_pk_add_f32 v[68:69], v[68:69], v[104:105]
	v_pk_add_f32 v[72:73], v[72:73], v[112:113]
	v_pk_mul_f32 v[122:123], v[126:127], v[122:123]
	v_mul_f32_e32 v126, 0xbfb8aa3b, v135
	v_exp_f32_e32 v126, v126
	s_nop 0
	v_add_f32_e32 v126, 1.0, v126
	v_rcp_f32_e32 v137, v126
	s_nop 0
	v_pk_mul_f32 v[126:127], v[134:135], v[136:137]
	v_mul_f32_e32 v134, 0xbfb8aa3b, v128
	v_mul_f32_e32 v135, 0xbfb8aa3b, v129
	v_exp_f32_e32 v134, v134
	v_exp_f32_e32 v135, v135
	v_cvt_pk_bf16_f32 v126, v126, v127
	v_add_f32_e32 v134, 1.0, v134
	v_add_f32_e32 v135, 1.0, v135
	v_rcp_f32_e32 v136, v134
	v_mul_f32_e32 v134, 0xbfb8aa3b, v124
	v_rcp_f32_e32 v137, v135
	v_mul_f32_e32 v135, 0xbfb8aa3b, v125
	v_exp_f32_e32 v134, v134
	v_exp_f32_e32 v135, v135
	v_pk_mul_f32 v[128:129], v[128:129], v[136:137]
	v_add_f32_e32 v134, 1.0, v134
	v_add_f32_e32 v135, 1.0, v135
	v_rcp_f32_e32 v134, v134
	v_rcp_f32_e32 v135, v135
	s_nop 0
	v_pk_mul_f32 v[134:135], v[124:125], v[134:135]
	v_cvt_pk_bf16_f32 v124, v122, v123
	v_or_b32_e32 v122, 16, v148
	v_ashrrev_i32_e32 v123, 31, v122
	v_lshl_add_u64 v[122:123], s[20:21], 0, v[122:123]
	v_lshlrev_b64 v[122:123], 9, v[122:123]
	v_lshl_add_u64 v[122:123], s[4:5], 0, v[122:123]
	v_cvt_pk_bf16_f32 v125, v128, v129
	v_cvt_pk_bf16_f32 v127, v134, v135
	v_lshl_add_u64 v[122:123], v[122:123], 0, v[132:133]
	global_store_dwordx4 v[122:123], v[124:127], off
	s_nop 1
	v_mul_f32_e32 v125, 0xbfb8aa3b, v114
	v_exp_f32_e32 v125, v125
	v_mul_f32_e32 v124, 0xbfb8aa3b, v118
	v_exp_f32_e32 v124, v124
	v_add_f32_e32 v125, 1.0, v125
	v_rcp_f32_e32 v126, v125
	v_mul_f32_e32 v125, 0xbfb8aa3b, v119
	v_exp_f32_e32 v125, v125
	v_add_f32_e32 v124, 1.0, v124
	v_rcp_f32_e32 v124, v124
	v_add_f32_e32 v125, 1.0, v125
	v_rcp_f32_e32 v125, v125
	s_nop 0
	v_pk_mul_f32 v[118:119], v[118:119], v[124:125]
	v_mul_f32_e32 v124, 0xbfb8aa3b, v115
	v_exp_f32_e32 v124, v124
	v_mul_f32_e32 v125, 0xbfb8aa3b, v116
	v_exp_f32_e32 v125, v125
	v_add_f32_e32 v124, 1.0, v124
	v_rcp_f32_e32 v127, v124
	v_add_f32_e32 v125, 1.0, v125
	v_mul_f32_e32 v124, 0xbfb8aa3b, v120
	v_exp_f32_e32 v124, v124
	v_pk_mul_f32 v[114:115], v[114:115], v[126:127]
	v_rcp_f32_e32 v126, v125
	v_mul_f32_e32 v125, 0xbfb8aa3b, v121
	v_exp_f32_e32 v125, v125
	v_add_f32_e32 v124, 1.0, v124
	v_rcp_f32_e32 v124, v124
	v_add_f32_e32 v125, 1.0, v125
	v_rcp_f32_e32 v125, v125
	s_nop 0
	v_pk_mul_f32 v[120:121], v[120:121], v[124:125]
	v_mul_f32_e32 v124, 0xbfb8aa3b, v117
	v_exp_f32_e32 v124, v124
	s_nop 0
	v_add_f32_e32 v124, 1.0, v124
	v_rcp_f32_e32 v127, v124
	s_nop 0
	v_pk_mul_f32 v[124:125], v[116:117], v[126:127]
	v_cvt_pk_bf16_f32 v116, v118, v119
	v_cvt_pk_bf16_f32 v118, v114, v115
	v_or_b32_e32 v114, 32, v148
	v_ashrrev_i32_e32 v115, 31, v114
	v_lshl_add_u64 v[114:115], s[20:21], 0, v[114:115]
	v_lshlrev_b64 v[114:115], 9, v[114:115]
	v_lshl_add_u64 v[114:115], s[4:5], 0, v[114:115]
	v_cvt_pk_bf16_f32 v117, v120, v121
	v_cvt_pk_bf16_f32 v119, v124, v125
	v_lshl_add_u64 v[114:115], v[114:115], 0, v[132:133]
	global_store_dwordx4 v[114:115], v[116:119], off
	s_nop 1
	v_mul_f32_e32 v117, 0xbfb8aa3b, v98
	v_exp_f32_e32 v117, v117
	v_mul_f32_e32 v116, 0xbfb8aa3b, v106
	v_exp_f32_e32 v116, v116
	v_add_f32_e32 v117, 1.0, v117
	v_rcp_f32_e32 v118, v117
	v_mul_f32_e32 v117, 0xbfb8aa3b, v107
	v_exp_f32_e32 v117, v117
	v_add_f32_e32 v116, 1.0, v116
	v_rcp_f32_e32 v116, v116
	v_add_f32_e32 v117, 1.0, v117
	v_rcp_f32_e32 v117, v117
	s_nop 0
	v_pk_mul_f32 v[106:107], v[106:107], v[116:117]
	v_mul_f32_e32 v116, 0xbfb8aa3b, v99
	v_exp_f32_e32 v116, v116
	v_mul_f32_e32 v117, 0xbfb8aa3b, v100
	v_exp_f32_e32 v117, v117
	v_cvt_pk_bf16_f32 v106, v106, v107
	v_add_f32_e32 v116, 1.0, v116
	v_rcp_f32_e32 v119, v116
	v_add_f32_e32 v117, 1.0, v117
	v_mul_f32_e32 v116, 0xbfb8aa3b, v108
	v_exp_f32_e32 v116, v116
	v_pk_mul_f32 v[98:99], v[98:99], v[118:119]
	v_rcp_f32_e32 v118, v117
	v_mul_f32_e32 v117, 0xbfb8aa3b, v109
	v_exp_f32_e32 v117, v117
	v_add_f32_e32 v116, 1.0, v116
	v_rcp_f32_e32 v116, v116
	v_add_f32_e32 v117, 1.0, v117
	v_rcp_f32_e32 v117, v117
	s_nop 0
	v_pk_mul_f32 v[108:109], v[108:109], v[116:117]
	v_mul_f32_e32 v116, 0xbfb8aa3b, v101
	v_exp_f32_e32 v116, v116
	v_cvt_pk_bf16_f32 v107, v108, v109
	v_cvt_pk_bf16_f32 v108, v98, v99
	v_or_b32_e32 v98, 48, v148
	v_add_f32_e32 v116, 1.0, v116
	v_rcp_f32_e32 v119, v116
	v_ashrrev_i32_e32 v99, 31, v98
	v_lshl_add_u64 v[98:99], s[20:21], 0, v[98:99]
	v_lshlrev_b64 v[98:99], 9, v[98:99]
	v_pk_mul_f32 v[100:101], v[100:101], v[118:119]
	v_lshl_add_u64 v[98:99], s[4:5], 0, v[98:99]
	v_cvt_pk_bf16_f32 v109, v100, v101
	v_mul_f32_e32 v101, 0xbfb8aa3b, v94
	v_exp_f32_e32 v101, v101
	v_lshl_add_u64 v[98:99], v[98:99], 0, v[132:133]
	global_store_dwordx4 v[98:99], v[106:109], off
	v_add_u32_e32 v100, 0x80, v148
	v_add_f32_e32 v101, 1.0, v101
	v_rcp_f32_e32 v106, v101
	v_mul_f32_e32 v101, 0xbfb8aa3b, v90
	v_exp_f32_e32 v101, v101
	s_nop 0
	v_add_f32_e32 v101, 1.0, v101
	v_rcp_f32_e32 v108, v101
	v_mul_f32_e32 v101, 0xbfb8aa3b, v95
	v_exp_f32_e32 v101, v101
	s_nop 0
	v_add_f32_e32 v101, 1.0, v101
	v_rcp_f32_e32 v107, v101
	v_mul_f32_e32 v101, 0xbfb8aa3b, v91
	v_exp_f32_e32 v101, v101
	v_pk_mul_f32 v[94:95], v[94:95], v[106:107]
	v_add_f32_e32 v101, 1.0, v101
	v_rcp_f32_e32 v109, v101
	v_mul_f32_e32 v101, 0xbfb8aa3b, v96
	v_exp_f32_e32 v101, v101
	v_pk_mul_f32 v[90:91], v[90:91], v[108:109]
	v_add_f32_e32 v101, 1.0, v101
	v_rcp_f32_e32 v106, v101
	v_mul_f32_e32 v101, 0xbfb8aa3b, v92
	v_exp_f32_e32 v101, v101
	s_nop 0
	v_add_f32_e32 v101, 1.0, v101
	v_rcp_f32_e32 v108, v101
	v_mul_f32_e32 v101, 0xbfb8aa3b, v97
	v_exp_f32_e32 v101, v101
	s_nop 0
	v_add_f32_e32 v101, 1.0, v101
	v_rcp_f32_e32 v107, v101
	v_mul_f32_e32 v101, 0xbfb8aa3b, v93
	v_exp_f32_e32 v101, v101
	v_pk_mul_f32 v[96:97], v[96:97], v[106:107]
	v_add_f32_e32 v101, 1.0, v101
	v_rcp_f32_e32 v109, v101
	v_ashrrev_i32_e32 v101, 31, v100
	v_pk_mul_f32 v[106:107], v[92:93], v[108:109]
	v_cvt_pk_bf16_f32 v92, v94, v95
	v_cvt_pk_bf16_f32 v94, v90, v91
	v_lshl_add_u64 v[90:91], s[20:21], 0, v[100:101]
	v_lshlrev_b64 v[90:91], 9, v[90:91]
	v_lshl_add_u64 v[90:91], s[4:5], 0, v[90:91]
	v_cvt_pk_bf16_f32 v93, v96, v97
	v_cvt_pk_bf16_f32 v95, v106, v107
	v_lshl_add_u64 v[90:91], v[90:91], 0, v[132:133]
	global_store_dwordx4 v[90:91], v[92:95], off
	s_nop 1
	v_mul_f32_e32 v93, 0xbfb8aa3b, v82
	v_exp_f32_e32 v93, v93
	v_mul_f32_e32 v92, 0xbfb8aa3b, v86
	v_exp_f32_e32 v92, v92
	v_add_f32_e32 v93, 1.0, v93
	v_rcp_f32_e32 v94, v93
	v_mul_f32_e32 v93, 0xbfb8aa3b, v87
	v_exp_f32_e32 v93, v93
	v_add_f32_e32 v92, 1.0, v92
	v_rcp_f32_e32 v92, v92
	v_add_f32_e32 v93, 1.0, v93
	v_rcp_f32_e32 v93, v93
	s_nop 0
	v_pk_mul_f32 v[86:87], v[86:87], v[92:93]
	v_mul_f32_e32 v92, 0xbfb8aa3b, v83
	v_exp_f32_e32 v92, v92
	v_mul_f32_e32 v93, 0xbfb8aa3b, v84
	v_exp_f32_e32 v93, v93
	v_add_f32_e32 v92, 1.0, v92
	v_rcp_f32_e32 v95, v92
	v_add_f32_e32 v93, 1.0, v93
	v_mul_f32_e32 v92, 0xbfb8aa3b, v88
	v_exp_f32_e32 v92, v92
	v_pk_mul_f32 v[82:83], v[82:83], v[94:95]
	v_rcp_f32_e32 v94, v93
	v_mul_f32_e32 v93, 0xbfb8aa3b, v89
	v_exp_f32_e32 v93, v93
	v_add_f32_e32 v92, 1.0, v92
	v_rcp_f32_e32 v92, v92
	v_add_f32_e32 v93, 1.0, v93
	v_rcp_f32_e32 v93, v93
	s_nop 0
	v_pk_mul_f32 v[88:89], v[88:89], v[92:93]
	v_mul_f32_e32 v92, 0xbfb8aa3b, v85
	v_exp_f32_e32 v92, v92
	s_nop 0
	v_add_f32_e32 v92, 1.0, v92
	v_rcp_f32_e32 v95, v92
	s_nop 0
	v_pk_mul_f32 v[92:93], v[84:85], v[94:95]
	v_cvt_pk_bf16_f32 v84, v86, v87
	v_cvt_pk_bf16_f32 v86, v82, v83
	v_add_u32_e32 v82, 0x90, v148
	v_ashrrev_i32_e32 v83, 31, v82
	v_lshl_add_u64 v[82:83], s[20:21], 0, v[82:83]
	v_lshlrev_b64 v[82:83], 9, v[82:83]
	v_lshl_add_u64 v[82:83], s[4:5], 0, v[82:83]
	v_cvt_pk_bf16_f32 v85, v88, v89
	v_cvt_pk_bf16_f32 v87, v92, v93
	v_lshl_add_u64 v[82:83], v[82:83], 0, v[132:133]
	global_store_dwordx4 v[82:83], v[84:87], off
	s_nop 1
	v_mul_f32_e32 v85, 0xbfb8aa3b, v74
	v_exp_f32_e32 v85, v85
	v_mul_f32_e32 v84, 0xbfb8aa3b, v78
	v_exp_f32_e32 v84, v84
	v_add_f32_e32 v85, 1.0, v85
	v_rcp_f32_e32 v86, v85
	v_mul_f32_e32 v85, 0xbfb8aa3b, v79
	v_exp_f32_e32 v85, v85
	v_add_f32_e32 v84, 1.0, v84
	v_rcp_f32_e32 v84, v84
	v_add_f32_e32 v85, 1.0, v85
	v_rcp_f32_e32 v85, v85
	s_nop 0
	v_pk_mul_f32 v[78:79], v[78:79], v[84:85]
	v_mul_f32_e32 v84, 0xbfb8aa3b, v75
	v_exp_f32_e32 v84, v84
	v_mul_f32_e32 v85, 0xbfb8aa3b, v76
	v_exp_f32_e32 v85, v85
	v_add_f32_e32 v84, 1.0, v84
	v_rcp_f32_e32 v87, v84
	v_add_f32_e32 v85, 1.0, v85
	v_mul_f32_e32 v84, 0xbfb8aa3b, v80
	v_exp_f32_e32 v84, v84
	v_pk_mul_f32 v[74:75], v[74:75], v[86:87]
	v_rcp_f32_e32 v86, v85
	v_mul_f32_e32 v85, 0xbfb8aa3b, v81
	v_exp_f32_e32 v85, v85
	v_add_f32_e32 v84, 1.0, v84
	v_rcp_f32_e32 v84, v84
	v_add_f32_e32 v85, 1.0, v85
	v_rcp_f32_e32 v85, v85
	s_nop 0
	v_pk_mul_f32 v[80:81], v[80:81], v[84:85]
	v_mul_f32_e32 v84, 0xbfb8aa3b, v77
	v_exp_f32_e32 v84, v84
	s_nop 0
	v_add_f32_e32 v84, 1.0, v84
	v_rcp_f32_e32 v87, v84
	s_nop 0
	v_pk_mul_f32 v[84:85], v[76:77], v[86:87]
	v_cvt_pk_bf16_f32 v76, v78, v79
	v_cvt_pk_bf16_f32 v78, v74, v75
	v_add_u32_e32 v74, 0xa0, v148
	v_ashrrev_i32_e32 v75, 31, v74
	v_lshl_add_u64 v[74:75], s[20:21], 0, v[74:75]
	v_lshlrev_b64 v[74:75], 9, v[74:75]
	v_lshl_add_u64 v[74:75], s[4:5], 0, v[74:75]
	v_cvt_pk_bf16_f32 v77, v80, v81
	v_cvt_pk_bf16_f32 v79, v84, v85
	v_lshl_add_u64 v[74:75], v[74:75], 0, v[132:133]
	global_store_dwordx4 v[74:75], v[76:79], off
	s_nop 1
	v_mul_f32_e32 v77, 0xbfb8aa3b, v66
	v_exp_f32_e32 v77, v77
	v_mul_f32_e32 v76, 0xbfb8aa3b, v70
	v_exp_f32_e32 v76, v76
	v_add_f32_e32 v77, 1.0, v77
	v_rcp_f32_e32 v78, v77
	v_mul_f32_e32 v77, 0xbfb8aa3b, v71
	v_exp_f32_e32 v77, v77
	v_add_f32_e32 v76, 1.0, v76
	v_rcp_f32_e32 v76, v76
	v_add_f32_e32 v77, 1.0, v77
	v_rcp_f32_e32 v77, v77
	s_nop 0
	v_pk_mul_f32 v[70:71], v[70:71], v[76:77]
	v_mul_f32_e32 v76, 0xbfb8aa3b, v67
	v_exp_f32_e32 v76, v76
	s_nop 0
	v_add_f32_e32 v76, 1.0, v76
	v_rcp_f32_e32 v79, v76
	s_nop 0
	v_pk_mul_f32 v[76:77], v[66:67], v[78:79]
	v_mul_f32_e32 v67, 0xbfb8aa3b, v68
	v_exp_f32_e32 v67, v67
	v_mul_f32_e32 v66, 0xbfb8aa3b, v72
	v_exp_f32_e32 v66, v66
	v_add_f32_e32 v67, 1.0, v67
	v_rcp_f32_e32 v78, v67
	v_mul_f32_e32 v67, 0xbfb8aa3b, v73
	v_exp_f32_e32 v67, v67
	v_add_f32_e32 v66, 1.0, v66
	v_rcp_f32_e32 v66, v66
	v_add_f32_e32 v67, 1.0, v67
	v_rcp_f32_e32 v67, v67
	s_nop 0
	v_pk_mul_f32 v[72:73], v[72:73], v[66:67]
	v_mul_f32_e32 v66, 0xbfb8aa3b, v69
	v_exp_f32_e32 v66, v66
	v_cvt_pk_bf16_f32 v67, v72, v73
	v_add_f32_e32 v66, 1.0, v66
	v_rcp_f32_e32 v79, v66
	v_cvt_pk_bf16_f32 v66, v70, v71
	v_add_u32_e32 v70, 0xb0, v148
	v_ashrrev_i32_e32 v71, 31, v70
	v_lshl_add_u64 v[70:71], s[20:21], 0, v[70:71]
	v_lshlrev_b64 v[70:71], 9, v[70:71]
	v_pk_mul_f32 v[78:79], v[68:69], v[78:79]
	v_lshl_add_u64 v[70:71], s[4:5], 0, v[70:71]
	v_cvt_pk_bf16_f32 v68, v76, v77
	v_cvt_pk_bf16_f32 v69, v78, v79
	v_lshl_add_u64 v[76:77], v[70:71], 0, v[132:133]
	global_store_dwordx4 v[76:77], v[66:69], off
	global_load_dwordx4 v[66:69], v[150:151], off offset:528
	s_nop 0
	global_load_dwordx4 v[70:73], v[150:151], off offset:512
	s_mov_b64 s[20:21], s[12:13]
	s_waitcnt vmcnt(0)
	v_pk_add_f32 v[58:59], v[58:59], v[66:67]
	s_nop 0
	v_mul_f32_e32 v79, 0xbfb8aa3b, v58
	v_exp_f32_e32 v79, v79
	v_pk_add_f32 v[62:63], v[62:63], v[70:71]
	v_pk_add_f32 v[60:61], v[60:61], v[68:69]
	v_mul_f32_e32 v78, 0xbfb8aa3b, v62
	v_add_f32_e32 v79, 1.0, v79
	v_rcp_f32_e32 v80, v79
	v_mul_f32_e32 v79, 0xbfb8aa3b, v63
	v_exp_f32_e32 v78, v78
	v_exp_f32_e32 v79, v79
	v_pk_add_f32 v[64:65], v[64:65], v[72:73]
	v_pk_add_f32 v[50:51], v[50:51], v[66:67]
	v_add_f32_e32 v78, 1.0, v78
	v_add_f32_e32 v79, 1.0, v79
	v_rcp_f32_e32 v78, v78
	v_rcp_f32_e32 v79, v79
	v_pk_add_f32 v[54:55], v[54:55], v[70:71]
	v_pk_add_f32 v[52:53], v[52:53], v[68:69]
	v_pk_add_f32 v[56:57], v[56:57], v[72:73]
	v_pk_mul_f32 v[62:63], v[62:63], v[78:79]
	v_mul_f32_e32 v78, 0xbfb8aa3b, v59
	v_exp_f32_e32 v78, v78
	v_pk_add_f32 v[42:43], v[42:43], v[66:67]
	v_pk_add_f32 v[46:47], v[46:47], v[70:71]
	v_pk_add_f32 v[44:45], v[44:45], v[68:69]
	v_add_f32_e32 v78, 1.0, v78
	v_rcp_f32_e32 v81, v78
	v_pk_add_f32 v[48:49], v[48:49], v[72:73]
	v_pk_add_f32 v[34:35], v[34:35], v[66:67]
	v_pk_add_f32 v[38:39], v[38:39], v[70:71]
	v_pk_mul_f32 v[78:79], v[58:59], v[80:81]
	v_mul_f32_e32 v59, 0xbfb8aa3b, v60
	v_exp_f32_e32 v59, v59
	v_mul_f32_e32 v58, 0xbfb8aa3b, v64
	v_exp_f32_e32 v58, v58
	v_pk_add_f32 v[36:37], v[36:37], v[68:69]
	v_add_f32_e32 v59, 1.0, v59
	v_rcp_f32_e32 v80, v59
	v_mul_f32_e32 v59, 0xbfb8aa3b, v65
	v_exp_f32_e32 v59, v59
	v_add_f32_e32 v58, 1.0, v58
	v_rcp_f32_e32 v58, v58
	v_pk_add_f32 v[40:41], v[40:41], v[72:73]
	v_add_f32_e32 v59, 1.0, v59
	v_rcp_f32_e32 v59, v59
	v_pk_add_f32 v[26:27], v[26:27], v[66:67]
	v_pk_add_f32 v[30:31], v[30:31], v[70:71]
	v_pk_add_f32 v[28:29], v[28:29], v[68:69]
	v_pk_mul_f32 v[64:65], v[64:65], v[58:59]
	v_mul_f32_e32 v58, 0xbfb8aa3b, v61
	v_exp_f32_e32 v58, v58
	v_cvt_pk_bf16_f32 v59, v64, v65
	v_pk_add_f32 v[32:33], v[32:33], v[72:73]
	v_pk_add_f32 v[18:19], v[18:19], v[66:67]
	v_add_f32_e32 v58, 1.0, v58
	v_rcp_f32_e32 v81, v58
	v_cvt_pk_bf16_f32 v58, v62, v63
	v_pk_add_f32 v[22:23], v[22:23], v[70:71]
	v_pk_add_f32 v[20:21], v[20:21], v[68:69]
	v_pk_mul_f32 v[80:81], v[60:61], v[80:81]
	v_cvt_pk_bf16_f32 v60, v78, v79
	v_cvt_pk_bf16_f32 v61, v80, v81
	global_store_dwordx4 v[130:131], v[58:61], off offset:256
	v_pk_add_f32 v[24:25], v[24:25], v[72:73]
	v_pk_add_f32 v[10:11], v[10:11], v[66:67]
	v_mul_f32_e32 v59, 0xbfb8aa3b, v50
	v_exp_f32_e32 v59, v59
	v_mul_f32_e32 v58, 0xbfb8aa3b, v54
	v_exp_f32_e32 v58, v58
	v_pk_add_f32 v[14:15], v[14:15], v[70:71]
	v_add_f32_e32 v59, 1.0, v59
	v_rcp_f32_e32 v60, v59
	v_mul_f32_e32 v59, 0xbfb8aa3b, v55
	v_exp_f32_e32 v59, v59
	v_add_f32_e32 v58, 1.0, v58
	v_rcp_f32_e32 v58, v58
	v_pk_add_f32 v[12:13], v[12:13], v[68:69]
	v_add_f32_e32 v59, 1.0, v59
	v_rcp_f32_e32 v59, v59
	v_pk_add_f32 v[16:17], v[16:17], v[72:73]
	v_pk_add_f32 v[2:3], v[2:3], v[66:67]
	v_pk_add_f32 v[6:7], v[6:7], v[70:71]
	v_pk_mul_f32 v[54:55], v[54:55], v[58:59]
	v_mul_f32_e32 v58, 0xbfb8aa3b, v51
	v_exp_f32_e32 v58, v58
	v_pk_add_f32 v[4:5], v[4:5], v[68:69]
	v_pk_add_f32 v[8:9], v[8:9], v[72:73]
	v_add_f32_e32 v58, 1.0, v58
	v_rcp_f32_e32 v61, v58
	s_nop 0
	v_pk_mul_f32 v[58:59], v[50:51], v[60:61]
	v_mul_f32_e32 v51, 0xbfb8aa3b, v52
	v_exp_f32_e32 v51, v51
	v_mul_f32_e32 v50, 0xbfb8aa3b, v56
	v_exp_f32_e32 v50, v50
	v_add_f32_e32 v51, 1.0, v51
	v_rcp_f32_e32 v60, v51
	v_mul_f32_e32 v51, 0xbfb8aa3b, v57
	v_exp_f32_e32 v51, v51
	v_add_f32_e32 v50, 1.0, v50
	v_rcp_f32_e32 v50, v50
	v_add_f32_e32 v51, 1.0, v51
	v_rcp_f32_e32 v51, v51
	s_nop 0
	v_pk_mul_f32 v[56:57], v[56:57], v[50:51]
	v_mul_f32_e32 v50, 0xbfb8aa3b, v53
	v_exp_f32_e32 v50, v50
	v_cvt_pk_bf16_f32 v51, v56, v57
	v_add_f32_e32 v50, 1.0, v50
	v_rcp_f32_e32 v61, v50
	v_cvt_pk_bf16_f32 v50, v54, v55
	v_pk_mul_f32 v[60:61], v[52:53], v[60:61]
	v_cvt_pk_bf16_f32 v52, v58, v59
	v_cvt_pk_bf16_f32 v53, v60, v61
	global_store_dwordx4 v[122:123], v[50:53], off offset:256
	s_nop 1
	v_mul_f32_e32 v51, 0xbfb8aa3b, v42
	v_exp_f32_e32 v51, v51
	v_mul_f32_e32 v50, 0xbfb8aa3b, v46
	v_exp_f32_e32 v50, v50
	v_add_f32_e32 v51, 1.0, v51
	v_rcp_f32_e32 v52, v51
	v_mul_f32_e32 v51, 0xbfb8aa3b, v47
	v_exp_f32_e32 v51, v51
	v_add_f32_e32 v50, 1.0, v50
	v_rcp_f32_e32 v50, v50
	v_add_f32_e32 v51, 1.0, v51
	v_rcp_f32_e32 v51, v51
	s_nop 0
	v_pk_mul_f32 v[46:47], v[46:47], v[50:51]
	v_mul_f32_e32 v50, 0xbfb8aa3b, v43
	v_exp_f32_e32 v50, v50
	s_nop 0
	v_add_f32_e32 v50, 1.0, v50
	v_rcp_f32_e32 v53, v50
	s_nop 0
	v_pk_mul_f32 v[50:51], v[42:43], v[52:53]
	v_mul_f32_e32 v43, 0xbfb8aa3b, v44
	v_exp_f32_e32 v43, v43
	v_mul_f32_e32 v42, 0xbfb8aa3b, v48
	v_exp_f32_e32 v42, v42
	v_add_f32_e32 v43, 1.0, v43
	v_rcp_f32_e32 v52, v43
	v_mul_f32_e32 v43, 0xbfb8aa3b, v49
	v_exp_f32_e32 v43, v43
	v_add_f32_e32 v42, 1.0, v42
	v_rcp_f32_e32 v42, v42
	v_add_f32_e32 v43, 1.0, v43
	v_rcp_f32_e32 v43, v43
	s_nop 0
	v_pk_mul_f32 v[48:49], v[48:49], v[42:43]
	v_mul_f32_e32 v42, 0xbfb8aa3b, v45
	v_exp_f32_e32 v42, v42
	v_cvt_pk_bf16_f32 v43, v48, v49
	v_add_f32_e32 v42, 1.0, v42
	v_rcp_f32_e32 v53, v42
	v_cvt_pk_bf16_f32 v42, v46, v47
	v_pk_mul_f32 v[52:53], v[44:45], v[52:53]
	v_cvt_pk_bf16_f32 v44, v50, v51
	v_cvt_pk_bf16_f32 v45, v52, v53
	global_store_dwordx4 v[114:115], v[42:45], off offset:256
	s_nop 1
	v_mul_f32_e32 v43, 0xbfb8aa3b, v34
	v_exp_f32_e32 v43, v43
	v_mul_f32_e32 v42, 0xbfb8aa3b, v38
	v_exp_f32_e32 v42, v42
	v_add_f32_e32 v43, 1.0, v43
	v_rcp_f32_e32 v44, v43
	v_mul_f32_e32 v43, 0xbfb8aa3b, v39
	v_exp_f32_e32 v43, v43
	v_add_f32_e32 v42, 1.0, v42
	v_rcp_f32_e32 v42, v42
	v_add_f32_e32 v43, 1.0, v43
	v_rcp_f32_e32 v43, v43
	s_nop 0
	v_pk_mul_f32 v[38:39], v[38:39], v[42:43]
	v_mul_f32_e32 v42, 0xbfb8aa3b, v35
	v_exp_f32_e32 v42, v42
	s_nop 0
	v_add_f32_e32 v42, 1.0, v42
	v_rcp_f32_e32 v45, v42
	s_nop 0
	v_pk_mul_f32 v[42:43], v[34:35], v[44:45]
	v_mul_f32_e32 v35, 0xbfb8aa3b, v36
	v_exp_f32_e32 v35, v35
	v_mul_f32_e32 v34, 0xbfb8aa3b, v40
	v_exp_f32_e32 v34, v34
	v_add_f32_e32 v35, 1.0, v35
	v_rcp_f32_e32 v44, v35
	v_mul_f32_e32 v35, 0xbfb8aa3b, v41
	v_exp_f32_e32 v35, v35
	v_add_f32_e32 v34, 1.0, v34
	v_rcp_f32_e32 v34, v34
	v_add_f32_e32 v35, 1.0, v35
	v_rcp_f32_e32 v35, v35
	s_nop 0
	v_pk_mul_f32 v[40:41], v[40:41], v[34:35]
	v_mul_f32_e32 v34, 0xbfb8aa3b, v37
	v_exp_f32_e32 v34, v34
	v_cvt_pk_bf16_f32 v35, v40, v41
	v_add_f32_e32 v34, 1.0, v34
	v_rcp_f32_e32 v45, v34
	v_cvt_pk_bf16_f32 v34, v38, v39
	v_pk_mul_f32 v[44:45], v[36:37], v[44:45]
	v_cvt_pk_bf16_f32 v36, v42, v43
	v_cvt_pk_bf16_f32 v37, v44, v45
	global_store_dwordx4 v[98:99], v[34:37], off offset:256
	s_nop 1
	v_mul_f32_e32 v35, 0xbfb8aa3b, v26
	v_exp_f32_e32 v35, v35
	v_mul_f32_e32 v34, 0xbfb8aa3b, v30
	v_exp_f32_e32 v34, v34
	v_add_f32_e32 v35, 1.0, v35
	v_rcp_f32_e32 v36, v35
	v_mul_f32_e32 v35, 0xbfb8aa3b, v31
	v_exp_f32_e32 v35, v35
	v_add_f32_e32 v34, 1.0, v34
	v_rcp_f32_e32 v34, v34
	v_add_f32_e32 v35, 1.0, v35
	v_rcp_f32_e32 v35, v35
	s_nop 0
	v_pk_mul_f32 v[30:31], v[30:31], v[34:35]
	v_mul_f32_e32 v34, 0xbfb8aa3b, v27
	v_exp_f32_e32 v34, v34
	s_nop 0
	v_add_f32_e32 v34, 1.0, v34
	v_rcp_f32_e32 v37, v34
	s_nop 0
	v_pk_mul_f32 v[34:35], v[26:27], v[36:37]
	v_mul_f32_e32 v27, 0xbfb8aa3b, v28
	v_exp_f32_e32 v27, v27
	v_mul_f32_e32 v26, 0xbfb8aa3b, v32
	v_exp_f32_e32 v26, v26
	v_add_f32_e32 v27, 1.0, v27
	v_rcp_f32_e32 v36, v27
	v_mul_f32_e32 v27, 0xbfb8aa3b, v33
	v_exp_f32_e32 v27, v27
	v_add_f32_e32 v26, 1.0, v26
	v_rcp_f32_e32 v26, v26
	v_add_f32_e32 v27, 1.0, v27
	v_rcp_f32_e32 v27, v27
	s_nop 0
	v_pk_mul_f32 v[32:33], v[32:33], v[26:27]
	v_mul_f32_e32 v26, 0xbfb8aa3b, v29
	v_exp_f32_e32 v26, v26
	v_cvt_pk_bf16_f32 v27, v32, v33
	v_add_f32_e32 v26, 1.0, v26
	v_rcp_f32_e32 v37, v26
	v_cvt_pk_bf16_f32 v26, v30, v31
	v_pk_mul_f32 v[36:37], v[28:29], v[36:37]
	v_cvt_pk_bf16_f32 v28, v34, v35
	v_cvt_pk_bf16_f32 v29, v36, v37
	global_store_dwordx4 v[90:91], v[26:29], off offset:256
	s_nop 1
	v_mul_f32_e32 v27, 0xbfb8aa3b, v18
	v_exp_f32_e32 v27, v27
	v_mul_f32_e32 v26, 0xbfb8aa3b, v22
	v_exp_f32_e32 v26, v26
	v_add_f32_e32 v27, 1.0, v27
	v_rcp_f32_e32 v28, v27
	v_mul_f32_e32 v27, 0xbfb8aa3b, v23
	v_exp_f32_e32 v27, v27
	v_add_f32_e32 v26, 1.0, v26
	v_rcp_f32_e32 v26, v26
	v_add_f32_e32 v27, 1.0, v27
	v_rcp_f32_e32 v27, v27
	s_nop 0
	v_pk_mul_f32 v[22:23], v[22:23], v[26:27]
	v_mul_f32_e32 v26, 0xbfb8aa3b, v19
	v_exp_f32_e32 v26, v26
	s_nop 0
	v_add_f32_e32 v26, 1.0, v26
	v_rcp_f32_e32 v29, v26
	s_nop 0
	v_pk_mul_f32 v[26:27], v[18:19], v[28:29]
	v_mul_f32_e32 v19, 0xbfb8aa3b, v20
	v_exp_f32_e32 v19, v19
	v_mul_f32_e32 v18, 0xbfb8aa3b, v24
	v_exp_f32_e32 v18, v18
	v_add_f32_e32 v19, 1.0, v19
	v_rcp_f32_e32 v28, v19
	v_mul_f32_e32 v19, 0xbfb8aa3b, v25
	v_exp_f32_e32 v19, v19
	v_add_f32_e32 v18, 1.0, v18
	v_rcp_f32_e32 v18, v18
	v_add_f32_e32 v19, 1.0, v19
	v_rcp_f32_e32 v19, v19
	s_nop 0
	v_pk_mul_f32 v[24:25], v[24:25], v[18:19]
	v_mul_f32_e32 v18, 0xbfb8aa3b, v21
	v_exp_f32_e32 v18, v18
	v_cvt_pk_bf16_f32 v19, v24, v25
	v_add_f32_e32 v18, 1.0, v18
	v_rcp_f32_e32 v29, v18
	v_cvt_pk_bf16_f32 v18, v22, v23
	v_pk_mul_f32 v[28:29], v[20:21], v[28:29]
	v_cvt_pk_bf16_f32 v20, v26, v27
	v_cvt_pk_bf16_f32 v21, v28, v29
	global_store_dwordx4 v[82:83], v[18:21], off offset:256
	s_nop 1
	v_mul_f32_e32 v19, 0xbfb8aa3b, v10
	v_exp_f32_e32 v19, v19
	v_mul_f32_e32 v18, 0xbfb8aa3b, v14
	v_exp_f32_e32 v18, v18
	v_add_f32_e32 v19, 1.0, v19
	v_rcp_f32_e32 v20, v19
	v_mul_f32_e32 v19, 0xbfb8aa3b, v15
	v_exp_f32_e32 v19, v19
	v_add_f32_e32 v18, 1.0, v18
	v_rcp_f32_e32 v18, v18
	v_add_f32_e32 v19, 1.0, v19
	v_rcp_f32_e32 v19, v19
	s_nop 0
	v_pk_mul_f32 v[14:15], v[14:15], v[18:19]
	v_mul_f32_e32 v18, 0xbfb8aa3b, v11
	v_exp_f32_e32 v18, v18
	s_nop 0
	v_add_f32_e32 v18, 1.0, v18
	v_rcp_f32_e32 v21, v18
	s_nop 0
	v_pk_mul_f32 v[18:19], v[10:11], v[20:21]
	v_mul_f32_e32 v11, 0xbfb8aa3b, v12
	v_exp_f32_e32 v11, v11
	v_mul_f32_e32 v10, 0xbfb8aa3b, v16
	v_exp_f32_e32 v10, v10
	v_add_f32_e32 v11, 1.0, v11
	v_rcp_f32_e32 v20, v11
	v_mul_f32_e32 v11, 0xbfb8aa3b, v17
	v_exp_f32_e32 v11, v11
	v_add_f32_e32 v10, 1.0, v10
	v_rcp_f32_e32 v10, v10
	v_add_f32_e32 v11, 1.0, v11
	v_rcp_f32_e32 v11, v11
	s_nop 0
	v_pk_mul_f32 v[16:17], v[16:17], v[10:11]
	v_mul_f32_e32 v10, 0xbfb8aa3b, v13
	v_exp_f32_e32 v10, v10
	v_cvt_pk_bf16_f32 v11, v16, v17
	v_add_f32_e32 v10, 1.0, v10
	v_rcp_f32_e32 v21, v10
	v_cvt_pk_bf16_f32 v10, v14, v15
	v_pk_mul_f32 v[20:21], v[12:13], v[20:21]
	v_cvt_pk_bf16_f32 v12, v18, v19
	v_cvt_pk_bf16_f32 v13, v20, v21
	global_store_dwordx4 v[74:75], v[10:13], off offset:256
	s_nop 1
	v_mul_f32_e32 v11, 0xbfb8aa3b, v2
	v_exp_f32_e32 v11, v11
	v_mul_f32_e32 v10, 0xbfb8aa3b, v6
	v_exp_f32_e32 v10, v10
	v_add_f32_e32 v11, 1.0, v11
	v_rcp_f32_e32 v12, v11
	v_mul_f32_e32 v11, 0xbfb8aa3b, v7
	v_exp_f32_e32 v11, v11
	v_add_f32_e32 v10, 1.0, v10
	v_rcp_f32_e32 v10, v10
	v_add_f32_e32 v11, 1.0, v11
	v_rcp_f32_e32 v11, v11
	s_nop 0
	v_pk_mul_f32 v[6:7], v[6:7], v[10:11]
	v_mul_f32_e32 v10, 0xbfb8aa3b, v3
	v_exp_f32_e32 v10, v10
	s_nop 0
	v_add_f32_e32 v10, 1.0, v10
	v_rcp_f32_e32 v13, v10
	s_nop 0
	v_pk_mul_f32 v[10:11], v[2:3], v[12:13]
	v_mul_f32_e32 v3, 0xbfb8aa3b, v4
	v_exp_f32_e32 v3, v3
	v_mul_f32_e32 v2, 0xbfb8aa3b, v8
	v_exp_f32_e32 v2, v2
	v_add_f32_e32 v3, 1.0, v3
	v_rcp_f32_e32 v12, v3
	v_mul_f32_e32 v3, 0xbfb8aa3b, v9
	v_exp_f32_e32 v3, v3
	v_add_f32_e32 v2, 1.0, v2
	v_rcp_f32_e32 v2, v2
	v_add_f32_e32 v3, 1.0, v3
	v_rcp_f32_e32 v3, v3
	s_nop 0
	v_pk_mul_f32 v[8:9], v[8:9], v[2:3]
	v_mul_f32_e32 v2, 0xbfb8aa3b, v5
	v_exp_f32_e32 v2, v2
	v_cvt_pk_bf16_f32 v3, v8, v9
	v_add_f32_e32 v2, 1.0, v2
	v_rcp_f32_e32 v13, v2
	v_cvt_pk_bf16_f32 v2, v6, v7
	v_pk_mul_f32 v[12:13], v[4:5], v[12:13]
	v_cvt_pk_bf16_f32 v4, v10, v11
	v_cvt_pk_bf16_f32 v5, v12, v13
	global_store_dwordx4 v[76:77], v[2:5], off offset:256
	s_cbranch_vccz .LBB0_1143
	s_waitcnt vmcnt(0)
	s_cmpk_gt_u32 s27, 0xff
	s_cbranch_scc1 .LBB0_1154
	s_barrier

.LBB0_1474:
	v_mov_b64_e32 v[2:3], 0x200
	s_ashr_i32 s15, s14, 31
	v_cmp_lt_i64_e32 vcc, s[20:21], v[2:3]
	s_lshl_b64 s[20:21], s[14:15], 18
	s_add_u32 s20, s28, s20
	s_addc_u32 s21, s44, s21
	s_and_b64 s[34:35], vcc, exec
	ds_read_b128 v[2:5], v175
	ds_read_b128 v[6:9], v176
	ds_read_b128 v[10:13], v177
	ds_read_b128 v[14:17], v178
	s_cselect_b32 s15, s21, s41
	s_cselect_b32 s65, s20, s40
	s_ashr_i32 s13, s12, 31
	s_lshl_b64 s[34:35], s[12:13], 18
	s_add_u32 s34, s45, s34
	s_addc_u32 s35, s46, s35
	s_and_b64 s[42:43], vcc, exec
	s_cselect_b32 s13, s35, s39
	s_cselect_b32 s66, s34, s38
	s_add_u32 s42, s40, 0x20080
	s_addc_u32 s43, s41, 0
	s_add_i32 s67, s47, 0xc000
	v_add_u32_e32 v0, s55, v174
	v_lshl_add_u64 v[50:51], s[42:43], 0, v[164:165]
	s_mov_b32 m0, s67
	s_add_i32 s68, s47, 0xe000
	ds_read_b128 v[18:21], v0
	ds_read_b128 v[22:25], v0 offset:1024
	ds_read_b128 v[26:29], v0 offset:2048
	ds_read_b128 v[30:33], v0 offset:3072
	ds_read_b128 v[34:37], v0 offset:4096
	ds_read_b128 v[38:41], v0 offset:5120
	ds_read_b128 v[42:45], v0 offset:6144
	ds_read_b128 v[46:49], v0 offset:7168
	global_load_lds_dwordx4 v[50:51], off
	v_lshl_add_u64 v[50:51], s[42:43], 0, v[160:161]
	s_mov_b32 m0, s68
	s_nop 0
	global_load_lds_dwordx4 v[50:51], off
	s_waitcnt lgkmcnt(8)
	s_barrier
	s_setprio 1
	s_waitcnt lgkmcnt(6)
	v_mfma_scale_f32_16x16x128_f8f6f4 v[142:145], v[2:9], v[18:25], 0, v222, v222 op_sel_hi:[0,0,0]
	v_mfma_scale_f32_16x16x128_f8f6f4 v[138:141], v[10:17], v[18:25], 0, v222, v222 op_sel_hi:[0,0,0]
	s_waitcnt lgkmcnt(4)
	v_mfma_scale_f32_16x16x128_f8f6f4 v[122:125], v[2:9], v[26:33], 0, v222, v222 op_sel_hi:[0,0,0]
	v_mfma_scale_f32_16x16x128_f8f6f4 v[114:117], v[10:17], v[26:33], 0, v222, v222 op_sel_hi:[0,0,0]
	s_waitcnt lgkmcnt(2)
	v_mfma_scale_f32_16x16x128_f8f6f4 v[102:105], v[2:9], v[34:41], 0, v222, v222 op_sel_hi:[0,0,0]
	v_mfma_scale_f32_16x16x128_f8f6f4 v[98:101], v[10:17], v[34:41], 0, v222, v222 op_sel_hi:[0,0,0]
	s_waitcnt lgkmcnt(0)
	v_mfma_scale_f32_16x16x128_f8f6f4 v[82:85], v[2:9], v[42:49], 0, v222, v222 op_sel_hi:[0,0,0]
	v_mfma_scale_f32_16x16x128_f8f6f4 v[70:73], v[10:17], v[42:49], 0, v222, v222 op_sel_hi:[0,0,0]
	s_setprio 0
	s_barrier
	v_lshl_add_u64 v[150:151], s[38:39], 0, v[162:163]
	s_mov_b64 s[42:43], 0x100
	s_mov_b32 m0, s48
	v_lshl_add_u64 v[50:51], v[150:151], 0, s[42:43]
	v_lshl_add_u64 v[152:153], s[38:39], 0, v[158:159]
	ds_read_b128 v[202:205], v179
	ds_read_b128 v[206:209], v180
	ds_read_b128 v[210:213], v181
	ds_read_b128 v[214:217], v182
	global_load_lds_dwordx4 v[50:51], off
	v_lshl_add_u64 v[50:51], v[152:153], 0, s[42:43]
	s_mov_b32 m0, s49
	s_nop 0
	global_load_lds_dwordx4 v[50:51], off
	s_barrier
	s_setprio 1
	s_waitcnt lgkmcnt(2)
	v_mfma_scale_f32_16x16x128_f8f6f4 v[134:137], v[202:209], v[18:25], 0, v222, v222 op_sel_hi:[0,0,0]
	v_mfma_scale_f32_16x16x128_f8f6f4 v[126:129], v[202:209], v[26:33], 0, v222, v222 op_sel_hi:[0,0,0]
	v_mfma_scale_f32_16x16x128_f8f6f4 v[110:113], v[202:209], v[34:41], 0, v222, v222 op_sel_hi:[0,0,0]
	v_mfma_scale_f32_16x16x128_f8f6f4 v[90:93], v[202:209], v[42:49], 0, v222, v222 op_sel_hi:[0,0,0]
	s_waitcnt lgkmcnt(0)
	v_mfma_scale_f32_16x16x128_f8f6f4 v[130:133], v[210:217], v[18:25], 0, v222, v222 op_sel_hi:[0,0,0]
	v_mfma_scale_f32_16x16x128_f8f6f4 v[118:121], v[210:217], v[26:33], 0, v222, v222 op_sel_hi:[0,0,0]
	v_mfma_scale_f32_16x16x128_f8f6f4 v[106:109], v[210:217], v[34:41], 0, v222, v222 op_sel_hi:[0,0,0]
	v_mfma_scale_f32_16x16x128_f8f6f4 v[74:77], v[210:217], v[42:49], 0, v222, v222 op_sel_hi:[0,0,0]
	s_setprio 0
	v_lshl_add_u64 v[146:147], s[40:41], 0, v[164:165]
	s_mov_b32 m0, s47
	v_lshl_add_u64 v[26:27], v[146:147], 0, s[42:43]
	v_lshl_add_u64 v[148:149], s[40:41], 0, v[160:161]
	s_barrier
	ds_read_b128 v[18:21], v0 offset:16384
	ds_read_b128 v[22:25], v0 offset:17408
	ds_read_b128 v[34:37], v0 offset:18432
	ds_read_b128 v[38:41], v0 offset:19456
	ds_read_b128 v[232:235], v0 offset:20480
	ds_read_b128 v[236:239], v0 offset:21504
	ds_read_b128 v[240:243], v0 offset:22528
	ds_read_b128 v[244:247], v0 offset:23552
	global_load_lds_dwordx4 v[26:27], off
	v_lshl_add_u64 v[26:27], v[148:149], 0, s[42:43]
	s_mov_b32 m0, s50
	s_nop 0
	global_load_lds_dwordx4 v[26:27], off
	s_barrier
	s_setprio 1
	s_waitcnt lgkmcnt(6)
	v_mfma_scale_f32_16x16x128_f8f6f4 v[94:97], v[2:9], v[18:25], 0, v222, v222 op_sel_hi:[0,0,0]
	v_mfma_scale_f32_16x16x128_f8f6f4 v[86:89], v[10:17], v[18:25], 0, v222, v222 op_sel_hi:[0,0,0]
	s_waitcnt lgkmcnt(4)
	v_mfma_scale_f32_16x16x128_f8f6f4 v[62:65], v[2:9], v[34:41], 0, v222, v222 op_sel_hi:[0,0,0]
	v_mfma_scale_f32_16x16x128_f8f6f4 v[58:61], v[10:17], v[34:41], 0, v222, v222 op_sel_hi:[0,0,0]
	s_waitcnt lgkmcnt(2)
	v_mfma_scale_f32_16x16x128_f8f6f4 v[46:49], v[2:9], v[232:239], 0, v222, v222 op_sel_hi:[0,0,0]
	v_mfma_scale_f32_16x16x128_f8f6f4 v[42:45], v[10:17], v[232:239], 0, v222, v222 op_sel_hi:[0,0,0]
	s_waitcnt lgkmcnt(0)
	v_mfma_scale_f32_16x16x128_f8f6f4 v[30:33], v[2:9], v[240:247], 0, v222, v222 op_sel_hi:[0,0,0]
	v_mfma_scale_f32_16x16x128_f8f6f4 v[26:29], v[10:17], v[240:247], 0, v222, v222 op_sel_hi:[0,0,0]
	s_setprio 0
	s_barrier
	s_add_u32 s42, s38, 0x20100
	s_addc_u32 s43, s39, 0
	s_mov_b32 m0, s51
	v_lshl_add_u64 v[2:3], s[42:43], 0, v[162:163]
	global_load_lds_dwordx4 v[2:3], off
	v_lshl_add_u64 v[2:3], s[42:43], 0, v[158:159]
	s_mov_b32 m0, s52
	s_nop 0
	global_load_lds_dwordx4 v[2:3], off
	s_waitcnt vmcnt(6)
	s_barrier
	s_setprio 1
	v_mfma_scale_f32_16x16x128_f8f6f4 v[78:81], v[202:209], v[18:25], 0, v222, v222 op_sel_hi:[0,0,0]
	v_mfma_scale_f32_16x16x128_f8f6f4 v[66:69], v[210:217], v[18:25], 0, v222, v222 op_sel_hi:[0,0,0]
	v_mfma_scale_f32_16x16x128_f8f6f4 v[54:57], v[202:209], v[34:41], 0, v222, v222 op_sel_hi:[0,0,0]
	v_mfma_scale_f32_16x16x128_f8f6f4 v[50:53], v[210:217], v[34:41], 0, v222, v222 op_sel_hi:[0,0,0]
	v_mfma_scale_f32_16x16x128_f8f6f4 v[38:41], v[202:209], v[232:239], 0, v222, v222 op_sel_hi:[0,0,0]
	v_mfma_scale_f32_16x16x128_f8f6f4 v[34:37], v[210:217], v[232:239], 0, v222, v222 op_sel_hi:[0,0,0]
	v_mfma_scale_f32_16x16x128_f8f6f4 v[22:25], v[202:209], v[240:247], 0, v222, v222 op_sel_hi:[0,0,0]
	v_mfma_scale_f32_16x16x128_f8f6f4 v[18:21], v[210:217], v[240:247], 0, v222, v222 op_sel_hi:[0,0,0]
	s_setprio 0
	s_barrier
	ds_read_b128 v[2:5], v183
	ds_read_b128 v[6:9], v184
	ds_read_b128 v[10:13], v185
	ds_read_b128 v[14:17], v196
	s_add_u32 s42, s40, 0x20100
	s_addc_u32 s43, s41, 0
	s_mov_b32 m0, s53
	v_lshl_add_u64 v[154:155], s[42:43], 0, v[164:165]
	ds_read_b128 v[202:205], v0 offset:32768
	ds_read_b128 v[206:209], v0 offset:33792
	ds_read_b128 v[210:213], v0 offset:34816
	ds_read_b128 v[214:217], v0 offset:35840
	ds_read_b128 v[232:235], v0 offset:36864
	ds_read_b128 v[236:239], v0 offset:37888
	ds_read_b128 v[240:243], v0 offset:38912
	ds_read_b128 v[244:247], v0 offset:39936
	global_load_lds_dwordx4 v[154:155], off
	v_lshl_add_u64 v[154:155], s[42:43], 0, v[160:161]
	s_mov_b32 m0, s54
	s_nop 0
	global_load_lds_dwordx4 v[154:155], off
	s_waitcnt lgkmcnt(8)
	s_barrier
	s_setprio 1
	s_waitcnt lgkmcnt(6)
	v_mfma_scale_f32_16x16x128_f8f6f4 v[142:145], v[2:9], v[202:209], v[142:145], v222, v222 op_sel_hi:[0,0,0]
	v_mfma_scale_f32_16x16x128_f8f6f4 v[138:141], v[10:17], v[202:209], v[138:141], v222, v222 op_sel_hi:[0,0,0]
	s_waitcnt lgkmcnt(4)
	v_mfma_scale_f32_16x16x128_f8f6f4 v[122:125], v[2:9], v[210:217], v[122:125], v222, v222 op_sel_hi:[0,0,0]
	v_mfma_scale_f32_16x16x128_f8f6f4 v[114:117], v[10:17], v[210:217], v[114:117], v222, v222 op_sel_hi:[0,0,0]
	s_waitcnt lgkmcnt(2)
	v_mfma_scale_f32_16x16x128_f8f6f4 v[102:105], v[2:9], v[232:239], v[102:105], v222, v222 op_sel_hi:[0,0,0]
	v_mfma_scale_f32_16x16x128_f8f6f4 v[98:101], v[10:17], v[232:239], v[98:101], v222, v222 op_sel_hi:[0,0,0]
	s_waitcnt lgkmcnt(0)
	v_mfma_scale_f32_16x16x128_f8f6f4 v[82:85], v[2:9], v[240:247], v[82:85], v222, v222 op_sel_hi:[0,0,0]
	v_mfma_scale_f32_16x16x128_f8f6f4 v[70:73], v[10:17], v[240:247], v[70:73], v222, v222 op_sel_hi:[0,0,0]
	s_setprio 0
	s_barrier
	s_mov_b64 s[42:43], 0x180
	s_mov_b32 m0, s56
	v_lshl_add_u64 v[150:151], v[150:151], 0, s[42:43]
	ds_read_b128 v[188:191], v197
	ds_read_b128 v[192:195], v198
	ds_read_b128 v[166:169], v199
	ds_read_b128 v[170:173], v200
	global_load_lds_dwordx4 v[150:151], off
	v_lshl_add_u64 v[150:151], v[152:153], 0, s[42:43]
	s_mov_b32 m0, s57
	s_nop 0
	global_load_lds_dwordx4 v[150:151], off
	s_barrier
	s_setprio 1
	s_waitcnt lgkmcnt(2)
	v_mfma_scale_f32_16x16x128_f8f6f4 v[134:137], v[188:195], v[202:209], v[134:137], v222, v222 op_sel_hi:[0,0,0]
	v_mfma_scale_f32_16x16x128_f8f6f4 v[126:129], v[188:195], v[210:217], v[126:129], v222, v222 op_sel_hi:[0,0,0]
	v_mfma_scale_f32_16x16x128_f8f6f4 v[110:113], v[188:195], v[232:239], v[110:113], v222, v222 op_sel_hi:[0,0,0]
	v_mfma_scale_f32_16x16x128_f8f6f4 v[90:93], v[188:195], v[240:247], v[90:93], v222, v222 op_sel_hi:[0,0,0]
	s_waitcnt lgkmcnt(0)
	v_mfma_scale_f32_16x16x128_f8f6f4 v[130:133], v[166:173], v[202:209], v[130:133], v222, v222 op_sel_hi:[0,0,0]
	v_mfma_scale_f32_16x16x128_f8f6f4 v[118:121], v[166:173], v[210:217], v[118:121], v222, v222 op_sel_hi:[0,0,0]
	v_mfma_scale_f32_16x16x128_f8f6f4 v[106:109], v[166:173], v[232:239], v[106:109], v222, v222 op_sel_hi:[0,0,0]
	v_mfma_scale_f32_16x16x128_f8f6f4 v[74:77], v[166:173], v[240:247], v[74:77], v222, v222 op_sel_hi:[0,0,0]
	s_setprio 0
	s_mov_b32 m0, s58
	v_lshl_add_u64 v[146:147], v[146:147], 0, s[42:43]
	s_barrier
	ds_read_b128 v[150:153], v0 offset:49152
	ds_read_b128 v[154:157], v0 offset:50176
	ds_read_b128 v[202:205], v0 offset:51200
	ds_read_b128 v[206:209], v0 offset:52224
	ds_read_b128 v[210:213], v0 offset:53248
	ds_read_b128 v[214:217], v0 offset:54272
	ds_read_b128 v[232:235], v0 offset:55296
	ds_read_b128 v[236:239], v0 offset:56320
	global_load_lds_dwordx4 v[146:147], off
	v_lshl_add_u64 v[146:147], v[148:149], 0, s[42:43]
	s_mov_b32 m0, s59
	s_nop 0
	global_load_lds_dwordx4 v[146:147], off
	s_barrier
	s_setprio 1
	s_waitcnt lgkmcnt(6)
	v_mfma_scale_f32_16x16x128_f8f6f4 v[94:97], v[2:9], v[150:157], v[94:97], v222, v222 op_sel_hi:[0,0,0]
	v_mfma_scale_f32_16x16x128_f8f6f4 v[86:89], v[10:17], v[150:157], v[86:89], v222, v222 op_sel_hi:[0,0,0]
	s_waitcnt lgkmcnt(4)
	v_mfma_scale_f32_16x16x128_f8f6f4 v[62:65], v[2:9], v[202:209], v[62:65], v222, v222 op_sel_hi:[0,0,0]
	v_mfma_scale_f32_16x16x128_f8f6f4 v[58:61], v[10:17], v[202:209], v[58:61], v222, v222 op_sel_hi:[0,0,0]
	s_waitcnt lgkmcnt(2)
	v_mfma_scale_f32_16x16x128_f8f6f4 v[46:49], v[2:9], v[210:217], v[46:49], v222, v222 op_sel_hi:[0,0,0]
	v_mfma_scale_f32_16x16x128_f8f6f4 v[42:45], v[10:17], v[210:217], v[42:45], v222, v222 op_sel_hi:[0,0,0]
	s_waitcnt lgkmcnt(0)
	v_mfma_scale_f32_16x16x128_f8f6f4 v[30:33], v[2:9], v[232:239], v[30:33], v222, v222 op_sel_hi:[0,0,0]
	v_mfma_scale_f32_16x16x128_f8f6f4 v[26:29], v[10:17], v[232:239], v[26:29], v222, v222 op_sel_hi:[0,0,0]
	s_setprio 0
	s_barrier
	s_add_u32 s42, s38, 0x20180
	s_addc_u32 s43, s39, 0
	s_mov_b32 m0, s60
	v_lshl_add_u64 v[2:3], s[42:43], 0, v[162:163]
	global_load_lds_dwordx4 v[2:3], off
	v_lshl_add_u64 v[2:3], s[42:43], 0, v[158:159]
	s_mov_b32 m0, s61
	s_nop 0
	global_load_lds_dwordx4 v[2:3], off
	s_waitcnt vmcnt(6)
	s_barrier
	s_setprio 1
	v_mfma_scale_f32_16x16x128_f8f6f4 v[78:81], v[188:195], v[150:157], v[78:81], v222, v222 op_sel_hi:[0,0,0]
	v_mfma_scale_f32_16x16x128_f8f6f4 v[66:69], v[166:173], v[150:157], v[66:69], v222, v222 op_sel_hi:[0,0,0]
	v_mfma_scale_f32_16x16x128_f8f6f4 v[54:57], v[188:195], v[202:209], v[54:57], v222, v222 op_sel_hi:[0,0,0]
	v_mfma_scale_f32_16x16x128_f8f6f4 v[50:53], v[166:173], v[202:209], v[50:53], v222, v222 op_sel_hi:[0,0,0]
	v_mfma_scale_f32_16x16x128_f8f6f4 v[38:41], v[188:195], v[210:217], v[38:41], v222, v222 op_sel_hi:[0,0,0]
	v_mfma_scale_f32_16x16x128_f8f6f4 v[34:37], v[166:173], v[210:217], v[34:37], v222, v222 op_sel_hi:[0,0,0]
	v_mfma_scale_f32_16x16x128_f8f6f4 v[22:25], v[188:195], v[232:239], v[22:25], v222, v222 op_sel_hi:[0,0,0]
	v_mfma_scale_f32_16x16x128_f8f6f4 v[18:21], v[166:173], v[232:239], v[18:21], v222, v222 op_sel_hi:[0,0,0]
	s_setprio 0
	s_add_u32 s40, s40, 0x20180
	s_addc_u32 s41, s41, 0
	s_add_u32 s69, s38, 0x200
	s_addc_u32 s70, s39, 0
	s_mov_b32 s71, 0
	s_barrier
.LBB0_1475:
	ds_read_b128 v[10:13], v175
	ds_read_b128 v[14:17], v176
	ds_read_b128 v[146:149], v177
	ds_read_b128 v[150:153], v178
	s_add_u32 s38, s40, 0xfffe0080
	s_addc_u32 s39, s41, -1
	s_cmp_eq_u32 s71, 4
	s_cselect_b32 s43, s15, s39
	s_cselect_b32 s42, s65, s38
	s_cselect_b32 s39, s13, s70
	s_cselect_b32 s38, s66, s69
	s_mov_b32 m0, s67
	v_lshl_add_u64 v[2:3], s[40:41], 0, v[218:219]
	ds_read_b128 v[166:169], v0
	ds_read_b128 v[170:173], v0 offset:1024
	ds_read_b128 v[188:191], v0 offset:2048
	ds_read_b128 v[192:195], v0 offset:3072
	ds_read_b128 v[202:205], v0 offset:4096
	ds_read_b128 v[206:209], v0 offset:5120
	ds_read_b128 v[210:213], v0 offset:6144
	ds_read_b128 v[214:217], v0 offset:7168
	global_load_lds_dwordx4 v[2:3], off
	v_lshl_add_u64 v[2:3], s[40:41], 0, v[220:221]
	s_mov_b32 m0, s68
	s_nop 0
	global_load_lds_dwordx4 v[2:3], off
	s_waitcnt lgkmcnt(8)
	s_barrier
	s_setprio 1
	s_waitcnt lgkmcnt(6)
	v_mfma_scale_f32_16x16x128_f8f6f4 v[142:145], v[10:17], v[166:173], v[142:145], v222, v222 op_sel_hi:[0,0,0]
	v_mfma_scale_f32_16x16x128_f8f6f4 v[138:141], v[146:153], v[166:173], v[138:141], v222, v222 op_sel_hi:[0,0,0]
	s_waitcnt lgkmcnt(4)
	v_mfma_scale_f32_16x16x128_f8f6f4 v[122:125], v[10:17], v[188:195], v[122:125], v222, v222 op_sel_hi:[0,0,0]
	v_mfma_scale_f32_16x16x128_f8f6f4 v[114:117], v[146:153], v[188:195], v[114:117], v222, v222 op_sel_hi:[0,0,0]
	s_waitcnt lgkmcnt(2)
	v_mfma_scale_f32_16x16x128_f8f6f4 v[102:105], v[10:17], v[202:209], v[102:105], v222, v222 op_sel_hi:[0,0,0]
	v_mfma_scale_f32_16x16x128_f8f6f4 v[98:101], v[146:153], v[202:209], v[98:101], v222, v222 op_sel_hi:[0,0,0]
	s_waitcnt lgkmcnt(0)
	v_mfma_scale_f32_16x16x128_f8f6f4 v[82:85], v[10:17], v[210:217], v[82:85], v222, v222 op_sel_hi:[0,0,0]
	v_mfma_scale_f32_16x16x128_f8f6f4 v[70:73], v[146:153], v[210:217], v[70:73], v222, v222 op_sel_hi:[0,0,0]
	s_setprio 0
	s_barrier
	s_mov_b32 m0, s48
	v_lshl_add_u64 v[6:7], s[38:39], 0, v[162:163]
	ds_read_b128 v[232:235], v179
	ds_read_b128 v[236:239], v180
	ds_read_b128 v[240:243], v181
	ds_read_b128 v[244:247], v182
	global_load_lds_dwordx4 v[6:7], off
	v_lshl_add_u64 v[8:9], s[38:39], 0, v[158:159]
	s_mov_b32 m0, s49
	s_nop 0
	global_load_lds_dwordx4 v[8:9], off
	s_barrier
	s_setprio 1
	s_waitcnt lgkmcnt(2)
	v_mfma_scale_f32_16x16x128_f8f6f4 v[134:137], v[232:239], v[166:173], v[134:137], v222, v222 op_sel_hi:[0,0,0]
	v_mfma_scale_f32_16x16x128_f8f6f4 v[126:129], v[232:239], v[188:195], v[126:129], v222, v222 op_sel_hi:[0,0,0]
	v_mfma_scale_f32_16x16x128_f8f6f4 v[110:113], v[232:239], v[202:209], v[110:113], v222, v222 op_sel_hi:[0,0,0]
	v_mfma_scale_f32_16x16x128_f8f6f4 v[90:93], v[232:239], v[210:217], v[90:93], v222, v222 op_sel_hi:[0,0,0]
	s_waitcnt lgkmcnt(0)
	v_mfma_scale_f32_16x16x128_f8f6f4 v[130:133], v[240:247], v[166:173], v[130:133], v222, v222 op_sel_hi:[0,0,0]
	v_mfma_scale_f32_16x16x128_f8f6f4 v[118:121], v[240:247], v[188:195], v[118:121], v222, v222 op_sel_hi:[0,0,0]
	v_mfma_scale_f32_16x16x128_f8f6f4 v[106:109], v[240:247], v[202:209], v[106:109], v222, v222 op_sel_hi:[0,0,0]
	v_mfma_scale_f32_16x16x128_f8f6f4 v[74:77], v[240:247], v[210:217], v[74:77], v222, v222 op_sel_hi:[0,0,0]
	s_setprio 0
	s_mov_b32 m0, s47
	v_lshl_add_u64 v[2:3], s[42:43], 0, v[164:165]
	s_barrier
	ds_read_b128 v[166:169], v0 offset:16384
	ds_read_b128 v[170:173], v0 offset:17408
	ds_read_b128 v[188:191], v0 offset:18432
	ds_read_b128 v[192:195], v0 offset:19456
	ds_read_b128 v[202:205], v0 offset:20480
	ds_read_b128 v[206:209], v0 offset:21504
	ds_read_b128 v[210:213], v0 offset:22528
	ds_read_b128 v[214:217], v0 offset:23552
	global_load_lds_dwordx4 v[2:3], off
	v_lshl_add_u64 v[4:5], s[42:43], 0, v[160:161]
	s_mov_b32 m0, s50
	s_nop 0
	global_load_lds_dwordx4 v[4:5], off
	s_barrier
	s_setprio 1
	s_waitcnt lgkmcnt(6)
	v_mfma_scale_f32_16x16x128_f8f6f4 v[94:97], v[10:17], v[166:173], v[94:97], v222, v222 op_sel_hi:[0,0,0]
	v_mfma_scale_f32_16x16x128_f8f6f4 v[86:89], v[146:153], v[166:173], v[86:89], v222, v222 op_sel_hi:[0,0,0]
	s_waitcnt lgkmcnt(4)
	v_mfma_scale_f32_16x16x128_f8f6f4 v[62:65], v[10:17], v[188:195], v[62:65], v222, v222 op_sel_hi:[0,0,0]
	v_mfma_scale_f32_16x16x128_f8f6f4 v[58:61], v[146:153], v[188:195], v[58:61], v222, v222 op_sel_hi:[0,0,0]
	s_waitcnt lgkmcnt(2)
	v_mfma_scale_f32_16x16x128_f8f6f4 v[46:49], v[10:17], v[202:209], v[46:49], v222, v222 op_sel_hi:[0,0,0]
	v_mfma_scale_f32_16x16x128_f8f6f4 v[42:45], v[146:153], v[202:209], v[42:45], v222, v222 op_sel_hi:[0,0,0]
	s_waitcnt lgkmcnt(0)
	v_mfma_scale_f32_16x16x128_f8f6f4 v[30:33], v[10:17], v[210:217], v[30:33], v222, v222 op_sel_hi:[0,0,0]
	v_mfma_scale_f32_16x16x128_f8f6f4 v[26:29], v[146:153], v[210:217], v[26:29], v222, v222 op_sel_hi:[0,0,0]
	s_setprio 0
	s_barrier
	s_add_u32 s72, s38, 0x20000
	s_addc_u32 s73, s39, 0
	s_mov_b32 m0, s51
	v_lshl_add_u64 v[10:11], s[72:73], 0, v[162:163]
	global_load_lds_dwordx4 v[10:11], off
	v_lshl_add_u64 v[10:11], s[72:73], 0, v[158:159]
	s_mov_b32 m0, s52
	s_nop 0
	global_load_lds_dwordx4 v[10:11], off
	s_waitcnt vmcnt(6)
	s_barrier
	s_setprio 1
	v_mfma_scale_f32_16x16x128_f8f6f4 v[78:81], v[232:239], v[166:173], v[78:81], v222, v222 op_sel_hi:[0,0,0]
	v_mfma_scale_f32_16x16x128_f8f6f4 v[66:69], v[240:247], v[166:173], v[66:69], v222, v222 op_sel_hi:[0,0,0]
	v_mfma_scale_f32_16x16x128_f8f6f4 v[54:57], v[232:239], v[188:195], v[54:57], v222, v222 op_sel_hi:[0,0,0]
	v_mfma_scale_f32_16x16x128_f8f6f4 v[50:53], v[240:247], v[188:195], v[50:53], v222, v222 op_sel_hi:[0,0,0]
	v_mfma_scale_f32_16x16x128_f8f6f4 v[38:41], v[232:239], v[202:209], v[38:41], v222, v222 op_sel_hi:[0,0,0]
	v_mfma_scale_f32_16x16x128_f8f6f4 v[34:37], v[240:247], v[202:209], v[34:37], v222, v222 op_sel_hi:[0,0,0]
	v_mfma_scale_f32_16x16x128_f8f6f4 v[22:25], v[232:239], v[210:217], v[22:25], v222, v222 op_sel_hi:[0,0,0]
	v_mfma_scale_f32_16x16x128_f8f6f4 v[18:21], v[240:247], v[210:217], v[18:21], v222, v222 op_sel_hi:[0,0,0]
	s_setprio 0
	s_barrier
	ds_read_b128 v[10:13], v183
	ds_read_b128 v[14:17], v184
	ds_read_b128 v[146:149], v185
	ds_read_b128 v[150:153], v196
	s_add_u32 s42, s42, 0x20000
	s_addc_u32 s43, s43, 0
	s_mov_b32 m0, s53
	v_lshl_add_u64 v[154:155], s[42:43], 0, v[164:165]
	ds_read_b128 v[166:169], v0 offset:32768
	ds_read_b128 v[170:173], v0 offset:33792
	ds_read_b128 v[188:191], v0 offset:34816
	ds_read_b128 v[192:195], v0 offset:35840
	ds_read_b128 v[202:205], v0 offset:36864
	ds_read_b128 v[206:209], v0 offset:37888
	ds_read_b128 v[210:213], v0 offset:38912
	ds_read_b128 v[214:217], v0 offset:39936
	global_load_lds_dwordx4 v[154:155], off
	v_lshl_add_u64 v[154:155], s[42:43], 0, v[160:161]
	s_mov_b32 m0, s54
	s_nop 0
	global_load_lds_dwordx4 v[154:155], off
	s_waitcnt lgkmcnt(8)
	s_barrier
	s_setprio 1
	s_waitcnt lgkmcnt(6)
	v_mfma_scale_f32_16x16x128_f8f6f4 v[142:145], v[10:17], v[166:173], v[142:145], v222, v222 op_sel_hi:[0,0,0]
	v_mfma_scale_f32_16x16x128_f8f6f4 v[138:141], v[146:153], v[166:173], v[138:141], v222, v222 op_sel_hi:[0,0,0]
	s_waitcnt lgkmcnt(4)
	v_mfma_scale_f32_16x16x128_f8f6f4 v[122:125], v[10:17], v[188:195], v[122:125], v222, v222 op_sel_hi:[0,0,0]
	v_mfma_scale_f32_16x16x128_f8f6f4 v[114:117], v[146:153], v[188:195], v[114:117], v222, v222 op_sel_hi:[0,0,0]
	s_waitcnt lgkmcnt(2)
	v_mfma_scale_f32_16x16x128_f8f6f4 v[102:105], v[10:17], v[202:209], v[102:105], v222, v222 op_sel_hi:[0,0,0]
	v_mfma_scale_f32_16x16x128_f8f6f4 v[98:101], v[146:153], v[202:209], v[98:101], v222, v222 op_sel_hi:[0,0,0]
	s_waitcnt lgkmcnt(0)
	v_mfma_scale_f32_16x16x128_f8f6f4 v[82:85], v[10:17], v[210:217], v[82:85], v222, v222 op_sel_hi:[0,0,0]
	v_mfma_scale_f32_16x16x128_f8f6f4 v[70:73], v[146:153], v[210:217], v[70:73], v222, v222 op_sel_hi:[0,0,0]
	s_setprio 0
	s_barrier
	s_mov_b32 m0, s56
	v_lshl_add_u64 v[6:7], v[6:7], 0, s[24:25]
	ds_read_b128 v[232:235], v197
	ds_read_b128 v[236:239], v198
	ds_read_b128 v[240:243], v199
	ds_read_b128 v[244:247], v200
	global_load_lds_dwordx4 v[6:7], off
	v_lshl_add_u64 v[6:7], v[8:9], 0, s[24:25]
	s_mov_b32 m0, s57
	s_nop 0
	global_load_lds_dwordx4 v[6:7], off
	s_barrier
	s_setprio 1
	s_waitcnt lgkmcnt(2)
	v_mfma_scale_f32_16x16x128_f8f6f4 v[134:137], v[232:239], v[166:173], v[134:137], v222, v222 op_sel_hi:[0,0,0]
	v_mfma_scale_f32_16x16x128_f8f6f4 v[126:129], v[232:239], v[188:195], v[126:129], v222, v222 op_sel_hi:[0,0,0]
	v_mfma_scale_f32_16x16x128_f8f6f4 v[110:113], v[232:239], v[202:209], v[110:113], v222, v222 op_sel_hi:[0,0,0]
	v_mfma_scale_f32_16x16x128_f8f6f4 v[90:93], v[232:239], v[210:217], v[90:93], v222, v222 op_sel_hi:[0,0,0]
	s_waitcnt lgkmcnt(0)
	v_mfma_scale_f32_16x16x128_f8f6f4 v[130:133], v[240:247], v[166:173], v[130:133], v222, v222 op_sel_hi:[0,0,0]
	v_mfma_scale_f32_16x16x128_f8f6f4 v[118:121], v[240:247], v[188:195], v[118:121], v222, v222 op_sel_hi:[0,0,0]
	v_mfma_scale_f32_16x16x128_f8f6f4 v[106:109], v[240:247], v[202:209], v[106:109], v222, v222 op_sel_hi:[0,0,0]
	v_mfma_scale_f32_16x16x128_f8f6f4 v[74:77], v[240:247], v[210:217], v[74:77], v222, v222 op_sel_hi:[0,0,0]
	s_setprio 0
	s_mov_b32 m0, s58
	v_lshl_add_u64 v[2:3], v[2:3], 0, s[24:25]
	s_barrier
	ds_read_b128 v[166:169], v0 offset:49152
	ds_read_b128 v[170:173], v0 offset:50176
	ds_read_b128 v[188:191], v0 offset:51200
	ds_read_b128 v[192:195], v0 offset:52224
	ds_read_b128 v[202:205], v0 offset:53248
	ds_read_b128 v[206:209], v0 offset:54272
	ds_read_b128 v[210:213], v0 offset:55296
	ds_read_b128 v[214:217], v0 offset:56320
	global_load_lds_dwordx4 v[2:3], off
	v_lshl_add_u64 v[2:3], v[4:5], 0, s[24:25]
	s_mov_b32 m0, s59
	s_nop 0
	global_load_lds_dwordx4 v[2:3], off
	s_barrier
	s_setprio 1
	s_waitcnt lgkmcnt(6)
	v_mfma_scale_f32_16x16x128_f8f6f4 v[94:97], v[10:17], v[166:173], v[94:97], v222, v222 op_sel_hi:[0,0,0]
	v_mfma_scale_f32_16x16x128_f8f6f4 v[86:89], v[146:153], v[166:173], v[86:89], v222, v222 op_sel_hi:[0,0,0]
	s_waitcnt lgkmcnt(4)
	v_mfma_scale_f32_16x16x128_f8f6f4 v[62:65], v[10:17], v[188:195], v[62:65], v222, v222 op_sel_hi:[0,0,0]
	v_mfma_scale_f32_16x16x128_f8f6f4 v[58:61], v[146:153], v[188:195], v[58:61], v222, v222 op_sel_hi:[0,0,0]
	s_waitcnt lgkmcnt(2)
	v_mfma_scale_f32_16x16x128_f8f6f4 v[46:49], v[10:17], v[202:209], v[46:49], v222, v222 op_sel_hi:[0,0,0]
	v_mfma_scale_f32_16x16x128_f8f6f4 v[42:45], v[146:153], v[202:209], v[42:45], v222, v222 op_sel_hi:[0,0,0]
	s_waitcnt lgkmcnt(0)
	v_mfma_scale_f32_16x16x128_f8f6f4 v[30:33], v[10:17], v[210:217], v[30:33], v222, v222 op_sel_hi:[0,0,0]
	v_mfma_scale_f32_16x16x128_f8f6f4 v[26:29], v[146:153], v[210:217], v[26:29], v222, v222 op_sel_hi:[0,0,0]
	s_setprio 0
	s_barrier
	s_add_u32 s38, s38, 0x20080
	s_addc_u32 s39, s39, 0
	s_mov_b32 m0, s60
	v_lshl_add_u64 v[2:3], s[38:39], 0, v[162:163]
	global_load_lds_dwordx4 v[2:3], off
	v_lshl_add_u64 v[2:3], s[38:39], 0, v[158:159]
	s_mov_b32 m0, s61
	s_nop 0
	global_load_lds_dwordx4 v[2:3], off
	s_waitcnt vmcnt(6)
	s_barrier
	s_setprio 1
	v_mfma_scale_f32_16x16x128_f8f6f4 v[78:81], v[232:239], v[166:173], v[78:81], v222, v222 op_sel_hi:[0,0,0]
	v_mfma_scale_f32_16x16x128_f8f6f4 v[66:69], v[240:247], v[166:173], v[66:69], v222, v222 op_sel_hi:[0,0,0]
	v_mfma_scale_f32_16x16x128_f8f6f4 v[54:57], v[232:239], v[188:195], v[54:57], v222, v222 op_sel_hi:[0,0,0]
	v_mfma_scale_f32_16x16x128_f8f6f4 v[50:53], v[240:247], v[188:195], v[50:53], v222, v222 op_sel_hi:[0,0,0]
	v_mfma_scale_f32_16x16x128_f8f6f4 v[38:41], v[232:239], v[202:209], v[38:41], v222, v222 op_sel_hi:[0,0,0]
	v_mfma_scale_f32_16x16x128_f8f6f4 v[34:37], v[240:247], v[202:209], v[34:37], v222, v222 op_sel_hi:[0,0,0]
	v_mfma_scale_f32_16x16x128_f8f6f4 v[22:25], v[232:239], v[210:217], v[22:25], v222, v222 op_sel_hi:[0,0,0]
	v_mfma_scale_f32_16x16x128_f8f6f4 v[18:21], v[240:247], v[210:217], v[18:21], v222, v222 op_sel_hi:[0,0,0]
	s_setprio 0
	s_add_i32 s71, s71, 2
	s_add_u32 s40, s40, 0x100
	s_addc_u32 s41, s41, 0
	s_add_u32 s69, s69, 0x100
	s_addc_u32 s70, s70, 0
	s_cmp_gt_u32 s71, 5
	s_barrier
	s_cbranch_scc0 .LBB0_1475
	s_nop 15
	s_nop 15
	v_mbcnt_lo_u32_b32 v0, -1, 0
	v_mbcnt_hi_u32_b32 v0, -1, v0
	v_readlane_b32 s15, v252, 51
	v_and_b32_e32 v201, 15, v0
	v_bfe_u32 v0, v0, 4, 2
	v_readlane_b32 s13, v252, 52
	s_mov_b64 s[38:39], -1
	s_and_b64 vcc, exec, s[10:11]
	s_cbranch_vccz .LBB0_1478
	v_lshl_or_b32 v6, s15, 6, v201
	s_lshl_b32 s38, s13, 5
	s_lshl_b32 s41, s64, 8
	s_ashr_i32 s39, s38, 31
	v_lshl_or_b32 v2, v0, 3, s38
	v_add_u32_e32 v4, s41, v6
	s_lshl_b32 s38, s63, 8
	v_mov_b32_e32 v3, s39
	v_ashrrev_i32_e32 v5, 31, v4
	s_ashr_i32 s39, s38, 31
	v_lshlrev_b64 v[16:17], 10, v[4:5]
	v_lshl_add_u64 v[4:5], v[2:3], 0, s[38:39]
	v_lshl_add_u64 v[2:3], v[16:17], 0, v[4:5]
	v_lshl_add_u64 v[146:147], v[2:3], 2, s[8:9]
	global_load_dwordx4 v[8:11], v[146:147], off offset:16
	global_load_dwordx4 v[12:15], v[146:147], off
	v_lshl_add_u64 v[2:3], v[2:3], 1, s[6:7]
	s_or_b32 s38, s41, 16
	s_or_b32 s39, s41, 32
	s_or_b32 s40, s41, 48
	s_waitcnt vmcnt(0)
	v_pk_fma_f32 v[148:149], v[140:141], s[26:27], v[10:11] op_sel_hi:[1,0,1]
	v_pk_fma_f32 v[14:15], v[144:145], s[26:27], v[14:15] op_sel_hi:[1,0,1]
	v_pk_fma_f32 v[12:13], v[142:143], s[26:27], v[12:13] op_sel_hi:[1,0,1]
	v_pk_fma_f32 v[10:11], v[138:139], s[26:27], v[8:9] op_sel_hi:[1,0,1]
	v_cvt_pk_bf16_f32 v8, v12, v13
	v_cvt_pk_bf16_f32 v9, v14, v15
	v_cvt_pk_bf16_f32 v10, v10, v11
	v_cvt_pk_bf16_f32 v11, v148, v149
	global_store_dwordx4 v[2:3], v[8:11], off
	global_load_dwordx4 v[8:11], v[146:147], off offset:528
	s_nop 0
	global_load_dwordx4 v[12:15], v[146:147], off offset:512
	v_lshl_add_u64 v[2:3], v[4:5], 0, s[24:25]
	v_lshl_add_u64 v[16:17], v[2:3], 0, v[16:17]
	s_waitcnt vmcnt(0)
	v_pk_fma_f32 v[146:147], v[132:133], s[26:27], v[10:11] op_sel_hi:[1,0,1]
	v_pk_fma_f32 v[14:15], v[136:137], s[26:27], v[14:15] op_sel_hi:[1,0,1]
	v_pk_fma_f32 v[12:13], v[134:135], s[26:27], v[12:13] op_sel_hi:[1,0,1]
	v_pk_fma_f32 v[10:11], v[130:131], s[26:27], v[8:9] op_sel_hi:[1,0,1]
	v_cvt_pk_bf16_f32 v8, v12, v13
	v_cvt_pk_bf16_f32 v9, v14, v15
	v_cvt_pk_bf16_f32 v10, v10, v11
	v_cvt_pk_bf16_f32 v11, v146, v147
	v_lshl_add_u64 v[12:13], v[16:17], 1, s[6:7]
	global_store_dwordx4 v[12:13], v[8:11], off
	s_nop 1
	v_add_u32_e32 v8, s38, v6
	v_ashrrev_i32_e32 v9, 31, v8
	v_lshlrev_b64 v[16:17], 10, v[8:9]
	v_lshl_add_u64 v[146:147], v[16:17], 0, v[4:5]
	v_lshl_add_u64 v[148:149], v[146:147], 2, s[8:9]
	global_load_dwordx4 v[8:11], v[148:149], off offset:16
	global_load_dwordx4 v[12:15], v[148:149], off
	v_lshl_add_u64 v[16:17], v[16:17], 0, v[2:3]
	s_waitcnt vmcnt(0)
	v_pk_fma_f32 v[150:151], v[116:117], s[26:27], v[10:11] op_sel_hi:[1,0,1]
	v_pk_fma_f32 v[14:15], v[124:125], s[26:27], v[14:15] op_sel_hi:[1,0,1]
	v_pk_fma_f32 v[12:13], v[122:123], s[26:27], v[12:13] op_sel_hi:[1,0,1]
	v_pk_fma_f32 v[10:11], v[114:115], s[26:27], v[8:9] op_sel_hi:[1,0,1]
	v_cvt_pk_bf16_f32 v8, v12, v13
	v_cvt_pk_bf16_f32 v9, v14, v15
	v_cvt_pk_bf16_f32 v10, v10, v11
	v_cvt_pk_bf16_f32 v11, v150, v151
	v_lshl_add_u64 v[12:13], v[146:147], 1, s[6:7]
	global_store_dwordx4 v[12:13], v[8:11], off
	global_load_dwordx4 v[8:11], v[148:149], off offset:528
	s_nop 0
	global_load_dwordx4 v[12:15], v[148:149], off offset:512
	s_waitcnt vmcnt(0)
	v_pk_fma_f32 v[146:147], v[120:121], s[26:27], v[10:11] op_sel_hi:[1,0,1]
	v_pk_fma_f32 v[14:15], v[128:129], s[26:27], v[14:15] op_sel_hi:[1,0,1]
	v_pk_fma_f32 v[12:13], v[126:127], s[26:27], v[12:13] op_sel_hi:[1,0,1]
	v_pk_fma_f32 v[10:11], v[118:119], s[26:27], v[8:9] op_sel_hi:[1,0,1]
	v_cvt_pk_bf16_f32 v8, v12, v13
	v_cvt_pk_bf16_f32 v9, v14, v15
	v_cvt_pk_bf16_f32 v10, v10, v11
	v_cvt_pk_bf16_f32 v11, v146, v147
	v_lshl_add_u64 v[12:13], v[16:17], 1, s[6:7]
	global_store_dwordx4 v[12:13], v[8:11], off
	s_nop 1
	v_add_u32_e32 v8, s39, v6
	v_ashrrev_i32_e32 v9, 31, v8
	v_lshlrev_b64 v[16:17], 10, v[8:9]
	v_lshl_add_u64 v[146:147], v[16:17], 0, v[4:5]
	v_lshl_add_u64 v[148:149], v[146:147], 2, s[8:9]
	global_load_dwordx4 v[8:11], v[148:149], off offset:16
	global_load_dwordx4 v[12:15], v[148:149], off
	v_lshl_add_u64 v[16:17], v[16:17], 0, v[2:3]
	s_waitcnt vmcnt(0)
	v_pk_fma_f32 v[150:151], v[100:101], s[26:27], v[10:11] op_sel_hi:[1,0,1]
	v_pk_fma_f32 v[14:15], v[104:105], s[26:27], v[14:15] op_sel_hi:[1,0,1]
	v_pk_fma_f32 v[12:13], v[102:103], s[26:27], v[12:13] op_sel_hi:[1,0,1]
	v_pk_fma_f32 v[10:11], v[98:99], s[26:27], v[8:9] op_sel_hi:[1,0,1]
	v_cvt_pk_bf16_f32 v8, v12, v13
	v_cvt_pk_bf16_f32 v9, v14, v15
	v_cvt_pk_bf16_f32 v10, v10, v11
	v_cvt_pk_bf16_f32 v11, v150, v151
	v_lshl_add_u64 v[12:13], v[146:147], 1, s[6:7]
	global_store_dwordx4 v[12:13], v[8:11], off
	global_load_dwordx4 v[8:11], v[148:149], off offset:528
	s_nop 0
	global_load_dwordx4 v[12:15], v[148:149], off offset:512
	s_waitcnt vmcnt(0)
	v_pk_fma_f32 v[146:147], v[108:109], s[26:27], v[10:11] op_sel_hi:[1,0,1]
	v_pk_fma_f32 v[14:15], v[112:113], s[26:27], v[14:15] op_sel_hi:[1,0,1]
	v_pk_fma_f32 v[12:13], v[110:111], s[26:27], v[12:13] op_sel_hi:[1,0,1]
	v_pk_fma_f32 v[10:11], v[106:107], s[26:27], v[8:9] op_sel_hi:[1,0,1]
	v_cvt_pk_bf16_f32 v8, v12, v13
	v_cvt_pk_bf16_f32 v9, v14, v15
	v_cvt_pk_bf16_f32 v10, v10, v11
	v_cvt_pk_bf16_f32 v11, v146, v147
	v_lshl_add_u64 v[12:13], v[16:17], 1, s[6:7]
	global_store_dwordx4 v[12:13], v[8:11], off
	s_nop 1
	v_add_u32_e32 v8, s40, v6
	v_ashrrev_i32_e32 v9, 31, v8
	v_lshlrev_b64 v[16:17], 10, v[8:9]
	v_lshl_add_u64 v[146:147], v[16:17], 0, v[4:5]
	v_lshl_add_u64 v[148:149], v[146:147], 2, s[8:9]
	global_load_dwordx4 v[8:11], v[148:149], off offset:16
	global_load_dwordx4 v[12:15], v[148:149], off
	v_lshl_add_u64 v[16:17], v[16:17], 0, v[2:3]
	v_add_u32_e32 v6, 0x80, v6
	s_waitcnt vmcnt(0)
	v_pk_fma_f32 v[150:151], v[72:73], s[26:27], v[10:11] op_sel_hi:[1,0,1]
	v_pk_fma_f32 v[14:15], v[84:85], s[26:27], v[14:15] op_sel_hi:[1,0,1]
	v_pk_fma_f32 v[12:13], v[82:83], s[26:27], v[12:13] op_sel_hi:[1,0,1]
	v_pk_fma_f32 v[10:11], v[70:71], s[26:27], v[8:9] op_sel_hi:[1,0,1]
	v_cvt_pk_bf16_f32 v8, v12, v13
	v_cvt_pk_bf16_f32 v9, v14, v15
	v_cvt_pk_bf16_f32 v10, v10, v11
	v_cvt_pk_bf16_f32 v11, v150, v151
	v_lshl_add_u64 v[12:13], v[146:147], 1, s[6:7]
	global_store_dwordx4 v[12:13], v[8:11], off
	global_load_dwordx4 v[8:11], v[148:149], off offset:528
	s_nop 0
	global_load_dwordx4 v[12:15], v[148:149], off offset:512
	s_waitcnt vmcnt(0)
	v_pk_fma_f32 v[146:147], v[76:77], s[26:27], v[10:11] op_sel_hi:[1,0,1]
	v_pk_fma_f32 v[14:15], v[92:93], s[26:27], v[14:15] op_sel_hi:[1,0,1]
	v_pk_fma_f32 v[12:13], v[90:91], s[26:27], v[12:13] op_sel_hi:[1,0,1]
	v_pk_fma_f32 v[10:11], v[74:75], s[26:27], v[8:9] op_sel_hi:[1,0,1]
	v_cvt_pk_bf16_f32 v8, v12, v13
	v_cvt_pk_bf16_f32 v9, v14, v15
	v_cvt_pk_bf16_f32 v10, v10, v11
	v_cvt_pk_bf16_f32 v11, v146, v147
	v_lshl_add_u64 v[12:13], v[16:17], 1, s[6:7]
	global_store_dwordx4 v[12:13], v[8:11], off
	s_nop 1
	v_add_u32_e32 v8, s41, v6
	v_ashrrev_i32_e32 v9, 31, v8
	v_lshlrev_b64 v[16:17], 10, v[8:9]
	v_lshl_add_u64 v[146:147], v[16:17], 0, v[4:5]
	v_lshl_add_u64 v[148:149], v[146:147], 2, s[8:9]
	global_load_dwordx4 v[8:11], v[148:149], off offset:16
	global_load_dwordx4 v[12:15], v[148:149], off
	v_lshl_add_u64 v[16:17], v[16:17], 0, v[2:3]
	s_waitcnt vmcnt(0)
	v_pk_fma_f32 v[150:151], v[88:89], s[26:27], v[10:11] op_sel_hi:[1,0,1]
	v_pk_fma_f32 v[14:15], v[96:97], s[26:27], v[14:15] op_sel_hi:[1,0,1]
	v_pk_fma_f32 v[12:13], v[94:95], s[26:27], v[12:13] op_sel_hi:[1,0,1]
	v_pk_fma_f32 v[10:11], v[86:87], s[26:27], v[8:9] op_sel_hi:[1,0,1]
	v_cvt_pk_bf16_f32 v8, v12, v13
	v_cvt_pk_bf16_f32 v9, v14, v15
	v_cvt_pk_bf16_f32 v10, v10, v11
	v_cvt_pk_bf16_f32 v11, v150, v151
	v_lshl_add_u64 v[12:13], v[146:147], 1, s[6:7]
	global_store_dwordx4 v[12:13], v[8:11], off
	global_load_dwordx4 v[8:11], v[148:149], off offset:528
	s_nop 0
	global_load_dwordx4 v[12:15], v[148:149], off offset:512
	s_waitcnt vmcnt(0)
	v_pk_fma_f32 v[146:147], v[68:69], s[26:27], v[10:11] op_sel_hi:[1,0,1]
	v_pk_fma_f32 v[14:15], v[80:81], s[26:27], v[14:15] op_sel_hi:[1,0,1]
	v_pk_fma_f32 v[12:13], v[78:79], s[26:27], v[12:13] op_sel_hi:[1,0,1]
	v_pk_fma_f32 v[10:11], v[66:67], s[26:27], v[8:9] op_sel_hi:[1,0,1]
	v_cvt_pk_bf16_f32 v8, v12, v13
	v_cvt_pk_bf16_f32 v9, v14, v15
	v_cvt_pk_bf16_f32 v10, v10, v11
	v_cvt_pk_bf16_f32 v11, v146, v147
	v_lshl_add_u64 v[12:13], v[16:17], 1, s[6:7]
	global_store_dwordx4 v[12:13], v[8:11], off
	s_nop 1
	v_add_u32_e32 v8, s38, v6
	v_ashrrev_i32_e32 v9, 31, v8
	v_lshlrev_b64 v[16:17], 10, v[8:9]
	v_lshl_add_u64 v[146:147], v[16:17], 0, v[4:5]
	v_lshl_add_u64 v[148:149], v[146:147], 2, s[8:9]
	global_load_dwordx4 v[8:11], v[148:149], off offset:16
	global_load_dwordx4 v[12:15], v[148:149], off
	v_lshl_add_u64 v[16:17], v[16:17], 0, v[2:3]
	s_waitcnt vmcnt(0)
	v_pk_fma_f32 v[150:151], v[60:61], s[26:27], v[10:11] op_sel_hi:[1,0,1]
	v_pk_fma_f32 v[14:15], v[64:65], s[26:27], v[14:15] op_sel_hi:[1,0,1]
	v_pk_fma_f32 v[12:13], v[62:63], s[26:27], v[12:13] op_sel_hi:[1,0,1]
	v_pk_fma_f32 v[10:11], v[58:59], s[26:27], v[8:9] op_sel_hi:[1,0,1]
	v_cvt_pk_bf16_f32 v8, v12, v13
	v_cvt_pk_bf16_f32 v9, v14, v15
	v_cvt_pk_bf16_f32 v10, v10, v11
	v_cvt_pk_bf16_f32 v11, v150, v151
	v_lshl_add_u64 v[12:13], v[146:147], 1, s[6:7]
	global_store_dwordx4 v[12:13], v[8:11], off
	global_load_dwordx4 v[8:11], v[148:149], off offset:528
	s_nop 0
	global_load_dwordx4 v[12:15], v[148:149], off offset:512
	s_waitcnt vmcnt(0)
	v_pk_fma_f32 v[146:147], v[52:53], s[26:27], v[10:11] op_sel_hi:[1,0,1]
	v_pk_fma_f32 v[14:15], v[56:57], s[26:27], v[14:15] op_sel_hi:[1,0,1]
	v_pk_fma_f32 v[12:13], v[54:55], s[26:27], v[12:13] op_sel_hi:[1,0,1]
	v_pk_fma_f32 v[10:11], v[50:51], s[26:27], v[8:9] op_sel_hi:[1,0,1]
	v_cvt_pk_bf16_f32 v8, v12, v13
	v_cvt_pk_bf16_f32 v9, v14, v15
	v_cvt_pk_bf16_f32 v10, v10, v11
	v_cvt_pk_bf16_f32 v11, v146, v147
	v_lshl_add_u64 v[12:13], v[16:17], 1, s[6:7]
	global_store_dwordx4 v[12:13], v[8:11], off
	s_nop 1
	v_add_u32_e32 v8, s39, v6
	v_ashrrev_i32_e32 v9, 31, v8
	v_lshlrev_b64 v[16:17], 10, v[8:9]
	v_lshl_add_u64 v[146:147], v[16:17], 0, v[4:5]
	v_lshl_add_u64 v[148:149], v[146:147], 2, s[8:9]
	global_load_dwordx4 v[8:11], v[148:149], off offset:16
	global_load_dwordx4 v[12:15], v[148:149], off
	v_lshl_add_u64 v[16:17], v[16:17], 0, v[2:3]
	v_add_u32_e32 v6, s40, v6
	v_ashrrev_i32_e32 v7, 31, v6
	s_mov_b64 s[38:39], 0
	s_waitcnt vmcnt(0)
	v_pk_fma_f32 v[150:151], v[44:45], s[26:27], v[10:11] op_sel_hi:[1,0,1]
	v_pk_fma_f32 v[14:15], v[48:49], s[26:27], v[14:15] op_sel_hi:[1,0,1]
	v_pk_fma_f32 v[12:13], v[46:47], s[26:27], v[12:13] op_sel_hi:[1,0,1]
	v_pk_fma_f32 v[10:11], v[42:43], s[26:27], v[8:9] op_sel_hi:[1,0,1]
	v_cvt_pk_bf16_f32 v8, v12, v13
	v_cvt_pk_bf16_f32 v9, v14, v15
	v_cvt_pk_bf16_f32 v10, v10, v11
	v_cvt_pk_bf16_f32 v11, v150, v151
	v_lshl_add_u64 v[12:13], v[146:147], 1, s[6:7]
	global_store_dwordx4 v[12:13], v[8:11], off
	global_load_dwordx4 v[8:11], v[148:149], off offset:528
	s_nop 0
	global_load_dwordx4 v[12:15], v[148:149], off offset:512
	s_waitcnt vmcnt(0)
	v_pk_fma_f32 v[146:147], v[36:37], s[26:27], v[10:11] op_sel_hi:[1,0,1]
	v_pk_fma_f32 v[14:15], v[40:41], s[26:27], v[14:15] op_sel_hi:[1,0,1]
	v_pk_fma_f32 v[12:13], v[38:39], s[26:27], v[12:13] op_sel_hi:[1,0,1]
	v_pk_fma_f32 v[10:11], v[34:35], s[26:27], v[8:9] op_sel_hi:[1,0,1]
	v_cvt_pk_bf16_f32 v8, v12, v13
	v_cvt_pk_bf16_f32 v9, v14, v15
	v_cvt_pk_bf16_f32 v10, v10, v11
	v_cvt_pk_bf16_f32 v11, v146, v147
	v_lshl_add_u64 v[12:13], v[16:17], 1, s[6:7]
	global_store_dwordx4 v[12:13], v[8:11], off
	v_lshlrev_b64 v[12:13], 10, v[6:7]
	v_lshl_add_u64 v[14:15], v[12:13], 0, v[4:5]
	v_lshl_add_u64 v[16:17], v[14:15], 2, s[8:9]
	global_load_dwordx4 v[4:7], v[16:17], off offset:16
	global_load_dwordx4 v[8:11], v[16:17], off
	s_waitcnt vmcnt(0)
	v_pk_fma_f32 v[146:147], v[28:29], s[26:27], v[6:7] op_sel_hi:[1,0,1]
	v_pk_fma_f32 v[10:11], v[32:33], s[26:27], v[10:11] op_sel_hi:[1,0,1]
	v_pk_fma_f32 v[8:9], v[30:31], s[26:27], v[8:9] op_sel_hi:[1,0,1]
	v_pk_fma_f32 v[6:7], v[26:27], s[26:27], v[4:5] op_sel_hi:[1,0,1]
	v_cvt_pk_bf16_f32 v4, v8, v9
	v_cvt_pk_bf16_f32 v5, v10, v11
	v_cvt_pk_bf16_f32 v6, v6, v7
	v_cvt_pk_bf16_f32 v7, v146, v147
	v_lshl_add_u64 v[8:9], v[14:15], 1, s[6:7]
	global_store_dwordx4 v[8:9], v[4:7], off
	v_lshl_add_u64 v[10:11], v[12:13], 0, v[2:3]
	global_load_dwordx4 v[2:5], v[16:17], off offset:528
	global_load_dwordx4 v[6:9], v[16:17], off offset:512
	s_waitcnt vmcnt(0)
	v_pk_fma_f32 v[12:13], v[20:21], s[26:27], v[4:5] op_sel_hi:[1,0,1]
	v_pk_fma_f32 v[8:9], v[24:25], s[26:27], v[8:9] op_sel_hi:[1,0,1]
	v_pk_fma_f32 v[6:7], v[22:23], s[26:27], v[6:7] op_sel_hi:[1,0,1]
	v_pk_fma_f32 v[4:5], v[18:19], s[26:27], v[2:3] op_sel_hi:[1,0,1]
	v_cvt_pk_bf16_f32 v2, v6, v7
	v_cvt_pk_bf16_f32 v3, v8, v9
	v_cvt_pk_bf16_f32 v4, v4, v5
	v_cvt_pk_bf16_f32 v5, v12, v13
	v_lshl_add_u64 v[6:7], v[10:11], 1, s[6:7]
	global_store_dwordx4 v[6:7], v[2:5], off

.LBB0_1694:
	ds_read_b128 v[2:5], v205
	ds_read_b128 v[6:9], v206
	ds_read_b128 v[10:13], v207
	ds_read_b128 v[14:17], v208
	s_lshl_b32 s46, s46, 7
	s_ashr_i32 s47, s46, 31
	s_add_i32 s41, s60, 0xc000
	v_add_u32_e32 v221, s72, v204
	s_mov_b32 m0, s41
	s_add_i32 s43, s60, 0xe000
	ds_read_b128 v[18:21], v221
	ds_read_b128 v[22:25], v221 offset:1024
	ds_read_b128 v[26:29], v221 offset:2048
	ds_read_b128 v[30:33], v221 offset:3072
	ds_read_b128 v[34:37], v221 offset:4096
	ds_read_b128 v[38:41], v221 offset:5120
	ds_read_b128 v[42:45], v221 offset:6144
	ds_read_b128 v[46:49], v221 offset:7168
	global_load_lds_dwordx4 v184, s[14:15]
	s_mov_b32 m0, s43
	s_nop 0
	global_load_lds_dwordx4 v198, s[14:15]
	s_waitcnt lgkmcnt(8)
	s_barrier
	s_setprio 1
	s_waitcnt lgkmcnt(6)
	v_mfma_scale_f32_16x16x128_f8f6f4 v[166:169], v[2:9], v[18:25], 0, v222, v222 op_sel_hi:[0,0,0]
	v_mfma_scale_f32_16x16x128_f8f6f4 v[162:165], v[10:17], v[18:25], 0, v222, v222 op_sel_hi:[0,0,0]
	s_waitcnt lgkmcnt(4)
	v_mfma_scale_f32_16x16x128_f8f6f4 v[150:153], v[2:9], v[26:33], 0, v222, v222 op_sel_hi:[0,0,0]
	v_mfma_scale_f32_16x16x128_f8f6f4 v[146:149], v[10:17], v[26:33], 0, v222, v222 op_sel_hi:[0,0,0]
	s_waitcnt lgkmcnt(2)
	v_mfma_scale_f32_16x16x128_f8f6f4 v[134:137], v[2:9], v[34:41], 0, v222, v222 op_sel_hi:[0,0,0]
	v_mfma_scale_f32_16x16x128_f8f6f4 v[130:133], v[10:17], v[34:41], 0, v222, v222 op_sel_hi:[0,0,0]
	s_waitcnt lgkmcnt(0)
	v_mfma_scale_f32_16x16x128_f8f6f4 v[118:121], v[2:9], v[42:49], 0, v222, v222 op_sel_hi:[0,0,0]
	v_mfma_scale_f32_16x16x128_f8f6f4 v[114:117], v[10:17], v[42:49], 0, v222, v222 op_sel_hi:[0,0,0]
	s_setprio 0
	s_barrier
	v_lshl_add_u64 v[200:201], s[50:51], 0, v[182:183]
	s_mov_b64 s[8:9], 0x100
	s_mov_b32 m0, s61
	v_lshl_add_u64 v[50:51], v[200:201], 0, s[8:9]
	v_lshl_add_u64 v[202:203], s[50:51], 0, v[180:181]
	ds_read_b128 v[188:191], v209
	ds_read_b128 v[192:195], v210
	ds_read_b128 v[232:235], v211
	ds_read_b128 v[236:239], v212
	global_load_lds_dwordx4 v[50:51], off
	v_lshl_add_u64 v[50:51], v[202:203], 0, s[8:9]
	s_mov_b32 m0, s62
	s_nop 0
	global_load_lds_dwordx4 v[50:51], off
	s_barrier
	s_setprio 1
	s_waitcnt lgkmcnt(2)
	v_mfma_scale_f32_16x16x128_f8f6f4 v[174:177], v[188:195], v[18:25], 0, v222, v222 op_sel_hi:[0,0,0]
	v_mfma_scale_f32_16x16x128_f8f6f4 v[158:161], v[188:195], v[26:33], 0, v222, v222 op_sel_hi:[0,0,0]
	v_mfma_scale_f32_16x16x128_f8f6f4 v[142:145], v[188:195], v[34:41], 0, v222, v222 op_sel_hi:[0,0,0]
	v_mfma_scale_f32_16x16x128_f8f6f4 v[126:129], v[188:195], v[42:49], 0, v222, v222 op_sel_hi:[0,0,0]
	s_waitcnt lgkmcnt(0)
	v_mfma_scale_f32_16x16x128_f8f6f4 v[170:173], v[232:239], v[18:25], 0, v222, v222 op_sel_hi:[0,0,0]
	v_mfma_scale_f32_16x16x128_f8f6f4 v[154:157], v[232:239], v[26:33], 0, v222, v222 op_sel_hi:[0,0,0]
	v_mfma_scale_f32_16x16x128_f8f6f4 v[138:141], v[232:239], v[34:41], 0, v222, v222 op_sel_hi:[0,0,0]
	v_mfma_scale_f32_16x16x128_f8f6f4 v[122:125], v[232:239], v[42:49], 0, v222, v222 op_sel_hi:[0,0,0]
	s_setprio 0
	s_mov_b32 m0, s60
	s_barrier
	ds_read_b128 v[18:21], v221 offset:16384
	ds_read_b128 v[22:25], v221 offset:17408
	ds_read_b128 v[26:29], v221 offset:18432
	ds_read_b128 v[30:33], v221 offset:19456
	ds_read_b128 v[34:37], v221 offset:20480
	ds_read_b128 v[38:41], v221 offset:21504
	ds_read_b128 v[42:45], v221 offset:22528
	ds_read_b128 v[46:49], v221 offset:23552
	global_load_lds_dwordx4 v0, s[34:35]
	s_mov_b32 m0, s63
	s_nop 0
	global_load_lds_dwordx4 v196, s[34:35]
	s_barrier
	s_setprio 1
	s_waitcnt lgkmcnt(6)
	v_mfma_scale_f32_16x16x128_f8f6f4 v[102:105], v[2:9], v[18:25], 0, v222, v222 op_sel_hi:[0,0,0]
	v_mfma_scale_f32_16x16x128_f8f6f4 v[98:101], v[10:17], v[18:25], 0, v222, v222 op_sel_hi:[0,0,0]
	s_waitcnt lgkmcnt(4)
	v_mfma_scale_f32_16x16x128_f8f6f4 v[86:89], v[2:9], v[26:33], 0, v222, v222 op_sel_hi:[0,0,0]
	v_mfma_scale_f32_16x16x128_f8f6f4 v[82:85], v[10:17], v[26:33], 0, v222, v222 op_sel_hi:[0,0,0]
	s_waitcnt lgkmcnt(2)
	v_mfma_scale_f32_16x16x128_f8f6f4 v[70:73], v[2:9], v[34:41], 0, v222, v222 op_sel_hi:[0,0,0]
	v_mfma_scale_f32_16x16x128_f8f6f4 v[66:69], v[10:17], v[34:41], 0, v222, v222 op_sel_hi:[0,0,0]
	s_waitcnt lgkmcnt(0)
	v_mfma_scale_f32_16x16x128_f8f6f4 v[54:57], v[2:9], v[42:49], 0, v222, v222 op_sel_hi:[0,0,0]
	v_mfma_scale_f32_16x16x128_f8f6f4 v[50:53], v[10:17], v[42:49], 0, v222, v222 op_sel_hi:[0,0,0]
	s_setprio 0
	s_barrier
	s_add_u32 s8, s50, 0x20100
	s_addc_u32 s9, s51, 0
	s_mov_b32 m0, s64
	v_lshl_add_u64 v[2:3], s[8:9], 0, v[182:183]
	global_load_lds_dwordx4 v[2:3], off
	v_lshl_add_u64 v[2:3], s[8:9], 0, v[180:181]
	s_mov_b32 m0, s65
	s_nop 0
	global_load_lds_dwordx4 v[2:3], off
	s_waitcnt vmcnt(6)
	s_barrier
	s_setprio 1
	v_mfma_scale_f32_16x16x128_f8f6f4 v[110:113], v[188:195], v[18:25], 0, v222, v222 op_sel_hi:[0,0,0]
	v_mfma_scale_f32_16x16x128_f8f6f4 v[106:109], v[232:239], v[18:25], 0, v222, v222 op_sel_hi:[0,0,0]
	v_mfma_scale_f32_16x16x128_f8f6f4 v[94:97], v[188:195], v[26:33], 0, v222, v222 op_sel_hi:[0,0,0]
	v_mfma_scale_f32_16x16x128_f8f6f4 v[90:93], v[232:239], v[26:33], 0, v222, v222 op_sel_hi:[0,0,0]
	v_mfma_scale_f32_16x16x128_f8f6f4 v[78:81], v[188:195], v[34:41], 0, v222, v222 op_sel_hi:[0,0,0]
	v_mfma_scale_f32_16x16x128_f8f6f4 v[74:77], v[232:239], v[34:41], 0, v222, v222 op_sel_hi:[0,0,0]
	v_mfma_scale_f32_16x16x128_f8f6f4 v[62:65], v[188:195], v[42:49], 0, v222, v222 op_sel_hi:[0,0,0]
	v_mfma_scale_f32_16x16x128_f8f6f4 v[58:61], v[232:239], v[42:49], 0, v222, v222 op_sel_hi:[0,0,0]
	s_setprio 0
	s_barrier
	ds_read_b128 v[2:5], v213
	ds_read_b128 v[6:9], v214
	ds_read_b128 v[10:13], v215
	ds_read_b128 v[14:17], v216
	s_mov_b32 m0, s66
	ds_read_b128 v[18:21], v221 offset:32768
	ds_read_b128 v[22:25], v221 offset:33792
	ds_read_b128 v[26:29], v221 offset:34816
	ds_read_b128 v[30:33], v221 offset:35840
	ds_read_b128 v[34:37], v221 offset:36864
	ds_read_b128 v[38:41], v221 offset:37888
	ds_read_b128 v[42:45], v221 offset:38912
	ds_read_b128 v[46:49], v221 offset:39936
	global_load_lds_dwordx4 v184, s[34:35]
	s_mov_b32 m0, s67
	s_nop 0
	global_load_lds_dwordx4 v198, s[34:35]
	s_waitcnt lgkmcnt(8)
	s_barrier
	s_setprio 1
	s_waitcnt lgkmcnt(6)
	v_mfma_scale_f32_16x16x128_f8f6f4 v[166:169], v[2:9], v[18:25], v[166:169], v222, v222 op_sel_hi:[0,0,0]
	v_mfma_scale_f32_16x16x128_f8f6f4 v[162:165], v[10:17], v[18:25], v[162:165], v222, v222 op_sel_hi:[0,0,0]
	s_waitcnt lgkmcnt(4)
	v_mfma_scale_f32_16x16x128_f8f6f4 v[150:153], v[2:9], v[26:33], v[150:153], v222, v222 op_sel_hi:[0,0,0]
	v_mfma_scale_f32_16x16x128_f8f6f4 v[146:149], v[10:17], v[26:33], v[146:149], v222, v222 op_sel_hi:[0,0,0]
	s_waitcnt lgkmcnt(2)
	v_mfma_scale_f32_16x16x128_f8f6f4 v[134:137], v[2:9], v[34:41], v[134:137], v222, v222 op_sel_hi:[0,0,0]
	v_mfma_scale_f32_16x16x128_f8f6f4 v[130:133], v[10:17], v[34:41], v[130:133], v222, v222 op_sel_hi:[0,0,0]
	s_waitcnt lgkmcnt(0)
	v_mfma_scale_f32_16x16x128_f8f6f4 v[118:121], v[2:9], v[42:49], v[118:121], v222, v222 op_sel_hi:[0,0,0]
	v_mfma_scale_f32_16x16x128_f8f6f4 v[114:117], v[10:17], v[42:49], v[114:117], v222, v222 op_sel_hi:[0,0,0]
	s_setprio 0
	s_barrier
	s_mov_b64 s[8:9], 0x180
	s_mov_b32 m0, s73
	v_lshl_add_u64 v[200:201], v[200:201], 0, s[8:9]
	ds_read_b128 v[188:191], v217
	ds_read_b128 v[192:195], v218
	ds_read_b128 v[232:235], v219
	ds_read_b128 v[236:239], v220
	global_load_lds_dwordx4 v[200:201], off
	v_lshl_add_u64 v[200:201], v[202:203], 0, s[8:9]
	s_mov_b32 m0, s74
	s_nop 0
	global_load_lds_dwordx4 v[200:201], off
	s_barrier
	s_setprio 1
	s_waitcnt lgkmcnt(2)
	v_mfma_scale_f32_16x16x128_f8f6f4 v[174:177], v[188:195], v[18:25], v[174:177], v222, v222 op_sel_hi:[0,0,0]
	v_mfma_scale_f32_16x16x128_f8f6f4 v[158:161], v[188:195], v[26:33], v[158:161], v222, v222 op_sel_hi:[0,0,0]
	v_mfma_scale_f32_16x16x128_f8f6f4 v[142:145], v[188:195], v[34:41], v[142:145], v222, v222 op_sel_hi:[0,0,0]
	v_mfma_scale_f32_16x16x128_f8f6f4 v[126:129], v[188:195], v[42:49], v[126:129], v222, v222 op_sel_hi:[0,0,0]
	s_waitcnt lgkmcnt(0)
	v_mfma_scale_f32_16x16x128_f8f6f4 v[170:173], v[232:239], v[18:25], v[170:173], v222, v222 op_sel_hi:[0,0,0]
	v_mfma_scale_f32_16x16x128_f8f6f4 v[154:157], v[232:239], v[26:33], v[154:157], v222, v222 op_sel_hi:[0,0,0]
	v_mfma_scale_f32_16x16x128_f8f6f4 v[138:141], v[232:239], v[34:41], v[138:141], v222, v222 op_sel_hi:[0,0,0]
	v_mfma_scale_f32_16x16x128_f8f6f4 v[122:125], v[232:239], v[42:49], v[122:125], v222, v222 op_sel_hi:[0,0,0]
	s_setprio 0
	s_mov_b32 m0, s75
	s_barrier
	ds_read_b128 v[18:21], v221 offset:49152
	ds_read_b128 v[22:25], v221 offset:50176
	ds_read_b128 v[26:29], v221 offset:51200
	ds_read_b128 v[30:33], v221 offset:52224
	ds_read_b128 v[34:37], v221 offset:53248
	ds_read_b128 v[38:41], v221 offset:54272
	ds_read_b128 v[42:45], v221 offset:55296
	ds_read_b128 v[46:49], v221 offset:56320
	global_load_lds_dwordx4 v0, s[38:39]
	s_mov_b32 m0, s76
	s_nop 0
	global_load_lds_dwordx4 v196, s[38:39]
	s_barrier
	s_setprio 1
	s_waitcnt lgkmcnt(6)
	v_mfma_scale_f32_16x16x128_f8f6f4 v[102:105], v[2:9], v[18:25], v[102:105], v222, v222 op_sel_hi:[0,0,0]
	v_mfma_scale_f32_16x16x128_f8f6f4 v[98:101], v[10:17], v[18:25], v[98:101], v222, v222 op_sel_hi:[0,0,0]
	s_waitcnt lgkmcnt(4)
	v_mfma_scale_f32_16x16x128_f8f6f4 v[86:89], v[2:9], v[26:33], v[86:89], v222, v222 op_sel_hi:[0,0,0]
	v_mfma_scale_f32_16x16x128_f8f6f4 v[82:85], v[10:17], v[26:33], v[82:85], v222, v222 op_sel_hi:[0,0,0]
	s_waitcnt lgkmcnt(2)
	v_mfma_scale_f32_16x16x128_f8f6f4 v[70:73], v[2:9], v[34:41], v[70:73], v222, v222 op_sel_hi:[0,0,0]
	v_mfma_scale_f32_16x16x128_f8f6f4 v[66:69], v[10:17], v[34:41], v[66:69], v222, v222 op_sel_hi:[0,0,0]
	s_waitcnt lgkmcnt(0)
	v_mfma_scale_f32_16x16x128_f8f6f4 v[54:57], v[2:9], v[42:49], v[54:57], v222, v222 op_sel_hi:[0,0,0]
	v_mfma_scale_f32_16x16x128_f8f6f4 v[50:53], v[10:17], v[42:49], v[50:53], v222, v222 op_sel_hi:[0,0,0]
	s_setprio 0
	s_barrier
	s_add_u32 s8, s50, 0x20180
	s_addc_u32 s9, s51, 0
	s_mov_b32 m0, s77
	v_lshl_add_u64 v[2:3], s[8:9], 0, v[182:183]
	global_load_lds_dwordx4 v[2:3], off
	v_lshl_add_u64 v[2:3], s[8:9], 0, v[180:181]
	s_mov_b32 m0, s78
	s_nop 0
	global_load_lds_dwordx4 v[2:3], off
	s_waitcnt vmcnt(6)
	s_barrier
	s_setprio 1
	v_mfma_scale_f32_16x16x128_f8f6f4 v[110:113], v[188:195], v[18:25], v[110:113], v222, v222 op_sel_hi:[0,0,0]
	v_mfma_scale_f32_16x16x128_f8f6f4 v[106:109], v[232:239], v[18:25], v[106:109], v222, v222 op_sel_hi:[0,0,0]
	v_mfma_scale_f32_16x16x128_f8f6f4 v[94:97], v[188:195], v[26:33], v[94:97], v222, v222 op_sel_hi:[0,0,0]
	v_mfma_scale_f32_16x16x128_f8f6f4 v[90:93], v[232:239], v[26:33], v[90:93], v222, v222 op_sel_hi:[0,0,0]
	v_mfma_scale_f32_16x16x128_f8f6f4 v[78:81], v[188:195], v[34:41], v[78:81], v222, v222 op_sel_hi:[0,0,0]
	v_mfma_scale_f32_16x16x128_f8f6f4 v[74:77], v[232:239], v[34:41], v[74:77], v222, v222 op_sel_hi:[0,0,0]
	v_mfma_scale_f32_16x16x128_f8f6f4 v[62:65], v[188:195], v[42:49], v[62:65], v222, v222 op_sel_hi:[0,0,0]
	v_mfma_scale_f32_16x16x128_f8f6f4 v[58:61], v[232:239], v[42:49], v[58:61], v222, v222 op_sel_hi:[0,0,0]
	s_setprio 0
	s_lshl_b64 s[8:9], s[46:47], 2
	s_add_u32 s49, s70, s8
	s_addc_u32 s80, s71, s9
	s_add_u32 s81, s50, 0x200
	s_addc_u32 s82, s51, 0
	s_mov_b32 s83, 0
	s_mov_b64 s[50:51], 0
	s_barrier
	s_branch .LBB0_1696
.LBB0_1695:
	s_add_u32 s54, s50, 0x200
	s_addc_u32 s55, s51, 0
	s_and_b64 s[8:9], s[52:53], exec
	s_cselect_b32 s9, 0, s54
	s_cselect_b32 s8, 0, s55
	s_add_u32 s54, s12, s9
	s_addc_u32 s55, s13, s8
	s_add_u32 s84, s81, s50
	s_waitcnt lgkmcnt(8)
	s_barrier
	s_waitcnt lgkmcnt(0)
	s_addc_u32 s85, s82, s51
	s_and_b64 s[8:9], s[52:53], exec
	v_mov_b32_e32 v185, v1
	v_mov_b32_e32 v199, v1
	s_cselect_b32 s9, s45, s85
	s_cselect_b32 s8, s44, s84
	s_setprio 1
	s_waitcnt lgkmcnt(0)
	v_mfma_scale_f32_16x16x128_f8f6f4 v[166:169], v[10:17], v[42:49], v[166:169], v222, v222 op_sel_hi:[0,0,0]
	v_mfma_scale_f32_16x16x128_f8f6f4 v[162:165], v[2:9], v[42:49], v[162:165], v222, v222 op_sel_hi:[0,0,0]
	v_mfma_scale_f32_16x16x128_f8f6f4 v[150:153], v[10:17], v[34:41], v[150:153], v222, v222 op_sel_hi:[0,0,0]
	v_mfma_scale_f32_16x16x128_f8f6f4 v[146:149], v[2:9], v[34:41], v[146:149], v222, v222 op_sel_hi:[0,0,0]
	v_mfma_scale_f32_16x16x128_f8f6f4 v[134:137], v[10:17], v[26:33], v[134:137], v222, v222 op_sel_hi:[0,0,0]
	v_mfma_scale_f32_16x16x128_f8f6f4 v[130:133], v[2:9], v[26:33], v[130:133], v222, v222 op_sel_hi:[0,0,0]
	v_mfma_scale_f32_16x16x128_f8f6f4 v[118:121], v[10:17], v[18:25], v[118:121], v222, v222 op_sel_hi:[0,0,0]
	v_mfma_scale_f32_16x16x128_f8f6f4 v[114:117], v[2:9], v[18:25], v[114:117], v222, v222 op_sel_hi:[0,0,0]
	s_setprio 0
	s_barrier
	s_mov_b32 m0, s61
	v_lshl_add_u64 v[200:201], s[8:9], 0, v[182:183]
	ds_read_b128 v[188:191], v209
	ds_read_b128 v[192:195], v210
	ds_read_b128 v[232:235], v211
	ds_read_b128 v[236:239], v212
	global_load_lds_dwordx4 v[200:201], off
	v_lshl_add_u64 v[202:203], s[8:9], 0, v[180:181]
	s_mov_b32 m0, s62
	s_nop 0
	global_load_lds_dwordx4 v[202:203], off
	s_barrier
	s_setprio 1
	s_waitcnt lgkmcnt(2)
	v_mfma_scale_f32_16x16x128_f8f6f4 v[174:177], v[188:195], v[42:49], v[174:177], v222, v222 op_sel_hi:[0,0,0]
	v_mfma_scale_f32_16x16x128_f8f6f4 v[158:161], v[188:195], v[34:41], v[158:161], v222, v222 op_sel_hi:[0,0,0]
	v_mfma_scale_f32_16x16x128_f8f6f4 v[142:145], v[188:195], v[26:33], v[142:145], v222, v222 op_sel_hi:[0,0,0]
	v_mfma_scale_f32_16x16x128_f8f6f4 v[126:129], v[188:195], v[18:25], v[126:129], v222, v222 op_sel_hi:[0,0,0]
	s_waitcnt lgkmcnt(0)
	v_mfma_scale_f32_16x16x128_f8f6f4 v[170:173], v[232:239], v[42:49], v[170:173], v222, v222 op_sel_hi:[0,0,0]
	v_mfma_scale_f32_16x16x128_f8f6f4 v[154:157], v[232:239], v[34:41], v[154:157], v222, v222 op_sel_hi:[0,0,0]
	v_mfma_scale_f32_16x16x128_f8f6f4 v[138:141], v[232:239], v[26:33], v[138:141], v222, v222 op_sel_hi:[0,0,0]
	v_mfma_scale_f32_16x16x128_f8f6f4 v[122:125], v[232:239], v[18:25], v[122:125], v222, v222 op_sel_hi:[0,0,0]
	s_setprio 0
	s_mov_b32 m0, s60
	s_barrier
	ds_read_b128 v[22:25], v221 offset:16384
	ds_read_b128 v[26:29], v221 offset:17408
	ds_read_b128 v[30:33], v221 offset:18432
	ds_read_b128 v[34:37], v221 offset:19456
	ds_read_b128 v[38:41], v221 offset:20480
	ds_read_b128 v[42:45], v221 offset:21504
	ds_read_b128 v[240:243], v221 offset:22528
	ds_read_b128 v[244:247], v221 offset:23552
	global_load_lds_dwordx4 v0, s[54:55]
	s_mov_b32 m0, s63
	v_mov_b32_e32 v197, v1
	global_load_lds_dwordx4 v196, s[54:55]
	s_barrier
	s_waitcnt lgkmcnt(0)
	v_lshl_add_u64 v[20:21], s[54:55], 0, v[0:1]
	v_lshl_add_u64 v[18:19], s[54:55], 0, v[196:197]
	s_setprio 1
	s_waitcnt lgkmcnt(0)
	v_mfma_scale_f32_16x16x128_f8f6f4 v[102:105], v[10:17], v[22:29], v[102:105], v222, v222 op_sel_hi:[0,0,0]
	v_mfma_scale_f32_16x16x128_f8f6f4 v[98:101], v[2:9], v[22:29], v[98:101], v222, v222 op_sel_hi:[0,0,0]
	v_mfma_scale_f32_16x16x128_f8f6f4 v[86:89], v[10:17], v[30:37], v[86:89], v222, v222 op_sel_hi:[0,0,0]
	v_mfma_scale_f32_16x16x128_f8f6f4 v[82:85], v[2:9], v[30:37], v[82:85], v222, v222 op_sel_hi:[0,0,0]
	v_mfma_scale_f32_16x16x128_f8f6f4 v[70:73], v[10:17], v[38:45], v[70:73], v222, v222 op_sel_hi:[0,0,0]
	v_mfma_scale_f32_16x16x128_f8f6f4 v[66:69], v[2:9], v[38:45], v[66:69], v222, v222 op_sel_hi:[0,0,0]
	v_mfma_scale_f32_16x16x128_f8f6f4 v[54:57], v[10:17], v[240:247], v[54:57], v222, v222 op_sel_hi:[0,0,0]
	v_mfma_scale_f32_16x16x128_f8f6f4 v[50:53], v[2:9], v[240:247], v[50:53], v222, v222 op_sel_hi:[0,0,0]
	s_setprio 0
	s_barrier
	s_add_u32 s52, s8, 0x20000
	s_addc_u32 s53, s9, 0
	s_mov_b32 m0, s64
	v_lshl_add_u64 v[2:3], s[52:53], 0, v[182:183]
	global_load_lds_dwordx4 v[2:3], off
	v_lshl_add_u64 v[2:3], s[52:53], 0, v[180:181]
	s_mov_b32 m0, s65
	s_nop 0
	global_load_lds_dwordx4 v[2:3], off
	s_waitcnt vmcnt(6)
	s_barrier
	s_setprio 1
	v_mfma_scale_f32_16x16x128_f8f6f4 v[110:113], v[188:195], v[22:29], v[110:113], v222, v222 op_sel_hi:[0,0,0]
	v_mfma_scale_f32_16x16x128_f8f6f4 v[106:109], v[232:239], v[22:29], v[106:109], v222, v222 op_sel_hi:[0,0,0]
	v_mfma_scale_f32_16x16x128_f8f6f4 v[94:97], v[188:195], v[30:37], v[94:97], v222, v222 op_sel_hi:[0,0,0]
	v_mfma_scale_f32_16x16x128_f8f6f4 v[90:93], v[232:239], v[30:37], v[90:93], v222, v222 op_sel_hi:[0,0,0]
	v_mfma_scale_f32_16x16x128_f8f6f4 v[78:81], v[188:195], v[38:45], v[78:81], v222, v222 op_sel_hi:[0,0,0]
	v_mfma_scale_f32_16x16x128_f8f6f4 v[74:77], v[232:239], v[38:45], v[74:77], v222, v222 op_sel_hi:[0,0,0]
	v_mfma_scale_f32_16x16x128_f8f6f4 v[62:65], v[188:195], v[240:247], v[62:65], v222, v222 op_sel_hi:[0,0,0]
	v_mfma_scale_f32_16x16x128_f8f6f4 v[58:61], v[232:239], v[240:247], v[58:61], v222, v222 op_sel_hi:[0,0,0]
	s_setprio 0
	s_barrier
	ds_read_b128 v[2:5], v213
	ds_read_b128 v[6:9], v214
	ds_read_b128 v[10:13], v215
	ds_read_b128 v[14:17], v216
	s_mov_b32 m0, s66
	v_lshl_add_u64 v[46:47], s[54:55], 0, v[184:185]
	ds_read_b128 v[22:25], v221 offset:32768
	ds_read_b128 v[26:29], v221 offset:33792
	ds_read_b128 v[30:33], v221 offset:34816
	ds_read_b128 v[34:37], v221 offset:35840
	ds_read_b128 v[38:41], v221 offset:36864
	ds_read_b128 v[42:45], v221 offset:37888
	ds_read_b128 v[188:191], v221 offset:38912
	ds_read_b128 v[192:195], v221 offset:39936
	global_load_lds_dwordx4 v[46:47], off
	v_lshl_add_u64 v[46:47], s[54:55], 0, v[198:199]
	s_mov_b32 m0, s67
	s_nop 0
	global_load_lds_dwordx4 v[46:47], off
	s_waitcnt lgkmcnt(8)
	s_barrier
	s_setprio 1
	s_waitcnt lgkmcnt(6)
	v_mfma_scale_f32_16x16x128_f8f6f4 v[166:169], v[2:9], v[22:29], v[166:169], v222, v222 op_sel_hi:[0,0,0]
	v_mfma_scale_f32_16x16x128_f8f6f4 v[162:165], v[10:17], v[22:29], v[162:165], v222, v222 op_sel_hi:[0,0,0]
	s_waitcnt lgkmcnt(4)
	v_mfma_scale_f32_16x16x128_f8f6f4 v[150:153], v[2:9], v[30:37], v[150:153], v222, v222 op_sel_hi:[0,0,0]
	v_mfma_scale_f32_16x16x128_f8f6f4 v[146:149], v[10:17], v[30:37], v[146:149], v222, v222 op_sel_hi:[0,0,0]
	s_waitcnt lgkmcnt(2)
	v_mfma_scale_f32_16x16x128_f8f6f4 v[134:137], v[2:9], v[38:45], v[134:137], v222, v222 op_sel_hi:[0,0,0]
	v_mfma_scale_f32_16x16x128_f8f6f4 v[130:133], v[10:17], v[38:45], v[130:133], v222, v222 op_sel_hi:[0,0,0]
	s_waitcnt lgkmcnt(0)
	v_mfma_scale_f32_16x16x128_f8f6f4 v[118:121], v[2:9], v[188:195], v[118:121], v222, v222 op_sel_hi:[0,0,0]
	v_mfma_scale_f32_16x16x128_f8f6f4 v[114:117], v[10:17], v[188:195], v[114:117], v222, v222 op_sel_hi:[0,0,0]
	s_setprio 0
	s_barrier
	s_mov_b32 m0, s73
	v_lshl_add_u64 v[46:47], v[200:201], 0, s[24:25]
	ds_read_b128 v[232:235], v217
	ds_read_b128 v[236:239], v218
	ds_read_b128 v[240:243], v219
	ds_read_b128 v[244:247], v220
	global_load_lds_dwordx4 v[46:47], off
	v_lshl_add_u64 v[46:47], v[202:203], 0, s[24:25]
	s_mov_b32 m0, s74
	s_nop 0
	global_load_lds_dwordx4 v[46:47], off
	s_barrier
	s_setprio 1
	s_waitcnt lgkmcnt(2)
	v_mfma_scale_f32_16x16x128_f8f6f4 v[174:177], v[232:239], v[22:29], v[174:177], v222, v222 op_sel_hi:[0,0,0]
	v_mfma_scale_f32_16x16x128_f8f6f4 v[158:161], v[232:239], v[30:37], v[158:161], v222, v222 op_sel_hi:[0,0,0]
	v_mfma_scale_f32_16x16x128_f8f6f4 v[142:145], v[232:239], v[38:45], v[142:145], v222, v222 op_sel_hi:[0,0,0]
	v_mfma_scale_f32_16x16x128_f8f6f4 v[126:129], v[232:239], v[188:195], v[126:129], v222, v222 op_sel_hi:[0,0,0]
	s_waitcnt lgkmcnt(0)
	v_mfma_scale_f32_16x16x128_f8f6f4 v[170:173], v[240:247], v[22:29], v[170:173], v222, v222 op_sel_hi:[0,0,0]
	v_mfma_scale_f32_16x16x128_f8f6f4 v[154:157], v[240:247], v[30:37], v[154:157], v222, v222 op_sel_hi:[0,0,0]
	v_mfma_scale_f32_16x16x128_f8f6f4 v[138:141], v[240:247], v[38:45], v[138:141], v222, v222 op_sel_hi:[0,0,0]
	v_mfma_scale_f32_16x16x128_f8f6f4 v[122:125], v[240:247], v[188:195], v[122:125], v222, v222 op_sel_hi:[0,0,0]
	s_setprio 0
	s_mov_b32 m0, s75
	v_lshl_add_u64 v[20:21], v[20:21], 0, s[24:25]
	s_barrier
	ds_read_b128 v[22:25], v221 offset:49152
	ds_read_b128 v[26:29], v221 offset:50176
	ds_read_b128 v[30:33], v221 offset:51200
	ds_read_b128 v[34:37], v221 offset:52224
	ds_read_b128 v[38:41], v221 offset:53248
	ds_read_b128 v[42:45], v221 offset:54272
	ds_read_b128 v[188:191], v221 offset:55296
	ds_read_b128 v[192:195], v221 offset:56320
	global_load_lds_dwordx4 v[20:21], off
	v_lshl_add_u64 v[18:19], v[18:19], 0, s[24:25]
	s_mov_b32 m0, s76
	s_nop 0
	global_load_lds_dwordx4 v[18:19], off
	s_barrier
	s_setprio 1
	s_waitcnt lgkmcnt(6)
	v_mfma_scale_f32_16x16x128_f8f6f4 v[102:105], v[2:9], v[22:29], v[102:105], v222, v222 op_sel_hi:[0,0,0]
	v_mfma_scale_f32_16x16x128_f8f6f4 v[98:101], v[10:17], v[22:29], v[98:101], v222, v222 op_sel_hi:[0,0,0]
	s_waitcnt lgkmcnt(4)
	v_mfma_scale_f32_16x16x128_f8f6f4 v[86:89], v[2:9], v[30:37], v[86:89], v222, v222 op_sel_hi:[0,0,0]
	v_mfma_scale_f32_16x16x128_f8f6f4 v[82:85], v[10:17], v[30:37], v[82:85], v222, v222 op_sel_hi:[0,0,0]
	s_waitcnt lgkmcnt(2)
	v_mfma_scale_f32_16x16x128_f8f6f4 v[70:73], v[2:9], v[38:45], v[70:73], v222, v222 op_sel_hi:[0,0,0]
	v_mfma_scale_f32_16x16x128_f8f6f4 v[66:69], v[10:17], v[38:45], v[66:69], v222, v222 op_sel_hi:[0,0,0]
	s_waitcnt lgkmcnt(0)
	v_mfma_scale_f32_16x16x128_f8f6f4 v[54:57], v[2:9], v[188:195], v[54:57], v222, v222 op_sel_hi:[0,0,0]
	v_mfma_scale_f32_16x16x128_f8f6f4 v[50:53], v[10:17], v[188:195], v[50:53], v222, v222 op_sel_hi:[0,0,0]
	s_setprio 0
	s_barrier
	s_add_u32 s8, s8, 0x20080
	s_addc_u32 s9, s9, 0
	s_mov_b32 m0, s77
	v_lshl_add_u64 v[2:3], s[8:9], 0, v[182:183]
	global_load_lds_dwordx4 v[2:3], off
	v_lshl_add_u64 v[2:3], s[8:9], 0, v[180:181]
	s_mov_b32 m0, s78
	s_nop 0
	global_load_lds_dwordx4 v[2:3], off
	s_waitcnt vmcnt(6)
	s_barrier
	s_setprio 1
	v_mfma_scale_f32_16x16x128_f8f6f4 v[110:113], v[232:239], v[22:29], v[110:113], v222, v222 op_sel_hi:[0,0,0]
	v_mfma_scale_f32_16x16x128_f8f6f4 v[106:109], v[240:247], v[22:29], v[106:109], v222, v222 op_sel_hi:[0,0,0]
	v_mfma_scale_f32_16x16x128_f8f6f4 v[94:97], v[232:239], v[30:37], v[94:97], v222, v222 op_sel_hi:[0,0,0]
	v_mfma_scale_f32_16x16x128_f8f6f4 v[90:93], v[240:247], v[30:37], v[90:93], v222, v222 op_sel_hi:[0,0,0]
	v_mfma_scale_f32_16x16x128_f8f6f4 v[78:81], v[232:239], v[38:45], v[78:81], v222, v222 op_sel_hi:[0,0,0]
	v_mfma_scale_f32_16x16x128_f8f6f4 v[74:77], v[240:247], v[38:45], v[74:77], v222, v222 op_sel_hi:[0,0,0]
	v_mfma_scale_f32_16x16x128_f8f6f4 v[62:65], v[232:239], v[188:195], v[62:65], v222, v222 op_sel_hi:[0,0,0]
	v_mfma_scale_f32_16x16x128_f8f6f4 v[58:61], v[240:247], v[188:195], v[58:61], v222, v222 op_sel_hi:[0,0,0]
	s_setprio 0
	s_add_i32 s83, s83, 2
	s_add_u32 s50, s50, 0x100
	s_addc_u32 s51, s51, 0
	s_cmp_gt_u32 s83, 5
	s_barrier
	s_cbranch_scc1 .LBB0_1689

.LBB0_1718:
	s_add_u32 s43, s14, s42
	s_addc_u32 s51, s15, 0
	s_add_u32 s46, s43, 0x100
	s_addc_u32 s47, s51, 0
	s_and_b64 s[44:45], s[40:41], exec
	s_cselect_b32 s47, s9, s47
	s_cselect_b32 s46, s35, s46
	s_add_u32 s42, s12, s42
	s_addc_u32 s44, s13, 0
	s_add_u32 s42, s42, 0x100
	s_addc_u32 s44, s44, 0
	s_and_b64 s[40:41], s[40:41], exec
	s_cselect_b32 s49, s7, s44
	s_cselect_b32 s48, s74, s42
	s_add_u32 s50, s43, 0x10080
	s_addc_u32 s51, s51, 0
	s_add_i32 m0, s55, 0xc000
	s_add_i32 s75, s55, 0xe000
	ds_read_b128 v[156:159], v139
	ds_read_b128 v[160:163], v140
	ds_read_b128 v[164:167], v141
	ds_read_b128 v[168:171], v142
	s_add_u32 s44, s48, 0x10000
	s_addc_u32 s45, s49, 0
	s_add_u32 s42, s46, 0x10000
	s_addc_u32 s43, s47, 0
	s_add_u32 s40, s48, 0x10080
	s_addc_u32 s41, s49, 0
	v_add_u32_e32 v0, s65, v138
	v_lshl_add_u64 v[184:185], s[50:51], 0, v[136:137]
	ds_read_b128 v[172:175], v0
	ds_read_b128 v[176:179], v0 offset:1024
	ds_read_b128 v[180:183], v0 offset:2048
	ds_read_b128 v[188:191], v0 offset:3072
	ds_read_b128 v[192:195], v0 offset:4096
	ds_read_b128 v[196:199], v0 offset:5120
	ds_read_b128 v[200:203], v0 offset:6144
	ds_read_b128 v[204:207], v0 offset:7168
	global_load_lds_dwordx4 v[184:185], off
	v_lshl_add_u64 v[184:185], s[50:51], 0, v[132:133]
	s_mov_b32 m0, s75
	s_nop 0
	global_load_lds_dwordx4 v[184:185], off
	s_waitcnt lgkmcnt(8)
	s_barrier
	s_setprio 1
	s_waitcnt lgkmcnt(7)
	v_mfma_f32_16x16x32_bf16 v[126:129], v[156:159], v[172:175], v[126:129]
	v_mfma_f32_16x16x32_bf16 v[122:125], v[164:167], v[172:175], v[122:125]
	s_waitcnt lgkmcnt(6)
	v_mfma_f32_16x16x32_bf16 v[126:129], v[160:163], v[176:179], v[126:129]
	v_mfma_f32_16x16x32_bf16 v[122:125], v[168:171], v[176:179], v[122:125]
	s_waitcnt lgkmcnt(5)
	v_mfma_f32_16x16x32_bf16 v[118:121], v[156:159], v[180:183], v[118:121]
	v_mfma_f32_16x16x32_bf16 v[114:117], v[164:167], v[180:183], v[114:117]
	s_waitcnt lgkmcnt(4)
	v_mfma_f32_16x16x32_bf16 v[118:121], v[160:163], v[188:191], v[118:121]
	v_mfma_f32_16x16x32_bf16 v[114:117], v[168:171], v[188:191], v[114:117]
	s_waitcnt lgkmcnt(3)
	v_mfma_f32_16x16x32_bf16 v[102:105], v[156:159], v[192:195], v[102:105]
	v_mfma_f32_16x16x32_bf16 v[98:101], v[164:167], v[192:195], v[98:101]
	s_waitcnt lgkmcnt(2)
	v_mfma_f32_16x16x32_bf16 v[102:105], v[160:163], v[196:199], v[102:105]
	v_mfma_f32_16x16x32_bf16 v[98:101], v[168:171], v[196:199], v[98:101]
	s_waitcnt lgkmcnt(1)
	v_mfma_f32_16x16x32_bf16 v[86:89], v[156:159], v[200:203], v[86:89]
	v_mfma_f32_16x16x32_bf16 v[82:85], v[164:167], v[200:203], v[82:85]
	s_waitcnt lgkmcnt(0)
	v_mfma_f32_16x16x32_bf16 v[86:89], v[160:163], v[204:207], v[86:89]
	v_mfma_f32_16x16x32_bf16 v[82:85], v[168:171], v[204:207], v[82:85]
	s_setprio 0
	s_barrier
	s_mov_b32 m0, s56
	v_lshl_add_u64 v[184:185], s[48:49], 0, v[134:135]
	ds_read_b128 v[208:211], v143
	ds_read_b128 v[212:215], v144
	ds_read_b128 v[216:219], v145
	ds_read_b128 v[232:235], v146
	global_load_lds_dwordx4 v[184:185], off
	v_lshl_add_u64 v[220:221], s[48:49], 0, v[130:131]
	s_mov_b32 m0, s57
	s_nop 0
	global_load_lds_dwordx4 v[220:221], off
	s_barrier
	s_setprio 1
	s_waitcnt lgkmcnt(3)
	v_mfma_f32_16x16x32_bf16 v[110:113], v[208:211], v[172:175], v[110:113]
	v_mfma_f32_16x16x32_bf16 v[94:97], v[208:211], v[180:183], v[94:97]
	v_mfma_f32_16x16x32_bf16 v[78:81], v[208:211], v[192:195], v[78:81]
	v_mfma_f32_16x16x32_bf16 v[70:73], v[208:211], v[200:203], v[70:73]
	s_waitcnt lgkmcnt(2)
	v_mfma_f32_16x16x32_bf16 v[110:113], v[212:215], v[176:179], v[110:113]
	v_mfma_f32_16x16x32_bf16 v[94:97], v[212:215], v[188:191], v[94:97]
	v_mfma_f32_16x16x32_bf16 v[78:81], v[212:215], v[196:199], v[78:81]
	v_mfma_f32_16x16x32_bf16 v[70:73], v[212:215], v[204:207], v[70:73]
	s_waitcnt lgkmcnt(1)
	v_mfma_f32_16x16x32_bf16 v[106:109], v[216:219], v[172:175], v[106:109]
	v_mfma_f32_16x16x32_bf16 v[90:93], v[216:219], v[180:183], v[90:93]
	v_mfma_f32_16x16x32_bf16 v[74:77], v[216:219], v[192:195], v[74:77]
	v_mfma_f32_16x16x32_bf16 v[66:69], v[216:219], v[200:203], v[66:69]
	s_waitcnt lgkmcnt(0)
	v_mfma_f32_16x16x32_bf16 v[106:109], v[232:235], v[176:179], v[106:109]
	v_mfma_f32_16x16x32_bf16 v[90:93], v[232:235], v[188:191], v[90:93]
	v_mfma_f32_16x16x32_bf16 v[74:77], v[232:235], v[196:199], v[74:77]
	v_mfma_f32_16x16x32_bf16 v[66:69], v[232:235], v[204:207], v[66:69]
	s_setprio 0
	s_mov_b32 m0, s55
	v_lshl_add_u64 v[226:227], s[46:47], 0, v[136:137]
	s_barrier
	ds_read_b128 v[172:175], v0 offset:16384
	ds_read_b128 v[176:179], v0 offset:17408
	ds_read_b128 v[180:183], v0 offset:18432
	ds_read_b128 v[188:191], v0 offset:19456
	ds_read_b128 v[192:195], v0 offset:20480
	ds_read_b128 v[196:199], v0 offset:21504
	ds_read_b128 v[200:203], v0 offset:22528
	ds_read_b128 v[204:207], v0 offset:23552
	global_load_lds_dwordx4 v[226:227], off
	v_lshl_add_u64 v[236:237], s[46:47], 0, v[132:133]
	s_mov_b32 m0, s58
	s_nop 0
	global_load_lds_dwordx4 v[236:237], off
	s_barrier
	s_setprio 1
	s_waitcnt lgkmcnt(7)
	v_mfma_f32_16x16x32_bf16 v[62:65], v[156:159], v[172:175], v[62:65]
	v_mfma_f32_16x16x32_bf16 v[58:61], v[164:167], v[172:175], v[58:61]
	s_waitcnt lgkmcnt(6)
	v_mfma_f32_16x16x32_bf16 v[62:65], v[160:163], v[176:179], v[62:65]
	v_mfma_f32_16x16x32_bf16 v[58:61], v[168:171], v[176:179], v[58:61]
	s_waitcnt lgkmcnt(5)
	v_mfma_f32_16x16x32_bf16 v[54:57], v[156:159], v[180:183], v[54:57]
	v_mfma_f32_16x16x32_bf16 v[50:53], v[164:167], v[180:183], v[50:53]
	s_waitcnt lgkmcnt(4)
	v_mfma_f32_16x16x32_bf16 v[54:57], v[160:163], v[188:191], v[54:57]
	v_mfma_f32_16x16x32_bf16 v[50:53], v[168:171], v[188:191], v[50:53]
	s_waitcnt lgkmcnt(3)
	v_mfma_f32_16x16x32_bf16 v[38:41], v[156:159], v[192:195], v[38:41]
	v_mfma_f32_16x16x32_bf16 v[34:37], v[164:167], v[192:195], v[34:37]
	s_waitcnt lgkmcnt(2)
	v_mfma_f32_16x16x32_bf16 v[38:41], v[160:163], v[196:199], v[38:41]
	v_mfma_f32_16x16x32_bf16 v[34:37], v[168:171], v[196:199], v[34:37]
	s_waitcnt lgkmcnt(1)
	v_mfma_f32_16x16x32_bf16 v[22:25], v[156:159], v[200:203], v[22:25]
	v_mfma_f32_16x16x32_bf16 v[18:21], v[164:167], v[200:203], v[18:21]
	s_waitcnt lgkmcnt(0)
	v_mfma_f32_16x16x32_bf16 v[22:25], v[160:163], v[204:207], v[22:25]
	v_mfma_f32_16x16x32_bf16 v[18:21], v[168:171], v[204:207], v[18:21]
	s_setprio 0
	s_barrier
	s_mov_b32 m0, s59
	v_lshl_add_u64 v[156:157], s[44:45], 0, v[134:135]
	global_load_lds_dwordx4 v[156:157], off
	v_lshl_add_u64 v[156:157], s[44:45], 0, v[130:131]
	s_mov_b32 m0, s60
	s_nop 0
	global_load_lds_dwordx4 v[156:157], off
	s_waitcnt vmcnt(6)
	s_barrier
	s_setprio 1
	v_mfma_f32_16x16x32_bf16 v[46:49], v[208:211], v[172:175], v[46:49]
	v_mfma_f32_16x16x32_bf16 v[42:45], v[216:219], v[172:175], v[42:45]
	v_mfma_f32_16x16x32_bf16 v[30:33], v[208:211], v[180:183], v[30:33]
	v_mfma_f32_16x16x32_bf16 v[26:29], v[216:219], v[180:183], v[26:29]
	v_mfma_f32_16x16x32_bf16 v[14:17], v[208:211], v[192:195], v[14:17]
	v_mfma_f32_16x16x32_bf16 v[10:13], v[216:219], v[192:195], v[10:13]
	v_mfma_f32_16x16x32_bf16 v[6:9], v[208:211], v[200:203], v[6:9]
	v_mfma_f32_16x16x32_bf16 v[2:5], v[216:219], v[200:203], v[2:5]
	v_mfma_f32_16x16x32_bf16 v[46:49], v[212:215], v[176:179], v[46:49]
	v_mfma_f32_16x16x32_bf16 v[42:45], v[232:235], v[176:179], v[42:45]
	v_mfma_f32_16x16x32_bf16 v[30:33], v[212:215], v[188:191], v[30:33]
	v_mfma_f32_16x16x32_bf16 v[26:29], v[232:235], v[188:191], v[26:29]
	v_mfma_f32_16x16x32_bf16 v[14:17], v[212:215], v[196:199], v[14:17]
	v_mfma_f32_16x16x32_bf16 v[10:13], v[232:235], v[196:199], v[10:13]
	v_mfma_f32_16x16x32_bf16 v[6:9], v[212:215], v[204:207], v[6:9]
	v_mfma_f32_16x16x32_bf16 v[2:5], v[232:235], v[204:207], v[2:5]
	s_setprio 0
	s_barrier
	ds_read_b128 v[156:159], v147
	ds_read_b128 v[160:163], v148
	ds_read_b128 v[164:167], v149
	ds_read_b128 v[168:171], v150
	s_mov_b32 m0, s61
	v_lshl_add_u64 v[208:209], s[42:43], 0, v[136:137]
	ds_read_b128 v[172:175], v0 offset:32768
	ds_read_b128 v[176:179], v0 offset:33792
	ds_read_b128 v[180:183], v0 offset:34816
	ds_read_b128 v[188:191], v0 offset:35840
	ds_read_b128 v[192:195], v0 offset:36864
	ds_read_b128 v[196:199], v0 offset:37888
	ds_read_b128 v[200:203], v0 offset:38912
	ds_read_b128 v[204:207], v0 offset:39936
	global_load_lds_dwordx4 v[208:209], off
	v_lshl_add_u64 v[208:209], s[42:43], 0, v[132:133]
	s_mov_b32 m0, s62
	s_nop 0
	global_load_lds_dwordx4 v[208:209], off
	s_waitcnt lgkmcnt(8)
	s_barrier
	s_setprio 1
	s_waitcnt lgkmcnt(7)
	v_mfma_f32_16x16x32_bf16 v[126:129], v[156:159], v[172:175], v[126:129]
	v_mfma_f32_16x16x32_bf16 v[122:125], v[164:167], v[172:175], v[122:125]
	s_waitcnt lgkmcnt(6)
	v_mfma_f32_16x16x32_bf16 v[126:129], v[160:163], v[176:179], v[126:129]
	v_mfma_f32_16x16x32_bf16 v[122:125], v[168:171], v[176:179], v[122:125]
	s_waitcnt lgkmcnt(5)
	v_mfma_f32_16x16x32_bf16 v[118:121], v[156:159], v[180:183], v[118:121]
	v_mfma_f32_16x16x32_bf16 v[114:117], v[164:167], v[180:183], v[114:117]
	s_waitcnt lgkmcnt(4)
	v_mfma_f32_16x16x32_bf16 v[118:121], v[160:163], v[188:191], v[118:121]
	v_mfma_f32_16x16x32_bf16 v[114:117], v[168:171], v[188:191], v[114:117]
	s_waitcnt lgkmcnt(3)
	v_mfma_f32_16x16x32_bf16 v[102:105], v[156:159], v[192:195], v[102:105]
	v_mfma_f32_16x16x32_bf16 v[98:101], v[164:167], v[192:195], v[98:101]
	s_waitcnt lgkmcnt(2)
	v_mfma_f32_16x16x32_bf16 v[102:105], v[160:163], v[196:199], v[102:105]
	v_mfma_f32_16x16x32_bf16 v[98:101], v[168:171], v[196:199], v[98:101]
	s_waitcnt lgkmcnt(1)
	v_mfma_f32_16x16x32_bf16 v[86:89], v[156:159], v[200:203], v[86:89]
	v_mfma_f32_16x16x32_bf16 v[82:85], v[164:167], v[200:203], v[82:85]
	s_waitcnt lgkmcnt(0)
	v_mfma_f32_16x16x32_bf16 v[86:89], v[160:163], v[204:207], v[86:89]
	v_mfma_f32_16x16x32_bf16 v[82:85], v[168:171], v[204:207], v[82:85]
	s_setprio 0
	s_barrier
	s_mov_b32 m0, s66
	v_lshl_add_u64 v[184:185], v[184:185], 0, s[24:25]
	ds_read_b128 v[208:211], v151
	ds_read_b128 v[212:215], v152
	ds_read_b128 v[216:219], v153
	ds_read_b128 v[232:235], v154
	global_load_lds_dwordx4 v[184:185], off
	v_lshl_add_u64 v[184:185], v[220:221], 0, s[24:25]
	s_mov_b32 m0, s67
	s_nop 0
	global_load_lds_dwordx4 v[184:185], off
	s_barrier
	s_setprio 1
	s_waitcnt lgkmcnt(3)
	v_mfma_f32_16x16x32_bf16 v[110:113], v[208:211], v[172:175], v[110:113]
	v_mfma_f32_16x16x32_bf16 v[94:97], v[208:211], v[180:183], v[94:97]
	v_mfma_f32_16x16x32_bf16 v[78:81], v[208:211], v[192:195], v[78:81]
	v_mfma_f32_16x16x32_bf16 v[70:73], v[208:211], v[200:203], v[70:73]
	s_waitcnt lgkmcnt(2)
	v_mfma_f32_16x16x32_bf16 v[110:113], v[212:215], v[176:179], v[110:113]
	v_mfma_f32_16x16x32_bf16 v[94:97], v[212:215], v[188:191], v[94:97]
	v_mfma_f32_16x16x32_bf16 v[78:81], v[212:215], v[196:199], v[78:81]
	v_mfma_f32_16x16x32_bf16 v[70:73], v[212:215], v[204:207], v[70:73]
	s_waitcnt lgkmcnt(1)
	v_mfma_f32_16x16x32_bf16 v[106:109], v[216:219], v[172:175], v[106:109]
	v_mfma_f32_16x16x32_bf16 v[90:93], v[216:219], v[180:183], v[90:93]
	v_mfma_f32_16x16x32_bf16 v[74:77], v[216:219], v[192:195], v[74:77]
	v_mfma_f32_16x16x32_bf16 v[66:69], v[216:219], v[200:203], v[66:69]
	s_waitcnt lgkmcnt(0)
	v_mfma_f32_16x16x32_bf16 v[106:109], v[232:235], v[176:179], v[106:109]
	v_mfma_f32_16x16x32_bf16 v[90:93], v[232:235], v[188:191], v[90:93]
	v_mfma_f32_16x16x32_bf16 v[74:77], v[232:235], v[196:199], v[74:77]
	v_mfma_f32_16x16x32_bf16 v[66:69], v[232:235], v[204:207], v[66:69]
	s_setprio 0
	s_mov_b32 m0, s68
	v_lshl_add_u64 v[184:185], v[226:227], 0, s[24:25]
	s_barrier
	ds_read_b128 v[172:175], v0 offset:49152
	ds_read_b128 v[176:179], v0 offset:50176
	ds_read_b128 v[180:183], v0 offset:51200
	ds_read_b128 v[188:191], v0 offset:52224
	ds_read_b128 v[192:195], v0 offset:53248
	ds_read_b128 v[196:199], v0 offset:54272
	ds_read_b128 v[200:203], v0 offset:55296
	ds_read_b128 v[204:207], v0 offset:56320
	global_load_lds_dwordx4 v[184:185], off
	v_lshl_add_u64 v[184:185], v[236:237], 0, s[24:25]
	s_mov_b32 m0, s69
	s_nop 0
	global_load_lds_dwordx4 v[184:185], off
	s_barrier
	s_setprio 1
	s_waitcnt lgkmcnt(7)
	v_mfma_f32_16x16x32_bf16 v[62:65], v[156:159], v[172:175], v[62:65]
	v_mfma_f32_16x16x32_bf16 v[58:61], v[164:167], v[172:175], v[58:61]
	s_waitcnt lgkmcnt(6)
	v_mfma_f32_16x16x32_bf16 v[62:65], v[160:163], v[176:179], v[62:65]
	v_mfma_f32_16x16x32_bf16 v[58:61], v[168:171], v[176:179], v[58:61]
	s_waitcnt lgkmcnt(5)
	v_mfma_f32_16x16x32_bf16 v[54:57], v[156:159], v[180:183], v[54:57]
	v_mfma_f32_16x16x32_bf16 v[50:53], v[164:167], v[180:183], v[50:53]
	s_waitcnt lgkmcnt(4)
	v_mfma_f32_16x16x32_bf16 v[54:57], v[160:163], v[188:191], v[54:57]
	v_mfma_f32_16x16x32_bf16 v[50:53], v[168:171], v[188:191], v[50:53]
	s_waitcnt lgkmcnt(3)
	v_mfma_f32_16x16x32_bf16 v[38:41], v[156:159], v[192:195], v[38:41]
	v_mfma_f32_16x16x32_bf16 v[34:37], v[164:167], v[192:195], v[34:37]
	s_waitcnt lgkmcnt(2)
	v_mfma_f32_16x16x32_bf16 v[38:41], v[160:163], v[196:199], v[38:41]
	v_mfma_f32_16x16x32_bf16 v[34:37], v[168:171], v[196:199], v[34:37]
	s_waitcnt lgkmcnt(1)
	v_mfma_f32_16x16x32_bf16 v[22:25], v[156:159], v[200:203], v[22:25]
	v_mfma_f32_16x16x32_bf16 v[18:21], v[164:167], v[200:203], v[18:21]
	s_waitcnt lgkmcnt(0)
	v_mfma_f32_16x16x32_bf16 v[22:25], v[160:163], v[204:207], v[22:25]
	v_mfma_f32_16x16x32_bf16 v[18:21], v[168:171], v[204:207], v[18:21]
	s_setprio 0
	s_barrier
	s_mov_b32 m0, s70
	v_lshl_add_u64 v[156:157], s[40:41], 0, v[134:135]
	global_load_lds_dwordx4 v[156:157], off
	v_lshl_add_u64 v[156:157], s[40:41], 0, v[130:131]
	s_mov_b32 m0, s71
	s_nop 0
	global_load_lds_dwordx4 v[156:157], off
	s_waitcnt vmcnt(6)
	s_barrier
	s_setprio 1
	v_mfma_f32_16x16x32_bf16 v[46:49], v[208:211], v[172:175], v[46:49]
	v_mfma_f32_16x16x32_bf16 v[42:45], v[216:219], v[172:175], v[42:45]
	v_mfma_f32_16x16x32_bf16 v[30:33], v[208:211], v[180:183], v[30:33]
	v_mfma_f32_16x16x32_bf16 v[26:29], v[216:219], v[180:183], v[26:29]
	v_mfma_f32_16x16x32_bf16 v[14:17], v[208:211], v[192:195], v[14:17]
	v_mfma_f32_16x16x32_bf16 v[10:13], v[216:219], v[192:195], v[10:13]
	v_mfma_f32_16x16x32_bf16 v[6:9], v[208:211], v[200:203], v[6:9]
	v_mfma_f32_16x16x32_bf16 v[2:5], v[216:219], v[200:203], v[2:5]
	v_mfma_f32_16x16x32_bf16 v[46:49], v[212:215], v[176:179], v[46:49]
	v_mfma_f32_16x16x32_bf16 v[42:45], v[232:235], v[176:179], v[42:45]
	v_mfma_f32_16x16x32_bf16 v[30:33], v[212:215], v[188:191], v[30:33]
	v_mfma_f32_16x16x32_bf16 v[26:29], v[232:235], v[188:191], v[26:29]
	v_mfma_f32_16x16x32_bf16 v[14:17], v[212:215], v[196:199], v[14:17]
	v_mfma_f32_16x16x32_bf16 v[10:13], v[232:235], v[196:199], v[10:13]
	v_mfma_f32_16x16x32_bf16 v[6:9], v[212:215], v[204:207], v[6:9]
	v_mfma_f32_16x16x32_bf16 v[2:5], v[232:235], v[204:207], v[2:5]
	s_setprio 0
	s_movk_i32 s42, 0x100
	s_andn2_b64 vcc, exec, s[38:39]
	s_mov_b64 s[40:41], -1
	s_mov_b64 s[38:39], 0
	s_barrier
	s_cbranch_vccz .LBB0_1718
	v_readlane_b32 s7, v252, 52
	v_readlane_b32 s9, v252, 51
	v_mbcnt_lo_u32_b32 v0, -1, 0
	v_mbcnt_hi_u32_b32 v0, -1, v0
	s_lshl_b32 s38, s7, 5
	v_and_b32_e32 v155, 15, v0
	s_ashr_i32 s35, s34, 31
	v_lshl_or_b32 v156, s9, 6, v155
	s_ashr_i32 s39, s38, 31
	s_lshl_b64 s[12:13], s[34:35], 19
	s_add_u32 s12, s63, s12
	v_cvt_pk_bf16_f32 v70, v70, v71
	v_cvt_pk_bf16_f32 v71, v72, v73
	v_cvt_pk_bf16_f32 v72, v66, v67
	v_add_u32_e32 v66, 0x80, v156
	v_ashrrev_i32_e32 v157, 31, v156
	s_addc_u32 s13, s64, s13
	s_lshl_b32 s14, s73, 8
	v_cvt_pk_bf16_f32 v110, v110, v111
	v_cvt_pk_bf16_f32 v111, v112, v113
	v_cvt_pk_bf16_f32 v112, v106, v107
	v_or_b32_e32 v106, 16, v156
	v_ashrrev_i32_e32 v67, 31, v66
	v_cvt_pk_bf16_f32 v46, v46, v47
	v_cvt_pk_bf16_f32 v47, v48, v49
	v_cvt_pk_bf16_f32 v48, v42, v43
	v_add_u32_e32 v42, 0x90, v156
	v_lshlrev_b64 v[158:159], 11, v[156:157]
	s_ashr_i32 s15, s14, 31
	v_ashrrev_i32_e32 v107, 31, v106
	v_cvt_pk_bf16_f32 v94, v94, v95
	v_cvt_pk_bf16_f32 v95, v96, v97
	v_cvt_pk_bf16_f32 v96, v90, v91
	v_or_b32_e32 v90, 32, v156
	v_lshlrev_b64 v[66:67], 11, v[66:67]
	v_ashrrev_i32_e32 v43, 31, v42
	v_cvt_pk_bf16_f32 v30, v30, v31
	v_cvt_pk_bf16_f32 v31, v32, v33
	v_cvt_pk_bf16_f32 v32, v26, v27
	v_add_u32_e32 v26, 0xa0, v156
	v_lshl_add_u64 v[158:159], s[12:13], 0, v[158:159]
	s_lshl_b64 s[14:15], s[14:15], 1
	v_lshlrev_b64 v[106:107], 11, v[106:107]
	v_ashrrev_i32_e32 v91, 31, v90
	v_cvt_pk_bf16_f32 v78, v78, v79
	v_cvt_pk_bf16_f32 v79, v80, v81
	v_cvt_pk_bf16_f32 v80, v74, v75
	v_or_b32_e32 v74, 48, v156
	v_lshl_add_u64 v[66:67], s[12:13], 0, v[66:67]
	v_lshlrev_b64 v[42:43], 11, v[42:43]
	v_ashrrev_i32_e32 v27, 31, v26
	v_cvt_pk_bf16_f32 v14, v14, v15
	v_cvt_pk_bf16_f32 v15, v16, v17
	v_cvt_pk_bf16_f32 v16, v10, v11
	v_add_u32_e32 v10, 0xb0, v156
	v_lshl_add_u64 v[158:159], v[158:159], 0, s[14:15]
	s_lshl_b64 s[34:35], s[38:39], 1
	v_lshl_add_u64 v[106:107], s[12:13], 0, v[106:107]
	v_lshlrev_b64 v[90:91], 11, v[90:91]
	v_ashrrev_i32_e32 v75, 31, v74
	v_lshl_add_u64 v[66:67], v[66:67], 0, s[14:15]
	v_lshl_add_u64 v[42:43], s[12:13], 0, v[42:43]
	v_lshlrev_b64 v[26:27], 11, v[26:27]
	v_ashrrev_i32_e32 v11, 31, v10
	v_lshl_add_u64 v[158:159], v[158:159], 0, s[34:35]
	v_and_b32_e32 v0, 48, v0
	v_lshl_add_u64 v[106:107], v[106:107], 0, s[14:15]
	v_lshl_add_u64 v[90:91], s[12:13], 0, v[90:91]
	v_lshlrev_b64 v[74:75], 11, v[74:75]
	v_lshl_add_u64 v[66:67], v[66:67], 0, s[34:35]
	v_lshl_add_u64 v[42:43], v[42:43], 0, s[14:15]
	v_lshl_add_u64 v[26:27], s[12:13], 0, v[26:27]
	v_lshlrev_b64 v[10:11], 11, v[10:11]
	v_lshl_add_u64 v[158:159], v[158:159], 0, v[0:1]
	v_cvt_pk_bf16_f32 v113, v108, v109
	v_lshl_add_u64 v[106:107], v[106:107], 0, s[34:35]
	v_lshl_add_u64 v[90:91], v[90:91], 0, s[14:15]
	v_lshl_add_u64 v[74:75], s[12:13], 0, v[74:75]
	v_lshl_add_u64 v[66:67], v[66:67], 0, v[0:1]
	v_cvt_pk_bf16_f32 v49, v44, v45
	v_lshl_add_u64 v[42:43], v[42:43], 0, s[34:35]
	v_lshl_add_u64 v[26:27], v[26:27], 0, s[14:15]
	v_lshl_add_u64 v[10:11], s[12:13], 0, v[10:11]
	global_store_dwordx4 v[158:159], v[110:113], off offset:256
	v_cvt_pk_bf16_f32 v97, v92, v93
	v_lshl_add_u64 v[90:91], v[90:91], 0, s[34:35]
	v_lshl_add_u64 v[110:111], v[106:107], 0, v[0:1]
	v_lshl_add_u64 v[74:75], v[74:75], 0, s[14:15]
	global_store_dwordx4 v[66:67], v[46:49], off offset:256
	v_cvt_pk_bf16_f32 v33, v28, v29
	v_lshl_add_u64 v[26:27], v[26:27], 0, s[34:35]
	v_lshl_add_u64 v[46:47], v[42:43], 0, v[0:1]
	v_lshl_add_u64 v[10:11], v[10:11], 0, s[14:15]
	global_store_dwordx4 v[110:111], v[94:97], off offset:256
	v_cvt_pk_bf16_f32 v81, v76, v77
	v_lshl_add_u64 v[74:75], v[74:75], 0, s[34:35]
	v_lshl_add_u64 v[94:95], v[90:91], 0, v[0:1]
	global_store_dwordx4 v[46:47], v[30:33], off offset:256
	v_cvt_pk_bf16_f32 v17, v12, v13
	v_lshl_add_u64 v[10:11], v[10:11], 0, s[34:35]
	v_lshl_add_u64 v[30:31], v[26:27], 0, v[0:1]
	v_cvt_pk_bf16_f32 v126, v126, v127
	v_cvt_pk_bf16_f32 v127, v128, v129
	v_cvt_pk_bf16_f32 v128, v122, v123
	v_cvt_pk_bf16_f32 v129, v124, v125
	v_cvt_pk_bf16_f32 v106, v118, v119
	v_cvt_pk_bf16_f32 v107, v120, v121
	v_cvt_pk_bf16_f32 v108, v114, v115
	v_cvt_pk_bf16_f32 v109, v116, v117
	v_cvt_pk_bf16_f32 v90, v102, v103
	v_cvt_pk_bf16_f32 v91, v104, v105
	v_cvt_pk_bf16_f32 v92, v98, v99
	v_cvt_pk_bf16_f32 v93, v100, v101
	global_store_dwordx4 v[94:95], v[78:81], off offset:256
	v_cvt_pk_bf16_f32 v76, v82, v83
	v_cvt_pk_bf16_f32 v77, v84, v85
	v_lshl_add_u64 v[78:79], v[74:75], 0, v[0:1]
	v_cvt_pk_bf16_f32 v74, v86, v87
	v_cvt_pk_bf16_f32 v75, v88, v89
	v_cvt_pk_bf16_f32 v73, v68, v69
	v_cvt_pk_bf16_f32 v62, v62, v63
	v_cvt_pk_bf16_f32 v63, v64, v65
	v_cvt_pk_bf16_f32 v64, v58, v59
	v_cvt_pk_bf16_f32 v65, v60, v61
	v_cvt_pk_bf16_f32 v42, v54, v55
	v_cvt_pk_bf16_f32 v43, v56, v57
	v_cvt_pk_bf16_f32 v44, v50, v51
	v_cvt_pk_bf16_f32 v45, v52, v53
	v_cvt_pk_bf16_f32 v26, v38, v39
	v_cvt_pk_bf16_f32 v27, v40, v41
	v_cvt_pk_bf16_f32 v28, v34, v35
	v_cvt_pk_bf16_f32 v29, v36, v37
	global_store_dwordx4 v[30:31], v[14:17], off offset:256
	v_cvt_pk_bf16_f32 v12, v18, v19
	v_cvt_pk_bf16_f32 v13, v20, v21
	v_lshl_add_u64 v[14:15], v[10:11], 0, v[0:1]
	v_cvt_pk_bf16_f32 v10, v22, v23
	v_cvt_pk_bf16_f32 v11, v24, v25
	v_cvt_pk_bf16_f32 v6, v6, v7
	v_cvt_pk_bf16_f32 v7, v8, v9
	v_cvt_pk_bf16_f32 v8, v2, v3
	v_cvt_pk_bf16_f32 v9, v4, v5
	s_and_b64 vcc, exec, s[4:5]
	s_mov_b32 s73, s6
	s_mov_b32 s34, s8
	s_mov_b64 s[12:13], s[20:21]
	s_mov_b64 s[14:15], s[10:11]
	global_store_dwordx4 v[158:159], v[126:129], off
	global_store_dwordx4 v[110:111], v[106:109], off
	global_store_dwordx4 v[94:95], v[90:93], off
	global_store_dwordx4 v[78:79], v[74:77], off
	global_store_dwordx4 v[78:79], v[70:73], off offset:256
	global_store_dwordx4 v[66:67], v[62:65], off
	global_store_dwordx4 v[46:47], v[42:45], off
	global_store_dwordx4 v[30:31], v[26:29], off
	global_store_dwordx4 v[14:15], v[10:13], off
	global_store_dwordx4 v[14:15], v[6:9], off offset:256
	s_cbranch_vccz .LBB0_1711
	s_waitcnt vmcnt(0)
	s_cmpk_gt_u32 s27, 0xff
	s_cbranch_scc1 .LBB0_1722
	s_barrier

.LBB0_1791:
	s_ashr_i32 s21, s20, 31
	ds_read_b128 v[2:5], v165
	ds_read_b128 v[6:9], v166
	ds_read_b128 v[10:13], v167
	ds_read_b128 v[14:17], v168
	s_lshl_b64 s[34:35], s[20:21], 18
	s_add_u32 s34, s51, s34
	s_addc_u32 s35, s52, s35
	s_and_b64 s[6:7], s[6:7], exec
	s_cselect_b32 s15, s35, s45
	s_cselect_b32 s21, s34, s44
	s_lshl_b32 s40, s40, 8
	s_ashr_i32 s41, s40, 31
	s_add_u32 s6, s44, 0x20080
	s_addc_u32 s7, s45, 0
	s_add_i32 s39, s55, 0xc000
	v_add_u32_e32 v181, s66, v164
	v_lshl_add_u64 v[42:43], s[6:7], 0, v[146:147]
	s_mov_b32 m0, s39
	s_add_i32 s74, s55, 0xe000
	ds_read_b128 v[18:21], v181
	ds_read_b128 v[22:25], v181 offset:1024
	ds_read_b128 v[26:29], v181 offset:2048
	ds_read_b128 v[30:33], v181 offset:3072
	ds_read_b128 v[34:37], v181 offset:4096
	ds_read_b128 v[38:41], v181 offset:5120
	ds_read_b128 v[50:53], v181 offset:6144
	ds_read_b128 v[54:57], v181 offset:7168
	global_load_lds_dwordx4 v[42:43], off
	v_lshl_add_u64 v[42:43], s[6:7], 0, v[148:149]
	s_mov_b32 m0, s74
	s_nop 0
	global_load_lds_dwordx4 v[42:43], off
	s_waitcnt lgkmcnt(8)
	s_barrier
	s_waitcnt lgkmcnt(0)
	s_setprio 1
	s_waitcnt lgkmcnt(0)
	v_mfma_scale_f32_16x16x128_f8f6f4 v[142:145], v[2:9], v[18:25], 0, v222, v222 op_sel_hi:[0,0,0]
	v_mfma_scale_f32_16x16x128_f8f6f4 v[138:141], v[10:17], v[18:25], 0, v222, v222 op_sel_hi:[0,0,0]
	v_mfma_scale_f32_16x16x128_f8f6f4 v[134:137], v[2:9], v[26:33], 0, v222, v222 op_sel_hi:[0,0,0]
	v_mfma_scale_f32_16x16x128_f8f6f4 v[130:133], v[10:17], v[26:33], 0, v222, v222 op_sel_hi:[0,0,0]
	v_mfma_scale_f32_16x16x128_f8f6f4 v[122:125], v[2:9], v[34:41], 0, v222, v222 op_sel_hi:[0,0,0]
	v_mfma_scale_f32_16x16x128_f8f6f4 v[114:117], v[10:17], v[34:41], 0, v222, v222 op_sel_hi:[0,0,0]
	v_mfma_scale_f32_16x16x128_f8f6f4 v[106:109], v[2:9], v[50:57], 0, v222, v222 op_sel_hi:[0,0,0]
	v_mfma_scale_f32_16x16x128_f8f6f4 v[98:101], v[10:17], v[50:57], 0, v222, v222 op_sel_hi:[0,0,0]
	s_setprio 0
	s_barrier
	v_lshl_add_u64 v[160:161], s[42:43], 0, v[0:1]
	s_mov_b64 s[6:7], 0x100
	s_mov_b32 m0, s56
	v_lshl_add_u64 v[42:43], v[160:161], 0, s[6:7]
	v_lshl_add_u64 v[162:163], s[42:43], 0, v[150:151]
	ds_read_b128 v[188:191], v169
	ds_read_b128 v[192:195], v170
	ds_read_b128 v[196:199], v171
	ds_read_b128 v[200:203], v172
	global_load_lds_dwordx4 v[42:43], off
	v_lshl_add_u64 v[42:43], v[162:163], 0, s[6:7]
	s_mov_b32 m0, s57
	s_nop 0
	global_load_lds_dwordx4 v[42:43], off
	s_barrier
	s_setprio 1
	s_waitcnt lgkmcnt(2)
	v_mfma_scale_f32_16x16x128_f8f6f4 v[78:81], v[188:195], v[18:25], 0, v222, v222 op_sel_hi:[0,0,0]
	v_mfma_scale_f32_16x16x128_f8f6f4 v[70:73], v[188:195], v[26:33], 0, v222, v222 op_sel_hi:[0,0,0]
	v_mfma_scale_f32_16x16x128_f8f6f4 v[62:65], v[188:195], v[34:41], 0, v222, v222 op_sel_hi:[0,0,0]
	v_mfma_scale_f32_16x16x128_f8f6f4 v[46:49], v[188:195], v[50:57], 0, v222, v222 op_sel_hi:[0,0,0]
	s_waitcnt lgkmcnt(0)
	v_mfma_scale_f32_16x16x128_f8f6f4 v[74:77], v[196:203], v[18:25], 0, v222, v222 op_sel_hi:[0,0,0]
	v_mfma_scale_f32_16x16x128_f8f6f4 v[66:69], v[196:203], v[26:33], 0, v222, v222 op_sel_hi:[0,0,0]
	v_mfma_scale_f32_16x16x128_f8f6f4 v[58:61], v[196:203], v[34:41], 0, v222, v222 op_sel_hi:[0,0,0]
	v_mfma_scale_f32_16x16x128_f8f6f4 v[42:45], v[196:203], v[50:57], 0, v222, v222 op_sel_hi:[0,0,0]
	s_setprio 0
	v_lshl_add_u64 v[156:157], s[44:45], 0, v[146:147]
	s_mov_b32 m0, s55
	v_lshl_add_u64 v[34:35], v[156:157], 0, s[6:7]
	v_lshl_add_u64 v[158:159], s[44:45], 0, v[148:149]
	s_barrier
	ds_read_b128 v[18:21], v181 offset:16384
	ds_read_b128 v[22:25], v181 offset:17408
	ds_read_b128 v[26:29], v181 offset:18432
	ds_read_b128 v[30:33], v181 offset:19456
	ds_read_b128 v[204:207], v181 offset:20480
	ds_read_b128 v[208:211], v181 offset:21504
	ds_read_b128 v[212:215], v181 offset:22528
	ds_read_b128 v[216:219], v181 offset:23552
	global_load_lds_dwordx4 v[34:35], off
	v_lshl_add_u64 v[34:35], v[158:159], 0, s[6:7]
	s_mov_b32 m0, s58
	s_nop 0
	global_load_lds_dwordx4 v[34:35], off
	s_barrier
	s_setprio 1
	s_waitcnt lgkmcnt(6)
	v_mfma_scale_f32_16x16x128_f8f6f4 v[126:129], v[2:9], v[18:25], 0, v222, v222 op_sel_hi:[0,0,0]
	v_mfma_scale_f32_16x16x128_f8f6f4 v[118:121], v[10:17], v[18:25], 0, v222, v222 op_sel_hi:[0,0,0]
	s_waitcnt lgkmcnt(4)
	v_mfma_scale_f32_16x16x128_f8f6f4 v[110:113], v[2:9], v[26:33], 0, v222, v222 op_sel_hi:[0,0,0]
	v_mfma_scale_f32_16x16x128_f8f6f4 v[102:105], v[10:17], v[26:33], 0, v222, v222 op_sel_hi:[0,0,0]
	s_waitcnt lgkmcnt(2)
	v_mfma_scale_f32_16x16x128_f8f6f4 v[94:97], v[2:9], v[204:211], 0, v222, v222 op_sel_hi:[0,0,0]
	v_mfma_scale_f32_16x16x128_f8f6f4 v[90:93], v[10:17], v[204:211], 0, v222, v222 op_sel_hi:[0,0,0]
	s_waitcnt lgkmcnt(0)
	v_mfma_scale_f32_16x16x128_f8f6f4 v[86:89], v[2:9], v[212:219], 0, v222, v222 op_sel_hi:[0,0,0]
	v_mfma_scale_f32_16x16x128_f8f6f4 v[82:85], v[10:17], v[212:219], 0, v222, v222 op_sel_hi:[0,0,0]
	s_setprio 0
	s_barrier
	s_add_u32 s6, s42, 0x20100
	s_addc_u32 s7, s43, 0
	s_mov_b32 m0, s59
	v_lshl_add_u64 v[2:3], s[6:7], 0, v[0:1]
	global_load_lds_dwordx4 v[2:3], off
	v_lshl_add_u64 v[2:3], s[6:7], 0, v[150:151]
	s_mov_b32 m0, s60
	s_nop 0
	global_load_lds_dwordx4 v[2:3], off
	s_waitcnt vmcnt(6)
	s_barrier
	s_setprio 1
	v_mfma_scale_f32_16x16x128_f8f6f4 v[54:57], v[188:195], v[18:25], 0, v222, v222 op_sel_hi:[0,0,0]
	v_mfma_scale_f32_16x16x128_f8f6f4 v[50:53], v[196:203], v[18:25], 0, v222, v222 op_sel_hi:[0,0,0]
	v_mfma_scale_f32_16x16x128_f8f6f4 v[38:41], v[188:195], v[26:33], 0, v222, v222 op_sel_hi:[0,0,0]
	v_mfma_scale_f32_16x16x128_f8f6f4 v[34:37], v[196:203], v[26:33], 0, v222, v222 op_sel_hi:[0,0,0]
	v_mfma_scale_f32_16x16x128_f8f6f4 v[30:33], v[188:195], v[204:211], 0, v222, v222 op_sel_hi:[0,0,0]
	v_mfma_scale_f32_16x16x128_f8f6f4 v[26:29], v[196:203], v[204:211], 0, v222, v222 op_sel_hi:[0,0,0]
	v_mfma_scale_f32_16x16x128_f8f6f4 v[22:25], v[188:195], v[212:219], 0, v222, v222 op_sel_hi:[0,0,0]
	v_mfma_scale_f32_16x16x128_f8f6f4 v[18:21], v[196:203], v[212:219], 0, v222, v222 op_sel_hi:[0,0,0]
	s_setprio 0
	s_barrier
	ds_read_b128 v[2:5], v173
	ds_read_b128 v[6:9], v174
	ds_read_b128 v[10:13], v175
	ds_read_b128 v[14:17], v176
	s_add_u32 s6, s44, 0x20100
	s_addc_u32 s7, s45, 0
	s_mov_b32 m0, s61
	v_lshl_add_u64 v[182:183], s[6:7], 0, v[146:147]
	ds_read_b128 v[188:191], v181 offset:32768
	ds_read_b128 v[192:195], v181 offset:33792
	ds_read_b128 v[196:199], v181 offset:34816
	ds_read_b128 v[200:203], v181 offset:35840
	ds_read_b128 v[204:207], v181 offset:36864
	ds_read_b128 v[208:211], v181 offset:37888
	ds_read_b128 v[212:215], v181 offset:38912
	ds_read_b128 v[216:219], v181 offset:39936
	global_load_lds_dwordx4 v[182:183], off
	v_lshl_add_u64 v[182:183], s[6:7], 0, v[148:149]
	s_mov_b32 m0, s62
	s_nop 0
	global_load_lds_dwordx4 v[182:183], off
	s_waitcnt lgkmcnt(8)
	s_barrier
	s_setprio 1
	s_waitcnt lgkmcnt(6)
	v_mfma_scale_f32_16x16x128_f8f6f4 v[142:145], v[2:9], v[188:195], v[142:145], v222, v222 op_sel_hi:[0,0,0]
	v_mfma_scale_f32_16x16x128_f8f6f4 v[138:141], v[10:17], v[188:195], v[138:141], v222, v222 op_sel_hi:[0,0,0]
	s_waitcnt lgkmcnt(4)
	v_mfma_scale_f32_16x16x128_f8f6f4 v[134:137], v[2:9], v[196:203], v[134:137], v222, v222 op_sel_hi:[0,0,0]
	v_mfma_scale_f32_16x16x128_f8f6f4 v[130:133], v[10:17], v[196:203], v[130:133], v222, v222 op_sel_hi:[0,0,0]
	s_waitcnt lgkmcnt(2)
	v_mfma_scale_f32_16x16x128_f8f6f4 v[122:125], v[2:9], v[204:211], v[122:125], v222, v222 op_sel_hi:[0,0,0]
	v_mfma_scale_f32_16x16x128_f8f6f4 v[114:117], v[10:17], v[204:211], v[114:117], v222, v222 op_sel_hi:[0,0,0]
	s_waitcnt lgkmcnt(0)
	v_mfma_scale_f32_16x16x128_f8f6f4 v[106:109], v[2:9], v[212:219], v[106:109], v222, v222 op_sel_hi:[0,0,0]
	v_mfma_scale_f32_16x16x128_f8f6f4 v[98:101], v[10:17], v[212:219], v[98:101], v222, v222 op_sel_hi:[0,0,0]
	s_setprio 0
	s_barrier
	s_mov_b64 s[6:7], 0x180
	s_mov_b32 m0, s67
	v_lshl_add_u64 v[160:161], v[160:161], 0, s[6:7]
	ds_read_b128 v[232:235], v177
	ds_read_b128 v[236:239], v178
	ds_read_b128 v[240:243], v179
	ds_read_b128 v[244:247], v180
	global_load_lds_dwordx4 v[160:161], off
	v_lshl_add_u64 v[160:161], v[162:163], 0, s[6:7]
	s_mov_b32 m0, s68
	s_nop 0
	global_load_lds_dwordx4 v[160:161], off
	s_barrier
	s_setprio 1
	s_waitcnt lgkmcnt(2)
	v_mfma_scale_f32_16x16x128_f8f6f4 v[78:81], v[232:239], v[188:195], v[78:81], v222, v222 op_sel_hi:[0,0,0]
	v_mfma_scale_f32_16x16x128_f8f6f4 v[70:73], v[232:239], v[196:203], v[70:73], v222, v222 op_sel_hi:[0,0,0]
	v_mfma_scale_f32_16x16x128_f8f6f4 v[62:65], v[232:239], v[204:211], v[62:65], v222, v222 op_sel_hi:[0,0,0]
	v_mfma_scale_f32_16x16x128_f8f6f4 v[46:49], v[232:239], v[212:219], v[46:49], v222, v222 op_sel_hi:[0,0,0]
	s_waitcnt lgkmcnt(0)
	v_mfma_scale_f32_16x16x128_f8f6f4 v[74:77], v[240:247], v[188:195], v[74:77], v222, v222 op_sel_hi:[0,0,0]
	v_mfma_scale_f32_16x16x128_f8f6f4 v[66:69], v[240:247], v[196:203], v[66:69], v222, v222 op_sel_hi:[0,0,0]
	v_mfma_scale_f32_16x16x128_f8f6f4 v[58:61], v[240:247], v[204:211], v[58:61], v222, v222 op_sel_hi:[0,0,0]
	v_mfma_scale_f32_16x16x128_f8f6f4 v[42:45], v[240:247], v[212:219], v[42:45], v222, v222 op_sel_hi:[0,0,0]
	s_setprio 0
	s_mov_b32 m0, s69
	v_lshl_add_u64 v[156:157], v[156:157], 0, s[6:7]
	s_barrier
	ds_read_b128 v[188:191], v181 offset:49152
	ds_read_b128 v[192:195], v181 offset:50176
	ds_read_b128 v[196:199], v181 offset:51200
	ds_read_b128 v[200:203], v181 offset:52224
	ds_read_b128 v[204:207], v181 offset:53248
	ds_read_b128 v[208:211], v181 offset:54272
	ds_read_b128 v[212:215], v181 offset:55296
	ds_read_b128 v[216:219], v181 offset:56320
	global_load_lds_dwordx4 v[156:157], off
	v_lshl_add_u64 v[156:157], v[158:159], 0, s[6:7]
	s_mov_b32 m0, s70
	s_nop 0
	global_load_lds_dwordx4 v[156:157], off
	s_barrier
	s_setprio 1
	s_waitcnt lgkmcnt(6)
	v_mfma_scale_f32_16x16x128_f8f6f4 v[126:129], v[2:9], v[188:195], v[126:129], v222, v222 op_sel_hi:[0,0,0]
	v_mfma_scale_f32_16x16x128_f8f6f4 v[118:121], v[10:17], v[188:195], v[118:121], v222, v222 op_sel_hi:[0,0,0]
	s_waitcnt lgkmcnt(4)
	v_mfma_scale_f32_16x16x128_f8f6f4 v[110:113], v[2:9], v[196:203], v[110:113], v222, v222 op_sel_hi:[0,0,0]
	v_mfma_scale_f32_16x16x128_f8f6f4 v[102:105], v[10:17], v[196:203], v[102:105], v222, v222 op_sel_hi:[0,0,0]
	s_waitcnt lgkmcnt(2)
	v_mfma_scale_f32_16x16x128_f8f6f4 v[94:97], v[2:9], v[204:211], v[94:97], v222, v222 op_sel_hi:[0,0,0]
	v_mfma_scale_f32_16x16x128_f8f6f4 v[90:93], v[10:17], v[204:211], v[90:93], v222, v222 op_sel_hi:[0,0,0]
	s_waitcnt lgkmcnt(0)
	v_mfma_scale_f32_16x16x128_f8f6f4 v[86:89], v[2:9], v[212:219], v[86:89], v222, v222 op_sel_hi:[0,0,0]
	v_mfma_scale_f32_16x16x128_f8f6f4 v[82:85], v[10:17], v[212:219], v[82:85], v222, v222 op_sel_hi:[0,0,0]
	s_setprio 0
	s_barrier
	s_add_u32 s6, s42, 0x20180
	s_addc_u32 s7, s43, 0
	s_mov_b32 m0, s71
	v_lshl_add_u64 v[2:3], s[6:7], 0, v[0:1]
	global_load_lds_dwordx4 v[2:3], off
	v_lshl_add_u64 v[2:3], s[6:7], 0, v[150:151]
	s_mov_b32 m0, s72
	s_nop 0
	global_load_lds_dwordx4 v[2:3], off
	s_waitcnt vmcnt(6)
	s_barrier
	s_setprio 1
	v_mfma_scale_f32_16x16x128_f8f6f4 v[54:57], v[232:239], v[188:195], v[54:57], v222, v222 op_sel_hi:[0,0,0]
	v_mfma_scale_f32_16x16x128_f8f6f4 v[50:53], v[240:247], v[188:195], v[50:53], v222, v222 op_sel_hi:[0,0,0]
	v_mfma_scale_f32_16x16x128_f8f6f4 v[38:41], v[232:239], v[196:203], v[38:41], v222, v222 op_sel_hi:[0,0,0]
	v_mfma_scale_f32_16x16x128_f8f6f4 v[34:37], v[240:247], v[196:203], v[34:37], v222, v222 op_sel_hi:[0,0,0]
	v_mfma_scale_f32_16x16x128_f8f6f4 v[30:33], v[232:239], v[204:211], v[30:33], v222, v222 op_sel_hi:[0,0,0]
	v_mfma_scale_f32_16x16x128_f8f6f4 v[26:29], v[240:247], v[204:211], v[26:29], v222, v222 op_sel_hi:[0,0,0]
	v_mfma_scale_f32_16x16x128_f8f6f4 v[22:25], v[232:239], v[212:219], v[22:25], v222, v222 op_sel_hi:[0,0,0]
	v_mfma_scale_f32_16x16x128_f8f6f4 v[18:21], v[240:247], v[212:219], v[18:21], v222, v222 op_sel_hi:[0,0,0]
	s_setprio 0
	s_lshl_b64 s[6:7], s[40:41], 2
	s_add_u32 s41, s28, s6
	s_addc_u32 s75, s65, s7
	s_add_u32 s44, s44, 0x20180
	s_addc_u32 s45, s45, 0
	s_add_u32 s76, s42, 0x200
	s_addc_u32 s77, s43, 0
	s_mov_b32 s78, 0
	s_barrier
	s_branch .LBB0_1793
.LBB0_1792:
	ds_read_b128 v[10:13], v165
	ds_read_b128 v[14:17], v166
	ds_read_b128 v[156:159], v167
	ds_read_b128 v[160:163], v168
	s_add_u32 s79, s44, 0xfffe0080
	s_addc_u32 s80, s45, -1
	s_and_b64 s[6:7], s[42:43], exec
	s_cselect_b32 s43, s15, s80
	s_cselect_b32 s42, s21, s79
	s_cselect_b32 s7, s9, s77
	s_cselect_b32 s6, s8, s76
	s_mov_b32 m0, s39
	v_lshl_add_u64 v[2:3], s[44:45], 0, v[152:153]
	ds_read_b128 v[188:191], v181
	ds_read_b128 v[192:195], v181 offset:1024
	ds_read_b128 v[196:199], v181 offset:2048
	ds_read_b128 v[200:203], v181 offset:3072
	ds_read_b128 v[204:207], v181 offset:4096
	ds_read_b128 v[208:211], v181 offset:5120
	ds_read_b128 v[212:215], v181 offset:6144
	ds_read_b128 v[216:219], v181 offset:7168
	global_load_lds_dwordx4 v[2:3], off
	v_lshl_add_u64 v[2:3], s[44:45], 0, v[154:155]
	s_mov_b32 m0, s74
	s_nop 0
	global_load_lds_dwordx4 v[2:3], off
	s_waitcnt lgkmcnt(8)
	s_barrier
	s_setprio 1
	s_waitcnt lgkmcnt(6)
	v_mfma_scale_f32_16x16x128_f8f6f4 v[142:145], v[10:17], v[188:195], v[142:145], v222, v222 op_sel_hi:[0,0,0]
	v_mfma_scale_f32_16x16x128_f8f6f4 v[138:141], v[156:163], v[188:195], v[138:141], v222, v222 op_sel_hi:[0,0,0]
	s_waitcnt lgkmcnt(4)
	v_mfma_scale_f32_16x16x128_f8f6f4 v[134:137], v[10:17], v[196:203], v[134:137], v222, v222 op_sel_hi:[0,0,0]
	v_mfma_scale_f32_16x16x128_f8f6f4 v[130:133], v[156:163], v[196:203], v[130:133], v222, v222 op_sel_hi:[0,0,0]
	s_waitcnt lgkmcnt(2)
	v_mfma_scale_f32_16x16x128_f8f6f4 v[122:125], v[10:17], v[204:211], v[122:125], v222, v222 op_sel_hi:[0,0,0]
	v_mfma_scale_f32_16x16x128_f8f6f4 v[114:117], v[156:163], v[204:211], v[114:117], v222, v222 op_sel_hi:[0,0,0]
	s_waitcnt lgkmcnt(0)
	v_mfma_scale_f32_16x16x128_f8f6f4 v[106:109], v[10:17], v[212:219], v[106:109], v222, v222 op_sel_hi:[0,0,0]
	v_mfma_scale_f32_16x16x128_f8f6f4 v[98:101], v[156:163], v[212:219], v[98:101], v222, v222 op_sel_hi:[0,0,0]
	s_setprio 0
	s_barrier
	s_mov_b32 m0, s56
	v_lshl_add_u64 v[6:7], s[6:7], 0, v[0:1]
	ds_read_b128 v[232:235], v169
	ds_read_b128 v[236:239], v170
	ds_read_b128 v[240:243], v171
	ds_read_b128 v[244:247], v172
	global_load_lds_dwordx4 v[6:7], off
	v_lshl_add_u64 v[8:9], s[6:7], 0, v[150:151]
	s_mov_b32 m0, s57
	s_nop 0
	global_load_lds_dwordx4 v[8:9], off
	s_barrier
	s_setprio 1
	s_waitcnt lgkmcnt(2)
	v_mfma_scale_f32_16x16x128_f8f6f4 v[78:81], v[232:239], v[188:195], v[78:81], v222, v222 op_sel_hi:[0,0,0]
	v_mfma_scale_f32_16x16x128_f8f6f4 v[70:73], v[232:239], v[196:203], v[70:73], v222, v222 op_sel_hi:[0,0,0]
	v_mfma_scale_f32_16x16x128_f8f6f4 v[62:65], v[232:239], v[204:211], v[62:65], v222, v222 op_sel_hi:[0,0,0]
	v_mfma_scale_f32_16x16x128_f8f6f4 v[46:49], v[232:239], v[212:219], v[46:49], v222, v222 op_sel_hi:[0,0,0]
	s_waitcnt lgkmcnt(0)
	v_mfma_scale_f32_16x16x128_f8f6f4 v[74:77], v[240:247], v[188:195], v[74:77], v222, v222 op_sel_hi:[0,0,0]
	v_mfma_scale_f32_16x16x128_f8f6f4 v[66:69], v[240:247], v[196:203], v[66:69], v222, v222 op_sel_hi:[0,0,0]
	v_mfma_scale_f32_16x16x128_f8f6f4 v[58:61], v[240:247], v[204:211], v[58:61], v222, v222 op_sel_hi:[0,0,0]
	v_mfma_scale_f32_16x16x128_f8f6f4 v[42:45], v[240:247], v[212:219], v[42:45], v222, v222 op_sel_hi:[0,0,0]
	s_setprio 0
	s_mov_b32 m0, s55
	v_lshl_add_u64 v[2:3], s[42:43], 0, v[146:147]
	s_barrier
	ds_read_b128 v[188:191], v181 offset:16384
	ds_read_b128 v[192:195], v181 offset:17408
	ds_read_b128 v[196:199], v181 offset:18432
	ds_read_b128 v[200:203], v181 offset:19456
	ds_read_b128 v[204:207], v181 offset:20480
	ds_read_b128 v[208:211], v181 offset:21504
	ds_read_b128 v[212:215], v181 offset:22528
	ds_read_b128 v[216:219], v181 offset:23552
	global_load_lds_dwordx4 v[2:3], off
	v_lshl_add_u64 v[4:5], s[42:43], 0, v[148:149]
	s_mov_b32 m0, s58
	s_nop 0
	global_load_lds_dwordx4 v[4:5], off
	s_barrier
	s_setprio 1
	s_waitcnt lgkmcnt(6)
	v_mfma_scale_f32_16x16x128_f8f6f4 v[126:129], v[10:17], v[188:195], v[126:129], v222, v222 op_sel_hi:[0,0,0]
	v_mfma_scale_f32_16x16x128_f8f6f4 v[118:121], v[156:163], v[188:195], v[118:121], v222, v222 op_sel_hi:[0,0,0]
	s_waitcnt lgkmcnt(4)
	v_mfma_scale_f32_16x16x128_f8f6f4 v[110:113], v[10:17], v[196:203], v[110:113], v222, v222 op_sel_hi:[0,0,0]
	v_mfma_scale_f32_16x16x128_f8f6f4 v[102:105], v[156:163], v[196:203], v[102:105], v222, v222 op_sel_hi:[0,0,0]
	s_waitcnt lgkmcnt(2)
	v_mfma_scale_f32_16x16x128_f8f6f4 v[94:97], v[10:17], v[204:211], v[94:97], v222, v222 op_sel_hi:[0,0,0]
	v_mfma_scale_f32_16x16x128_f8f6f4 v[90:93], v[156:163], v[204:211], v[90:93], v222, v222 op_sel_hi:[0,0,0]
	s_waitcnt lgkmcnt(0)
	v_mfma_scale_f32_16x16x128_f8f6f4 v[86:89], v[10:17], v[212:219], v[86:89], v222, v222 op_sel_hi:[0,0,0]
	v_mfma_scale_f32_16x16x128_f8f6f4 v[82:85], v[156:163], v[212:219], v[82:85], v222, v222 op_sel_hi:[0,0,0]
	s_setprio 0
	s_barrier
	s_add_u32 s80, s6, 0x20000
	s_addc_u32 s81, s7, 0
	s_mov_b32 m0, s59
	v_lshl_add_u64 v[10:11], s[80:81], 0, v[0:1]
	global_load_lds_dwordx4 v[10:11], off
	v_lshl_add_u64 v[10:11], s[80:81], 0, v[150:151]
	s_mov_b32 m0, s60
	s_nop 0
	global_load_lds_dwordx4 v[10:11], off
	s_waitcnt vmcnt(6)
	s_barrier
	s_setprio 1
	v_mfma_scale_f32_16x16x128_f8f6f4 v[54:57], v[232:239], v[188:195], v[54:57], v222, v222 op_sel_hi:[0,0,0]
	v_mfma_scale_f32_16x16x128_f8f6f4 v[50:53], v[240:247], v[188:195], v[50:53], v222, v222 op_sel_hi:[0,0,0]
	v_mfma_scale_f32_16x16x128_f8f6f4 v[38:41], v[232:239], v[196:203], v[38:41], v222, v222 op_sel_hi:[0,0,0]
	v_mfma_scale_f32_16x16x128_f8f6f4 v[34:37], v[240:247], v[196:203], v[34:37], v222, v222 op_sel_hi:[0,0,0]
	v_mfma_scale_f32_16x16x128_f8f6f4 v[30:33], v[232:239], v[204:211], v[30:33], v222, v222 op_sel_hi:[0,0,0]
	v_mfma_scale_f32_16x16x128_f8f6f4 v[26:29], v[240:247], v[204:211], v[26:29], v222, v222 op_sel_hi:[0,0,0]
	v_mfma_scale_f32_16x16x128_f8f6f4 v[22:25], v[232:239], v[212:219], v[22:25], v222, v222 op_sel_hi:[0,0,0]
	v_mfma_scale_f32_16x16x128_f8f6f4 v[18:21], v[240:247], v[212:219], v[18:21], v222, v222 op_sel_hi:[0,0,0]
	s_setprio 0
	s_barrier
	ds_read_b128 v[10:13], v173
	ds_read_b128 v[14:17], v174
	ds_read_b128 v[156:159], v175
	ds_read_b128 v[160:163], v176
	s_add_u32 s42, s42, 0x20000
	s_addc_u32 s43, s43, 0
	s_mov_b32 m0, s61
	v_lshl_add_u64 v[182:183], s[42:43], 0, v[146:147]
	ds_read_b128 v[188:191], v181 offset:32768
	ds_read_b128 v[192:195], v181 offset:33792
	ds_read_b128 v[196:199], v181 offset:34816
	ds_read_b128 v[200:203], v181 offset:35840
	ds_read_b128 v[204:207], v181 offset:36864
	ds_read_b128 v[208:211], v181 offset:37888
	ds_read_b128 v[212:215], v181 offset:38912
	ds_read_b128 v[216:219], v181 offset:39936
	global_load_lds_dwordx4 v[182:183], off
	v_lshl_add_u64 v[182:183], s[42:43], 0, v[148:149]
	s_mov_b32 m0, s62
	s_nop 0
	global_load_lds_dwordx4 v[182:183], off
	s_waitcnt lgkmcnt(8)
	s_barrier
	s_setprio 1
	s_waitcnt lgkmcnt(6)
	v_mfma_scale_f32_16x16x128_f8f6f4 v[142:145], v[10:17], v[188:195], v[142:145], v222, v222 op_sel_hi:[0,0,0]
	v_mfma_scale_f32_16x16x128_f8f6f4 v[138:141], v[156:163], v[188:195], v[138:141], v222, v222 op_sel_hi:[0,0,0]
	s_waitcnt lgkmcnt(4)
	v_mfma_scale_f32_16x16x128_f8f6f4 v[134:137], v[10:17], v[196:203], v[134:137], v222, v222 op_sel_hi:[0,0,0]
	v_mfma_scale_f32_16x16x128_f8f6f4 v[130:133], v[156:163], v[196:203], v[130:133], v222, v222 op_sel_hi:[0,0,0]
	s_waitcnt lgkmcnt(2)
	v_mfma_scale_f32_16x16x128_f8f6f4 v[122:125], v[10:17], v[204:211], v[122:125], v222, v222 op_sel_hi:[0,0,0]
	v_mfma_scale_f32_16x16x128_f8f6f4 v[114:117], v[156:163], v[204:211], v[114:117], v222, v222 op_sel_hi:[0,0,0]
	s_waitcnt lgkmcnt(0)
	v_mfma_scale_f32_16x16x128_f8f6f4 v[106:109], v[10:17], v[212:219], v[106:109], v222, v222 op_sel_hi:[0,0,0]
	v_mfma_scale_f32_16x16x128_f8f6f4 v[98:101], v[156:163], v[212:219], v[98:101], v222, v222 op_sel_hi:[0,0,0]
	s_setprio 0
	s_barrier
	s_mov_b32 m0, s67
	v_lshl_add_u64 v[6:7], v[6:7], 0, s[24:25]
	ds_read_b128 v[232:235], v177
	ds_read_b128 v[236:239], v178
	ds_read_b128 v[240:243], v179
	ds_read_b128 v[244:247], v180
	global_load_lds_dwordx4 v[6:7], off
	v_lshl_add_u64 v[6:7], v[8:9], 0, s[24:25]
	s_mov_b32 m0, s68
	s_nop 0
	global_load_lds_dwordx4 v[6:7], off
	s_barrier
	s_setprio 1
	s_waitcnt lgkmcnt(2)
	v_mfma_scale_f32_16x16x128_f8f6f4 v[78:81], v[232:239], v[188:195], v[78:81], v222, v222 op_sel_hi:[0,0,0]
	v_mfma_scale_f32_16x16x128_f8f6f4 v[70:73], v[232:239], v[196:203], v[70:73], v222, v222 op_sel_hi:[0,0,0]
	v_mfma_scale_f32_16x16x128_f8f6f4 v[62:65], v[232:239], v[204:211], v[62:65], v222, v222 op_sel_hi:[0,0,0]
	v_mfma_scale_f32_16x16x128_f8f6f4 v[46:49], v[232:239], v[212:219], v[46:49], v222, v222 op_sel_hi:[0,0,0]
	s_waitcnt lgkmcnt(0)
	v_mfma_scale_f32_16x16x128_f8f6f4 v[74:77], v[240:247], v[188:195], v[74:77], v222, v222 op_sel_hi:[0,0,0]
	v_mfma_scale_f32_16x16x128_f8f6f4 v[66:69], v[240:247], v[196:203], v[66:69], v222, v222 op_sel_hi:[0,0,0]
	v_mfma_scale_f32_16x16x128_f8f6f4 v[58:61], v[240:247], v[204:211], v[58:61], v222, v222 op_sel_hi:[0,0,0]
	v_mfma_scale_f32_16x16x128_f8f6f4 v[42:45], v[240:247], v[212:219], v[42:45], v222, v222 op_sel_hi:[0,0,0]
	s_setprio 0
	s_mov_b32 m0, s69
	v_lshl_add_u64 v[2:3], v[2:3], 0, s[24:25]
	s_barrier
	ds_read_b128 v[188:191], v181 offset:49152
	ds_read_b128 v[192:195], v181 offset:50176
	ds_read_b128 v[196:199], v181 offset:51200
	ds_read_b128 v[200:203], v181 offset:52224
	ds_read_b128 v[204:207], v181 offset:53248
	ds_read_b128 v[208:211], v181 offset:54272
	ds_read_b128 v[212:215], v181 offset:55296
	ds_read_b128 v[216:219], v181 offset:56320
	global_load_lds_dwordx4 v[2:3], off
	v_lshl_add_u64 v[2:3], v[4:5], 0, s[24:25]
	s_mov_b32 m0, s70
	s_nop 0
	global_load_lds_dwordx4 v[2:3], off
	s_barrier
	s_setprio 1
	s_waitcnt lgkmcnt(6)
	v_mfma_scale_f32_16x16x128_f8f6f4 v[126:129], v[10:17], v[188:195], v[126:129], v222, v222 op_sel_hi:[0,0,0]
	v_mfma_scale_f32_16x16x128_f8f6f4 v[118:121], v[156:163], v[188:195], v[118:121], v222, v222 op_sel_hi:[0,0,0]
	s_waitcnt lgkmcnt(4)
	v_mfma_scale_f32_16x16x128_f8f6f4 v[110:113], v[10:17], v[196:203], v[110:113], v222, v222 op_sel_hi:[0,0,0]
	v_mfma_scale_f32_16x16x128_f8f6f4 v[102:105], v[156:163], v[196:203], v[102:105], v222, v222 op_sel_hi:[0,0,0]
	s_waitcnt lgkmcnt(2)
	v_mfma_scale_f32_16x16x128_f8f6f4 v[94:97], v[10:17], v[204:211], v[94:97], v222, v222 op_sel_hi:[0,0,0]
	v_mfma_scale_f32_16x16x128_f8f6f4 v[90:93], v[156:163], v[204:211], v[90:93], v222, v222 op_sel_hi:[0,0,0]
	s_waitcnt lgkmcnt(0)
	v_mfma_scale_f32_16x16x128_f8f6f4 v[86:89], v[10:17], v[212:219], v[86:89], v222, v222 op_sel_hi:[0,0,0]
	v_mfma_scale_f32_16x16x128_f8f6f4 v[82:85], v[156:163], v[212:219], v[82:85], v222, v222 op_sel_hi:[0,0,0]
	s_setprio 0
	s_barrier
	s_add_u32 s6, s6, 0x20080
	s_addc_u32 s7, s7, 0
	s_mov_b32 m0, s71
	v_lshl_add_u64 v[2:3], s[6:7], 0, v[0:1]
	global_load_lds_dwordx4 v[2:3], off
	v_lshl_add_u64 v[2:3], s[6:7], 0, v[150:151]
	s_mov_b32 m0, s72
	s_nop 0
	global_load_lds_dwordx4 v[2:3], off
	s_waitcnt vmcnt(6)
	s_barrier
	s_setprio 1
	v_mfma_scale_f32_16x16x128_f8f6f4 v[54:57], v[232:239], v[188:195], v[54:57], v222, v222 op_sel_hi:[0,0,0]
	v_mfma_scale_f32_16x16x128_f8f6f4 v[50:53], v[240:247], v[188:195], v[50:53], v222, v222 op_sel_hi:[0,0,0]
	v_mfma_scale_f32_16x16x128_f8f6f4 v[38:41], v[232:239], v[196:203], v[38:41], v222, v222 op_sel_hi:[0,0,0]
	v_mfma_scale_f32_16x16x128_f8f6f4 v[34:37], v[240:247], v[196:203], v[34:37], v222, v222 op_sel_hi:[0,0,0]
	v_mfma_scale_f32_16x16x128_f8f6f4 v[30:33], v[232:239], v[204:211], v[30:33], v222, v222 op_sel_hi:[0,0,0]
	v_mfma_scale_f32_16x16x128_f8f6f4 v[26:29], v[240:247], v[204:211], v[26:29], v222, v222 op_sel_hi:[0,0,0]
	v_mfma_scale_f32_16x16x128_f8f6f4 v[22:25], v[232:239], v[212:219], v[22:25], v222, v222 op_sel_hi:[0,0,0]
	v_mfma_scale_f32_16x16x128_f8f6f4 v[18:21], v[240:247], v[212:219], v[18:21], v222, v222 op_sel_hi:[0,0,0]
	s_setprio 0
	s_add_i32 s78, s78, 2
	s_add_u32 s44, s44, 0x100
	s_addc_u32 s45, s45, 0
	s_add_u32 s76, s76, 0x100
	s_addc_u32 s77, s77, 0
	s_cmp_gt_u32 s78, 5
	s_barrier
	s_cbranch_scc1 .LBB0_1782

.LBB0_1925:
	ds_read_b128 v[2:5], v233
	ds_read_b128 v[6:9], v234
	ds_read_b128 v[10:13], v235
	ds_read_b128 v[14:17], v236
	s_add_u32 s40, s6, 0xfffe0080
	s_addc_u32 s41, s7, -1
	s_cmp_eq_u32 s71, 4
	s_cselect_b32 s43, s21, s41
	s_cselect_b32 s42, s67, s40
	s_cselect_b32 s41, s15, s70
	s_cselect_b32 s40, s68, s69
	v_add_u32_e32 v0, s55, v232
	v_lshl_add_u64 v[146:147], s[6:7], 0, v[204:205]
	s_add_i32 m0, s47, 0xc000
	ds_read_b128 v[150:153], v0
	ds_read_b128 v[154:157], v0 offset:1024
	ds_read_b128 v[158:161], v0 offset:2048
	ds_read_b128 v[162:165], v0 offset:3072
	ds_read_b128 v[166:169], v0 offset:4096
	ds_read_b128 v[170:173], v0 offset:5120
	ds_read_b128 v[174:177], v0 offset:6144
	ds_read_b128 v[178:181], v0 offset:7168
	global_load_lds_dwordx4 v[146:147], off
	v_lshl_add_u64 v[146:147], s[6:7], 0, v[206:207]
	s_add_i32 m0, s47, 0xe000
	s_nop 0
	global_load_lds_dwordx4 v[146:147], off
	s_waitcnt lgkmcnt(8)
	s_barrier
	s_setprio 1
	s_waitcnt lgkmcnt(6)
	v_mfma_scale_f32_16x16x128_f8f6f4 v[142:145], v[2:9], v[150:157], v[142:145], v222, v222 op_sel_hi:[0,0,0]
	v_mfma_scale_f32_16x16x128_f8f6f4 v[138:141], v[10:17], v[150:157], v[138:141], v222, v222 op_sel_hi:[0,0,0]
	s_waitcnt lgkmcnt(4)
	v_mfma_scale_f32_16x16x128_f8f6f4 v[126:129], v[2:9], v[158:165], v[126:129], v222, v222 op_sel_hi:[0,0,0]
	v_mfma_scale_f32_16x16x128_f8f6f4 v[122:125], v[10:17], v[158:165], v[122:125], v222, v222 op_sel_hi:[0,0,0]
	s_waitcnt lgkmcnt(2)
	v_mfma_scale_f32_16x16x128_f8f6f4 v[110:113], v[2:9], v[166:173], v[110:113], v222, v222 op_sel_hi:[0,0,0]
	v_mfma_scale_f32_16x16x128_f8f6f4 v[106:109], v[10:17], v[166:173], v[106:109], v222, v222 op_sel_hi:[0,0,0]
	s_waitcnt lgkmcnt(0)
	v_mfma_scale_f32_16x16x128_f8f6f4 v[94:97], v[2:9], v[174:181], v[94:97], v222, v222 op_sel_hi:[0,0,0]
	v_mfma_scale_f32_16x16x128_f8f6f4 v[90:93], v[10:17], v[174:181], v[90:93], v222, v222 op_sel_hi:[0,0,0]
	s_setprio 0
	s_barrier
	s_mov_b32 m0, s48
	v_lshl_add_u64 v[146:147], s[40:41], 0, v[200:201]
	ds_read_b128 v[188:191], v237
	ds_read_b128 v[192:195], v238
	ds_read_b128 v[208:211], v239
	ds_read_b128 v[212:215], v240
	global_load_lds_dwordx4 v[146:147], off
	v_lshl_add_u64 v[148:149], s[40:41], 0, v[196:197]
	s_mov_b32 m0, s49
	s_nop 0
	global_load_lds_dwordx4 v[148:149], off
	s_barrier
	s_setprio 1
	s_waitcnt lgkmcnt(2)
	v_mfma_scale_f32_16x16x128_f8f6f4 v[134:137], v[188:195], v[150:157], v[134:137], v222, v222 op_sel_hi:[0,0,0]
	v_mfma_scale_f32_16x16x128_f8f6f4 v[118:121], v[188:195], v[158:165], v[118:121], v222, v222 op_sel_hi:[0,0,0]
	v_mfma_scale_f32_16x16x128_f8f6f4 v[102:105], v[188:195], v[166:173], v[102:105], v222, v222 op_sel_hi:[0,0,0]
	v_mfma_scale_f32_16x16x128_f8f6f4 v[86:89], v[188:195], v[174:181], v[86:89], v222, v222 op_sel_hi:[0,0,0]
	s_waitcnt lgkmcnt(0)
	v_mfma_scale_f32_16x16x128_f8f6f4 v[130:133], v[208:215], v[150:157], v[130:133], v222, v222 op_sel_hi:[0,0,0]
	v_mfma_scale_f32_16x16x128_f8f6f4 v[114:117], v[208:215], v[158:165], v[114:117], v222, v222 op_sel_hi:[0,0,0]
	v_mfma_scale_f32_16x16x128_f8f6f4 v[98:101], v[208:215], v[166:173], v[98:101], v222, v222 op_sel_hi:[0,0,0]
	v_mfma_scale_f32_16x16x128_f8f6f4 v[82:85], v[208:215], v[174:181], v[82:85], v222, v222 op_sel_hi:[0,0,0]
	s_setprio 0
	s_mov_b32 m0, s47
	v_lshl_add_u64 v[150:151], s[42:43], 0, v[202:203]
	s_barrier
	ds_read_b128 v[154:157], v0 offset:16384
	ds_read_b128 v[158:161], v0 offset:17408
	ds_read_b128 v[162:165], v0 offset:18432
	ds_read_b128 v[166:169], v0 offset:19456
	ds_read_b128 v[170:173], v0 offset:20480
	ds_read_b128 v[174:177], v0 offset:21504
	ds_read_b128 v[178:181], v0 offset:22528
	ds_read_b128 v[182:185], v0 offset:23552
	global_load_lds_dwordx4 v[150:151], off
	v_lshl_add_u64 v[152:153], s[42:43], 0, v[198:199]
	s_mov_b32 m0, s50
	s_nop 0
	global_load_lds_dwordx4 v[152:153], off
	s_barrier
	s_setprio 1
	s_waitcnt lgkmcnt(6)
	v_mfma_scale_f32_16x16x128_f8f6f4 v[78:81], v[2:9], v[154:161], v[78:81], v222, v222 op_sel_hi:[0,0,0]
	v_mfma_scale_f32_16x16x128_f8f6f4 v[74:77], v[10:17], v[154:161], v[74:77], v222, v222 op_sel_hi:[0,0,0]
	s_waitcnt lgkmcnt(4)
	v_mfma_scale_f32_16x16x128_f8f6f4 v[62:65], v[2:9], v[162:169], v[62:65], v222, v222 op_sel_hi:[0,0,0]
	v_mfma_scale_f32_16x16x128_f8f6f4 v[58:61], v[10:17], v[162:169], v[58:61], v222, v222 op_sel_hi:[0,0,0]
	s_waitcnt lgkmcnt(2)
	v_mfma_scale_f32_16x16x128_f8f6f4 v[46:49], v[2:9], v[170:177], v[46:49], v222, v222 op_sel_hi:[0,0,0]
	v_mfma_scale_f32_16x16x128_f8f6f4 v[42:45], v[10:17], v[170:177], v[42:45], v222, v222 op_sel_hi:[0,0,0]
	s_waitcnt lgkmcnt(0)
	v_mfma_scale_f32_16x16x128_f8f6f4 v[30:33], v[2:9], v[178:185], v[30:33], v222, v222 op_sel_hi:[0,0,0]
	v_mfma_scale_f32_16x16x128_f8f6f4 v[26:29], v[10:17], v[178:185], v[26:29], v222, v222 op_sel_hi:[0,0,0]
	s_setprio 0
	s_barrier
	s_add_u32 s72, s40, 0x20000
	s_addc_u32 s73, s41, 0
	s_mov_b32 m0, s51
	v_lshl_add_u64 v[2:3], s[72:73], 0, v[200:201]
	global_load_lds_dwordx4 v[2:3], off
	v_lshl_add_u64 v[2:3], s[72:73], 0, v[196:197]
	s_mov_b32 m0, s52
	s_nop 0
	global_load_lds_dwordx4 v[2:3], off
	s_waitcnt vmcnt(6)
	s_barrier
	s_setprio 1
	v_mfma_scale_f32_16x16x128_f8f6f4 v[70:73], v[188:195], v[154:161], v[70:73], v222, v222 op_sel_hi:[0,0,0]
	v_mfma_scale_f32_16x16x128_f8f6f4 v[66:69], v[208:215], v[154:161], v[66:69], v222, v222 op_sel_hi:[0,0,0]
	v_mfma_scale_f32_16x16x128_f8f6f4 v[54:57], v[188:195], v[162:169], v[54:57], v222, v222 op_sel_hi:[0,0,0]
	v_mfma_scale_f32_16x16x128_f8f6f4 v[50:53], v[208:215], v[162:169], v[50:53], v222, v222 op_sel_hi:[0,0,0]
	v_mfma_scale_f32_16x16x128_f8f6f4 v[38:41], v[188:195], v[170:177], v[38:41], v222, v222 op_sel_hi:[0,0,0]
	v_mfma_scale_f32_16x16x128_f8f6f4 v[34:37], v[208:215], v[170:177], v[34:37], v222, v222 op_sel_hi:[0,0,0]
	v_mfma_scale_f32_16x16x128_f8f6f4 v[22:25], v[188:195], v[178:185], v[22:25], v222, v222 op_sel_hi:[0,0,0]
	v_mfma_scale_f32_16x16x128_f8f6f4 v[18:21], v[208:215], v[178:185], v[18:21], v222, v222 op_sel_hi:[0,0,0]
	s_setprio 0
	s_barrier
	ds_read_b128 v[2:5], v241
	ds_read_b128 v[6:9], v242
	ds_read_b128 v[10:13], v243
	ds_read_b128 v[14:17], v244
	s_add_u32 s42, s42, 0x20000
	s_addc_u32 s43, s43, 0
	s_mov_b32 m0, s53
	v_lshl_add_u64 v[188:189], s[42:43], 0, v[202:203]
	ds_read_b128 v[154:157], v0 offset:32768
	ds_read_b128 v[158:161], v0 offset:33792
	ds_read_b128 v[162:165], v0 offset:34816
	ds_read_b128 v[166:169], v0 offset:35840
	ds_read_b128 v[170:173], v0 offset:36864
	ds_read_b128 v[174:177], v0 offset:37888
	ds_read_b128 v[178:181], v0 offset:38912
	ds_read_b128 v[182:185], v0 offset:39936
	global_load_lds_dwordx4 v[188:189], off
	v_lshl_add_u64 v[188:189], s[42:43], 0, v[198:199]
	s_mov_b32 m0, s54
	s_nop 0
	global_load_lds_dwordx4 v[188:189], off
	s_waitcnt lgkmcnt(8)
	s_barrier
	s_setprio 1
	s_waitcnt lgkmcnt(6)
	v_mfma_scale_f32_16x16x128_f8f6f4 v[142:145], v[2:9], v[154:161], v[142:145], v222, v222 op_sel_hi:[0,0,0]
	v_mfma_scale_f32_16x16x128_f8f6f4 v[138:141], v[10:17], v[154:161], v[138:141], v222, v222 op_sel_hi:[0,0,0]
	s_waitcnt lgkmcnt(4)
	v_mfma_scale_f32_16x16x128_f8f6f4 v[126:129], v[2:9], v[162:169], v[126:129], v222, v222 op_sel_hi:[0,0,0]
	v_mfma_scale_f32_16x16x128_f8f6f4 v[122:125], v[10:17], v[162:169], v[122:125], v222, v222 op_sel_hi:[0,0,0]
	s_waitcnt lgkmcnt(2)
	v_mfma_scale_f32_16x16x128_f8f6f4 v[110:113], v[2:9], v[170:177], v[110:113], v222, v222 op_sel_hi:[0,0,0]
	v_mfma_scale_f32_16x16x128_f8f6f4 v[106:109], v[10:17], v[170:177], v[106:109], v222, v222 op_sel_hi:[0,0,0]
	s_waitcnt lgkmcnt(0)
	v_mfma_scale_f32_16x16x128_f8f6f4 v[94:97], v[2:9], v[178:185], v[94:97], v222, v222 op_sel_hi:[0,0,0]
	v_mfma_scale_f32_16x16x128_f8f6f4 v[90:93], v[10:17], v[178:185], v[90:93], v222, v222 op_sel_hi:[0,0,0]
	s_setprio 0
	s_barrier
	s_mov_b32 m0, s58
	v_lshl_add_u64 v[146:147], v[146:147], 0, s[24:25]
	ds_read_b128 v[188:191], v245
	ds_read_b128 v[192:195], v246
	ds_read_b128 v[208:211], v247
	ds_read_b128 v[212:215], v248
	global_load_lds_dwordx4 v[146:147], off
	v_lshl_add_u64 v[146:147], v[148:149], 0, s[24:25]
	s_mov_b32 m0, s59
	s_nop 0
	global_load_lds_dwordx4 v[146:147], off
	s_barrier
	s_setprio 1
	s_waitcnt lgkmcnt(2)
	v_mfma_scale_f32_16x16x128_f8f6f4 v[134:137], v[188:195], v[154:161], v[134:137], v222, v222 op_sel_hi:[0,0,0]
	v_mfma_scale_f32_16x16x128_f8f6f4 v[118:121], v[188:195], v[162:169], v[118:121], v222, v222 op_sel_hi:[0,0,0]
	v_mfma_scale_f32_16x16x128_f8f6f4 v[102:105], v[188:195], v[170:177], v[102:105], v222, v222 op_sel_hi:[0,0,0]
	v_mfma_scale_f32_16x16x128_f8f6f4 v[86:89], v[188:195], v[178:185], v[86:89], v222, v222 op_sel_hi:[0,0,0]
	s_waitcnt lgkmcnt(0)
	v_mfma_scale_f32_16x16x128_f8f6f4 v[130:133], v[208:215], v[154:161], v[130:133], v222, v222 op_sel_hi:[0,0,0]
	v_mfma_scale_f32_16x16x128_f8f6f4 v[114:117], v[208:215], v[162:169], v[114:117], v222, v222 op_sel_hi:[0,0,0]
	v_mfma_scale_f32_16x16x128_f8f6f4 v[98:101], v[208:215], v[170:177], v[98:101], v222, v222 op_sel_hi:[0,0,0]
	v_mfma_scale_f32_16x16x128_f8f6f4 v[82:85], v[208:215], v[178:185], v[82:85], v222, v222 op_sel_hi:[0,0,0]
	s_setprio 0
	s_mov_b32 m0, s60
	v_lshl_add_u64 v[146:147], v[150:151], 0, s[24:25]
	s_barrier
	ds_read_b128 v[154:157], v0 offset:49152
	ds_read_b128 v[158:161], v0 offset:50176
	ds_read_b128 v[162:165], v0 offset:51200
	ds_read_b128 v[166:169], v0 offset:52224
	ds_read_b128 v[170:173], v0 offset:53248
	ds_read_b128 v[174:177], v0 offset:54272
	ds_read_b128 v[178:181], v0 offset:55296
	ds_read_b128 v[182:185], v0 offset:56320
	global_load_lds_dwordx4 v[146:147], off
	v_lshl_add_u64 v[146:147], v[152:153], 0, s[24:25]
	s_mov_b32 m0, s61
	s_nop 0
	global_load_lds_dwordx4 v[146:147], off
	s_barrier
	s_setprio 1
	s_waitcnt lgkmcnt(6)
	v_mfma_scale_f32_16x16x128_f8f6f4 v[78:81], v[2:9], v[154:161], v[78:81], v222, v222 op_sel_hi:[0,0,0]
	v_mfma_scale_f32_16x16x128_f8f6f4 v[74:77], v[10:17], v[154:161], v[74:77], v222, v222 op_sel_hi:[0,0,0]
	s_waitcnt lgkmcnt(4)
	v_mfma_scale_f32_16x16x128_f8f6f4 v[62:65], v[2:9], v[162:169], v[62:65], v222, v222 op_sel_hi:[0,0,0]
	v_mfma_scale_f32_16x16x128_f8f6f4 v[58:61], v[10:17], v[162:169], v[58:61], v222, v222 op_sel_hi:[0,0,0]
	s_waitcnt lgkmcnt(2)
	v_mfma_scale_f32_16x16x128_f8f6f4 v[46:49], v[2:9], v[170:177], v[46:49], v222, v222 op_sel_hi:[0,0,0]
	v_mfma_scale_f32_16x16x128_f8f6f4 v[42:45], v[10:17], v[170:177], v[42:45], v222, v222 op_sel_hi:[0,0,0]
	s_waitcnt lgkmcnt(0)
	v_mfma_scale_f32_16x16x128_f8f6f4 v[30:33], v[2:9], v[178:185], v[30:33], v222, v222 op_sel_hi:[0,0,0]
	v_mfma_scale_f32_16x16x128_f8f6f4 v[26:29], v[10:17], v[178:185], v[26:29], v222, v222 op_sel_hi:[0,0,0]
	s_setprio 0
	s_barrier
	s_add_u32 s40, s40, 0x20080
	s_addc_u32 s41, s41, 0
	s_mov_b32 m0, s62
	v_lshl_add_u64 v[2:3], s[40:41], 0, v[200:201]
	global_load_lds_dwordx4 v[2:3], off
	v_lshl_add_u64 v[2:3], s[40:41], 0, v[196:197]
	s_mov_b32 m0, s63
	s_nop 0
	global_load_lds_dwordx4 v[2:3], off
	s_waitcnt vmcnt(6)
	s_barrier
	s_setprio 1
	v_mfma_scale_f32_16x16x128_f8f6f4 v[70:73], v[188:195], v[154:161], v[70:73], v222, v222 op_sel_hi:[0,0,0]
	v_mfma_scale_f32_16x16x128_f8f6f4 v[66:69], v[208:215], v[154:161], v[66:69], v222, v222 op_sel_hi:[0,0,0]
	v_mfma_scale_f32_16x16x128_f8f6f4 v[54:57], v[188:195], v[162:169], v[54:57], v222, v222 op_sel_hi:[0,0,0]
	v_mfma_scale_f32_16x16x128_f8f6f4 v[50:53], v[208:215], v[162:169], v[50:53], v222, v222 op_sel_hi:[0,0,0]
	v_mfma_scale_f32_16x16x128_f8f6f4 v[38:41], v[188:195], v[170:177], v[38:41], v222, v222 op_sel_hi:[0,0,0]
	v_mfma_scale_f32_16x16x128_f8f6f4 v[34:37], v[208:215], v[170:177], v[34:37], v222, v222 op_sel_hi:[0,0,0]
	v_mfma_scale_f32_16x16x128_f8f6f4 v[22:25], v[188:195], v[178:185], v[22:25], v222, v222 op_sel_hi:[0,0,0]
	v_mfma_scale_f32_16x16x128_f8f6f4 v[18:21], v[208:215], v[178:185], v[18:21], v222, v222 op_sel_hi:[0,0,0]
	s_setprio 0
	s_add_i32 s71, s71, 2
	s_add_u32 s6, s6, 0x100
	s_addc_u32 s7, s7, 0
	s_add_u32 s69, s69, 0x100
	s_addc_u32 s70, s70, 0
	s_cmp_gt_u32 s71, 5
	s_barrier
	s_cbranch_scc0 .LBB0_1925
	v_readlane_b32 s21, v252, 52
	v_readlane_b32 s6, v252, 51
	s_nop 15
	s_nop 15
	v_mbcnt_lo_u32_b32 v0, -1, 0
	v_mbcnt_hi_u32_b32 v0, -1, v0
	s_lshl_b32 s42, s6, 6
	s_lshl_b32 s6, s65, 8
	s_ashr_i32 s7, s6, 31
	s_lshl_b32 s40, s21, 5
	s_lshl_b32 s15, s66, 8
	s_ashr_i32 s41, s40, 31
	s_lshl_b64 s[66:67], s[6:7], 1
	s_add_u32 s21, s10, s66
	s_addc_u32 s43, s11, s67
	s_lshl_b64 s[68:69], s[40:41], 1
	s_add_u32 s70, s21, s68
	s_addc_u32 s71, s43, s69
	s_add_u32 s21, s56, s66
	v_and_b32_e32 v249, 15, v0
	v_lshrrev_b32_e32 v0, 1, v0
	s_addc_u32 s43, s57, s67
	v_and_b32_e32 v217, 24, v0
	s_add_u32 s66, s21, s68
	v_lshlrev_b32_e32 v0, 1, v217
	s_addc_u32 s67, s43, s69
	v_or_b32_e32 v2, s15, v249
	v_lshl_add_u64 v[210:211], s[70:71], 0, v[0:1]
	v_lshl_add_u64 v[212:213], s[66:67], 0, v[0:1]
	v_or_b32_e32 v0, s42, v249
	v_add_u32_e32 v2, s42, v2
	v_add_u32_e32 v216, s15, v0
	v_ashrrev_i32_e32 v3, 31, v2
	v_or_b32_e32 v214, 32, v216
	v_lshlrev_b64 v[4:5], 11, v[2:3]
	v_ashrrev_i32_e32 v215, 31, v214
	v_lshl_add_u64 v[6:7], v[210:211], 0, v[4:5]
	v_lshl_add_u64 v[4:5], v[212:213], 0, v[4:5]
	v_lshlrev_b64 v[8:9], 11, v[214:215]
	global_load_dwordx4 v[188:191], v[6:7], off
	global_load_dwordx4 v[192:195], v[4:5], off
	v_lshl_add_u64 v[10:11], v[210:211], 0, v[8:9]
	v_lshl_add_u64 v[8:9], v[212:213], 0, v[8:9]
	global_load_dwordx4 v[182:185], v[6:7], off offset:256
	global_load_dwordx4 v[178:181], v[4:5], off offset:256
	global_load_dwordx4 v[166:169], v[10:11], off
	global_load_dwordx4 v[158:161], v[10:11], off offset:256
	global_load_dwordx4 v[162:165], v[8:9], off
	global_load_dwordx4 v[154:157], v[8:9], off offset:256
	v_or_b32_e32 v2, 16, v2
	v_or_b32_e32 v6, 48, v216
	v_ashrrev_i32_e32 v3, 31, v2
	v_ashrrev_i32_e32 v7, 31, v6
	v_lshlrev_b64 v[2:3], 11, v[2:3]
	v_lshlrev_b64 v[6:7], 11, v[6:7]
	v_lshl_add_u64 v[4:5], v[210:211], 0, v[2:3]
	v_lshl_add_u64 v[2:3], v[212:213], 0, v[2:3]
	v_lshl_add_u64 v[8:9], v[210:211], 0, v[6:7]
	v_lshl_add_u64 v[208:209], v[212:213], 0, v[6:7]
	global_load_dwordx4 v[174:177], v[4:5], off
	global_load_dwordx4 v[14:17], v[4:5], off offset:256
	global_load_dwordx4 v[170:173], v[2:3], off
	global_load_dwordx4 v[10:13], v[2:3], off offset:256
	global_load_dwordx4 v[150:153], v[8:9], off
	s_nop 0
	global_load_dwordx4 v[6:9], v[8:9], off offset:256
	s_nop 0
	global_load_dwordx4 v[146:149], v[208:209], off
	global_load_dwordx4 v[2:5], v[208:209], off offset:256
	v_pk_mul_f32 v[144:145], v[144:145], s[18:19] op_sel_hi:[1,0]
	v_pk_mul_f32 v[142:143], v[142:143], s[18:19] op_sel_hi:[1,0]
	v_pk_mul_f32 v[140:141], v[140:141], s[18:19] op_sel_hi:[1,0]
	v_pk_mul_f32 v[138:139], v[138:139], s[18:19] op_sel_hi:[1,0]
	v_exp_f32_e32 v142, v142
	v_exp_f32_e32 v138, v138
	v_exp_f32_e32 v143, v143
	v_exp_f32_e32 v139, v139
	v_exp_f32_e32 v144, v144
	v_exp_f32_e32 v145, v145
	v_exp_f32_e32 v140, v140
	v_exp_f32_e32 v141, v141
	v_pk_add_f32 v[142:143], v[142:143], 1.0 op_sel_hi:[1,0]
	v_pk_add_f32 v[144:145], v[144:145], 1.0 op_sel_hi:[1,0]
	v_pk_add_f32 v[138:139], v[138:139], 1.0 op_sel_hi:[1,0]
	v_pk_add_f32 v[140:141], v[140:141], 1.0 op_sel_hi:[1,0]
	v_rcp_f32_e32 v142, v142
	v_rcp_f32_e32 v230, v138
	v_rcp_f32_e32 v143, v143
	v_rcp_f32_e32 v231, v139
	v_rcp_f32_e32 v138, v144
	v_rcp_f32_e32 v139, v145
	v_rcp_f32_e32 v144, v140
	v_rcp_f32_e32 v145, v141
	v_or_b32_e32 v208, s40, v217
	v_mov_b32_e32 v209, s41
	v_ashrrev_i32_e32 v217, 31, v216
	v_lshl_add_u64 v[208:209], v[208:209], 0, s[6:7]
	v_lshlrev_b64 v[216:217], 10, v[216:217]
	v_lshl_add_u64 v[220:221], v[216:217], 0, v[208:209]
	s_and_b64 vcc, exec, s[12:13]
	s_waitcnt vmcnt(0)
	v_lshlrev_b32_e32 v218, 16, v188
	v_and_b32_e32 v219, 0xffff0000, v188
	v_lshlrev_b32_e32 v188, 16, v189
	v_and_b32_e32 v189, 0xffff0000, v189
	v_lshlrev_b32_e32 v226, 16, v190
	v_and_b32_e32 v227, 0xffff0000, v190
	v_lshlrev_b32_e32 v190, 16, v191
	v_and_b32_e32 v191, 0xffff0000, v191
	v_lshlrev_b32_e32 v250, 16, v192
	v_and_b32_e32 v251, 0xffff0000, v192
	v_lshlrev_b32_e32 v192, 16, v193
	v_and_b32_e32 v193, 0xffff0000, v193
	v_lshlrev_b32_e32 v224, 16, v194
	v_and_b32_e32 v225, 0xffff0000, v194
	v_lshlrev_b32_e32 v194, 16, v195
	v_and_b32_e32 v195, 0xffff0000, v195
	v_pk_fma_f32 v[140:141], v[138:139], v[192:193], v[188:189]
	v_pk_fma_f32 v[138:139], v[142:143], v[250:251], v[218:219]
	v_pk_fma_f32 v[144:145], v[144:145], v[194:195], v[190:191]
	v_pk_fma_f32 v[142:143], v[230:231], v[224:225], v[226:227]
	v_lshl_add_u64 v[218:219], v[220:221], 2, s[8:9]
	s_cbranch_vccz .LBB0_1973
	global_store_dwordx4 v[218:219], v[138:141], off
	global_store_dwordx4 v[218:219], v[142:145], off offset:16
	v_mov_b64_e32 v[250:251], v[186:187]
	s_cbranch_execnz .LBB0_1929
